# GEMM epilogues: cross-lane xor-16/xor-32 adds via v_permlane16/32_swap instead of ds_bpermute + lgkmcnt waits (160 sites, bit-identical sums)
# baseline (speedup 1.0000x reference)
; __device__ __forceinline__ float rstd_fin4(const f32x4 a) { float s = (a[0] + a[1]) + (a[2] + a[3]); s += __shfl_xor(s, 16); s += __shfl_xor(s, 32); return __builtin_amdgcn_rsqf(s * (1.f / 1024.f) + 1e-6f); }
;     __device__ __forceinline__ void operator()(const f32x4 (&acc)[2][2][4][2], const Unit& u, int wr, int wc, int fr, int fq) const {
;         asm volatile("" : "+v"(fr), "+v"(fq));
;         const int row0 = u.pm * BM + wr * 64 + fr;
;         unsigned char* const hb = (unsigned char*)H + (size_t)(u.pm * (FFH / 128) + u.pn + pn0) * 32768 + (((wr * 4 + wc) * 8) * 64 + (fq >> 1) * 32 + fr * 2 + (fq & 1)) * 8;
;         f32x4 pa[2][4];
; #pragma unroll
;         for (int ai = 0; ai < 2; ++ai)
; #pragma unroll
;             for (int m = 0; m < 4; ++m) pa[ai][m] = rstd_ld4(ss, row0 + ai * HALF + m * 16, fq);
; #pragma unroll
;         for (int ai = 0; ai < 2; ++ai)
; #pragma unroll
;             for (int m = 0; m < 4; ++m) { const float rs = rstd_fin4(pa[ai][m]) * sc;
;                 const float rsl = rs * 1.4426950408889634f, rsu = rs * 0.6931471805599453f;
;                 f32x4 h0, h1;
; #pragma unroll
;                 for (int n = 0; n < 2; ++n) { const f32x4 G = acc[ai][0][m][n], U = acc[ai][1][m][n]; f32x4 hv;
; #pragma unroll
;                     for (int q = 0; q < 2; ++q) { const f32x2 g2 = (f32x2){G[2 * q], G[2 * q + 1]} * rsl, u2 = (f32x2){U[2 * q], U[2 * q + 1]} * rsu;
;                         f32x2 r2; r2.x = __builtin_amdgcn_rcpf(1.f + __builtin_amdgcn_exp2f(-g2.x)); r2.y = __builtin_amdgcn_rcpf(1.f + __builtin_amdgcn_exp2f(-g2.y));
;                         const f32x2 o2 = g2 * u2 * r2; hv[2 * q] = o2.x; hv[2 * q + 1] = o2.y; }
;                     if (n == 0) h0 = hv; else h1 = hv; }
;                 unsigned w0 = 0u, w1 = 0u;
;                 w0 = __builtin_amdgcn_cvt_pk_fp8_f32(h0[0], h0[1], w0, false); w0 = __builtin_amdgcn_cvt_pk_fp8_f32(h0[2], h0[3], w0, true); w1 = __builtin_amdgcn_cvt_pk_fp8_f32(h1[0], h1[1], w1, false); w1 = __builtin_amdgcn_cvt_pk_fp8_f32(h1[2], h1[3], w1, true);
;                 *(u32x2*)(hb + (ai * 4 + m) * 512) = (u32x2){w0, w1}; asm volatile("" ::: "memory"); }
.LBB0_434:
	s_lshl_b32 s4, s71, 8
	v_mov_b32_e32 v142, v1
	v_mov_b32_e32 v143, v164
	s_add_i32 s4, s4, s47
	v_and_b32_e32 v145, 64, v246
	v_add_u32_e32 v132, s4, v142
	v_lshlrev_b32_e32 v134, 2, v143
	v_ashrrev_i32_e32 v135, 31, v134
	v_ashrrev_i32_e32 v133, 31, v132
	v_lshl_add_u64 v[134:135], v[134:135], 2, s[48:49]
	v_lshlrev_b64 v[132:133], 6, v[132:133]
	v_lshl_add_u64 v[140:141], v[134:135], 0, v[132:133]
	global_load_dwordx4 v[132:135], v[140:141], off
	global_load_dwordx4 v[136:139], v[140:141], off offset:1024
	global_load_dwordx4 v[170:173], v[140:141], off offset:2048
	global_load_dwordx4 v[148:151], v[140:141], off offset:3072
	v_xor_b32_e32 v144, 16, v246
	v_add_u32_e32 v145, 64, v145
	v_xor_b32_e32 v146, 32, v246
	v_cmp_lt_i32_e32 vcc, v144, v145
	s_mul_i32 s4, s71, 22
	s_add_i32 s4, s4, s70
	v_cndmask_b32_e32 v144, v246, v144, vcc
	v_cmp_lt_i32_e32 vcc, v146, v145
	v_lshlrev_b32_e32 v168, 2, v144
	s_ashr_i32 s5, s4, 31
	v_cndmask_b32_e32 v145, v246, v146, vcc
	v_lshlrev_b32_e32 v167, 2, v145
	v_lshlrev_b32_e32 v147, 4, v143
	v_lshl_add_u32 v142, v142, 1, s68
	s_lshl_b64 s[4:5], s[4:5], 15
	v_and_b32_e32 v146, 0x1fffffe0, v147
	v_and_or_b32 v142, v143, 1, v142
	v_add_lshl_u32 v142, v142, v146, 3
	s_add_u32 s4, s22, s4
	v_ashrrev_i32_e32 v143, 31, v142
	s_addc_u32 s5, s23, s5
	v_lshl_add_u64 v[162:163], s[4:5], 0, v[142:143]
	v_mov_b32_e32 v174, v3
	v_mov_b32_e32 v175, v3
	s_mov_b64 s[4:5], -1
	s_waitcnt vmcnt(0)
	v_mov_b32_e32 v144, v133
	v_mov_b32_e32 v145, v134
	v_mov_b32_e32 v133, v135
	v_mov_b32_e32 v134, v137
	v_mov_b32_e32 v135, v138
	v_mov_b32_e32 v137, v139
	v_pk_add_f32 v[134:135], v[134:135], v[136:137]
	v_pk_add_f32 v[132:133], v[144:145], v[132:133]
	v_add_f32_e32 v134, v134, v135
	v_add_f32_e32 v136, v132, v133
	v_mov_b32_e32 v137, v134
	s_nop 1
	v_permlane16_swap_b32_e32 v137, v134
	v_mov_b32_e32 v135, v136
	s_nop 1
	v_permlane16_swap_b32_e32 v135, v136
	v_add_co_u32_e32 v132, vcc, s88, v140
	s_waitcnt lgkmcnt(1)
	v_add_f32_e32 v134, v134, v137
	s_waitcnt lgkmcnt(0)
	v_add_f32_e32 v135, v136, v135
	v_mov_b32_e32 v137, v134
	s_nop 1
	v_permlane32_swap_b32_e32 v137, v134
	v_mov_b32_e32 v136, v135
	s_nop 1
	v_permlane32_swap_b32_e32 v136, v135
	v_addc_co_u32_e32 v133, vcc, 0, v141, vcc
	global_load_dwordx4 v[144:147], v[132:133], off
	global_load_dwordx4 v[140:143], v[132:133], off offset:1024
	s_waitcnt lgkmcnt(1)
	v_add_f32_e32 v134, v134, v137
	s_waitcnt lgkmcnt(0)
	v_add_f32_e32 v135, v135, v136
	v_fmamk_f32 v134, v134, 0x3a800000, v227
	v_fmamk_f32 v135, v135, 0x3a800000, v227
	v_rsq_f32_e32 v177, v134
	v_rsq_f32_e32 v169, v135
	global_load_dwordx4 v[136:139], v[132:133], off offset:2048
	s_nop 0
	global_load_dwordx4 v[132:135], v[132:133], off offset:3072
	s_andn2_b64 vcc, exec, s[38:39]
	v_mul_f32_e32 v180, 0x3fb8aa3b, v177
	v_mul_f32_e32 v182, 0x3f317218, v177
	v_mul_f32_e32 v176, 0x3fb8aa3b, v169
	v_mul_f32_e32 v178, 0x3f317218, v169
	v_pk_mul_f32 v[112:113], v[112:113], v[180:181] op_sel_hi:[1,0]
	v_pk_mul_f32 v[104:105], v[104:105], v[182:183] op_sel_hi:[1,0]
	v_pk_mul_f32 v[128:129], v[128:129], v[176:177] op_sel_hi:[1,0]
	v_pk_mul_f32 v[120:121], v[120:121], v[178:179] op_sel_hi:[1,0]
	v_pk_mul_f32 v[130:131], v[130:131], v[176:177] op_sel_hi:[1,0]
	v_pk_mul_f32 v[122:123], v[122:123], v[178:179] op_sel_hi:[1,0]
	v_pk_mul_f32 v[124:125], v[124:125], v[176:177] op_sel_hi:[1,0]
	v_pk_mul_f32 v[116:117], v[116:117], v[178:179] op_sel_hi:[1,0]
	v_pk_mul_f32 v[126:127], v[126:127], v[176:177] op_sel_hi:[1,0]
	v_pk_mul_f32 v[118:119], v[118:119], v[178:179] op_sel_hi:[1,0]
	v_exp_f32_e64 v177, -v112
	v_exp_f32_e64 v178, -v113
	v_pk_mul_f32 v[104:105], v[112:113], v[104:105]
	v_pk_mul_f32 v[112:113], v[114:115], v[180:181] op_sel_hi:[1,0]
	v_pk_mul_f32 v[106:107], v[106:107], v[182:183] op_sel_hi:[1,0]
	v_exp_f32_e64 v114, -v112
	v_exp_f32_e64 v115, -v113
	v_pk_mul_f32 v[108:109], v[108:109], v[180:181] op_sel_hi:[1,0]
	v_pk_mul_f32 v[106:107], v[112:113], v[106:107]
	v_add_f32_e32 v114, 1.0, v114
	v_add_f32_e32 v115, 1.0, v115
	v_exp_f32_e64 v112, -v108
	v_exp_f32_e64 v113, -v109
	v_rcp_f32_e32 v114, v114
	v_rcp_f32_e32 v115, v115
	v_exp_f32_e64 v169, -v128
	v_exp_f32_e64 v176, -v129
	v_pk_mul_f32 v[120:121], v[128:129], v[120:121]
	v_exp_f32_e64 v128, -v130
	v_exp_f32_e64 v129, -v131
	v_pk_mul_f32 v[122:123], v[130:131], v[122:123]
	v_exp_f32_e64 v130, -v124
	v_exp_f32_e64 v131, -v125
	v_pk_mul_f32 v[116:117], v[124:125], v[116:117]
	v_exp_f32_e64 v124, -v126
	v_exp_f32_e64 v125, -v127
	v_add_f32_e32 v112, 1.0, v112
	v_add_f32_e32 v113, 1.0, v113
	v_pk_mul_f32 v[110:111], v[110:111], v[180:181] op_sel_hi:[1,0]
	v_pk_mul_f32 v[106:107], v[106:107], v[114:115]
	v_rcp_f32_e32 v112, v112
	v_rcp_f32_e32 v113, v113
	v_exp_f32_e64 v114, -v110
	v_pk_mul_f32 v[100:101], v[100:101], v[182:183] op_sel_hi:[1,0]
	v_pk_mul_f32 v[118:119], v[126:127], v[118:119]
	v_add_f32_e32 v126, 1.0, v169
	v_add_f32_e32 v127, 1.0, v176
	v_pk_mul_f32 v[100:101], v[108:109], v[100:101]
	v_mov_b32_e32 v108, v171
	v_mov_b32_e32 v109, v172
	v_mov_b32_e32 v171, v173
	v_add_f32_e32 v169, 1.0, v124
	v_add_f32_e32 v176, 1.0, v125
	v_rcp_f32_e32 v124, v126
	v_rcp_f32_e32 v125, v127
	v_pk_add_f32 v[108:109], v[108:109], v[170:171]
	v_pk_mul_f32 v[100:101], v[100:101], v[112:113]
	v_add_f32_e32 v112, 1.0, v114
	v_add_f32_e32 v114, v108, v109
	v_add_f32_e32 v128, 1.0, v128
	v_add_f32_e32 v129, 1.0, v129
	v_add_f32_e32 v130, 1.0, v130
	v_add_f32_e32 v131, 1.0, v131
	v_mov_b32_e32 v115, v114
	s_nop 1
	v_permlane16_swap_b32_e32 v115, v114
	v_rcp_f32_e32 v126, v128
	v_rcp_f32_e32 v127, v129
	v_rcp_f32_e32 v128, v130
	v_rcp_f32_e32 v129, v131
	v_pk_mul_f32 v[120:121], v[120:121], v[124:125]
	v_exp_f32_e64 v113, -v111
	v_cvt_pk_fp8_f32 v174, v120, v121
	v_pk_mul_f32 v[116:117], v[116:117], v[128:129]
	v_rcp_f32_e32 v108, v112
	s_waitcnt lgkmcnt(0)
; __device__ __forceinline__ float rstd_fin4(const f32x4 a) { float s = (a[0] + a[1]) + (a[2] + a[3]); s += __shfl_xor(s, 16); s += __shfl_xor(s, 32); return __builtin_amdgcn_rsqf(s * (1.f / 1024.f) + 1e-6f); }
;     __device__ __forceinline__ void operator()(const f32x4 (&acc)[2][2][4][2], const Unit& u, int wr, int wc, int fr, int fq) const {
;     ...
;             for (int m = 0; m < 4; ++m) { const float rs = rstd_fin4(pa[ai][m]) * sc;
;                 const float rsl = rs * 1.4426950408889634f, rsu = rs * 0.6931471805599453f;
;                 f32x4 h0, h1;
; #pragma unroll
;                 for (int n = 0; n < 2; ++n) { const f32x4 G = acc[ai][0][m][n], U = acc[ai][1][m][n]; f32x4 hv;
; #pragma unroll
;                     for (int q = 0; q < 2; ++q) { const f32x2 g2 = (f32x2){G[2 * q], G[2 * q + 1]} * rsl, u2 = (f32x2){U[2 * q], U[2 * q + 1]} * rsu;
;                         f32x2 r2; r2.x = __builtin_amdgcn_rcpf(1.f + __builtin_amdgcn_exp2f(-g2.x)); r2.y = __builtin_amdgcn_rcpf(1.f + __builtin_amdgcn_exp2f(-g2.y));
;                         const f32x2 o2 = g2 * u2 * r2; hv[2 * q] = o2.x; hv[2 * q + 1] = o2.y; }
;                     if (n == 0) h0 = hv; else h1 = hv; }
;                 unsigned w0 = 0u, w1 = 0u;
;                 w0 = __builtin_amdgcn_cvt_pk_fp8_f32(h0[0], h0[1], w0, false); w0 = __builtin_amdgcn_cvt_pk_fp8_f32(h0[2], h0[3], w0, true); w1 = __builtin_amdgcn_cvt_pk_fp8_f32(h1[0], h1[1], w1, false); w1 = __builtin_amdgcn_cvt_pk_fp8_f32(h1[2], h1[3], w1, true);
;                 *(u32x2*)(hb + (ai * 4 + m) * 512) = (u32x2){w0, w1}; asm volatile("" ::: "memory"); }
	v_add_f32_e32 v112, v114, v115
	v_cvt_pk_fp8_f32 v175, v116, v117
	v_pk_mul_f32 v[116:117], v[122:123], v[126:127]
	v_add_f32_e32 v109, 1.0, v113
	v_mov_b32_e32 v113, v112
	s_nop 1
	v_permlane32_swap_b32_e32 v113, v112
	v_cvt_pk_fp8_f32 v174, v116, v117 op_sel:[0,0,1]
	v_add_f32_e32 v116, 1.0, v177
	v_add_f32_e32 v117, 1.0, v178
	v_rcp_f32_e32 v116, v116
	v_rcp_f32_e32 v117, v117
	v_pk_mul_f32 v[102:103], v[102:103], v[182:183] op_sel_hi:[1,0]
	v_rcp_f32_e32 v109, v109
	v_pk_mul_f32 v[102:103], v[110:111], v[102:103]
	v_mov_b32_e32 v111, v3
	v_cvt_pk_fp8_f32 v111, v100, v101
	s_waitcnt lgkmcnt(0)
	v_add_f32_e32 v100, v112, v113
	v_pk_mul_f32 v[104:105], v[104:105], v[116:117]
	v_mov_b32_e32 v110, v3
	v_fmamk_f32 v100, v100, 0x3a800000, v227
	v_cvt_pk_fp8_f32 v110, v104, v105
	v_rsq_f32_e32 v104, v100
	v_pk_mul_f32 v[100:101], v[102:103], v[108:109]
	v_rcp_f32_e32 v130, v169
	v_cvt_pk_fp8_f32 v111, v100, v101 op_sel:[0,0,1]
	v_mul_f32_e32 v100, 0x3fb8aa3b, v104
	v_pk_mul_f32 v[96:97], v[96:97], v[100:101] op_sel_hi:[1,0]
	v_mul_f32_e32 v102, 0x3f317218, v104
	v_exp_f32_e64 v101, -v96
	v_exp_f32_e64 v103, -v97
	v_rcp_f32_e32 v131, v176
	v_cvt_pk_fp8_f32 v110, v106, v107 op_sel:[0,0,1]
	v_add_f32_e32 v101, 1.0, v101
	v_pk_mul_f32 v[88:89], v[88:89], v[102:103] op_sel_hi:[1,0]
	v_rcp_f32_e32 v104, v101
	v_add_f32_e32 v101, 1.0, v103
	v_pk_mul_f32 v[88:89], v[96:97], v[88:89]
	v_pk_mul_f32 v[96:97], v[98:99], v[100:101] op_sel_hi:[1,0]
	v_pk_mul_f32 v[90:91], v[90:91], v[102:103] op_sel_hi:[1,0]
	v_pk_mul_f32 v[92:93], v[92:93], v[100:101] op_sel_hi:[1,0]
	v_exp_f32_e64 v98, -v96
	v_exp_f32_e64 v99, -v97
	v_pk_mul_f32 v[90:91], v[96:97], v[90:91]
	v_exp_f32_e64 v96, -v92
	v_exp_f32_e64 v97, -v93
	v_add_f32_e32 v98, 1.0, v98
	v_add_f32_e32 v99, 1.0, v99
	v_add_f32_e32 v96, 1.0, v96
	v_add_f32_e32 v97, 1.0, v97
	v_rcp_f32_e32 v96, v96
	v_rcp_f32_e32 v97, v97
	v_rcp_f32_e32 v98, v98
	v_rcp_f32_e32 v99, v99
	v_pk_mul_f32 v[84:85], v[84:85], v[102:103] op_sel_hi:[1,0]
	v_rcp_f32_e32 v105, v101
	v_pk_mul_f32 v[84:85], v[92:93], v[84:85]
	v_pk_mul_f32 v[90:91], v[90:91], v[98:99]
	v_pk_mul_f32 v[84:85], v[84:85], v[96:97]
	v_mov_b32_e32 v96, v149
	v_mov_b32_e32 v97, v150
	v_mov_b32_e32 v149, v151
	v_pk_add_f32 v[96:97], v[96:97], v[148:149]
	v_pk_mul_f32 v[92:93], v[94:95], v[100:101] op_sel_hi:[1,0]
	v_add_f32_e32 v98, v96, v97
	v_mov_b32_e32 v99, v98
	s_nop 1
	v_permlane16_swap_b32_e32 v99, v98
	v_exp_f32_e64 v94, -v92
	v_exp_f32_e64 v95, -v93
	v_pk_mul_f32 v[88:89], v[88:89], v[104:105]
	v_mov_b32_e32 v96, v3
	v_add_f32_e32 v94, 1.0, v94
	v_add_f32_e32 v95, 1.0, v95
	v_cvt_pk_fp8_f32 v96, v88, v89
	s_waitcnt lgkmcnt(0)
	v_add_f32_e32 v88, v98, v99
	v_rcp_f32_e32 v94, v94
	v_rcp_f32_e32 v95, v95
	v_mov_b32_e32 v97, v3
	v_mov_b32_e32 v89, v88
	s_nop 1
	v_permlane32_swap_b32_e32 v89, v88
	v_cvt_pk_fp8_f32 v97, v84, v85
	v_pk_mul_f32 v[86:87], v[86:87], v[102:103] op_sel_hi:[1,0]
	v_pk_mul_f32 v[118:119], v[118:119], v[130:131]
	v_pk_mul_f32 v[84:85], v[92:93], v[86:87]
	v_cvt_pk_fp8_f32 v175, v118, v119 op_sel:[0,0,1]
	v_pk_mul_f32 v[84:85], v[84:85], v[94:95]
	v_cvt_pk_fp8_f32 v96, v90, v91 op_sel:[0,0,1]
	v_cvt_pk_fp8_f32 v97, v84, v85 op_sel:[0,0,1]
	s_waitcnt lgkmcnt(0)
	v_add_f32_e32 v84, v88, v89
	v_fmamk_f32 v84, v84, 0x3a800000, v227
	v_rsq_f32_e32 v85, v84
	global_store_dwordx2 v[162:163], v[174:175], off
	global_store_dwordx2 v[162:163], v[110:111], off offset:512
	v_mul_f32_e32 v84, 0x3fb8aa3b, v85
	v_pk_mul_f32 v[80:81], v[80:81], v[84:85] op_sel_hi:[1,0]
	v_mul_f32_e32 v86, 0x3f317218, v85
	v_exp_f32_e64 v87, -v80
	v_exp_f32_e64 v85, -v81
	global_store_dwordx2 v[162:163], v[96:97], off offset:1024
	v_pk_mul_f32 v[72:73], v[72:73], v[86:87] op_sel_hi:[1,0]
	v_add_f32_e32 v87, 1.0, v87
	v_add_f32_e32 v85, 1.0, v85
	v_pk_mul_f32 v[72:73], v[80:81], v[72:73]
	v_pk_mul_f32 v[80:81], v[82:83], v[84:85] op_sel_hi:[1,0]
	v_pk_mul_f32 v[74:75], v[74:75], v[86:87] op_sel_hi:[1,0]
	v_pk_mul_f32 v[76:77], v[76:77], v[84:85] op_sel_hi:[1,0]
	v_exp_f32_e64 v82, -v80
	v_exp_f32_e64 v83, -v81
	v_pk_mul_f32 v[74:75], v[80:81], v[74:75]
	v_exp_f32_e64 v80, -v76
	v_exp_f32_e64 v81, -v77
	v_add_f32_e32 v82, 1.0, v82
	v_add_f32_e32 v83, 1.0, v83
	v_add_f32_e32 v80, 1.0, v80
	v_add_f32_e32 v81, 1.0, v81
	v_rcp_f32_e32 v80, v80
	v_rcp_f32_e32 v81, v81
	v_rcp_f32_e32 v82, v82
	v_rcp_f32_e32 v83, v83
	v_pk_mul_f32 v[68:69], v[68:69], v[86:87] op_sel_hi:[1,0]
	v_rcp_f32_e32 v88, v87
	v_pk_mul_f32 v[68:69], v[76:77], v[68:69]
	v_pk_mul_f32 v[74:75], v[74:75], v[82:83]
	v_pk_mul_f32 v[68:69], v[68:69], v[80:81]
	s_waitcnt vmcnt(6)
	v_mov_b32_e32 v80, v145
	v_mov_b32_e32 v81, v146
	v_mov_b32_e32 v145, v147
	v_pk_add_f32 v[80:81], v[80:81], v[144:145]
	v_rcp_f32_e32 v89, v85
	v_add_f32_e32 v82, v80, v81
	v_pk_mul_f32 v[76:77], v[78:79], v[84:85] op_sel_hi:[1,0]
	v_mov_b32_e32 v83, v82
	s_nop 1
	v_permlane16_swap_b32_e32 v83, v82
	v_exp_f32_e64 v78, -v76
	v_exp_f32_e64 v79, -v77
	v_pk_mul_f32 v[72:73], v[72:73], v[88:89]
	v_mov_b32_e32 v80, v3
	v_add_f32_e32 v78, 1.0, v78
	v_add_f32_e32 v79, 1.0, v79
	v_cvt_pk_fp8_f32 v80, v72, v73
	s_waitcnt lgkmcnt(0)
	v_add_f32_e32 v72, v82, v83
	v_rcp_f32_e32 v78, v78
	v_rcp_f32_e32 v79, v79
	v_mov_b32_e32 v81, v3
	v_mov_b32_e32 v73, v72
	s_nop 1
	v_permlane32_swap_b32_e32 v73, v72
	v_cvt_pk_fp8_f32 v81, v68, v69
	v_pk_mul_f32 v[70:71], v[70:71], v[86:87] op_sel_hi:[1,0]
	v_cvt_pk_fp8_f32 v80, v74, v75 op_sel:[0,0,1]
	v_pk_mul_f32 v[68:69], v[76:77], v[70:71]
	s_nop 0
	v_pk_mul_f32 v[68:69], v[68:69], v[78:79]
	s_nop 0
	v_cvt_pk_fp8_f32 v81, v68, v69 op_sel:[0,0,1]
	s_waitcnt lgkmcnt(0)
; __device__ __forceinline__ float rstd_fin4(const f32x4 a) { float s = (a[0] + a[1]) + (a[2] + a[3]); s += __shfl_xor(s, 16); s += __shfl_xor(s, 32); return __builtin_amdgcn_rsqf(s * (1.f / 1024.f) + 1e-6f); }
;     __device__ __forceinline__ void operator()(const f32x4 (&acc)[2][2][4][2], const Unit& u, int wr, int wc, int fr, int fq) const {
;     ...
;             for (int m = 0; m < 4; ++m) { const float rs = rstd_fin4(pa[ai][m]) * sc;
;                 const float rsl = rs * 1.4426950408889634f, rsu = rs * 0.6931471805599453f;
;                 f32x4 h0, h1;
; #pragma unroll
;                 for (int n = 0; n < 2; ++n) { const f32x4 G = acc[ai][0][m][n], U = acc[ai][1][m][n]; f32x4 hv;
; #pragma unroll
;                     for (int q = 0; q < 2; ++q) { const f32x2 g2 = (f32x2){G[2 * q], G[2 * q + 1]} * rsl, u2 = (f32x2){U[2 * q], U[2 * q + 1]} * rsu;
;                         f32x2 r2; r2.x = __builtin_amdgcn_rcpf(1.f + __builtin_amdgcn_exp2f(-g2.x)); r2.y = __builtin_amdgcn_rcpf(1.f + __builtin_amdgcn_exp2f(-g2.y));
;                         const f32x2 o2 = g2 * u2 * r2; hv[2 * q] = o2.x; hv[2 * q + 1] = o2.y; }
;                     if (n == 0) h0 = hv; else h1 = hv; }
;                 unsigned w0 = 0u, w1 = 0u;
;                 w0 = __builtin_amdgcn_cvt_pk_fp8_f32(h0[0], h0[1], w0, false); w0 = __builtin_amdgcn_cvt_pk_fp8_f32(h0[2], h0[3], w0, true); w1 = __builtin_amdgcn_cvt_pk_fp8_f32(h1[0], h1[1], w1, false); w1 = __builtin_amdgcn_cvt_pk_fp8_f32(h1[2], h1[3], w1, true);
;                 *(u32x2*)(hb + (ai * 4 + m) * 512) = (u32x2){w0, w1}; asm volatile("" ::: "memory"); }
	v_add_f32_e32 v68, v72, v73
	v_fmamk_f32 v68, v68, 0x3a800000, v227
	v_rsq_f32_e32 v69, v68
	global_store_dwordx2 v[162:163], v[80:81], off offset:1536
	v_mul_f32_e32 v68, 0x3fb8aa3b, v69
	v_pk_mul_f32 v[64:65], v[64:65], v[68:69] op_sel_hi:[1,0]
	v_mul_f32_e32 v70, 0x3f317218, v69
	v_exp_f32_e64 v71, -v64
	v_exp_f32_e64 v69, -v65
	v_pk_mul_f32 v[56:57], v[56:57], v[70:71] op_sel_hi:[1,0]
	v_add_f32_e32 v69, 1.0, v69
	v_pk_mul_f32 v[56:57], v[64:65], v[56:57]
	v_pk_mul_f32 v[64:65], v[66:67], v[68:69] op_sel_hi:[1,0]
	v_add_f32_e32 v71, 1.0, v71
	v_exp_f32_e64 v66, -v64
	v_exp_f32_e64 v67, -v65
	v_pk_mul_f32 v[58:59], v[58:59], v[70:71] op_sel_hi:[1,0]
	v_pk_mul_f32 v[60:61], v[60:61], v[68:69] op_sel_hi:[1,0]
	v_add_f32_e32 v66, 1.0, v66
	v_add_f32_e32 v67, 1.0, v67
	v_pk_mul_f32 v[58:59], v[64:65], v[58:59]
	v_exp_f32_e64 v64, -v60
	v_exp_f32_e64 v65, -v61
	v_rcp_f32_e32 v66, v66
	v_rcp_f32_e32 v67, v67
	v_add_f32_e32 v64, 1.0, v64
	v_add_f32_e32 v65, 1.0, v65
	v_pk_mul_f32 v[62:63], v[62:63], v[68:69] op_sel_hi:[1,0]
	v_pk_mul_f32 v[58:59], v[58:59], v[66:67]
	v_rcp_f32_e32 v64, v64
	v_rcp_f32_e32 v65, v65
	v_exp_f32_e64 v66, -v62
	v_pk_mul_f32 v[52:53], v[52:53], v[70:71] op_sel_hi:[1,0]
	v_rcp_f32_e32 v72, v71
	v_pk_mul_f32 v[52:53], v[60:61], v[52:53]
	s_waitcnt vmcnt(6)
	v_mov_b32_e32 v60, v141
	v_mov_b32_e32 v61, v142
	v_mov_b32_e32 v141, v143
	v_pk_add_f32 v[60:61], v[60:61], v[140:141]
	v_pk_mul_f32 v[52:53], v[52:53], v[64:65]
	v_add_f32_e32 v64, 1.0, v66
	v_add_f32_e32 v66, v60, v61
	v_mov_b32_e32 v67, v66
	s_nop 1
	v_permlane16_swap_b32_e32 v67, v66
	v_exp_f32_e64 v65, -v63
	v_rcp_f32_e32 v60, v64
	v_rcp_f32_e32 v73, v69
	v_pk_mul_f32 v[54:55], v[54:55], v[70:71] op_sel_hi:[1,0]
	s_waitcnt lgkmcnt(0)
	v_add_f32_e32 v64, v66, v67
	v_add_f32_e32 v61, 1.0, v65
	v_mov_b32_e32 v65, v64
	s_nop 1
	v_permlane32_swap_b32_e32 v65, v64
	v_pk_mul_f32 v[54:55], v[62:63], v[54:55]
	v_mov_b32_e32 v63, v3
	v_cvt_pk_fp8_f32 v63, v52, v53
	v_pk_mul_f32 v[56:57], v[56:57], v[72:73]
	s_waitcnt lgkmcnt(0)
	v_add_f32_e32 v52, v64, v65
	v_rcp_f32_e32 v61, v61
	v_mov_b32_e32 v62, v3
	v_fmamk_f32 v52, v52, 0x3a800000, v227
	v_cvt_pk_fp8_f32 v62, v56, v57
	v_rsq_f32_e32 v56, v52
	v_pk_mul_f32 v[52:53], v[54:55], v[60:61]
	v_cvt_pk_fp8_f32 v62, v58, v59 op_sel:[0,0,1]
	v_cvt_pk_fp8_f32 v63, v52, v53 op_sel:[0,0,1]
	v_mul_f32_e32 v52, 0x3fb8aa3b, v56
	v_pk_mul_f32 v[48:49], v[48:49], v[52:53] op_sel_hi:[1,0]
	v_mul_f32_e32 v54, 0x3f317218, v56
	v_exp_f32_e64 v53, -v48
	v_exp_f32_e64 v55, -v49
	global_store_dwordx2 v[162:163], v[62:63], off offset:2048
	v_add_f32_e32 v53, 1.0, v53
	v_pk_mul_f32 v[40:41], v[40:41], v[54:55] op_sel_hi:[1,0]
	v_rcp_f32_e32 v56, v53
	v_add_f32_e32 v53, 1.0, v55
	v_pk_mul_f32 v[40:41], v[48:49], v[40:41]
	v_pk_mul_f32 v[48:49], v[50:51], v[52:53] op_sel_hi:[1,0]
	v_pk_mul_f32 v[42:43], v[42:43], v[54:55] op_sel_hi:[1,0]
	v_pk_mul_f32 v[44:45], v[44:45], v[52:53] op_sel_hi:[1,0]
	v_exp_f32_e64 v50, -v48
	v_exp_f32_e64 v51, -v49
	v_pk_mul_f32 v[42:43], v[48:49], v[42:43]
	v_exp_f32_e64 v48, -v44
	v_exp_f32_e64 v49, -v45
	v_add_f32_e32 v50, 1.0, v50
	v_add_f32_e32 v51, 1.0, v51
	v_add_f32_e32 v48, 1.0, v48
	v_add_f32_e32 v49, 1.0, v49
	v_rcp_f32_e32 v48, v48
	v_rcp_f32_e32 v49, v49
	v_rcp_f32_e32 v50, v50
	v_rcp_f32_e32 v51, v51
	v_pk_mul_f32 v[36:37], v[36:37], v[54:55] op_sel_hi:[1,0]
	v_rcp_f32_e32 v57, v53
	v_pk_mul_f32 v[36:37], v[44:45], v[36:37]
	v_pk_mul_f32 v[42:43], v[42:43], v[50:51]
	v_pk_mul_f32 v[36:37], v[36:37], v[48:49]
	s_waitcnt vmcnt(6)
	v_mov_b32_e32 v48, v137
	v_mov_b32_e32 v49, v138
	v_mov_b32_e32 v137, v139
	v_pk_add_f32 v[48:49], v[48:49], v[136:137]
	v_pk_mul_f32 v[44:45], v[46:47], v[52:53] op_sel_hi:[1,0]
	v_add_f32_e32 v50, v48, v49
	v_mov_b32_e32 v51, v50
	s_nop 1
	v_permlane16_swap_b32_e32 v51, v50
	v_exp_f32_e64 v46, -v44
	v_exp_f32_e64 v47, -v45
	v_pk_mul_f32 v[40:41], v[40:41], v[56:57]
	v_mov_b32_e32 v48, v3
	v_add_f32_e32 v46, 1.0, v46
	v_add_f32_e32 v47, 1.0, v47
	v_cvt_pk_fp8_f32 v48, v40, v41
	s_waitcnt lgkmcnt(0)
	v_add_f32_e32 v40, v50, v51
	v_rcp_f32_e32 v46, v46
	v_rcp_f32_e32 v47, v47
	v_mov_b32_e32 v49, v3
	v_mov_b32_e32 v41, v40
	s_nop 1
	v_permlane32_swap_b32_e32 v41, v40
	v_cvt_pk_fp8_f32 v49, v36, v37
	v_pk_mul_f32 v[38:39], v[38:39], v[54:55] op_sel_hi:[1,0]
	v_cvt_pk_fp8_f32 v48, v42, v43 op_sel:[0,0,1]
	v_pk_mul_f32 v[36:37], v[44:45], v[38:39]
	s_nop 0
	v_pk_mul_f32 v[36:37], v[36:37], v[46:47]
	s_nop 0
	v_cvt_pk_fp8_f32 v49, v36, v37 op_sel:[0,0,1]
	s_waitcnt lgkmcnt(0)
; __device__ __forceinline__ float rstd_fin4(const f32x4 a) { float s = (a[0] + a[1]) + (a[2] + a[3]); s += __shfl_xor(s, 16); s += __shfl_xor(s, 32); return __builtin_amdgcn_rsqf(s * (1.f / 1024.f) + 1e-6f); }
;     __device__ __forceinline__ void operator()(const f32x4 (&acc)[2][2][4][2], const Unit& u, int wr, int wc, int fr, int fq) const {
;     ...
;             for (int m = 0; m < 4; ++m) { const float rs = rstd_fin4(pa[ai][m]) * sc;
;                 const float rsl = rs * 1.4426950408889634f, rsu = rs * 0.6931471805599453f;
;                 f32x4 h0, h1;
; #pragma unroll
;                 for (int n = 0; n < 2; ++n) { const f32x4 G = acc[ai][0][m][n], U = acc[ai][1][m][n]; f32x4 hv;
; #pragma unroll
;                     for (int q = 0; q < 2; ++q) { const f32x2 g2 = (f32x2){G[2 * q], G[2 * q + 1]} * rsl, u2 = (f32x2){U[2 * q], U[2 * q + 1]} * rsu;
;                         f32x2 r2; r2.x = __builtin_amdgcn_rcpf(1.f + __builtin_amdgcn_exp2f(-g2.x)); r2.y = __builtin_amdgcn_rcpf(1.f + __builtin_amdgcn_exp2f(-g2.y));
;                         const f32x2 o2 = g2 * u2 * r2; hv[2 * q] = o2.x; hv[2 * q + 1] = o2.y; }
;                     if (n == 0) h0 = hv; else h1 = hv; }
;                 unsigned w0 = 0u, w1 = 0u;
;                 w0 = __builtin_amdgcn_cvt_pk_fp8_f32(h0[0], h0[1], w0, false); w0 = __builtin_amdgcn_cvt_pk_fp8_f32(h0[2], h0[3], w0, true); w1 = __builtin_amdgcn_cvt_pk_fp8_f32(h1[0], h1[1], w1, false); w1 = __builtin_amdgcn_cvt_pk_fp8_f32(h1[2], h1[3], w1, true);
;                 *(u32x2*)(hb + (ai * 4 + m) * 512) = (u32x2){w0, w1}; asm volatile("" ::: "memory"); }
	v_add_f32_e32 v36, v40, v41
	v_fmamk_f32 v36, v36, 0x3a800000, v227
	v_rsq_f32_e32 v37, v36
	global_store_dwordx2 v[162:163], v[48:49], off offset:2560
	v_mul_f32_e32 v36, 0x3fb8aa3b, v37
	v_pk_mul_f32 v[32:33], v[32:33], v[36:37] op_sel_hi:[1,0]
	v_mul_f32_e32 v38, 0x3f317218, v37
	v_exp_f32_e64 v39, -v32
	v_exp_f32_e64 v37, -v33
	v_pk_mul_f32 v[24:25], v[24:25], v[38:39] op_sel_hi:[1,0]
	v_add_f32_e32 v37, 1.0, v37
	v_pk_mul_f32 v[24:25], v[32:33], v[24:25]
	v_pk_mul_f32 v[32:33], v[34:35], v[36:37] op_sel_hi:[1,0]
	v_add_f32_e32 v39, 1.0, v39
	v_exp_f32_e64 v34, -v32
	v_exp_f32_e64 v35, -v33
	v_pk_mul_f32 v[26:27], v[26:27], v[38:39] op_sel_hi:[1,0]
	v_pk_mul_f32 v[28:29], v[28:29], v[36:37] op_sel_hi:[1,0]
	v_add_f32_e32 v34, 1.0, v34
	v_add_f32_e32 v35, 1.0, v35
	v_pk_mul_f32 v[26:27], v[32:33], v[26:27]
	v_exp_f32_e64 v32, -v28
	v_exp_f32_e64 v33, -v29
	v_rcp_f32_e32 v34, v34
	v_rcp_f32_e32 v35, v35
	v_add_f32_e32 v32, 1.0, v32
	v_add_f32_e32 v33, 1.0, v33
	v_pk_mul_f32 v[30:31], v[30:31], v[36:37] op_sel_hi:[1,0]
	v_pk_mul_f32 v[26:27], v[26:27], v[34:35]
	v_rcp_f32_e32 v32, v32
	v_rcp_f32_e32 v33, v33
	v_exp_f32_e64 v34, -v30
	v_pk_mul_f32 v[20:21], v[20:21], v[38:39] op_sel_hi:[1,0]
	v_rcp_f32_e32 v40, v39
	v_pk_mul_f32 v[20:21], v[28:29], v[20:21]
	s_waitcnt vmcnt(6)
	v_mov_b32_e32 v28, v133
	v_mov_b32_e32 v29, v134
	v_mov_b32_e32 v133, v135
	v_pk_add_f32 v[28:29], v[28:29], v[132:133]
	v_pk_mul_f32 v[20:21], v[20:21], v[32:33]
	v_add_f32_e32 v32, 1.0, v34
	v_add_f32_e32 v34, v28, v29
	v_mov_b32_e32 v35, v34
	s_nop 1
	v_permlane16_swap_b32_e32 v35, v34
	v_exp_f32_e64 v33, -v31
	v_rcp_f32_e32 v28, v32
	v_rcp_f32_e32 v41, v37
	v_pk_mul_f32 v[22:23], v[22:23], v[38:39] op_sel_hi:[1,0]
	s_waitcnt lgkmcnt(0)
	v_add_f32_e32 v32, v34, v35
	v_add_f32_e32 v29, 1.0, v33
	v_mov_b32_e32 v33, v32
	s_nop 1
	v_permlane32_swap_b32_e32 v33, v32
	v_pk_mul_f32 v[22:23], v[30:31], v[22:23]
	v_mov_b32_e32 v31, v3
	v_cvt_pk_fp8_f32 v31, v20, v21
	v_pk_mul_f32 v[24:25], v[24:25], v[40:41]
	s_waitcnt lgkmcnt(0)
	v_add_f32_e32 v20, v32, v33
	v_rcp_f32_e32 v29, v29
	v_mov_b32_e32 v30, v3
	v_fmamk_f32 v20, v20, 0x3a800000, v227
	v_cvt_pk_fp8_f32 v30, v24, v25
	v_rsq_f32_e32 v24, v20
	v_pk_mul_f32 v[20:21], v[22:23], v[28:29]
	v_cvt_pk_fp8_f32 v30, v26, v27 op_sel:[0,0,1]
	v_cvt_pk_fp8_f32 v31, v20, v21 op_sel:[0,0,1]
	v_mul_f32_e32 v20, 0x3fb8aa3b, v24
	v_pk_mul_f32 v[16:17], v[16:17], v[20:21] op_sel_hi:[1,0]
	v_mul_f32_e32 v22, 0x3f317218, v24
	v_exp_f32_e64 v21, -v16
	v_exp_f32_e64 v23, -v17
	global_store_dwordx2 v[162:163], v[30:31], off offset:3072
	v_add_f32_e32 v21, 1.0, v21
	v_pk_mul_f32 v[8:9], v[8:9], v[22:23] op_sel_hi:[1,0]
	v_rcp_f32_e32 v24, v21
	v_add_f32_e32 v21, 1.0, v23
	v_pk_mul_f32 v[8:9], v[16:17], v[8:9]
	v_pk_mul_f32 v[16:17], v[18:19], v[20:21] op_sel_hi:[1,0]
	v_pk_mul_f32 v[10:11], v[10:11], v[22:23] op_sel_hi:[1,0]
	v_pk_mul_f32 v[12:13], v[12:13], v[20:21] op_sel_hi:[1,0]
	v_exp_f32_e64 v18, -v16
	v_exp_f32_e64 v19, -v17
	v_pk_mul_f32 v[10:11], v[16:17], v[10:11]
	v_exp_f32_e64 v16, -v12
	v_exp_f32_e64 v17, -v13
	v_pk_mul_f32 v[4:5], v[4:5], v[22:23] op_sel_hi:[1,0]
	v_rcp_f32_e32 v25, v21
	v_pk_mul_f32 v[4:5], v[12:13], v[4:5]
	v_pk_mul_f32 v[12:13], v[14:15], v[20:21] op_sel_hi:[1,0]
	v_add_f32_e32 v16, 1.0, v16
	v_add_f32_e32 v17, 1.0, v17
	v_exp_f32_e64 v14, -v12
	v_exp_f32_e64 v15, -v13
	v_rcp_f32_e32 v16, v16
	v_rcp_f32_e32 v17, v17
	v_add_f32_e32 v18, 1.0, v18
	v_add_f32_e32 v19, 1.0, v19
	v_add_f32_e32 v14, 1.0, v14
	v_add_f32_e32 v15, 1.0, v15
	v_pk_mul_f32 v[8:9], v[8:9], v[24:25]
	v_rcp_f32_e32 v18, v18
	v_rcp_f32_e32 v19, v19
	v_pk_mul_f32 v[4:5], v[4:5], v[16:17]
	v_rcp_f32_e32 v14, v14
	v_rcp_f32_e32 v15, v15
	v_mov_b32_e32 v16, v3
	v_mov_b32_e32 v17, v3
	v_cvt_pk_fp8_f32 v16, v8, v9
	v_cvt_pk_fp8_f32 v17, v4, v5
	v_pk_mul_f32 v[6:7], v[6:7], v[22:23] op_sel_hi:[1,0]
	v_pk_mul_f32 v[10:11], v[10:11], v[18:19]
	v_pk_mul_f32 v[4:5], v[12:13], v[6:7]
	v_cvt_pk_fp8_f32 v16, v10, v11 op_sel:[0,0,1]
	v_pk_mul_f32 v[4:5], v[4:5], v[14:15]
	s_nop 0
	v_cvt_pk_fp8_f32 v17, v4, v5 op_sel:[0,0,1]
	global_store_dwordx2 v[162:163], v[16:17], off offset:3584
	s_cbranch_vccnz .LBB0_427
	s_andn2_b64 vcc, exec, s[44:45]
	s_cbranch_vccnz .LBB0_426
	s_barrier
	s_branch .LBB0_426

;     __device__ __forceinline__ void operator()(const f32x4 (&acc)[2][2][4][2], const Unit& u, int wr, int wc, int fr, int fq) const {
;         asm volatile("" : "+v"(fr), "+v"(fq));
;         const int row0 = u.pm * BM + wr * 64 + fr, col0 = u.pn * BM + wc * 32 + fq * 8;
;         u32x4 xcur[2][2], xnxt[2][2];
; #pragma unroll
;         for (int h2 = 0; h2 < 2; ++h2)
; #pragma unroll
;             for (int bj = 0; bj < 2; ++bj) xcur[h2][bj] = *(const u32x4*)(X + (size_t)(row0 + h2 * 16) * 1024 + col0 + bj * HALF);
; #pragma unroll
;         for (int q = 0; q < 8; ++q) { const int ai = q >> 2, m = q & 3; const int row = row0 + ai * HALF + m * 16; float s = 0.f;
;             if ((q & 1) == 0 && q + 2 < 8) {
; #pragma unroll
;                 for (int h2 = 0; h2 < 2; ++h2)
; #pragma unroll
;                     for (int bj = 0; bj < 2; ++bj) { const int qn = q + 2 + h2; xnxt[h2][bj] = *(const u32x4*)(X + (size_t)(row0 + (qn >> 2) * HALF + (qn & 3) * 16) * 1024 + col0 + bj * HALF); } }
; #pragma unroll
;                 for (int bj = 0; bj < 2; ++bj) { bf16_t* p = X + (size_t)row * 1024 + col0 + bj * HALF; const u32x4 xv = xcur[q & 1][bj];
;                     f32x4 a = acc[ai][bj][m][0] * scale, b = acc[ai][bj][m][1] * scale;
;                     a[0] += bflo(xv.x); a[1] += bfhi(xv.x); a[2] += bflo(xv.y); a[3] += bfhi(xv.y); b[0] += bflo(xv.z); b[1] += bfhi(xv.z); b[2] += bflo(xv.w); b[3] += bfhi(xv.w);
;                     const u32x4 w = pack8(a, b); *(u32x4*)p = w;
;                     if constexpr (WX8) { unsigned q0 = 0u, q1 = 0u; q0 = __builtin_amdgcn_cvt_pk_fp8_f32(bflo(w.x), bfhi(w.x), q0, false); q0 = __builtin_amdgcn_cvt_pk_fp8_f32(bflo(w.y), bfhi(w.y), q0, true); q1 = __builtin_amdgcn_cvt_pk_fp8_f32(bflo(w.z), bfhi(w.z), q1, false); q1 = __builtin_amdgcn_cvt_pk_fp8_f32(bflo(w.w), bfhi(w.w), q1, true);
;                         *(u32x2*)((unsigned char*)X + (WS_X8 - WS_X) + (size_t)row * 1024 + col0 + bj * HALF) = (u32x2){q0, q1}; }
;                     s += (bflo(w.x) * bflo(w.x) + bfhi(w.x) * bfhi(w.x)) + (bflo(w.y) * bflo(w.y) + bfhi(w.y) * bfhi(w.y)) + (bflo(w.z) * bflo(w.z) + bfhi(w.z) * bfhi(w.z)) + (bflo(w.w) * bflo(w.w) + bfhi(w.w) * bfhi(w.w)); }
;                 s += __shfl_xor(s, 16); s += __shfl_xor(s, 32);
;                 if (fq == 0) ssn[(size_t)row * 16 + u.pn * 4 + wc] = s;
.LBB0_511:
	s_lshl_b32 s4, s70, 8
	v_mov_b32_e32 v4, v1
	v_mov_b32_e32 v185, v182
	s_add_i32 s4, s4, s23
	v_pk_mul_f32 v[190:191], v[152:153], s[28:29] op_sel_hi:[1,0]
	v_add_u32_e32 v176, s4, v4
	s_lshl_b32 s4, s69, 8
	s_or_b32 s4, s4, s47
	v_lshl_add_u32 v174, v185, 3, s4
	v_ashrrev_i32_e32 v175, 31, v174
	v_lshlrev_b64 v[4:5], 1, v[174:175]
	v_ashrrev_i32_e32 v177, 31, v176
	v_lshl_add_u64 v[178:179], s[44:45], 0, v[4:5]
	v_lshlrev_b64 v[6:7], 11, v[176:177]
	v_lshl_add_u64 v[8:9], v[178:179], 0, v[6:7]
	global_load_dwordx4 v[28:31], v[8:9], off
	global_load_dwordx4 v[186:189], v[8:9], off offset:256
	v_add_u32_e32 v20, 16, v176
	v_add_u32_e32 v152, 32, v176
	v_pk_mul_f32 v[194:195], v[148:149], s[28:29] op_sel_hi:[1,0]
	v_add_u32_e32 v148, 48, v176
	v_ashrrev_i32_e32 v21, 31, v20
	v_ashrrev_i32_e32 v153, 31, v152
	v_pk_mul_f32 v[180:181], v[154:155], s[28:29] op_sel_hi:[1,0]
	v_ashrrev_i32_e32 v149, 31, v148
	v_lshlrev_b64 v[22:23], 11, v[20:21]
	v_lshlrev_b64 v[154:155], 11, v[152:153]
	v_pk_mul_f32 v[192:193], v[150:151], s[28:29] op_sel_hi:[1,0]
	v_lshlrev_b64 v[150:151], 11, v[148:149]
	v_lshl_add_u64 v[6:7], s[44:45], 0, v[6:7]
	v_lshl_add_u64 v[8:9], v[178:179], 0, v[22:23]
	v_lshl_add_u64 v[10:11], v[178:179], 0, v[154:155]
	v_lshl_add_u64 v[208:209], v[178:179], 0, v[150:151]
	v_lshl_add_u64 v[210:211], v[6:7], 0, v[4:5]
	global_load_dwordx4 v[12:15], v[8:9], off
	global_load_dwordx4 v[4:7], v[8:9], off offset:256
	global_load_dwordx4 v[32:35], v[10:11], off
	global_load_dwordx4 v[24:27], v[10:11], off offset:256
	global_load_dwordx4 v[16:19], v[208:209], off
	s_nop 0
	global_load_dwordx4 v[8:11], v[208:209], off offset:256
	v_pk_mul_f32 v[162:163], v[162:163], s[28:29] op_sel_hi:[1,0]
	v_pk_mul_f32 v[160:161], v[160:161], s[28:29] op_sel_hi:[1,0]
	v_pk_mul_f32 v[158:159], v[158:159], s[28:29] op_sel_hi:[1,0]
	v_pk_mul_f32 v[156:157], v[156:157], s[28:29] op_sel_hi:[1,0]
	s_lshl_b32 s54, s69, 2
	s_ashr_i32 s55, s54, 31
	s_waitcnt vmcnt(0)
	v_lshlrev_b32_e32 v204, 16, v28
	v_and_b32_e32 v28, 0xffff0000, v28
	v_lshlrev_b32_e32 v205, 16, v29
	v_and_b32_e32 v29, 0xffff0000, v29
	v_lshlrev_b32_e32 v206, 16, v30
	v_and_b32_e32 v30, 0xffff0000, v30
	v_lshlrev_b32_e32 v207, 16, v31
	v_and_b32_e32 v31, 0xffff0000, v31
	v_add_f32_e32 v28, v161, v28
	v_add_f32_e32 v29, v163, v29
	v_add_f32_e32 v160, v160, v204
	v_add_f32_e32 v161, v162, v205
	v_add_f32_e32 v156, v156, v206
	v_add_f32_e32 v30, v157, v30
	v_add_f32_e32 v157, v158, v207
	v_add_f32_e32 v31, v159, v31
	v_cvt_pk_bf16_f32 v28, v160, v28
	v_cvt_pk_bf16_f32 v29, v161, v29
	v_cvt_pk_bf16_f32 v30, v156, v30
	v_cvt_pk_bf16_f32 v31, v157, v31
	global_store_dwordx4 v[210:211], v[28:31], off
	v_lshlrev_b32_e32 v156, 16, v28
	v_lshlrev_b32_e32 v157, 16, v29
	v_and_b32_e32 v28, 0xffff0000, v28
	v_and_b32_e32 v29, 0xffff0000, v29
	v_lshlrev_b32_e32 v160, 16, v30
	v_and_b32_e32 v30, 0xffff0000, v30
	v_mul_f32_e32 v28, v28, v28
	v_mul_f32_e32 v29, v29, v29
	v_lshlrev_b32_e32 v161, 16, v31
	v_and_b32_e32 v31, 0xffff0000, v31
	v_mul_f32_e32 v30, v30, v30
	v_fmac_f32_e32 v28, v156, v156
	v_fmac_f32_e32 v29, v157, v157
	v_mul_f32_e32 v31, v31, v31
	v_fmac_f32_e32 v30, v160, v160
	v_add_f32_e32 v28, v28, v29
	v_lshlrev_b32_e32 v208, 16, v186
	v_and_b32_e32 v186, 0xffff0000, v186
	v_fmac_f32_e32 v31, v161, v161
	v_add_f32_e32 v28, v28, v30
	v_lshlrev_b32_e32 v30, 16, v189
	v_lshlrev_b32_e32 v209, 16, v187
	v_and_b32_e32 v187, 0xffff0000, v187
	v_lshlrev_b32_e32 v212, 16, v188
	v_and_b32_e32 v188, 0xffff0000, v188
	v_add_f32_e32 v158, v190, v208
	v_add_f32_e32 v159, v191, v186
	v_add_f32_e32 v28, v28, v31
	v_add_f32_e32 v30, v192, v30
	v_and_b32_e32 v31, 0xffff0000, v189
	v_add_f32_e32 v162, v180, v209
	v_add_f32_e32 v163, v181, v187
	v_add_f32_e32 v180, v194, v212
	v_add_f32_e32 v29, v195, v188
	v_add_f32_e32 v31, v193, v31
	v_cvt_pk_bf16_f32 v158, v158, v159
	v_cvt_pk_bf16_f32 v159, v162, v163
	v_cvt_pk_bf16_f32 v160, v180, v29
	v_cvt_pk_bf16_f32 v161, v30, v31
	global_store_dwordx4 v[210:211], v[158:161], off offset:256
	v_and_b32_e32 v30, 0xffff0000, v158
	v_lshlrev_b32_e32 v29, 16, v158
	v_mul_f32_e32 v30, v30, v30
	v_and_b32_e32 v31, 0xffff0000, v159
	v_fmac_f32_e32 v30, v29, v29
	v_lshlrev_b32_e32 v29, 16, v159
	v_mul_f32_e32 v31, v31, v31
	v_fmac_f32_e32 v31, v29, v29
	v_add_f32_e32 v29, v30, v31
	v_and_b32_e32 v31, 0xffff0000, v160
	v_lshlrev_b32_e32 v30, 16, v160
	v_mul_f32_e32 v31, v31, v31
	v_fmac_f32_e32 v31, v30, v30
	v_add_f32_e32 v29, v29, v31
	v_and_b32_e32 v31, 0xffff0000, v161
	v_lshlrev_b32_e32 v30, 16, v161
	v_mul_f32_e32 v31, v31, v31
	v_fmac_f32_e32 v31, v30, v30
	v_add_f32_e32 v29, v29, v31
	v_and_b32_e32 v30, 64, v246
	v_add_f32_e32 v28, v28, v29
	v_xor_b32_e32 v29, 16, v246
	v_add_u32_e32 v30, 64, v30
	v_cmp_lt_i32_e32 vcc, v29, v30
	s_nop 1
	v_cndmask_b32_e32 v29, v246, v29, vcc
	v_lshlrev_b32_e32 v156, 2, v29
	v_mov_b32_e32 v29, v28
	s_nop 1
	v_permlane16_swap_b32_e32 v29, v28
	s_waitcnt lgkmcnt(0)
	v_add_f32_e32 v28, v28, v29
	v_xor_b32_e32 v29, 32, v246
	v_cmp_lt_i32_e32 vcc, v29, v30
	s_nop 1
	v_cndmask_b32_e32 v29, v246, v29, vcc
	v_lshlrev_b32_e32 v157, 2, v29
	v_mov_b32_e32 v29, v28
	s_nop 1
	v_permlane32_swap_b32_e32 v29, v28
	v_cmp_eq_u32_e32 vcc, 0, v185
	s_and_saveexec_b64 s[4:5], vcc
	s_cbranch_execz .LBB0_513
	v_lshlrev_b64 v[30:31], 6, v[176:177]
	v_lshl_add_u64 v[30:31], s[48:49], 0, v[30:31]
	v_lshl_add_u64 v[30:31], s[54:55], 2, v[30:31]
	s_lshl_b32 s92, s22, 2
	v_lshl_add_u64 v[30:31], v[30:31], 0, s[92:93]
	s_waitcnt lgkmcnt(0)
	v_add_f32_e32 v28, v28, v29
	global_store_dword v[30:31], v28, off
; __device__ __forceinline__ float bflo(unsigned w) { return __uint_as_float(w << 16); }
; __device__ __forceinline__ float bfhi(unsigned w) { return __uint_as_float(w & 0xffff0000u); }
; __device__ __forceinline__ u32x4 pack8(const f32x4 a, const f32x4 b) { u32x4 w; w.x = cvt_pk_bf16(a[0], a[1]); w.y = cvt_pk_bf16(a[2], a[3]); w.z = cvt_pk_bf16(b[0], b[1]); w.w = cvt_pk_bf16(b[2], b[3]); return w; }
;     __device__ __forceinline__ void operator()(const f32x4 (&acc)[2][2][4][2], const Unit& u, int wr, int wc, int fr, int fq) const {
;     ...
;         for (int q = 0; q < 8; ++q) { const int ai = q >> 2, m = q & 3; const int row = row0 + ai * HALF + m * 16; float s = 0.f;
;             if ((q & 1) == 0 && q + 2 < 8) {
; #pragma unroll
;                 for (int h2 = 0; h2 < 2; ++h2)
; #pragma unroll
;                     for (int bj = 0; bj < 2; ++bj) { const int qn = q + 2 + h2; xnxt[h2][bj] = *(const u32x4*)(X + (size_t)(row0 + (qn >> 2) * HALF + (qn & 3) * 16) * 1024 + col0 + bj * HALF); } }
; #pragma unroll
;                 for (int bj = 0; bj < 2; ++bj) { bf16_t* p = X + (size_t)row * 1024 + col0 + bj * HALF; const u32x4 xv = xcur[q & 1][bj];
;                     f32x4 a = acc[ai][bj][m][0] * scale, b = acc[ai][bj][m][1] * scale;
;                     a[0] += bflo(xv.x); a[1] += bfhi(xv.x); a[2] += bflo(xv.y); a[3] += bfhi(xv.y); b[0] += bflo(xv.z); b[1] += bfhi(xv.z); b[2] += bflo(xv.w); b[3] += bfhi(xv.w);
;                     const u32x4 w = pack8(a, b); *(u32x4*)p = w;
;                     if constexpr (WX8) { unsigned q0 = 0u, q1 = 0u; q0 = __builtin_amdgcn_cvt_pk_fp8_f32(bflo(w.x), bfhi(w.x), q0, false); q0 = __builtin_amdgcn_cvt_pk_fp8_f32(bflo(w.y), bfhi(w.y), q0, true); q1 = __builtin_amdgcn_cvt_pk_fp8_f32(bflo(w.z), bfhi(w.z), q1, false); q1 = __builtin_amdgcn_cvt_pk_fp8_f32(bflo(w.w), bfhi(w.w), q1, true);
;                         *(u32x2*)((unsigned char*)X + (WS_X8 - WS_X) + (size_t)row * 1024 + col0 + bj * HALF) = (u32x2){q0, q1}; }
;                     s += (bflo(w.x) * bflo(w.x) + bfhi(w.x) * bfhi(w.x)) + (bflo(w.y) * bflo(w.y) + bfhi(w.y) * bfhi(w.y)) + (bflo(w.z) * bflo(w.z) + bfhi(w.z) * bfhi(w.z)) + (bflo(w.w) * bflo(w.w) + bfhi(w.w) * bfhi(w.w)); }
;                 s += __shfl_xor(s, 16); s += __shfl_xor(s, 32);
;                 if (fq == 0) ssn[(size_t)row * 16 + u.pn * 4 + wc] = s;
.LBB0_513:
	s_or_b64 exec, exec, s[4:5]
	v_pk_mul_f32 v[30:31], v[144:145], s[28:29] op_sel_hi:[1,0]
	v_lshlrev_b32_e32 v144, 16, v12
	v_and_b32_e32 v12, 0xffff0000, v12
	s_waitcnt lgkmcnt(0)
	v_pk_mul_f32 v[28:29], v[146:147], s[28:29] op_sel_hi:[1,0]
	v_add_f32_e32 v12, v31, v12
	v_lshlrev_b32_e32 v31, 16, v13
	v_and_b32_e32 v13, 0xffff0000, v13
	v_lshl_add_u64 v[22:23], s[44:45], 0, v[22:23]
	v_pk_mul_f32 v[142:143], v[142:143], s[28:29] op_sel_hi:[1,0]
	v_pk_mul_f32 v[140:141], v[140:141], s[28:29] op_sel_hi:[1,0]
	v_add_f32_e32 v28, v28, v31
	v_add_f32_e32 v13, v29, v13
	v_lshlrev_b32_e32 v29, 16, v14
	v_and_b32_e32 v14, 0xffff0000, v14
	v_lshlrev_b32_e32 v31, 16, v15
	v_and_b32_e32 v15, 0xffff0000, v15
	v_lshl_add_u64 v[22:23], v[174:175], 1, v[22:23]
	v_add_f32_e32 v30, v30, v144
	v_add_f32_e32 v14, v141, v14
	v_add_f32_e32 v15, v143, v15
	v_cvt_pk_bf16_f32 v12, v30, v12
	v_add_f32_e32 v29, v140, v29
	v_add_f32_e32 v31, v142, v31
	v_cvt_pk_bf16_f32 v13, v28, v13
	v_cvt_pk_bf16_f32 v14, v29, v14
	v_cvt_pk_bf16_f32 v15, v31, v15
	global_store_dwordx4 v[22:23], v[12:15], off
	v_lshlrev_b32_e32 v28, 16, v12
	v_pk_mul_f32 v[30:31], v[132:133], s[28:29] op_sel_hi:[1,0]
	v_and_b32_e32 v12, 0xffff0000, v12
	v_mul_f32_e32 v12, v12, v12
	v_fmac_f32_e32 v12, v28, v28
	v_lshlrev_b32_e32 v28, 16, v13
	v_and_b32_e32 v13, 0xffff0000, v13
	v_mul_f32_e32 v13, v13, v13
	v_fmac_f32_e32 v13, v28, v28
	v_add_f32_e32 v12, v12, v13
	v_lshlrev_b32_e32 v13, 16, v14
	v_and_b32_e32 v14, 0xffff0000, v14
	v_mul_f32_e32 v14, v14, v14
	v_fmac_f32_e32 v14, v13, v13
	v_add_f32_e32 v12, v12, v14
	v_and_b32_e32 v14, 0xffff0000, v15
	v_lshlrev_b32_e32 v13, 16, v15
	v_mul_f32_e32 v14, v14, v14
	v_fmac_f32_e32 v14, v13, v13
	v_add_f32_e32 v140, v12, v14
	v_pk_mul_f32 v[14:15], v[136:137], s[28:29] op_sel_hi:[1,0]
	v_lshlrev_b32_e32 v132, 16, v4
	v_and_b32_e32 v4, 0xffff0000, v4
	v_pk_mul_f32 v[12:13], v[138:139], s[28:29] op_sel_hi:[1,0]
	v_add_f32_e32 v4, v15, v4
	v_lshlrev_b32_e32 v15, 16, v5
	v_add_f32_e32 v15, v12, v15
	v_and_b32_e32 v5, 0xffff0000, v5
	v_lshlrev_b32_e32 v12, 16, v6
	v_pk_mul_f32 v[28:29], v[134:135], s[28:29] op_sel_hi:[1,0]
	v_add_f32_e32 v5, v13, v5
	v_add_f32_e32 v30, v30, v12
	v_and_b32_e32 v6, 0xffff0000, v6
	v_lshlrev_b32_e32 v12, 16, v7
	v_add_f32_e32 v14, v14, v132
	v_add_f32_e32 v6, v31, v6
	v_add_f32_e32 v28, v28, v12
	v_cvt_pk_bf16_f32 v12, v14, v4
	v_cvt_pk_bf16_f32 v13, v15, v5
	v_cvt_pk_bf16_f32 v14, v30, v6
	v_and_b32_e32 v7, 0xffff0000, v7
	v_and_b32_e32 v5, 0xffff0000, v12
	v_lshlrev_b32_e32 v4, 16, v12
	v_mul_f32_e32 v5, v5, v5
	v_and_b32_e32 v6, 0xffff0000, v13
	v_fmac_f32_e32 v5, v4, v4
	v_lshlrev_b32_e32 v4, 16, v13
	v_mul_f32_e32 v6, v6, v6
	v_fmac_f32_e32 v6, v4, v4
	v_add_f32_e32 v4, v5, v6
	v_and_b32_e32 v6, 0xffff0000, v14
	v_lshlrev_b32_e32 v5, 16, v14
	v_mul_f32_e32 v6, v6, v6
	v_fmac_f32_e32 v6, v5, v5
	v_add_f32_e32 v7, v29, v7
	v_cvt_pk_bf16_f32 v15, v28, v7
	v_add_f32_e32 v4, v4, v6
	v_and_b32_e32 v6, 0xffff0000, v15
	v_lshlrev_b32_e32 v5, 16, v15
	v_mul_f32_e32 v6, v6, v6
	v_fmac_f32_e32 v6, v5, v5
	v_add_f32_e32 v4, v4, v6
	v_add_f32_e32 v4, v140, v4
	v_mov_b32_e32 v5, v4
	s_nop 1
	v_permlane16_swap_b32_e32 v5, v4
	global_store_dwordx4 v[22:23], v[12:15], off offset:256
	s_waitcnt lgkmcnt(0)
	v_add_f32_e32 v4, v4, v5
	v_mov_b32_e32 v5, v4
	s_nop 1
	v_permlane32_swap_b32_e32 v5, v4
	s_and_saveexec_b64 s[4:5], vcc
	s_cbranch_execz .LBB0_515
	v_lshlrev_b64 v[6:7], 6, v[20:21]
	v_lshl_add_u64 v[6:7], s[48:49], 0, v[6:7]
	v_lshl_add_u64 v[6:7], s[54:55], 2, v[6:7]
	s_lshl_b32 s92, s22, 2
	v_lshl_add_u64 v[6:7], v[6:7], 0, s[92:93]
	s_waitcnt lgkmcnt(0)
	v_add_f32_e32 v4, v4, v5
	global_store_dword v[6:7], v4, off
.LBB0_515:
	s_or_b64 exec, exec, s[4:5]
	v_add_u32_e32 v134, 0x80, v176
	v_ashrrev_i32_e32 v135, 31, v134
	v_add_u32_e32 v132, 0x90, v176
	v_lshlrev_b64 v[138:139], 11, v[134:135]
	v_ashrrev_i32_e32 v133, 31, v132
	s_waitcnt lgkmcnt(0)
	v_lshl_add_u64 v[4:5], v[178:179], 0, v[138:139]
	v_lshlrev_b64 v[136:137], 11, v[132:133]
	global_load_dwordx4 v[28:31], v[4:5], off
	global_load_dwordx4 v[20:23], v[4:5], off offset:256
	v_lshl_add_u64 v[4:5], v[178:179], 0, v[136:137]
	global_load_dwordx4 v[12:15], v[4:5], off
	s_nop 0
	global_load_dwordx4 v[4:7], v[4:5], off offset:256
	v_pk_mul_f32 v[128:129], v[128:129], s[28:29] op_sel_hi:[1,0]
	v_lshlrev_b32_e32 v142, 16, v32
	v_and_b32_e32 v32, 0xffff0000, v32
	v_pk_mul_f32 v[130:131], v[130:131], s[28:29] op_sel_hi:[1,0]
	v_add_f32_e32 v32, v129, v32
	v_lshlrev_b32_e32 v129, 16, v33
	v_pk_mul_f32 v[124:125], v[124:125], s[28:29] op_sel_hi:[1,0]
	v_add_f32_e32 v129, v130, v129
	v_lshlrev_b32_e32 v130, 16, v34
	v_and_b32_e32 v34, 0xffff0000, v34
	v_lshl_add_u64 v[140:141], s[44:45], 0, v[154:155]
	v_pk_mul_f32 v[126:127], v[126:127], s[28:29] op_sel_hi:[1,0]
	v_and_b32_e32 v33, 0xffff0000, v33
	v_add_f32_e32 v34, v125, v34
	v_lshlrev_b32_e32 v125, 16, v35
	v_and_b32_e32 v35, 0xffff0000, v35
	v_lshl_add_u64 v[140:141], v[174:175], 1, v[140:141]
	v_add_f32_e32 v128, v128, v142
	v_add_f32_e32 v33, v131, v33
	v_add_f32_e32 v124, v124, v130
	v_add_f32_e32 v35, v127, v35
	v_cvt_pk_bf16_f32 v32, v128, v32
	v_add_f32_e32 v125, v126, v125
	v_cvt_pk_bf16_f32 v33, v129, v33
	v_cvt_pk_bf16_f32 v34, v124, v34
	v_cvt_pk_bf16_f32 v35, v125, v35
	global_store_dwordx4 v[140:141], v[32:35], off
	v_lshlrev_b32_e32 v124, 16, v32
	v_pk_mul_f32 v[116:117], v[116:117], s[28:29] op_sel_hi:[1,0]
	v_and_b32_e32 v32, 0xffff0000, v32
	v_mul_f32_e32 v32, v32, v32
	v_fmac_f32_e32 v32, v124, v124
	v_lshlrev_b32_e32 v124, 16, v33
	v_and_b32_e32 v33, 0xffff0000, v33
	v_mul_f32_e32 v33, v33, v33
; __device__ __forceinline__ float bflo(unsigned w) { return __uint_as_float(w << 16); }
; __device__ __forceinline__ float bfhi(unsigned w) { return __uint_as_float(w & 0xffff0000u); }
; __device__ __forceinline__ u32x4 pack8(const f32x4 a, const f32x4 b) { u32x4 w; w.x = cvt_pk_bf16(a[0], a[1]); w.y = cvt_pk_bf16(a[2], a[3]); w.z = cvt_pk_bf16(b[0], b[1]); w.w = cvt_pk_bf16(b[2], b[3]); return w; }
;     __device__ __forceinline__ void operator()(const f32x4 (&acc)[2][2][4][2], const Unit& u, int wr, int wc, int fr, int fq) const {
;     ...
;         for (int q = 0; q < 8; ++q) { const int ai = q >> 2, m = q & 3; const int row = row0 + ai * HALF + m * 16; float s = 0.f;
;             if ((q & 1) == 0 && q + 2 < 8) {
; #pragma unroll
;                 for (int h2 = 0; h2 < 2; ++h2)
; #pragma unroll
;                     for (int bj = 0; bj < 2; ++bj) { const int qn = q + 2 + h2; xnxt[h2][bj] = *(const u32x4*)(X + (size_t)(row0 + (qn >> 2) * HALF + (qn & 3) * 16) * 1024 + col0 + bj * HALF); } }
; #pragma unroll
;                 for (int bj = 0; bj < 2; ++bj) { bf16_t* p = X + (size_t)row * 1024 + col0 + bj * HALF; const u32x4 xv = xcur[q & 1][bj];
;                     f32x4 a = acc[ai][bj][m][0] * scale, b = acc[ai][bj][m][1] * scale;
;                     a[0] += bflo(xv.x); a[1] += bfhi(xv.x); a[2] += bflo(xv.y); a[3] += bfhi(xv.y); b[0] += bflo(xv.z); b[1] += bfhi(xv.z); b[2] += bflo(xv.w); b[3] += bfhi(xv.w);
;                     const u32x4 w = pack8(a, b); *(u32x4*)p = w;
;                     if constexpr (WX8) { unsigned q0 = 0u, q1 = 0u; q0 = __builtin_amdgcn_cvt_pk_fp8_f32(bflo(w.x), bfhi(w.x), q0, false); q0 = __builtin_amdgcn_cvt_pk_fp8_f32(bflo(w.y), bfhi(w.y), q0, true); q1 = __builtin_amdgcn_cvt_pk_fp8_f32(bflo(w.z), bfhi(w.z), q1, false); q1 = __builtin_amdgcn_cvt_pk_fp8_f32(bflo(w.w), bfhi(w.w), q1, true);
;                         *(u32x2*)((unsigned char*)X + (WS_X8 - WS_X) + (size_t)row * 1024 + col0 + bj * HALF) = (u32x2){q0, q1}; }
;                     s += (bflo(w.x) * bflo(w.x) + bfhi(w.x) * bfhi(w.x)) + (bflo(w.y) * bflo(w.y) + bfhi(w.y) * bfhi(w.y)) + (bflo(w.z) * bflo(w.z) + bfhi(w.z) * bfhi(w.z)) + (bflo(w.w) * bflo(w.w) + bfhi(w.w) * bfhi(w.w)); }
;                 s += __shfl_xor(s, 16); s += __shfl_xor(s, 32);
;                 if (fq == 0) ssn[(size_t)row * 16 + u.pn * 4 + wc] = s;
	v_fmac_f32_e32 v33, v124, v124
	v_add_f32_e32 v32, v32, v33
	v_lshlrev_b32_e32 v33, 16, v34
	v_and_b32_e32 v34, 0xffff0000, v34
	v_mul_f32_e32 v34, v34, v34
	v_fmac_f32_e32 v34, v33, v33
	v_add_f32_e32 v32, v32, v34
	v_and_b32_e32 v34, 0xffff0000, v35
	v_lshlrev_b32_e32 v33, 16, v35
	v_mul_f32_e32 v34, v34, v34
	v_fmac_f32_e32 v34, v33, v33
	v_add_f32_e32 v124, v32, v34
	v_pk_mul_f32 v[34:35], v[120:121], s[28:29] op_sel_hi:[1,0]
	v_lshlrev_b32_e32 v120, 16, v24
	v_and_b32_e32 v24, 0xffff0000, v24
	v_pk_mul_f32 v[32:33], v[122:123], s[28:29] op_sel_hi:[1,0]
	v_add_f32_e32 v24, v35, v24
	v_lshlrev_b32_e32 v35, 16, v25
	v_add_f32_e32 v35, v32, v35
	v_and_b32_e32 v25, 0xffff0000, v25
	v_lshlrev_b32_e32 v32, 16, v26
	v_pk_mul_f32 v[118:119], v[118:119], s[28:29] op_sel_hi:[1,0]
	v_add_f32_e32 v25, v33, v25
	v_add_f32_e32 v116, v116, v32
	v_and_b32_e32 v26, 0xffff0000, v26
	v_lshlrev_b32_e32 v32, 16, v27
	v_add_f32_e32 v34, v34, v120
	v_add_f32_e32 v26, v117, v26
	v_add_f32_e32 v117, v118, v32
	v_cvt_pk_bf16_f32 v32, v34, v24
	v_cvt_pk_bf16_f32 v33, v35, v25
	v_cvt_pk_bf16_f32 v34, v116, v26
	v_and_b32_e32 v27, 0xffff0000, v27
	v_and_b32_e32 v25, 0xffff0000, v32
	v_lshlrev_b32_e32 v24, 16, v32
	v_mul_f32_e32 v25, v25, v25
	v_and_b32_e32 v26, 0xffff0000, v33
	v_fmac_f32_e32 v25, v24, v24
	v_lshlrev_b32_e32 v24, 16, v33
	v_mul_f32_e32 v26, v26, v26
	v_fmac_f32_e32 v26, v24, v24
	v_add_f32_e32 v24, v25, v26
	v_and_b32_e32 v26, 0xffff0000, v34
	v_lshlrev_b32_e32 v25, 16, v34
	v_mul_f32_e32 v26, v26, v26
	v_fmac_f32_e32 v26, v25, v25
	v_add_f32_e32 v27, v119, v27
	v_cvt_pk_bf16_f32 v35, v117, v27
	v_add_f32_e32 v24, v24, v26
	v_and_b32_e32 v26, 0xffff0000, v35
	v_lshlrev_b32_e32 v25, 16, v35
	v_mul_f32_e32 v26, v26, v26
	v_fmac_f32_e32 v26, v25, v25
	v_add_f32_e32 v24, v24, v26
	v_add_f32_e32 v24, v124, v24
	v_mov_b32_e32 v25, v24
	s_nop 1
	v_permlane16_swap_b32_e32 v25, v24
	global_store_dwordx4 v[140:141], v[32:35], off offset:256
	s_waitcnt lgkmcnt(0)
	v_add_f32_e32 v24, v24, v25
	v_mov_b32_e32 v25, v24
	s_nop 1
	v_permlane32_swap_b32_e32 v25, v24
	s_and_saveexec_b64 s[4:5], vcc
	s_cbranch_execz .LBB0_517
	v_lshlrev_b64 v[26:27], 6, v[152:153]
	v_lshl_add_u64 v[26:27], s[48:49], 0, v[26:27]
	v_lshl_add_u64 v[26:27], s[54:55], 2, v[26:27]
	s_lshl_b32 s92, s22, 2
	v_lshl_add_u64 v[26:27], v[26:27], 0, s[92:93]
	s_waitcnt lgkmcnt(0)
	v_add_f32_e32 v24, v24, v25
	global_store_dword v[26:27], v24, off
.LBB0_517:
	s_or_b64 exec, exec, s[4:5]
	v_pk_mul_f32 v[32:33], v[112:113], s[28:29] op_sel_hi:[1,0]
	v_pk_mul_f32 v[34:35], v[110:111], s[28:29] op_sel_hi:[1,0]
	v_lshlrev_b32_e32 v110, 16, v16
	v_and_b32_e32 v16, 0xffff0000, v16
	v_pk_mul_f32 v[26:27], v[114:115], s[28:29] op_sel_hi:[1,0]
	v_add_f32_e32 v16, v33, v16
	v_lshlrev_b32_e32 v33, 16, v17
	v_and_b32_e32 v17, 0xffff0000, v17
	s_waitcnt lgkmcnt(0)
	v_lshl_add_u64 v[24:25], s[44:45], 0, v[150:151]
	v_pk_mul_f32 v[108:109], v[108:109], s[28:29] op_sel_hi:[1,0]
	v_add_f32_e32 v26, v26, v33
	v_add_f32_e32 v17, v27, v17
	v_lshlrev_b32_e32 v27, 16, v18
	v_and_b32_e32 v18, 0xffff0000, v18
	v_lshlrev_b32_e32 v33, 16, v19
	v_and_b32_e32 v19, 0xffff0000, v19
	v_lshl_add_u64 v[24:25], v[174:175], 1, v[24:25]
	v_add_f32_e32 v32, v32, v110
	v_add_f32_e32 v18, v109, v18
	v_add_f32_e32 v19, v35, v19
	v_cvt_pk_bf16_f32 v16, v32, v16
	v_add_f32_e32 v27, v108, v27
	v_add_f32_e32 v33, v34, v33
	v_cvt_pk_bf16_f32 v17, v26, v17
	v_cvt_pk_bf16_f32 v18, v27, v18
	v_cvt_pk_bf16_f32 v19, v33, v19
	global_store_dwordx4 v[24:25], v[16:19], off
	v_lshlrev_b32_e32 v26, 16, v16
	v_lshlrev_b32_e32 v35, 16, v8
	v_and_b32_e32 v16, 0xffff0000, v16
	v_mul_f32_e32 v16, v16, v16
	v_fmac_f32_e32 v16, v26, v26
	v_lshlrev_b32_e32 v26, 16, v17
	v_and_b32_e32 v17, 0xffff0000, v17
	v_mul_f32_e32 v17, v17, v17
	v_fmac_f32_e32 v17, v26, v26
	v_add_f32_e32 v16, v16, v17
	v_lshlrev_b32_e32 v17, 16, v18
	v_and_b32_e32 v18, 0xffff0000, v18
	v_mul_f32_e32 v18, v18, v18
	v_fmac_f32_e32 v18, v17, v17
	v_add_f32_e32 v16, v16, v18
	v_and_b32_e32 v18, 0xffff0000, v19
	v_lshlrev_b32_e32 v17, 16, v19
	v_mul_f32_e32 v18, v18, v18
	v_fmac_f32_e32 v18, v17, v17
	v_add_f32_e32 v34, v16, v18
	v_pk_mul_f32 v[18:19], v[104:105], s[28:29] op_sel_hi:[1,0]
	v_and_b32_e32 v8, 0xffff0000, v8
	v_pk_mul_f32 v[16:17], v[106:107], s[28:29] op_sel_hi:[1,0]
	v_add_f32_e32 v8, v19, v8
	v_lshlrev_b32_e32 v19, 16, v9
	v_pk_mul_f32 v[32:33], v[100:101], s[28:29] op_sel_hi:[1,0]
	v_add_f32_e32 v19, v16, v19
	v_and_b32_e32 v9, 0xffff0000, v9
	v_lshlrev_b32_e32 v16, 16, v10
	v_pk_mul_f32 v[26:27], v[102:103], s[28:29] op_sel_hi:[1,0]
	v_add_f32_e32 v9, v17, v9
	v_add_f32_e32 v32, v32, v16
	v_and_b32_e32 v10, 0xffff0000, v10
	v_lshlrev_b32_e32 v16, 16, v11
	v_add_f32_e32 v18, v18, v35
	v_add_f32_e32 v10, v33, v10
	v_add_f32_e32 v26, v26, v16
	v_cvt_pk_bf16_f32 v16, v18, v8
	v_cvt_pk_bf16_f32 v17, v19, v9
	v_cvt_pk_bf16_f32 v18, v32, v10
	v_and_b32_e32 v11, 0xffff0000, v11
	v_and_b32_e32 v9, 0xffff0000, v16
	v_lshlrev_b32_e32 v8, 16, v16
	v_mul_f32_e32 v9, v9, v9
	v_and_b32_e32 v10, 0xffff0000, v17
	v_fmac_f32_e32 v9, v8, v8
	v_lshlrev_b32_e32 v8, 16, v17
	v_mul_f32_e32 v10, v10, v10
	v_fmac_f32_e32 v10, v8, v8
	v_add_f32_e32 v8, v9, v10
	v_and_b32_e32 v10, 0xffff0000, v18
	v_lshlrev_b32_e32 v9, 16, v18
	v_mul_f32_e32 v10, v10, v10
	v_fmac_f32_e32 v10, v9, v9
	v_add_f32_e32 v11, v27, v11
	v_cvt_pk_bf16_f32 v19, v26, v11
	v_add_f32_e32 v8, v8, v10
	v_and_b32_e32 v10, 0xffff0000, v19
	v_lshlrev_b32_e32 v9, 16, v19
	v_mul_f32_e32 v10, v10, v10
	v_fmac_f32_e32 v10, v9, v9
	v_add_f32_e32 v8, v8, v10
	v_add_f32_e32 v8, v34, v8
	v_mov_b32_e32 v9, v8
	s_nop 1
	v_permlane16_swap_b32_e32 v9, v8
	global_store_dwordx4 v[24:25], v[16:19], off offset:256
	s_waitcnt lgkmcnt(0)
	v_add_f32_e32 v8, v8, v9
	v_mov_b32_e32 v9, v8
	s_nop 1
	v_permlane32_swap_b32_e32 v9, v8
	s_and_saveexec_b64 s[4:5], vcc
	s_cbranch_execz .LBB0_519
	v_lshlrev_b64 v[10:11], 6, v[148:149]
	v_lshl_add_u64 v[10:11], s[48:49], 0, v[10:11]
	v_lshl_add_u64 v[10:11], s[54:55], 2, v[10:11]
	s_lshl_b32 s92, s22, 2
	v_lshl_add_u64 v[10:11], v[10:11], 0, s[92:93]
	s_waitcnt lgkmcnt(0)
	v_add_f32_e32 v8, v8, v9
	global_store_dword v[10:11], v8, off
; __device__ __forceinline__ float bflo(unsigned w) { return __uint_as_float(w << 16); }
; __device__ __forceinline__ float bfhi(unsigned w) { return __uint_as_float(w & 0xffff0000u); }
; __device__ __forceinline__ u32x4 pack8(const f32x4 a, const f32x4 b) { u32x4 w; w.x = cvt_pk_bf16(a[0], a[1]); w.y = cvt_pk_bf16(a[2], a[3]); w.z = cvt_pk_bf16(b[0], b[1]); w.w = cvt_pk_bf16(b[2], b[3]); return w; }
;     __device__ __forceinline__ void operator()(const f32x4 (&acc)[2][2][4][2], const Unit& u, int wr, int wc, int fr, int fq) const {
;     ...
;         for (int q = 0; q < 8; ++q) { const int ai = q >> 2, m = q & 3; const int row = row0 + ai * HALF + m * 16; float s = 0.f;
;             if ((q & 1) == 0 && q + 2 < 8) {
; #pragma unroll
;                 for (int h2 = 0; h2 < 2; ++h2)
; #pragma unroll
;                     for (int bj = 0; bj < 2; ++bj) { const int qn = q + 2 + h2; xnxt[h2][bj] = *(const u32x4*)(X + (size_t)(row0 + (qn >> 2) * HALF + (qn & 3) * 16) * 1024 + col0 + bj * HALF); } }
; #pragma unroll
;                 for (int bj = 0; bj < 2; ++bj) { bf16_t* p = X + (size_t)row * 1024 + col0 + bj * HALF; const u32x4 xv = xcur[q & 1][bj];
;                     f32x4 a = acc[ai][bj][m][0] * scale, b = acc[ai][bj][m][1] * scale;
;                     a[0] += bflo(xv.x); a[1] += bfhi(xv.x); a[2] += bflo(xv.y); a[3] += bfhi(xv.y); b[0] += bflo(xv.z); b[1] += bfhi(xv.z); b[2] += bflo(xv.w); b[3] += bfhi(xv.w);
;                     const u32x4 w = pack8(a, b); *(u32x4*)p = w;
;                     if constexpr (WX8) { unsigned q0 = 0u, q1 = 0u; q0 = __builtin_amdgcn_cvt_pk_fp8_f32(bflo(w.x), bfhi(w.x), q0, false); q0 = __builtin_amdgcn_cvt_pk_fp8_f32(bflo(w.y), bfhi(w.y), q0, true); q1 = __builtin_amdgcn_cvt_pk_fp8_f32(bflo(w.z), bfhi(w.z), q1, false); q1 = __builtin_amdgcn_cvt_pk_fp8_f32(bflo(w.w), bfhi(w.w), q1, true);
;                         *(u32x2*)((unsigned char*)X + (WS_X8 - WS_X) + (size_t)row * 1024 + col0 + bj * HALF) = (u32x2){q0, q1}; }
;                     s += (bflo(w.x) * bflo(w.x) + bfhi(w.x) * bfhi(w.x)) + (bflo(w.y) * bflo(w.y) + bfhi(w.y) * bfhi(w.y)) + (bflo(w.z) * bflo(w.z) + bfhi(w.z) * bfhi(w.z)) + (bflo(w.w) * bflo(w.w) + bfhi(w.w) * bfhi(w.w)); }
;                 s += __shfl_xor(s, 16); s += __shfl_xor(s, 32);
;                 if (fq == 0) ssn[(size_t)row * 16 + u.pn * 4 + wc] = s;
.LBB0_519:
	s_or_b64 exec, exec, s[4:5]
	v_add_u32_e32 v102, 0xa0, v176
	v_ashrrev_i32_e32 v103, 31, v102
	v_add_u32_e32 v100, 0xb0, v176
	v_lshlrev_b64 v[106:107], 11, v[102:103]
	v_ashrrev_i32_e32 v101, 31, v100
	s_waitcnt lgkmcnt(0)
	v_lshl_add_u64 v[8:9], v[178:179], 0, v[106:107]
	v_lshlrev_b64 v[104:105], 11, v[100:101]
	global_load_dwordx4 v[32:35], v[8:9], off
	global_load_dwordx4 v[24:27], v[8:9], off offset:256
	v_lshl_add_u64 v[8:9], v[178:179], 0, v[104:105]
	global_load_dwordx4 v[16:19], v[8:9], off
	s_nop 0
	global_load_dwordx4 v[8:11], v[8:9], off offset:256
	v_pk_mul_f32 v[96:97], v[96:97], s[28:29] op_sel_hi:[1,0]
	s_waitcnt vmcnt(11)
	v_lshlrev_b32_e32 v110, 16, v28
	v_and_b32_e32 v28, 0xffff0000, v28
	v_pk_mul_f32 v[98:99], v[98:99], s[28:29] op_sel_hi:[1,0]
	v_add_f32_e32 v28, v97, v28
	v_lshlrev_b32_e32 v97, 16, v29
	v_pk_mul_f32 v[92:93], v[92:93], s[28:29] op_sel_hi:[1,0]
	v_add_f32_e32 v97, v98, v97
	v_lshlrev_b32_e32 v98, 16, v30
	v_and_b32_e32 v30, 0xffff0000, v30
	v_lshl_add_u64 v[108:109], s[44:45], 0, v[138:139]
	v_pk_mul_f32 v[94:95], v[94:95], s[28:29] op_sel_hi:[1,0]
	v_and_b32_e32 v29, 0xffff0000, v29
	v_add_f32_e32 v30, v93, v30
	v_lshlrev_b32_e32 v93, 16, v31
	v_and_b32_e32 v31, 0xffff0000, v31
	v_lshl_add_u64 v[108:109], v[174:175], 1, v[108:109]
	v_add_f32_e32 v96, v96, v110
	v_add_f32_e32 v29, v99, v29
	v_add_f32_e32 v92, v92, v98
	v_add_f32_e32 v31, v95, v31
	v_cvt_pk_bf16_f32 v28, v96, v28
	v_add_f32_e32 v93, v94, v93
	v_cvt_pk_bf16_f32 v29, v97, v29
	v_cvt_pk_bf16_f32 v30, v92, v30
	v_cvt_pk_bf16_f32 v31, v93, v31
	global_store_dwordx4 v[108:109], v[28:31], off
	v_lshlrev_b32_e32 v92, 16, v28
	v_pk_mul_f32 v[84:85], v[84:85], s[28:29] op_sel_hi:[1,0]
	v_and_b32_e32 v28, 0xffff0000, v28
	v_mul_f32_e32 v28, v28, v28
	v_fmac_f32_e32 v28, v92, v92
	v_lshlrev_b32_e32 v92, 16, v29
	v_and_b32_e32 v29, 0xffff0000, v29
	v_mul_f32_e32 v29, v29, v29
	v_fmac_f32_e32 v29, v92, v92
	v_add_f32_e32 v28, v28, v29
	v_lshlrev_b32_e32 v29, 16, v30
	v_and_b32_e32 v30, 0xffff0000, v30
	v_mul_f32_e32 v30, v30, v30
	v_fmac_f32_e32 v30, v29, v29
	v_add_f32_e32 v28, v28, v30
	v_and_b32_e32 v30, 0xffff0000, v31
	v_lshlrev_b32_e32 v29, 16, v31
	v_mul_f32_e32 v30, v30, v30
	v_fmac_f32_e32 v30, v29, v29
	v_add_f32_e32 v92, v28, v30
	v_pk_mul_f32 v[30:31], v[88:89], s[28:29] op_sel_hi:[1,0]
	s_waitcnt vmcnt(11)
	v_lshlrev_b32_e32 v88, 16, v20
	v_and_b32_e32 v20, 0xffff0000, v20
	v_pk_mul_f32 v[28:29], v[90:91], s[28:29] op_sel_hi:[1,0]
	v_add_f32_e32 v20, v31, v20
	v_lshlrev_b32_e32 v31, 16, v21
	v_add_f32_e32 v31, v28, v31
	v_and_b32_e32 v21, 0xffff0000, v21
	v_lshlrev_b32_e32 v28, 16, v22
	v_pk_mul_f32 v[86:87], v[86:87], s[28:29] op_sel_hi:[1,0]
	v_add_f32_e32 v21, v29, v21
	v_add_f32_e32 v84, v84, v28
	v_and_b32_e32 v22, 0xffff0000, v22
	v_lshlrev_b32_e32 v28, 16, v23
	v_add_f32_e32 v30, v30, v88
	v_add_f32_e32 v22, v85, v22
	v_add_f32_e32 v85, v86, v28
	v_cvt_pk_bf16_f32 v28, v30, v20
	v_cvt_pk_bf16_f32 v29, v31, v21
	v_cvt_pk_bf16_f32 v30, v84, v22
	v_and_b32_e32 v23, 0xffff0000, v23
	v_and_b32_e32 v21, 0xffff0000, v28
	v_lshlrev_b32_e32 v20, 16, v28
	v_mul_f32_e32 v21, v21, v21
	v_and_b32_e32 v22, 0xffff0000, v29
	v_fmac_f32_e32 v21, v20, v20
	v_lshlrev_b32_e32 v20, 16, v29
	v_mul_f32_e32 v22, v22, v22
	v_fmac_f32_e32 v22, v20, v20
	v_add_f32_e32 v20, v21, v22
	v_and_b32_e32 v22, 0xffff0000, v30
	v_lshlrev_b32_e32 v21, 16, v30
	v_mul_f32_e32 v22, v22, v22
	v_fmac_f32_e32 v22, v21, v21
	v_add_f32_e32 v23, v87, v23
	v_cvt_pk_bf16_f32 v31, v85, v23
	v_add_f32_e32 v20, v20, v22
	v_and_b32_e32 v22, 0xffff0000, v31
	v_lshlrev_b32_e32 v21, 16, v31
	v_mul_f32_e32 v22, v22, v22
	v_fmac_f32_e32 v22, v21, v21
	v_add_f32_e32 v20, v20, v22
	v_add_f32_e32 v20, v92, v20
	v_mov_b32_e32 v21, v20
	s_nop 1
	v_permlane16_swap_b32_e32 v21, v20
	global_store_dwordx4 v[108:109], v[28:31], off offset:256
	s_waitcnt lgkmcnt(0)
	v_add_f32_e32 v20, v20, v21
	v_mov_b32_e32 v21, v20
	s_nop 1
	v_permlane32_swap_b32_e32 v21, v20
	s_and_saveexec_b64 s[4:5], vcc
	s_cbranch_execz .LBB0_521
	v_lshlrev_b64 v[22:23], 6, v[134:135]
	v_lshl_add_u64 v[22:23], s[48:49], 0, v[22:23]
	v_lshl_add_u64 v[22:23], s[54:55], 2, v[22:23]
	s_lshl_b32 s92, s22, 2
	v_lshl_add_u64 v[22:23], v[22:23], 0, s[92:93]
	s_waitcnt lgkmcnt(0)
	v_add_f32_e32 v20, v20, v21
	global_store_dword v[22:23], v20, off
; __device__ __forceinline__ float bflo(unsigned w) { return __uint_as_float(w << 16); }
; __device__ __forceinline__ float bfhi(unsigned w) { return __uint_as_float(w & 0xffff0000u); }
; __device__ __forceinline__ u32x4 pack8(const f32x4 a, const f32x4 b) { u32x4 w; w.x = cvt_pk_bf16(a[0], a[1]); w.y = cvt_pk_bf16(a[2], a[3]); w.z = cvt_pk_bf16(b[0], b[1]); w.w = cvt_pk_bf16(b[2], b[3]); return w; }
;     __device__ __forceinline__ void operator()(const f32x4 (&acc)[2][2][4][2], const Unit& u, int wr, int wc, int fr, int fq) const {
;     ...
;         for (int q = 0; q < 8; ++q) { const int ai = q >> 2, m = q & 3; const int row = row0 + ai * HALF + m * 16; float s = 0.f;
;             if ((q & 1) == 0 && q + 2 < 8) {
; #pragma unroll
;                 for (int h2 = 0; h2 < 2; ++h2)
; #pragma unroll
;                     for (int bj = 0; bj < 2; ++bj) { const int qn = q + 2 + h2; xnxt[h2][bj] = *(const u32x4*)(X + (size_t)(row0 + (qn >> 2) * HALF + (qn & 3) * 16) * 1024 + col0 + bj * HALF); } }
; #pragma unroll
;                 for (int bj = 0; bj < 2; ++bj) { bf16_t* p = X + (size_t)row * 1024 + col0 + bj * HALF; const u32x4 xv = xcur[q & 1][bj];
;                     f32x4 a = acc[ai][bj][m][0] * scale, b = acc[ai][bj][m][1] * scale;
;                     a[0] += bflo(xv.x); a[1] += bfhi(xv.x); a[2] += bflo(xv.y); a[3] += bfhi(xv.y); b[0] += bflo(xv.z); b[1] += bfhi(xv.z); b[2] += bflo(xv.w); b[3] += bfhi(xv.w);
;                     const u32x4 w = pack8(a, b); *(u32x4*)p = w;
;                     if constexpr (WX8) { unsigned q0 = 0u, q1 = 0u; q0 = __builtin_amdgcn_cvt_pk_fp8_f32(bflo(w.x), bfhi(w.x), q0, false); q0 = __builtin_amdgcn_cvt_pk_fp8_f32(bflo(w.y), bfhi(w.y), q0, true); q1 = __builtin_amdgcn_cvt_pk_fp8_f32(bflo(w.z), bfhi(w.z), q1, false); q1 = __builtin_amdgcn_cvt_pk_fp8_f32(bflo(w.w), bfhi(w.w), q1, true);
;                         *(u32x2*)((unsigned char*)X + (WS_X8 - WS_X) + (size_t)row * 1024 + col0 + bj * HALF) = (u32x2){q0, q1}; }
;                     s += (bflo(w.x) * bflo(w.x) + bfhi(w.x) * bfhi(w.x)) + (bflo(w.y) * bflo(w.y) + bfhi(w.y) * bfhi(w.y)) + (bflo(w.z) * bflo(w.z) + bfhi(w.z) * bfhi(w.z)) + (bflo(w.w) * bflo(w.w) + bfhi(w.w) * bfhi(w.w)); }
;                 s += __shfl_xor(s, 16); s += __shfl_xor(s, 32);
;                 if (fq == 0) ssn[(size_t)row * 16 + u.pn * 4 + wc] = s;
.LBB0_521:
	s_or_b64 exec, exec, s[4:5]
	v_pk_mul_f32 v[28:29], v[80:81], s[28:29] op_sel_hi:[1,0]
	v_pk_mul_f32 v[30:31], v[78:79], s[28:29] op_sel_hi:[1,0]
	s_waitcnt vmcnt(11)
	v_lshlrev_b32_e32 v78, 16, v12
	v_and_b32_e32 v12, 0xffff0000, v12
	v_pk_mul_f32 v[22:23], v[82:83], s[28:29] op_sel_hi:[1,0]
	v_add_f32_e32 v12, v29, v12
	v_lshlrev_b32_e32 v29, 16, v13
	v_and_b32_e32 v13, 0xffff0000, v13
	s_waitcnt lgkmcnt(0)
	v_lshl_add_u64 v[20:21], s[44:45], 0, v[136:137]
	v_pk_mul_f32 v[76:77], v[76:77], s[28:29] op_sel_hi:[1,0]
	v_add_f32_e32 v22, v22, v29
	v_add_f32_e32 v13, v23, v13
	v_lshlrev_b32_e32 v23, 16, v14
	v_and_b32_e32 v14, 0xffff0000, v14
	v_lshlrev_b32_e32 v29, 16, v15
	v_and_b32_e32 v15, 0xffff0000, v15
	v_lshl_add_u64 v[20:21], v[174:175], 1, v[20:21]
	v_add_f32_e32 v28, v28, v78
	v_add_f32_e32 v14, v77, v14
	v_add_f32_e32 v15, v31, v15
	v_cvt_pk_bf16_f32 v12, v28, v12
	v_add_f32_e32 v23, v76, v23
	v_add_f32_e32 v29, v30, v29
	v_cvt_pk_bf16_f32 v13, v22, v13
	v_cvt_pk_bf16_f32 v14, v23, v14
	v_cvt_pk_bf16_f32 v15, v29, v15
	global_store_dwordx4 v[20:21], v[12:15], off
	v_lshlrev_b32_e32 v22, 16, v12
	s_waitcnt vmcnt(11)
	v_lshlrev_b32_e32 v31, 16, v4
	v_and_b32_e32 v12, 0xffff0000, v12
	v_mul_f32_e32 v12, v12, v12
	v_fmac_f32_e32 v12, v22, v22
	v_lshlrev_b32_e32 v22, 16, v13
	v_and_b32_e32 v13, 0xffff0000, v13
	v_mul_f32_e32 v13, v13, v13
	v_fmac_f32_e32 v13, v22, v22
	v_add_f32_e32 v12, v12, v13
	v_lshlrev_b32_e32 v13, 16, v14
	v_and_b32_e32 v14, 0xffff0000, v14
	v_mul_f32_e32 v14, v14, v14
	v_fmac_f32_e32 v14, v13, v13
	v_add_f32_e32 v12, v12, v14
	v_and_b32_e32 v14, 0xffff0000, v15
	v_lshlrev_b32_e32 v13, 16, v15
	v_mul_f32_e32 v14, v14, v14
	v_fmac_f32_e32 v14, v13, v13
	v_add_f32_e32 v30, v12, v14
	v_pk_mul_f32 v[14:15], v[72:73], s[28:29] op_sel_hi:[1,0]
	v_and_b32_e32 v4, 0xffff0000, v4
	v_pk_mul_f32 v[12:13], v[74:75], s[28:29] op_sel_hi:[1,0]
	v_add_f32_e32 v4, v15, v4
	v_lshlrev_b32_e32 v15, 16, v5
	v_pk_mul_f32 v[28:29], v[68:69], s[28:29] op_sel_hi:[1,0]
	v_add_f32_e32 v15, v12, v15
	v_and_b32_e32 v5, 0xffff0000, v5
	v_lshlrev_b32_e32 v12, 16, v6
	v_pk_mul_f32 v[22:23], v[70:71], s[28:29] op_sel_hi:[1,0]
	v_add_f32_e32 v5, v13, v5
	v_add_f32_e32 v28, v28, v12
	v_and_b32_e32 v6, 0xffff0000, v6
	v_lshlrev_b32_e32 v12, 16, v7
	v_add_f32_e32 v14, v14, v31
	v_add_f32_e32 v6, v29, v6
	v_add_f32_e32 v22, v22, v12
	v_cvt_pk_bf16_f32 v12, v14, v4
	v_cvt_pk_bf16_f32 v13, v15, v5
	v_cvt_pk_bf16_f32 v14, v28, v6
	v_and_b32_e32 v7, 0xffff0000, v7
	v_and_b32_e32 v5, 0xffff0000, v12
	v_lshlrev_b32_e32 v4, 16, v12
	v_mul_f32_e32 v5, v5, v5
	v_and_b32_e32 v6, 0xffff0000, v13
	v_fmac_f32_e32 v5, v4, v4
	v_lshlrev_b32_e32 v4, 16, v13
	v_mul_f32_e32 v6, v6, v6
	v_fmac_f32_e32 v6, v4, v4
	v_add_f32_e32 v4, v5, v6
	v_and_b32_e32 v6, 0xffff0000, v14
	v_lshlrev_b32_e32 v5, 16, v14
	v_mul_f32_e32 v6, v6, v6
	v_fmac_f32_e32 v6, v5, v5
	v_add_f32_e32 v7, v23, v7
	v_cvt_pk_bf16_f32 v15, v22, v7
	v_add_f32_e32 v4, v4, v6
	v_and_b32_e32 v6, 0xffff0000, v15
	v_lshlrev_b32_e32 v5, 16, v15
	v_mul_f32_e32 v6, v6, v6
	v_fmac_f32_e32 v6, v5, v5
	v_add_f32_e32 v4, v4, v6
	v_add_f32_e32 v4, v30, v4
	v_mov_b32_e32 v5, v4
	s_nop 1
	v_permlane16_swap_b32_e32 v5, v4
	global_store_dwordx4 v[20:21], v[12:15], off offset:256
	s_waitcnt lgkmcnt(0)
	v_add_f32_e32 v4, v4, v5
	v_mov_b32_e32 v5, v4
	s_nop 1
	v_permlane32_swap_b32_e32 v5, v4
	s_and_saveexec_b64 s[4:5], vcc
	s_cbranch_execz .LBB0_523
	v_lshlrev_b64 v[6:7], 6, v[132:133]
	v_lshl_add_u64 v[6:7], s[48:49], 0, v[6:7]
	v_lshl_add_u64 v[6:7], s[54:55], 2, v[6:7]
	s_lshl_b32 s92, s22, 2
	v_lshl_add_u64 v[6:7], v[6:7], 0, s[92:93]
	s_waitcnt lgkmcnt(0)
	v_add_f32_e32 v4, v4, v5
	global_store_dword v[6:7], v4, off
.LBB0_523:
	s_or_b64 exec, exec, s[4:5]
	v_pk_mul_f32 v[6:7], v[64:65], s[28:29] op_sel_hi:[1,0]
	s_waitcnt vmcnt(7)
	v_lshlrev_b32_e32 v22, 16, v32
	s_waitcnt lgkmcnt(0)
	v_lshl_add_u64 v[4:5], s[44:45], 0, v[106:107]
	v_add_f32_e32 v6, v6, v22
	v_and_b32_e32 v22, 0xffff0000, v32
	v_lshl_add_u64 v[20:21], v[174:175], 1, v[4:5]
	v_pk_mul_f32 v[4:5], v[66:67], s[28:29] op_sel_hi:[1,0]
	v_add_f32_e32 v7, v7, v22
	v_lshlrev_b32_e32 v22, 16, v33
	v_add_f32_e32 v22, v4, v22
	v_and_b32_e32 v4, 0xffff0000, v33
	v_pk_mul_f32 v[14:15], v[60:61], s[28:29] op_sel_hi:[1,0]
	v_add_f32_e32 v5, v5, v4
	v_lshlrev_b32_e32 v4, 16, v34
	v_add_f32_e32 v14, v14, v4
	v_and_b32_e32 v4, 0xffff0000, v34
	v_pk_mul_f32 v[12:13], v[62:63], s[28:29] op_sel_hi:[1,0]
	v_add_f32_e32 v15, v15, v4
	v_lshlrev_b32_e32 v4, 16, v35
	v_add_f32_e32 v12, v12, v4
	v_and_b32_e32 v4, 0xffff0000, v35
	v_add_f32_e32 v13, v13, v4
	v_cvt_pk_bf16_f32 v4, v6, v7
	v_cvt_pk_bf16_f32 v5, v22, v5
	v_cvt_pk_bf16_f32 v6, v14, v15
	v_cvt_pk_bf16_f32 v7, v12, v13
	global_store_dwordx4 v[20:21], v[4:7], off
	v_lshlrev_b32_e32 v12, 16, v4
	s_waitcnt vmcnt(7)
; __device__ __forceinline__ float bflo(unsigned w) { return __uint_as_float(w << 16); }
; __device__ __forceinline__ float bfhi(unsigned w) { return __uint_as_float(w & 0xffff0000u); }
; __device__ __forceinline__ u32x4 pack8(const f32x4 a, const f32x4 b) { u32x4 w; w.x = cvt_pk_bf16(a[0], a[1]); w.y = cvt_pk_bf16(a[2], a[3]); w.z = cvt_pk_bf16(b[0], b[1]); w.w = cvt_pk_bf16(b[2], b[3]); return w; }
;     __device__ __forceinline__ void operator()(const f32x4 (&acc)[2][2][4][2], const Unit& u, int wr, int wc, int fr, int fq) const {
;     ...
;         for (int q = 0; q < 8; ++q) { const int ai = q >> 2, m = q & 3; const int row = row0 + ai * HALF + m * 16; float s = 0.f;
;             if ((q & 1) == 0 && q + 2 < 8) {
; #pragma unroll
;                 for (int h2 = 0; h2 < 2; ++h2)
; #pragma unroll
;                     for (int bj = 0; bj < 2; ++bj) { const int qn = q + 2 + h2; xnxt[h2][bj] = *(const u32x4*)(X + (size_t)(row0 + (qn >> 2) * HALF + (qn & 3) * 16) * 1024 + col0 + bj * HALF); } }
; #pragma unroll
;                 for (int bj = 0; bj < 2; ++bj) { bf16_t* p = X + (size_t)row * 1024 + col0 + bj * HALF; const u32x4 xv = xcur[q & 1][bj];
;                     f32x4 a = acc[ai][bj][m][0] * scale, b = acc[ai][bj][m][1] * scale;
;                     a[0] += bflo(xv.x); a[1] += bfhi(xv.x); a[2] += bflo(xv.y); a[3] += bfhi(xv.y); b[0] += bflo(xv.z); b[1] += bfhi(xv.z); b[2] += bflo(xv.w); b[3] += bfhi(xv.w);
;                     const u32x4 w = pack8(a, b); *(u32x4*)p = w;
;                     if constexpr (WX8) { unsigned q0 = 0u, q1 = 0u; q0 = __builtin_amdgcn_cvt_pk_fp8_f32(bflo(w.x), bfhi(w.x), q0, false); q0 = __builtin_amdgcn_cvt_pk_fp8_f32(bflo(w.y), bfhi(w.y), q0, true); q1 = __builtin_amdgcn_cvt_pk_fp8_f32(bflo(w.z), bfhi(w.z), q1, false); q1 = __builtin_amdgcn_cvt_pk_fp8_f32(bflo(w.w), bfhi(w.w), q1, true);
;                         *(u32x2*)((unsigned char*)X + (WS_X8 - WS_X) + (size_t)row * 1024 + col0 + bj * HALF) = (u32x2){q0, q1}; }
;                     s += (bflo(w.x) * bflo(w.x) + bfhi(w.x) * bfhi(w.x)) + (bflo(w.y) * bflo(w.y) + bfhi(w.y) * bfhi(w.y)) + (bflo(w.z) * bflo(w.z) + bfhi(w.z) * bfhi(w.z)) + (bflo(w.w) * bflo(w.w) + bfhi(w.w) * bfhi(w.w)); }
;                 s += __shfl_xor(s, 16); s += __shfl_xor(s, 32);
;                 if (fq == 0) ssn[(size_t)row * 16 + u.pn * 4 + wc] = s;
	v_lshlrev_b32_e32 v23, 16, v24
	v_and_b32_e32 v4, 0xffff0000, v4
	v_mul_f32_e32 v4, v4, v4
	v_fmac_f32_e32 v4, v12, v12
	v_lshlrev_b32_e32 v12, 16, v5
	v_and_b32_e32 v5, 0xffff0000, v5
	v_mul_f32_e32 v5, v5, v5
	v_fmac_f32_e32 v5, v12, v12
	v_add_f32_e32 v4, v4, v5
	v_lshlrev_b32_e32 v5, 16, v6
	v_and_b32_e32 v6, 0xffff0000, v6
	v_mul_f32_e32 v6, v6, v6
	v_fmac_f32_e32 v6, v5, v5
	v_add_f32_e32 v4, v4, v6
	v_and_b32_e32 v6, 0xffff0000, v7
	v_lshlrev_b32_e32 v5, 16, v7
	v_mul_f32_e32 v6, v6, v6
	v_fmac_f32_e32 v6, v5, v5
	v_add_f32_e32 v22, v4, v6
	v_pk_mul_f32 v[6:7], v[56:57], s[28:29] op_sel_hi:[1,0]
	v_pk_mul_f32 v[4:5], v[58:59], s[28:29] op_sel_hi:[1,0]
	v_add_f32_e32 v6, v6, v23
	v_and_b32_e32 v23, 0xffff0000, v24
	v_add_f32_e32 v7, v7, v23
	v_lshlrev_b32_e32 v23, 16, v25
	v_add_f32_e32 v4, v4, v23
	v_and_b32_e32 v23, 0xffff0000, v25
	v_pk_mul_f32 v[14:15], v[52:53], s[28:29] op_sel_hi:[1,0]
	v_add_f32_e32 v5, v5, v23
	v_lshlrev_b32_e32 v23, 16, v26
	v_add_f32_e32 v14, v14, v23
	v_and_b32_e32 v23, 0xffff0000, v26
	v_pk_mul_f32 v[12:13], v[54:55], s[28:29] op_sel_hi:[1,0]
	v_add_f32_e32 v15, v15, v23
	v_lshlrev_b32_e32 v23, 16, v27
	v_add_f32_e32 v23, v12, v23
	v_and_b32_e32 v12, 0xffff0000, v27
	v_add_f32_e32 v24, v13, v12
	v_cvt_pk_bf16_f32 v12, v6, v7
	v_cvt_pk_bf16_f32 v13, v4, v5
	v_cvt_pk_bf16_f32 v14, v14, v15
	v_cvt_pk_bf16_f32 v15, v23, v24
	global_store_dwordx4 v[20:21], v[12:15], off offset:256
	v_and_b32_e32 v5, 0xffff0000, v12
	v_lshlrev_b32_e32 v4, 16, v12
	v_mul_f32_e32 v5, v5, v5
	v_and_b32_e32 v6, 0xffff0000, v13
	v_fmac_f32_e32 v5, v4, v4
	v_lshlrev_b32_e32 v4, 16, v13
	v_mul_f32_e32 v6, v6, v6
	v_fmac_f32_e32 v6, v4, v4
	v_add_f32_e32 v4, v5, v6
	v_and_b32_e32 v6, 0xffff0000, v14
	v_lshlrev_b32_e32 v5, 16, v14
	v_mul_f32_e32 v6, v6, v6
	v_fmac_f32_e32 v6, v5, v5
	v_add_f32_e32 v4, v4, v6
	v_and_b32_e32 v6, 0xffff0000, v15
	v_lshlrev_b32_e32 v5, 16, v15
	v_mul_f32_e32 v6, v6, v6
	v_fmac_f32_e32 v6, v5, v5
	v_add_f32_e32 v4, v4, v6
	v_add_f32_e32 v4, v22, v4
	v_mov_b32_e32 v5, v4
	s_nop 1
	v_permlane16_swap_b32_e32 v5, v4
	s_waitcnt lgkmcnt(0)
	v_add_f32_e32 v4, v4, v5
	v_mov_b32_e32 v5, v4
	s_nop 1
	v_permlane32_swap_b32_e32 v5, v4
	s_and_saveexec_b64 s[4:5], vcc
	s_cbranch_execz .LBB0_525
	v_lshlrev_b64 v[6:7], 6, v[102:103]
	v_lshl_add_u64 v[6:7], s[48:49], 0, v[6:7]
	v_lshl_add_u64 v[6:7], s[54:55], 2, v[6:7]
	s_lshl_b32 s92, s22, 2
	v_lshl_add_u64 v[6:7], v[6:7], 0, s[92:93]
	s_waitcnt lgkmcnt(0)
	v_add_f32_e32 v4, v4, v5
	global_store_dword v[6:7], v4, off
.LBB0_525:
	s_or_b64 exec, exec, s[4:5]
	s_waitcnt lgkmcnt(0)
	v_lshl_add_u64 v[4:5], s[44:45], 0, v[104:105]
	v_pk_mul_f32 v[6:7], v[48:49], s[28:29] op_sel_hi:[1,0]
	s_waitcnt vmcnt(7)
	v_lshlrev_b32_e32 v22, 16, v16
	v_and_b32_e32 v16, 0xffff0000, v16
	v_lshl_add_u64 v[12:13], v[174:175], 1, v[4:5]
	v_pk_mul_f32 v[4:5], v[50:51], s[28:29] op_sel_hi:[1,0]
	v_add_f32_e32 v7, v7, v16
	v_lshlrev_b32_e32 v16, 16, v17
	v_add_f32_e32 v16, v4, v16
	v_and_b32_e32 v4, 0xffff0000, v17
	v_pk_mul_f32 v[20:21], v[44:45], s[28:29] op_sel_hi:[1,0]
	v_add_f32_e32 v5, v5, v4
	v_lshlrev_b32_e32 v4, 16, v18
	v_add_f32_e32 v17, v20, v4
	v_and_b32_e32 v4, 0xffff0000, v18
	v_pk_mul_f32 v[14:15], v[46:47], s[28:29] op_sel_hi:[1,0]
	v_add_f32_e32 v18, v21, v4
	v_lshlrev_b32_e32 v4, 16, v19
	v_add_f32_e32 v14, v14, v4
	v_and_b32_e32 v4, 0xffff0000, v19
	v_add_f32_e32 v6, v6, v22
	v_add_f32_e32 v15, v15, v4
	v_cvt_pk_bf16_f32 v4, v6, v7
	v_cvt_pk_bf16_f32 v5, v16, v5
	v_cvt_pk_bf16_f32 v6, v17, v18
	v_cvt_pk_bf16_f32 v7, v14, v15
	global_store_dwordx4 v[12:13], v[4:7], off
	v_lshlrev_b32_e32 v14, 16, v4
	s_waitcnt vmcnt(7)
	v_lshlrev_b32_e32 v19, 16, v8
	v_and_b32_e32 v4, 0xffff0000, v4
	v_mul_f32_e32 v4, v4, v4
	v_fmac_f32_e32 v4, v14, v14
	v_lshlrev_b32_e32 v14, 16, v5
	v_and_b32_e32 v5, 0xffff0000, v5
	v_mul_f32_e32 v5, v5, v5
	v_fmac_f32_e32 v5, v14, v14
	v_add_f32_e32 v4, v4, v5
	v_lshlrev_b32_e32 v5, 16, v6
	v_and_b32_e32 v6, 0xffff0000, v6
	v_mul_f32_e32 v6, v6, v6
	v_fmac_f32_e32 v6, v5, v5
	v_add_f32_e32 v4, v4, v6
	v_and_b32_e32 v6, 0xffff0000, v7
	v_lshlrev_b32_e32 v5, 16, v7
	v_mul_f32_e32 v6, v6, v6
	v_fmac_f32_e32 v6, v5, v5
	v_add_f32_e32 v18, v4, v6
	v_pk_mul_f32 v[6:7], v[40:41], s[28:29] op_sel_hi:[1,0]
	v_and_b32_e32 v8, 0xffff0000, v8
	v_pk_mul_f32 v[4:5], v[42:43], s[28:29] op_sel_hi:[1,0]
	v_add_f32_e32 v7, v7, v8
	v_lshlrev_b32_e32 v8, 16, v9
	v_add_f32_e32 v4, v4, v8
	v_and_b32_e32 v8, 0xffff0000, v9
	v_pk_mul_f32 v[14:15], v[38:39], s[28:29] op_sel_hi:[1,0]
	v_pk_mul_f32 v[16:17], v[36:37], s[28:29] op_sel_hi:[1,0]
	v_add_f32_e32 v6, v6, v19
	v_add_f32_e32 v5, v5, v8
	v_lshlrev_b32_e32 v8, 16, v10
	v_and_b32_e32 v9, 0xffff0000, v10
	v_lshlrev_b32_e32 v10, 16, v11
	v_add_f32_e32 v8, v16, v8
	v_add_f32_e32 v9, v17, v9
	v_add_f32_e32 v10, v14, v10
	v_and_b32_e32 v11, 0xffff0000, v11
	v_cvt_pk_bf16_f32 v6, v6, v7
	v_cvt_pk_bf16_f32 v7, v4, v5
	v_add_f32_e32 v11, v15, v11
	v_and_b32_e32 v5, 0xffff0000, v6
	v_cvt_pk_bf16_f32 v8, v8, v9
	v_cvt_pk_bf16_f32 v9, v10, v11
	v_lshlrev_b32_e32 v4, 16, v6
	v_mul_f32_e32 v5, v5, v5
	v_and_b32_e32 v10, 0xffff0000, v7
	v_fmac_f32_e32 v5, v4, v4
	v_lshlrev_b32_e32 v4, 16, v7
	v_mul_f32_e32 v10, v10, v10
	v_fmac_f32_e32 v10, v4, v4
	v_add_f32_e32 v4, v5, v10
	v_and_b32_e32 v10, 0xffff0000, v8
	v_lshlrev_b32_e32 v5, 16, v8
	v_mul_f32_e32 v10, v10, v10
	v_fmac_f32_e32 v10, v5, v5
	v_add_f32_e32 v4, v4, v10
	v_and_b32_e32 v10, 0xffff0000, v9
	v_lshlrev_b32_e32 v5, 16, v9
	v_mul_f32_e32 v10, v10, v10
	v_fmac_f32_e32 v10, v5, v5
	v_add_f32_e32 v4, v4, v10
	v_add_f32_e32 v4, v18, v4
	v_mov_b32_e32 v5, v4
	s_nop 1
	v_permlane16_swap_b32_e32 v5, v4
	global_store_dwordx4 v[12:13], v[6:9], off offset:256
	s_waitcnt lgkmcnt(0)
	v_add_f32_e32 v4, v4, v5
	v_mov_b32_e32 v5, v4
	s_nop 1
	v_permlane32_swap_b32_e32 v5, v4
	s_and_saveexec_b64 s[4:5], vcc
	s_cbranch_execz .LBB0_527
	v_lshlrev_b64 v[6:7], 6, v[100:101]
	v_lshl_add_u64 v[6:7], s[48:49], 0, v[6:7]
	v_lshl_add_u64 v[6:7], s[54:55], 2, v[6:7]
	s_lshl_b32 s92, s22, 2
	v_lshl_add_u64 v[6:7], v[6:7], 0, s[92:93]
	s_waitcnt lgkmcnt(0)
	v_add_f32_e32 v4, v4, v5
	global_store_dword v[6:7], v4, off

; __device__ __forceinline__ float rstd_fin4(const f32x4 a) { float s = (a[0] + a[1]) + (a[2] + a[3]); s += __shfl_xor(s, 16); s += __shfl_xor(s, 32); return __builtin_amdgcn_rsqf(s * (1.f / 1024.f) + 1e-6f); }
;     __device__ __forceinline__ void operator()(const f32x4 (&acc)[2][2][4][2], const Unit& u, int wr, int wc, int fr, int fq) const {
;         asm volatile("" : "+v"(fr), "+v"(fq));
;         const int row0 = u.pm * BM + wr * 64 + fr, t = u.pn, c8 = wc * 32 + fq * 8;
;         bf16_t* const HG = (bf16_t*)(ws + WS_HG); bf16_t* const U = (bf16_t*)(ws + WS_U); bf16_t* const BG = (bf16_t*)(ws + WS_BG); bf16_t* const Q = (bf16_t*)(ws + WS_Q); bf16_t* const K = (bf16_t*)(ws + WS_K);
;         bf16_t* const V = (bf16_t*)(ws + WS_V); bf16_t* const QI = (bf16_t*)(ws + WS_QI); bf16_t* const KI = (bf16_t*)(ws + WS_KI); float* const WI = (float*)(ws + WS_WI); const float* const cs = (const float*)(ws + WS_COS); const float* const sn = (const float*)(ws + WS_SIN);
;         float rsv[8];
;         { f32x4 pa[8];
; #pragma unroll
;           for (int q = 0; q < 8; ++q) pa[q] = rstd_ld4(ss, row0 + (q >> 2) * HALF + (q & 3) * 16, fq);
; #pragma unroll
;           for (int q = 0; q < 8; ++q) rsv[q] = rstd_fin4(pa[q]); }
.LBB0_654:
	s_lshl_b32 s4, s73, 8
	v_mov_b32_e32 v211, v1
	v_mov_b32_e32 v132, v187
	s_add_i32 s4, s21, s4
	v_and_b32_e32 v166, 64, v246
	v_add_u32_e32 v220, s4, v211
	v_lshlrev_b32_e32 v134, 2, v132
	v_add_u32_e32 v216, 16, v220
	v_ashrrev_i32_e32 v135, 31, v134
	v_ashrrev_i32_e32 v221, 31, v220
	v_ashrrev_i32_e32 v217, 31, v216
	v_add_u32_e32 v212, 32, v220
	v_add_u32_e32 v208, 48, v220
	v_lshl_add_u64 v[162:163], v[134:135], 2, s[50:51]
	v_lshlrev_b64 v[134:135], 6, v[220:221]
	v_lshlrev_b64 v[136:137], 6, v[216:217]
	v_ashrrev_i32_e32 v213, 31, v212
	v_ashrrev_i32_e32 v209, 31, v208
	v_lshl_add_u64 v[134:135], v[162:163], 0, v[134:135]
	v_lshl_add_u64 v[138:139], v[162:163], 0, v[136:137]
	v_lshlrev_b64 v[142:143], 6, v[212:213]
	v_lshlrev_b64 v[144:145], 6, v[208:209]
	global_load_dwordx4 v[134:137], v[134:135], off
	s_nop 0
	global_load_dwordx4 v[138:141], v[138:139], off
	v_lshl_add_u64 v[142:143], v[162:163], 0, v[142:143]
	v_lshl_add_u64 v[146:147], v[162:163], 0, v[144:145]
	v_add_u32_e32 v192, 0x80, v220
	global_load_dwordx4 v[142:145], v[142:143], off
	s_nop 0
	global_load_dwordx4 v[146:149], v[146:147], off
	v_ashrrev_i32_e32 v193, 31, v192
	v_lshlrev_b64 v[150:151], 6, v[192:193]
	v_lshl_add_u64 v[150:151], v[162:163], 0, v[150:151]
	global_load_dwordx4 v[150:153], v[150:151], off
	v_add_u32_e32 v188, 0x90, v220
	v_ashrrev_i32_e32 v189, 31, v188
	v_lshlrev_b64 v[154:155], 6, v[188:189]
	v_lshl_add_u64 v[154:155], v[162:163], 0, v[154:155]
	global_load_dwordx4 v[154:157], v[154:155], off
	v_add_u32_e32 v184, 0xa0, v220
	v_add_u32_e32 v182, 0xb0, v220
	v_ashrrev_i32_e32 v185, 31, v184
	v_ashrrev_i32_e32 v183, 31, v182
	v_lshlrev_b64 v[158:159], 6, v[184:185]
	v_lshlrev_b64 v[164:165], 6, v[182:183]
	v_lshl_add_u64 v[158:159], v[162:163], 0, v[158:159]
	v_lshl_add_u64 v[162:163], v[162:163], 0, v[164:165]
	global_load_dwordx4 v[158:161], v[158:159], off
	v_xor_b32_e32 v133, 16, v246
	global_load_dwordx4 v[162:165], v[162:163], off
	v_add_u32_e32 v166, 64, v166
	v_cmp_lt_i32_e32 vcc, v133, v166
	v_xor_b32_e32 v167, 32, v246
	v_cmp_lt_i32_e64 s[42:43], v167, v166
	v_cndmask_b32_e32 v133, v246, v133, vcc
	v_lshlrev_b32_e32 v133, 2, v133
	v_cndmask_b32_e64 v166, v246, v167, s[42:43]
	v_lshlrev_b32_e32 v166, 2, v166
	s_sub_i32 s75, s72, s6
	s_cmp_gt_i32 s75, 4
	s_cselect_b64 s[4:5], -1, 0
	s_add_i32 s42, s75, -9
	s_cmp_gt_u32 s42, 1
	s_cselect_b64 s[42:43], -1, 0
	s_and_b64 s[42:43], s[4:5], s[42:43]
	v_lshlrev_b32_e32 v224, 3, v132
	s_mov_b64 s[4:5], -1
	s_and_b64 vcc, exec, s[42:43]
	s_waitcnt vmcnt(0)
	v_add_f32_e32 v134, v134, v135
	v_add_f32_e32 v135, v136, v137
	v_add_f32_e32 v134, v134, v135
	v_add_f32_e32 v135, v138, v139
	v_add_f32_e32 v136, v140, v141
	v_add_f32_e32 v137, v142, v143
	v_add_f32_e32 v138, v144, v145
	v_add_f32_e32 v139, v146, v147
	v_add_f32_e32 v140, v148, v149
	v_mov_b32_e32 v145, v134
	s_nop 1
	v_permlane16_swap_b32_e32 v145, v134
	v_add_f32_e32 v135, v135, v136
	v_add_f32_e32 v136, v137, v138
	v_add_f32_e32 v137, v139, v140
	v_mov_b32_e32 v139, v135
	s_nop 1
	v_permlane16_swap_b32_e32 v139, v135
	v_mov_b32_e32 v140, v136
	s_nop 1
	v_permlane16_swap_b32_e32 v140, v136
	v_add_f32_e32 v141, v150, v151
	v_add_f32_e32 v142, v152, v153
	v_add_f32_e32 v138, v141, v142
	v_mov_b32_e32 v141, v137
	s_nop 1
	v_permlane16_swap_b32_e32 v141, v137
	s_waitcnt lgkmcnt(3)
	v_add_f32_e32 v134, v134, v145
	v_mov_b32_e32 v142, v138
	s_nop 1
	v_permlane16_swap_b32_e32 v142, v138
	v_mov_b32_e32 v145, v134
	s_nop 1
	v_permlane32_swap_b32_e32 v145, v134
	s_waitcnt lgkmcnt(4)
	v_add_f32_e32 v135, v135, v139
	s_waitcnt lgkmcnt(3)
	v_add_f32_e32 v136, v136, v140
	v_mov_b32_e32 v139, v135
	s_nop 1
	v_permlane32_swap_b32_e32 v139, v135
	v_mov_b32_e32 v140, v136
	s_nop 1
	v_permlane32_swap_b32_e32 v140, v136
	s_waitcnt lgkmcnt(4)
	v_add_f32_e32 v137, v137, v141
	v_mov_b32_e32 v141, v137
	s_nop 1
	v_permlane32_swap_b32_e32 v141, v137
	s_waitcnt lgkmcnt(4)
	v_add_f32_e32 v138, v138, v142
	s_waitcnt lgkmcnt(3)
	v_add_f32_e32 v134, v134, v145
	v_mov_b32_e32 v142, v138
	s_nop 1
	v_permlane32_swap_b32_e32 v142, v138
	v_fmamk_f32 v134, v134, 0x3a800000, v227
	s_waitcnt lgkmcnt(3)
	v_add_f32_e32 v135, v135, v139
	v_add_f32_e32 v143, v154, v155
	v_add_f32_e32 v144, v156, v157
	s_waitcnt lgkmcnt(2)
	v_add_f32_e32 v136, v136, v140
	v_rsq_f32_e32 v226, v134
	v_fmamk_f32 v134, v135, 0x3a800000, v227
	v_fmamk_f32 v135, v136, 0x3a800000, v227
	v_rsq_f32_e32 v222, v134
	v_add_f32_e32 v134, v143, v144
	s_waitcnt lgkmcnt(1)
	v_add_f32_e32 v137, v137, v141
	v_rsq_f32_e32 v218, v135
	v_mov_b32_e32 v135, v134
	s_nop 1
	v_permlane16_swap_b32_e32 v135, v134
	v_fmamk_f32 v136, v137, 0x3a800000, v227
	v_rsq_f32_e32 v214, v136
	s_waitcnt lgkmcnt(1)
	v_add_f32_e32 v136, v138, v142
	v_fmamk_f32 v136, v136, 0x3a800000, v227
	v_rsq_f32_e32 v210, v136
	v_add_f32_e32 v136, v158, v159
	v_add_f32_e32 v137, v160, v161
	v_add_f32_e32 v138, v162, v163
	v_add_f32_e32 v139, v164, v165
	s_waitcnt lgkmcnt(0)
	v_add_f32_e32 v134, v134, v135
	v_add_f32_e32 v136, v136, v137
	v_add_f32_e32 v138, v138, v139
	v_mov_b32_e32 v135, v134
	s_nop 1
	v_permlane32_swap_b32_e32 v135, v134
	v_mov_b32_e32 v137, v136
	s_nop 1
	v_permlane16_swap_b32_e32 v137, v136
	v_mov_b32_e32 v133, v138
	s_nop 1
	v_permlane16_swap_b32_e32 v133, v138
	s_waitcnt lgkmcnt(2)
	v_add_f32_e32 v134, v134, v135
	s_waitcnt lgkmcnt(1)
	v_add_f32_e32 v135, v136, v137
	s_waitcnt lgkmcnt(0)
	v_add_f32_e32 v133, v138, v133
	v_mov_b32_e32 v136, v135
	s_nop 1
	v_permlane32_swap_b32_e32 v136, v135
	v_mov_b32_e32 v137, v133
	s_nop 1
	v_permlane32_swap_b32_e32 v137, v133
	v_fmamk_f32 v134, v134, 0x3a800000, v227
	v_rsq_f32_e32 v194, v134
	s_waitcnt lgkmcnt(1)
	v_add_f32_e32 v134, v135, v136
	s_waitcnt lgkmcnt(0)
	v_add_f32_e32 v133, v133, v137
	v_fmamk_f32 v134, v134, 0x3a800000, v227
	v_fmamk_f32 v133, v133, 0x3a800000, v227
	v_rsq_f32_e32 v190, v134
	v_rsq_f32_e32 v186, v133
	s_cbranch_vccz .LBB0_776
;     __device__ __forceinline__ void operator()(const f32x4 (&acc)[2][2][4][2], const Unit& u, int wr, int wc, int fr, int fq) const {
;     ...
;             f32x4 cc[4], cn[4];
;             { const size_t o = (size_t)row0 * 32 + fq * 8; cc[0] = *(const f32x4*)(cs + o); cc[1] = *(const f32x4*)(cs + o + 4); cc[2] = *(const f32x4*)(sn + o); cc[3] = *(const f32x4*)(sn + o + 4); }
; #pragma unroll
;             for (int q = 0; q < 8; ++q) { const int ai = q >> 2, m = q & 3; const int row = row0 + ai * HALF + m * 16; const float rs = rsv[q];
;                 if (q + 1 < 8) { const size_t o = (size_t)(row0 + ((q + 1) >> 2) * HALF + ((q + 1) & 3) * 16) * 32 + fq * 8; cn[0] = *(const f32x4*)(cs + o); cn[1] = *(const f32x4*)(cs + o + 4); cn[2] = *(const f32x4*)(sn + o); cn[3] = *(const f32x4*)(sn + o + 4); }
;                 const f32x4 a0 = acc[ai][0][m][0] * rs, a1 = acc[ai][0][m][1] * rs, b0 = acc[ai][1][m][0] * rs, b1 = acc[ai][1][m][1] * rs;
;                 const f32x4 c0 = cc[0], c1 = cc[1], s0 = cc[2], s1 = cc[3];
;                 f32x4 p0 = a0 * c0 - b0 * s0, p1 = a1 * c1 - b1 * s1, r0 = b0 * c0 + a0 * s0, r1 = b1 * c1 + a1 * s1;
	v_lshlrev_b64 v[134:135], 5, v[220:221]
	v_ashrrev_i32_e32 v225, 31, v224
	v_lshl_add_u64 v[134:135], v[134:135], 0, v[224:225]
	v_lshlrev_b64 v[134:135], 2, v[134:135]
	v_lshl_add_u64 v[136:137], s[56:57], 0, v[134:135]
	v_lshl_add_u64 v[134:135], s[62:63], 0, v[134:135]
	global_load_dwordx4 v[234:237], v[136:137], off offset:16
	global_load_dwordx4 v[154:157], v[136:137], off
	global_load_dwordx4 v[238:241], v[134:135], off offset:16
	global_load_dwordx4 v[158:161], v[134:135], off
	v_ashrrev_i32_e32 v134, 1, v132
	v_ashrrev_i32_e32 v135, 31, v134
	v_lshlrev_b64 v[232:233], 6, v[134:135]
	v_lshlrev_b32_e32 v133, 5, v132
	v_and_or_b32 v232, v133, 32, v232
	v_cmp_eq_u32_e32 vcc, 0, v132
	v_lshlrev_b64 v[132:133], 5, v[216:217]
	v_lshl_add_u64 v[132:133], v[132:133], 0, v[224:225]
	v_lshlrev_b64 v[140:141], 2, v[132:133]
	v_lshl_add_u64 v[136:137], s[56:57], 0, v[140:141]
	v_lshl_add_u64 v[144:145], s[62:63], 0, v[140:141]
	global_load_dwordx4 v[132:135], v[136:137], off offset:16
	s_nop 0
	global_load_dwordx4 v[136:139], v[136:137], off
	s_nop 0
	global_load_dwordx4 v[140:143], v[144:145], off offset:16
	s_nop 0
	global_load_dwordx4 v[144:147], v[144:145], off
	s_cmp_gt_u32 s75, 6
	s_cselect_b64 s[42:43], -1, 0
	s_cmp_gt_u32 s75, 8
	s_cselect_b64 s[94:95], -1, 0
	s_cmp_lg_u32 s75, 11
	s_cselect_b64 s[90:91], -1, 0
	s_lshl_b32 s44, s75, 8
	s_add_i32 s92, s23, s44
	s_and_b64 s[72:73], s[68:69], vcc
	s_lshl_b64 s[4:5], s[92:93], 1
	v_readlane_b32 s45, v252, 32
	s_add_u32 s4, s45, s4
	v_readlane_b32 s45, v252, 33
	v_lshlrev_b64 v[152:153], 1, v[224:225]
	s_addc_u32 s5, s45, s5
	s_add_i32 s92, s81, s44
	v_pk_mul_f32 v[170:171], v[130:131], v[226:227] op_sel_hi:[1,0]
	v_pk_mul_f32 v[242:243], v[128:129], v[226:227] op_sel_hi:[1,0]
	v_pk_mul_f32 v[150:151], v[122:123], v[226:227] op_sel_hi:[1,0]
	v_pk_mul_f32 v[148:149], v[120:121], v[226:227] op_sel_hi:[1,0]
	v_lshl_add_u64 v[228:229], s[4:5], 0, v[152:153]
	s_lshl_b64 s[4:5], s[92:93], 1
	v_readlane_b32 s44, v252, 34
	v_pk_mul_f32 v[248:249], v[126:127], v[226:227] op_sel_hi:[1,0]
	v_pk_mul_f32 v[250:251], v[124:125], v[226:227] op_sel_hi:[1,0]
	v_pk_mul_f32 v[204:205], v[118:119], v[226:227] op_sel_hi:[1,0]
	v_pk_mul_f32 v[206:207], v[116:117], v[226:227] op_sel_hi:[1,0]
	s_add_u32 s44, s44, s4
	v_readlane_b32 s4, v252, 35
	v_mov_b64_e32 v[202:203], 0x200
	v_mov_b64_e32 v[200:201], 0xaff
	v_mov_b64_e32 v[198:199], 0xb00
	v_mov_b64_e32 v[196:197], 0x900
	v_lshlrev_b32_e32 v230, 6, v224
	v_mov_b32_e32 v231, 0
	v_lshl_add_u64 v[230:231], v[230:231], 0, s[70:71]
	s_addc_u32 s45, s4, s5
	s_mov_b64 s[96:97], -1
	s_and_b64 vcc, exec, s[42:43]
	s_waitcnt vmcnt(4)
	v_pk_mul_f32 v[162:163], v[150:151], v[160:161]
	v_pk_mul_f32 v[166:167], v[148:149], v[158:159]
	v_pk_mul_f32 v[160:161], v[170:171], v[160:161]
	v_pk_mul_f32 v[158:159], v[242:243], v[158:159]
	v_pk_fma_f32 v[164:165], v[170:171], v[156:157], v[162:163] neg_lo:[0,0,1] neg_hi:[0,0,1]
	v_pk_fma_f32 v[168:169], v[242:243], v[154:155], v[166:167] neg_lo:[0,0,1] neg_hi:[0,0,1]
	v_pk_mul_f32 v[162:163], v[204:205], v[240:241]
	v_pk_mul_f32 v[166:167], v[206:207], v[238:239]
	v_pk_fma_f32 v[156:157], v[150:151], v[156:157], v[160:161]
	v_pk_fma_f32 v[160:161], v[148:149], v[154:155], v[158:159]
	v_pk_mul_f32 v[154:155], v[248:249], v[240:241]
	v_pk_mul_f32 v[158:159], v[250:251], v[238:239]
	v_pk_fma_f32 v[162:163], v[248:249], v[236:237], v[162:163] neg_lo:[0,0,1] neg_hi:[0,0,1]
	v_pk_fma_f32 v[166:167], v[250:251], v[234:235], v[166:167] neg_lo:[0,0,1] neg_hi:[0,0,1]
	v_pk_fma_f32 v[154:155], v[204:205], v[236:237], v[154:155]
	v_pk_fma_f32 v[158:159], v[206:207], v[234:235], v[158:159]
	s_cbranch_vccz .LBB0_668
	s_mov_b64 s[4:5], -1
	s_and_b64 vcc, exec, s[94:95]
	s_cbranch_vccz .LBB0_665
	s_and_b64 vcc, exec, s[90:91]
	s_cbranch_vccz .LBB0_662
	s_andn2_b64 vcc, exec, s[66:67]
	s_cbranch_vccz .LBB0_877
	s_and_saveexec_b64 s[4:5], s[72:73]
	s_cbranch_execz .LBB0_661

;     __device__ __forceinline__ void operator()(const f32x4 (&acc)[2][2][4][2], const Unit& u, int wr, int wc, int fr, int fq) const {
;         asm volatile("" : "+v"(fr), "+v"(fq));
;         const int row0 = u.pm * BM + wr * 64 + fr, col0 = u.pn * BM + wc * 32 + fq * 8;
;         u32x4 xcur[2][2], xnxt[2][2];
; #pragma unroll
;         for (int h2 = 0; h2 < 2; ++h2)
; #pragma unroll
;             for (int bj = 0; bj < 2; ++bj) xcur[h2][bj] = *(const u32x4*)(X + (size_t)(row0 + h2 * 16) * 1024 + col0 + bj * HALF);
; #pragma unroll
;         for (int q = 0; q < 8; ++q) { const int ai = q >> 2, m = q & 3; const int row = row0 + ai * HALF + m * 16; float s = 0.f;
;             if ((q & 1) == 0 && q + 2 < 8) {
; #pragma unroll
;                 for (int h2 = 0; h2 < 2; ++h2)
; #pragma unroll
;                     for (int bj = 0; bj < 2; ++bj) { const int qn = q + 2 + h2; xnxt[h2][bj] = *(const u32x4*)(X + (size_t)(row0 + (qn >> 2) * HALF + (qn & 3) * 16) * 1024 + col0 + bj * HALF); } }
; #pragma unroll
;                 for (int bj = 0; bj < 2; ++bj) { bf16_t* p = X + (size_t)row * 1024 + col0 + bj * HALF; const u32x4 xv = xcur[q & 1][bj];
;                     f32x4 a = acc[ai][bj][m][0] * scale, b = acc[ai][bj][m][1] * scale;
;                     a[0] += bflo(xv.x); a[1] += bfhi(xv.x); a[2] += bflo(xv.y); a[3] += bfhi(xv.y); b[0] += bflo(xv.z); b[1] += bfhi(xv.z); b[2] += bflo(xv.w); b[3] += bfhi(xv.w);
;                     const u32x4 w = pack8(a, b); *(u32x4*)p = w;
;                     if constexpr (WX8) { unsigned q0 = 0u, q1 = 0u; q0 = __builtin_amdgcn_cvt_pk_fp8_f32(bflo(w.x), bfhi(w.x), q0, false); q0 = __builtin_amdgcn_cvt_pk_fp8_f32(bflo(w.y), bfhi(w.y), q0, true); q1 = __builtin_amdgcn_cvt_pk_fp8_f32(bflo(w.z), bfhi(w.z), q1, false); q1 = __builtin_amdgcn_cvt_pk_fp8_f32(bflo(w.w), bfhi(w.w), q1, true);
;                         *(u32x2*)((unsigned char*)X + (WS_X8 - WS_X) + (size_t)row * 1024 + col0 + bj * HALF) = (u32x2){q0, q1}; }
;                     s += (bflo(w.x) * bflo(w.x) + bfhi(w.x) * bfhi(w.x)) + (bflo(w.y) * bflo(w.y) + bfhi(w.y) * bfhi(w.y)) + (bflo(w.z) * bflo(w.z) + bfhi(w.z) * bfhi(w.z)) + (bflo(w.w) * bflo(w.w) + bfhi(w.w) * bfhi(w.w)); }
;                 s += __shfl_xor(s, 16); s += __shfl_xor(s, 32);
;                 if (fq == 0) ssn[(size_t)row * 16 + u.pn * 4 + wc] = s;
.LBB0_1414:
	s_lshl_b32 s4, s69, 8
	v_mov_b32_e32 v126, v194
	v_mov_b32_e32 v124, v1
	s_add_i32 s4, s4, s23
	s_lshl_b32 s60, s68, 2
	v_add_u32_e32 v172, s4, v124
	s_lshl_b32 s4, s68, 8
	s_or_b32 s4, s4, s64
	v_lshl_add_u32 v170, v126, 3, s4
	v_ashrrev_i32_e32 v171, 31, v170
	v_lshlrev_b64 v[192:193], 1, v[170:171]
	v_ashrrev_i32_e32 v173, 31, v172
	v_lshl_add_u64 v[174:175], s[44:45], 0, v[192:193]
	v_lshlrev_b64 v[190:191], 11, v[172:173]
	v_lshl_add_u64 v[124:125], v[174:175], 0, v[190:191]
	global_load_dwordx4 v[210:213], v[124:125], off
	global_load_dwordx4 v[156:159], v[124:125], off offset:256
	v_add_u32_e32 v182, 16, v172
	v_ashrrev_i32_e32 v183, 31, v182
	v_add_u32_e32 v180, 32, v172
	v_lshlrev_b64 v[186:187], 11, v[182:183]
	v_ashrrev_i32_e32 v181, 31, v180
	v_add_u32_e32 v176, 48, v172
	v_lshl_add_u64 v[124:125], v[174:175], 0, v[186:187]
	v_lshlrev_b64 v[184:185], 11, v[180:181]
	v_ashrrev_i32_e32 v177, 31, v176
	global_load_dwordx4 v[144:147], v[124:125], off
	global_load_dwordx4 v[140:143], v[124:125], off offset:256
	v_lshl_add_u64 v[124:125], v[174:175], 0, v[184:185]
	v_lshlrev_b64 v[178:179], 11, v[176:177]
	global_load_dwordx4 v[136:139], v[124:125], off
	global_load_dwordx4 v[132:135], v[124:125], off offset:256
	v_lshl_add_u64 v[124:125], v[174:175], 0, v[178:179]
	v_cmp_eq_u32_e32 vcc, 0, v126
	global_load_dwordx4 v[128:131], v[124:125], off
	s_nop 0
	global_load_dwordx4 v[124:127], v[124:125], off offset:256
	v_lshl_add_u64 v[190:191], s[44:45], 0, v[190:191]
	v_lshl_add_u64 v[192:193], v[190:191], 0, v[192:193]
	v_lshlrev_b64 v[188:189], 10, v[172:173]
	s_ashr_i32 s61, s60, 31
	s_waitcnt vmcnt(0)
	v_lshlrev_b32_e32 v204, 16, v210
	v_add_f32_e32 v152, v152, v204
	v_and_b32_e32 v204, 0xffff0000, v210
	v_add_f32_e32 v153, v153, v204
	v_lshlrev_b32_e32 v204, 16, v211
	v_add_f32_e32 v154, v154, v204
	v_and_b32_e32 v204, 0xffff0000, v211
	v_add_f32_e32 v155, v155, v204
	v_lshlrev_b32_e32 v204, 16, v212
	v_add_f32_e32 v204, v148, v204
	v_and_b32_e32 v148, 0xffff0000, v212
	v_add_f32_e32 v205, v149, v148
	v_lshlrev_b32_e32 v148, 16, v213
	v_add_f32_e32 v206, v150, v148
	v_and_b32_e32 v148, 0xffff0000, v213
	v_add_f32_e32 v151, v151, v148
	v_cvt_pk_bf16_f32 v148, v152, v153
	v_cvt_pk_bf16_f32 v149, v154, v155
	v_cvt_pk_bf16_f32 v150, v204, v205
	v_cvt_pk_bf16_f32 v151, v206, v151
	global_store_dwordx4 v[192:193], v[148:151], off
	v_lshlrev_b32_e32 v152, 16, v148
	v_and_b32_e32 v153, 0xffff0000, v148
	v_mov_b32_e32 v148, v3
	v_lshlrev_b32_e32 v154, 16, v149
	v_and_b32_e32 v155, 0xffff0000, v149
	v_lshlrev_b32_e32 v204, 16, v150
	v_and_b32_e32 v205, 0xffff0000, v150
	v_mov_b32_e32 v149, v3
	v_cvt_pk_fp8_f32 v148, v152, v153
	v_cvt_pk_fp8_f32 v149, v204, v205
	v_lshlrev_b32_e32 v206, 16, v151
	v_and_b32_e32 v207, 0xffff0000, v151
	v_cvt_pk_fp8_f32 v148, v154, v155 op_sel:[0,0,1]
	v_cvt_pk_fp8_f32 v149, v206, v207 op_sel:[0,0,1]
	v_lshl_add_u64 v[150:151], s[48:49], 0, v[188:189]
	v_lshl_add_u64 v[150:151], v[150:151], 0, v[170:171]
	global_store_dwordx2 v[150:151], v[148:149], off
	v_mul_f32_e32 v148, v153, v153
	v_mul_f32_e32 v149, v155, v155
	v_fmac_f32_e32 v148, v152, v152
	v_fmac_f32_e32 v149, v154, v154
	v_add_f32_e32 v148, v148, v149
	v_mul_f32_e32 v149, v205, v205
	v_fmac_f32_e32 v149, v204, v204
	v_add_f32_e32 v148, v148, v149
	v_mul_f32_e32 v149, v207, v207
	v_fmac_f32_e32 v149, v206, v206
	v_add_f32_e32 v148, v148, v149
	v_lshlrev_b32_e32 v149, 16, v156
	v_add_f32_e32 v120, v120, v149
	v_and_b32_e32 v149, 0xffff0000, v156
	v_add_f32_e32 v121, v121, v149
	v_lshlrev_b32_e32 v149, 16, v157
	v_add_f32_e32 v122, v122, v149
	v_and_b32_e32 v149, 0xffff0000, v157
	v_add_f32_e32 v123, v123, v149
	v_lshlrev_b32_e32 v149, 16, v158
	v_add_f32_e32 v149, v116, v149
	v_and_b32_e32 v116, 0xffff0000, v158
	v_add_f32_e32 v150, v117, v116
	v_lshlrev_b32_e32 v116, 16, v159
	v_add_f32_e32 v151, v118, v116
	v_and_b32_e32 v116, 0xffff0000, v159
	v_add_f32_e32 v119, v119, v116
	v_cvt_pk_bf16_f32 v116, v120, v121
	v_cvt_pk_bf16_f32 v117, v122, v123
	v_cvt_pk_bf16_f32 v118, v149, v150
	v_cvt_pk_bf16_f32 v119, v151, v119
	global_store_dwordx4 v[192:193], v[116:119], off offset:256
	v_lshlrev_b32_e32 v120, 16, v116
	v_and_b32_e32 v121, 0xffff0000, v116
	v_mov_b32_e32 v116, v3
	v_lshlrev_b32_e32 v122, 16, v117
	v_and_b32_e32 v123, 0xffff0000, v117
	v_lshlrev_b32_e32 v149, 16, v118
	v_and_b32_e32 v150, 0xffff0000, v118
	v_mov_b32_e32 v117, v3
	v_cvt_pk_fp8_f32 v116, v120, v121
	v_cvt_pk_fp8_f32 v117, v149, v150
	v_sub_co_u32_e64 v118, s[42:43], 0, v188
	v_lshlrev_b32_e32 v151, 16, v119
	v_and_b32_e32 v152, 0xffff0000, v119
	v_subb_co_u32_e64 v119, s[42:43], 0, v189, s[42:43]
	v_cvt_pk_fp8_f32 v116, v122, v123 op_sel:[0,0,1]
	v_cvt_pk_fp8_f32 v117, v151, v152 op_sel:[0,0,1]
	v_lshl_add_u64 v[118:119], v[190:191], 0, v[118:119]
	v_lshl_add_u64 v[118:119], v[118:119], 0, v[170:171]
	v_add_co_u32_e64 v118, s[42:43], s15, v118
	s_nop 1
	v_addc_co_u32_e64 v119, s[42:43], 0, v119, s[42:43]
	global_store_dwordx2 v[118:119], v[116:117], off offset:128
	v_mul_f32_e32 v116, v121, v121
	v_mul_f32_e32 v117, v123, v123
	v_fmac_f32_e32 v116, v120, v120
	v_fmac_f32_e32 v117, v122, v122
	v_add_f32_e32 v116, v116, v117
	v_mul_f32_e32 v117, v150, v150
	v_fmac_f32_e32 v117, v149, v149
	v_add_f32_e32 v116, v116, v117
	v_mul_f32_e32 v117, v152, v152
	v_fmac_f32_e32 v117, v151, v151
	v_and_b32_e32 v118, 64, v246
	v_add_f32_e32 v116, v116, v117
	v_xor_b32_e32 v117, 16, v246
	v_add_u32_e32 v118, 64, v118
	v_cmp_lt_i32_e64 s[42:43], v117, v118
	v_add_f32_e32 v116, v148, v116
	s_nop 0
	v_cndmask_b32_e64 v117, v246, v117, s[42:43]
	v_lshlrev_b32_e32 v148, 2, v117
	v_mov_b32_e32 v117, v116
	s_nop 1
	v_permlane16_swap_b32_e32 v117, v116
	s_waitcnt lgkmcnt(0)
	v_add_f32_e32 v116, v116, v117
	v_xor_b32_e32 v117, 32, v246
	v_cmp_lt_i32_e64 s[42:43], v117, v118
	s_nop 1
	v_cndmask_b32_e64 v117, v246, v117, s[42:43]
	v_lshlrev_b32_e32 v149, 2, v117
	v_mov_b32_e32 v117, v116
	s_nop 1
	v_permlane32_swap_b32_e32 v117, v116
	s_and_saveexec_b64 s[4:5], vcc
	s_cbranch_execz .LBB0_1416
	v_lshlrev_b64 v[118:119], 6, v[172:173]
	v_lshl_add_u64 v[118:119], s[46:47], 0, v[118:119]
	v_lshl_add_u64 v[118:119], s[60:61], 2, v[118:119]
	s_lshl_b32 s92, s22, 2
	v_lshl_add_u64 v[118:119], v[118:119], 0, s[92:93]
	s_waitcnt lgkmcnt(0)
	v_add_f32_e32 v116, v116, v117
	global_store_dword v[118:119], v116, off
; __device__ __forceinline__ float bflo(unsigned w) { return __uint_as_float(w << 16); }
; __device__ __forceinline__ float bfhi(unsigned w) { return __uint_as_float(w & 0xffff0000u); }
; __device__ __forceinline__ u32x4 pack8(const f32x4 a, const f32x4 b) { u32x4 w; w.x = cvt_pk_bf16(a[0], a[1]); w.y = cvt_pk_bf16(a[2], a[3]); w.z = cvt_pk_bf16(b[0], b[1]); w.w = cvt_pk_bf16(b[2], b[3]); return w; }
;     __device__ __forceinline__ void operator()(const f32x4 (&acc)[2][2][4][2], const Unit& u, int wr, int wc, int fr, int fq) const {
;     ...
;         for (int q = 0; q < 8; ++q) { const int ai = q >> 2, m = q & 3; const int row = row0 + ai * HALF + m * 16; float s = 0.f;
;             if ((q & 1) == 0 && q + 2 < 8) {
; #pragma unroll
;                 for (int h2 = 0; h2 < 2; ++h2)
; #pragma unroll
;                     for (int bj = 0; bj < 2; ++bj) { const int qn = q + 2 + h2; xnxt[h2][bj] = *(const u32x4*)(X + (size_t)(row0 + (qn >> 2) * HALF + (qn & 3) * 16) * 1024 + col0 + bj * HALF); } }
; #pragma unroll
;                 for (int bj = 0; bj < 2; ++bj) { bf16_t* p = X + (size_t)row * 1024 + col0 + bj * HALF; const u32x4 xv = xcur[q & 1][bj];
;                     f32x4 a = acc[ai][bj][m][0] * scale, b = acc[ai][bj][m][1] * scale;
;                     a[0] += bflo(xv.x); a[1] += bfhi(xv.x); a[2] += bflo(xv.y); a[3] += bfhi(xv.y); b[0] += bflo(xv.z); b[1] += bfhi(xv.z); b[2] += bflo(xv.w); b[3] += bfhi(xv.w);
;                     const u32x4 w = pack8(a, b); *(u32x4*)p = w;
;                     if constexpr (WX8) { unsigned q0 = 0u, q1 = 0u; q0 = __builtin_amdgcn_cvt_pk_fp8_f32(bflo(w.x), bfhi(w.x), q0, false); q0 = __builtin_amdgcn_cvt_pk_fp8_f32(bflo(w.y), bfhi(w.y), q0, true); q1 = __builtin_amdgcn_cvt_pk_fp8_f32(bflo(w.z), bfhi(w.z), q1, false); q1 = __builtin_amdgcn_cvt_pk_fp8_f32(bflo(w.w), bfhi(w.w), q1, true);
;                         *(u32x2*)((unsigned char*)X + (WS_X8 - WS_X) + (size_t)row * 1024 + col0 + bj * HALF) = (u32x2){q0, q1}; }
;                     s += (bflo(w.x) * bflo(w.x) + bfhi(w.x) * bfhi(w.x)) + (bflo(w.y) * bflo(w.y) + bfhi(w.y) * bfhi(w.y)) + (bflo(w.z) * bflo(w.z) + bfhi(w.z) * bfhi(w.z)) + (bflo(w.w) * bflo(w.w) + bfhi(w.w) * bfhi(w.w)); }
;                 s += __shfl_xor(s, 16); s += __shfl_xor(s, 32);
;                 if (fq == 0) ssn[(size_t)row * 16 + u.pn * 4 + wc] = s;
.LBB0_1416:
	s_or_b64 exec, exec, s[4:5]
	v_lshlrev_b32_e32 v122, 16, v144
	v_add_f32_e32 v112, v112, v122
	v_and_b32_e32 v122, 0xffff0000, v144
	v_add_f32_e32 v113, v113, v122
	v_lshlrev_b32_e32 v122, 16, v145
	v_add_f32_e32 v114, v114, v122
	v_and_b32_e32 v122, 0xffff0000, v145
	v_add_f32_e32 v115, v115, v122
	v_lshlrev_b32_e32 v122, 16, v146
	v_add_f32_e32 v122, v108, v122
	v_and_b32_e32 v108, 0xffff0000, v146
	v_add_f32_e32 v123, v109, v108
	v_lshlrev_b32_e32 v108, 16, v147
	v_add_f32_e32 v144, v110, v108
	v_and_b32_e32 v108, 0xffff0000, v147
	v_add_f32_e32 v111, v111, v108
	v_cvt_pk_bf16_f32 v108, v112, v113
	v_cvt_pk_bf16_f32 v109, v114, v115
	v_cvt_pk_bf16_f32 v110, v122, v123
	v_cvt_pk_bf16_f32 v111, v144, v111
	v_mov_b32_e32 v112, v3
	v_lshlrev_b32_e32 v114, 16, v108
	v_and_b32_e32 v115, 0xffff0000, v108
	v_lshlrev_b32_e32 v144, 16, v110
	v_and_b32_e32 v145, 0xffff0000, v110
	v_mov_b32_e32 v113, v3
	v_cvt_pk_fp8_f32 v112, v114, v115
	v_cvt_pk_fp8_f32 v113, v144, v145
	v_lshlrev_b32_e32 v122, 16, v109
	v_and_b32_e32 v123, 0xffff0000, v109
	v_lshlrev_b32_e32 v146, 16, v111
	v_and_b32_e32 v147, 0xffff0000, v111
	v_lshl_add_u64 v[118:119], s[44:45], 0, v[186:187]
	v_cvt_pk_fp8_f32 v112, v122, v123 op_sel:[0,0,1]
	v_cvt_pk_fp8_f32 v113, v146, v147 op_sel:[0,0,1]
	s_waitcnt lgkmcnt(0)
	v_lshlrev_b64 v[116:117], 10, v[182:183]
	v_lshl_add_u64 v[120:121], v[170:171], 1, v[118:119]
	global_store_dwordx4 v[120:121], v[108:111], off
	s_nop 1
	v_lshl_add_u64 v[108:109], s[48:49], 0, v[116:117]
	v_lshl_add_u64 v[108:109], v[108:109], 0, v[170:171]
	global_store_dwordx2 v[108:109], v[112:113], off
	v_mul_f32_e32 v108, v115, v115
	v_mul_f32_e32 v109, v123, v123
	v_fmac_f32_e32 v108, v114, v114
	v_fmac_f32_e32 v109, v122, v122
	v_add_f32_e32 v108, v108, v109
	v_mul_f32_e32 v109, v145, v145
	v_fmac_f32_e32 v109, v144, v144
	v_add_f32_e32 v108, v108, v109
	v_mul_f32_e32 v109, v147, v147
	v_fmac_f32_e32 v109, v146, v146
	v_add_f32_e32 v108, v108, v109
	v_lshlrev_b32_e32 v109, 16, v140
	v_add_f32_e32 v104, v104, v109
	v_and_b32_e32 v109, 0xffff0000, v140
	v_add_f32_e32 v105, v105, v109
	v_lshlrev_b32_e32 v109, 16, v141
	v_add_f32_e32 v106, v106, v109
	v_and_b32_e32 v109, 0xffff0000, v141
	v_add_f32_e32 v107, v107, v109
	v_lshlrev_b32_e32 v109, 16, v142
	v_add_f32_e32 v109, v100, v109
	v_and_b32_e32 v100, 0xffff0000, v142
	v_add_f32_e32 v110, v101, v100
	v_lshlrev_b32_e32 v100, 16, v143
	v_add_f32_e32 v111, v102, v100
	v_and_b32_e32 v100, 0xffff0000, v143
	v_add_f32_e32 v103, v103, v100
	v_cvt_pk_bf16_f32 v100, v104, v105
	v_cvt_pk_bf16_f32 v101, v106, v107
	v_cvt_pk_bf16_f32 v102, v109, v110
	v_cvt_pk_bf16_f32 v103, v111, v103
	global_store_dwordx4 v[120:121], v[100:103], off offset:256
	v_lshlrev_b32_e32 v106, 16, v100
	v_mov_b32_e32 v104, v3
	v_and_b32_e32 v100, 0xffff0000, v100
	v_cvt_pk_fp8_f32 v104, v106, v100
	v_lshlrev_b32_e32 v107, 16, v101
	v_and_b32_e32 v101, 0xffff0000, v101
	v_mul_f32_e32 v100, v100, v100
	v_cvt_pk_fp8_f32 v104, v107, v101 op_sel:[0,0,1]
	v_mul_f32_e32 v101, v101, v101
	v_lshlrev_b32_e32 v109, 16, v102
	v_and_b32_e32 v102, 0xffff0000, v102
	v_fmac_f32_e32 v100, v106, v106
	v_fmac_f32_e32 v101, v107, v107
	v_add_f32_e32 v100, v100, v101
	v_mul_f32_e32 v101, v102, v102
	v_lshlrev_b32_e32 v110, 16, v103
	v_and_b32_e32 v103, 0xffff0000, v103
	v_fmac_f32_e32 v101, v109, v109
	v_add_f32_e32 v100, v100, v101
	v_mul_f32_e32 v101, v103, v103
	v_fmac_f32_e32 v101, v110, v110
	v_add_f32_e32 v100, v100, v101
	v_add_f32_e32 v106, v108, v100
	v_mov_b32_e32 v105, v3
	v_mov_b32_e32 v107, v106
	s_nop 1
	v_permlane16_swap_b32_e32 v107, v106
	v_cvt_pk_fp8_f32 v105, v109, v102
	v_sub_co_u32_e64 v100, s[42:43], 0, v116
	v_cvt_pk_fp8_f32 v105, v110, v103 op_sel:[0,0,1]
	s_nop 0
	v_subb_co_u32_e64 v101, s[42:43], 0, v117, s[42:43]
	v_lshl_add_u64 v[100:101], v[118:119], 0, v[100:101]
	v_lshl_add_u64 v[102:103], v[100:101], 0, v[170:171]
	s_waitcnt lgkmcnt(0)
	v_add_f32_e32 v100, v106, v107
	v_mov_b32_e32 v101, v100
	s_nop 1
	v_permlane32_swap_b32_e32 v101, v100
	v_add_co_u32_e64 v102, s[42:43], s15, v102
	s_nop 1
	v_addc_co_u32_e64 v103, s[42:43], 0, v103, s[42:43]
	global_store_dwordx2 v[102:103], v[104:105], off offset:128
	s_and_saveexec_b64 s[4:5], vcc
	s_cbranch_execz .LBB0_1418
	v_lshlrev_b64 v[102:103], 6, v[182:183]
	v_lshl_add_u64 v[102:103], s[46:47], 0, v[102:103]
	v_lshl_add_u64 v[102:103], s[60:61], 2, v[102:103]
	s_lshl_b32 s92, s22, 2
	v_lshl_add_u64 v[102:103], v[102:103], 0, s[92:93]
	s_waitcnt lgkmcnt(0)
	v_add_f32_e32 v100, v100, v101
	global_store_dword v[102:103], v100, off
; __device__ __forceinline__ float bflo(unsigned w) { return __uint_as_float(w << 16); }
; __device__ __forceinline__ float bfhi(unsigned w) { return __uint_as_float(w & 0xffff0000u); }
; __device__ __forceinline__ u32x4 pack8(const f32x4 a, const f32x4 b) { u32x4 w; w.x = cvt_pk_bf16(a[0], a[1]); w.y = cvt_pk_bf16(a[2], a[3]); w.z = cvt_pk_bf16(b[0], b[1]); w.w = cvt_pk_bf16(b[2], b[3]); return w; }
;     __device__ __forceinline__ void operator()(const f32x4 (&acc)[2][2][4][2], const Unit& u, int wr, int wc, int fr, int fq) const {
;     ...
;             if ((q & 1) == 0 && q + 2 < 8) {
; #pragma unroll
;                 for (int h2 = 0; h2 < 2; ++h2)
; #pragma unroll
;                     for (int bj = 0; bj < 2; ++bj) { const int qn = q + 2 + h2; xnxt[h2][bj] = *(const u32x4*)(X + (size_t)(row0 + (qn >> 2) * HALF + (qn & 3) * 16) * 1024 + col0 + bj * HALF); } }
; #pragma unroll
;                 for (int bj = 0; bj < 2; ++bj) { bf16_t* p = X + (size_t)row * 1024 + col0 + bj * HALF; const u32x4 xv = xcur[q & 1][bj];
;                     f32x4 a = acc[ai][bj][m][0] * scale, b = acc[ai][bj][m][1] * scale;
;                     a[0] += bflo(xv.x); a[1] += bfhi(xv.x); a[2] += bflo(xv.y); a[3] += bfhi(xv.y); b[0] += bflo(xv.z); b[1] += bfhi(xv.z); b[2] += bflo(xv.w); b[3] += bfhi(xv.w);
;                     const u32x4 w = pack8(a, b); *(u32x4*)p = w;
;                     if constexpr (WX8) { unsigned q0 = 0u, q1 = 0u; q0 = __builtin_amdgcn_cvt_pk_fp8_f32(bflo(w.x), bfhi(w.x), q0, false); q0 = __builtin_amdgcn_cvt_pk_fp8_f32(bflo(w.y), bfhi(w.y), q0, true); q1 = __builtin_amdgcn_cvt_pk_fp8_f32(bflo(w.z), bfhi(w.z), q1, false); q1 = __builtin_amdgcn_cvt_pk_fp8_f32(bflo(w.w), bfhi(w.w), q1, true);
;                         *(u32x2*)((unsigned char*)X + (WS_X8 - WS_X) + (size_t)row * 1024 + col0 + bj * HALF) = (u32x2){q0, q1}; }
;                     s += (bflo(w.x) * bflo(w.x) + bfhi(w.x) * bfhi(w.x)) + (bflo(w.y) * bflo(w.y) + bfhi(w.y) * bfhi(w.y)) + (bflo(w.z) * bflo(w.z) + bfhi(w.z) * bfhi(w.z)) + (bflo(w.w) * bflo(w.w) + bfhi(w.w) * bfhi(w.w)); }
;                 s += __shfl_xor(s, 16); s += __shfl_xor(s, 32);
;                 if (fq == 0) ssn[(size_t)row * 16 + u.pn * 4 + wc] = s;
.LBB0_1418:
	s_or_b64 exec, exec, s[4:5]
	v_add_u32_e32 v118, 0x80, v172
	v_ashrrev_i32_e32 v119, 31, v118
	v_add_u32_e32 v116, 0x90, v172
	v_lshlrev_b64 v[122:123], 11, v[118:119]
	v_ashrrev_i32_e32 v117, 31, v116
	s_waitcnt lgkmcnt(0)
	v_lshl_add_u64 v[100:101], v[174:175], 0, v[122:123]
	v_lshlrev_b64 v[120:121], 11, v[116:117]
	global_load_dwordx4 v[112:115], v[100:101], off
	global_load_dwordx4 v[108:111], v[100:101], off offset:256
	v_lshl_add_u64 v[100:101], v[174:175], 0, v[120:121]
	global_load_dwordx4 v[104:107], v[100:101], off
	s_nop 0
	global_load_dwordx4 v[100:103], v[100:101], off offset:256
	v_lshlrev_b32_e32 v146, 16, v136
	v_and_b32_e32 v136, 0xffff0000, v136
	v_add_f32_e32 v97, v97, v136
	v_lshlrev_b32_e32 v136, 16, v137
	v_add_f32_e32 v98, v98, v136
	v_and_b32_e32 v136, 0xffff0000, v137
	v_add_f32_e32 v99, v99, v136
	v_lshlrev_b32_e32 v136, 16, v138
	v_add_f32_e32 v136, v92, v136
	v_and_b32_e32 v92, 0xffff0000, v138
	v_add_f32_e32 v137, v93, v92
	v_lshlrev_b32_e32 v92, 16, v139
	v_add_f32_e32 v138, v94, v92
	v_and_b32_e32 v92, 0xffff0000, v139
	v_add_f32_e32 v96, v96, v146
	v_add_f32_e32 v95, v95, v92
	v_cvt_pk_bf16_f32 v92, v96, v97
	v_cvt_pk_bf16_f32 v93, v98, v99
	v_cvt_pk_bf16_f32 v94, v136, v137
	v_cvt_pk_bf16_f32 v95, v138, v95
	v_mov_b32_e32 v96, v3
	v_lshlrev_b32_e32 v98, 16, v92
	v_and_b32_e32 v99, 0xffff0000, v92
	v_lshlrev_b32_e32 v138, 16, v94
	v_and_b32_e32 v139, 0xffff0000, v94
	v_mov_b32_e32 v97, v3
	v_cvt_pk_fp8_f32 v96, v98, v99
	v_cvt_pk_fp8_f32 v97, v138, v139
	v_lshlrev_b32_e32 v136, 16, v93
	v_and_b32_e32 v137, 0xffff0000, v93
	v_lshlrev_b32_e32 v146, 16, v95
	v_and_b32_e32 v147, 0xffff0000, v95
	v_lshl_add_u64 v[142:143], s[44:45], 0, v[184:185]
	v_cvt_pk_fp8_f32 v96, v136, v137 op_sel:[0,0,1]
	v_cvt_pk_fp8_f32 v97, v146, v147 op_sel:[0,0,1]
	v_lshlrev_b64 v[140:141], 10, v[180:181]
	v_lshl_add_u64 v[144:145], v[170:171], 1, v[142:143]
	global_store_dwordx4 v[144:145], v[92:95], off
	s_nop 1
	v_lshl_add_u64 v[92:93], s[48:49], 0, v[140:141]
	v_lshl_add_u64 v[92:93], v[92:93], 0, v[170:171]
	global_store_dwordx2 v[92:93], v[96:97], off
	v_mul_f32_e32 v92, v99, v99
	v_mul_f32_e32 v93, v137, v137
	v_fmac_f32_e32 v92, v98, v98
	v_fmac_f32_e32 v93, v136, v136
	v_add_f32_e32 v92, v92, v93
	v_mul_f32_e32 v93, v139, v139
	v_fmac_f32_e32 v93, v138, v138
	v_add_f32_e32 v92, v92, v93
	v_mul_f32_e32 v93, v147, v147
	v_fmac_f32_e32 v93, v146, v146
	v_add_f32_e32 v92, v92, v93
	v_lshlrev_b32_e32 v93, 16, v132
	v_add_f32_e32 v88, v88, v93
	v_and_b32_e32 v93, 0xffff0000, v132
	v_add_f32_e32 v89, v89, v93
	v_lshlrev_b32_e32 v93, 16, v133
	v_add_f32_e32 v90, v90, v93
	v_and_b32_e32 v93, 0xffff0000, v133
	v_add_f32_e32 v91, v91, v93
	v_lshlrev_b32_e32 v93, 16, v134
	v_add_f32_e32 v93, v84, v93
	v_and_b32_e32 v84, 0xffff0000, v134
	v_add_f32_e32 v94, v85, v84
	v_lshlrev_b32_e32 v84, 16, v135
	v_add_f32_e32 v95, v86, v84
	v_and_b32_e32 v84, 0xffff0000, v135
	v_add_f32_e32 v87, v87, v84
	v_cvt_pk_bf16_f32 v84, v88, v89
	v_cvt_pk_bf16_f32 v85, v90, v91
	v_cvt_pk_bf16_f32 v86, v93, v94
	v_cvt_pk_bf16_f32 v87, v95, v87
	global_store_dwordx4 v[144:145], v[84:87], off offset:256
	v_lshlrev_b32_e32 v90, 16, v84
	v_mov_b32_e32 v88, v3
	v_and_b32_e32 v84, 0xffff0000, v84
	v_cvt_pk_fp8_f32 v88, v90, v84
	v_lshlrev_b32_e32 v91, 16, v85
	v_and_b32_e32 v85, 0xffff0000, v85
	v_mul_f32_e32 v84, v84, v84
	v_cvt_pk_fp8_f32 v88, v91, v85 op_sel:[0,0,1]
	v_mul_f32_e32 v85, v85, v85
	v_lshlrev_b32_e32 v93, 16, v86
	v_and_b32_e32 v86, 0xffff0000, v86
	v_fmac_f32_e32 v84, v90, v90
	v_fmac_f32_e32 v85, v91, v91
	v_add_f32_e32 v84, v84, v85
	v_mul_f32_e32 v85, v86, v86
	v_lshlrev_b32_e32 v94, 16, v87
	v_and_b32_e32 v87, 0xffff0000, v87
	v_fmac_f32_e32 v85, v93, v93
	v_add_f32_e32 v84, v84, v85
	v_mul_f32_e32 v85, v87, v87
	v_fmac_f32_e32 v85, v94, v94
	v_add_f32_e32 v84, v84, v85
	v_add_f32_e32 v90, v92, v84
	v_mov_b32_e32 v89, v3
	v_mov_b32_e32 v91, v90
	s_nop 1
	v_permlane16_swap_b32_e32 v91, v90
	v_cvt_pk_fp8_f32 v89, v93, v86
	v_sub_co_u32_e64 v84, s[42:43], 0, v140
	v_cvt_pk_fp8_f32 v89, v94, v87 op_sel:[0,0,1]
	s_nop 0
	v_subb_co_u32_e64 v85, s[42:43], 0, v141, s[42:43]
	v_lshl_add_u64 v[84:85], v[142:143], 0, v[84:85]
	v_lshl_add_u64 v[86:87], v[84:85], 0, v[170:171]
	s_waitcnt lgkmcnt(0)
	v_add_f32_e32 v84, v90, v91
	v_mov_b32_e32 v85, v84
	s_nop 1
	v_permlane32_swap_b32_e32 v85, v84
	v_add_co_u32_e64 v86, s[42:43], s15, v86
	s_nop 1
	v_addc_co_u32_e64 v87, s[42:43], 0, v87, s[42:43]
	global_store_dwordx2 v[86:87], v[88:89], off offset:128
	s_and_saveexec_b64 s[4:5], vcc
	s_cbranch_execz .LBB0_1420
	v_lshlrev_b64 v[86:87], 6, v[180:181]
	v_lshl_add_u64 v[86:87], s[46:47], 0, v[86:87]
	v_lshl_add_u64 v[86:87], s[60:61], 2, v[86:87]
	s_lshl_b32 s92, s22, 2
	v_lshl_add_u64 v[86:87], v[86:87], 0, s[92:93]
	s_waitcnt lgkmcnt(0)
	v_add_f32_e32 v84, v84, v85
	global_store_dword v[86:87], v84, off
; __device__ __forceinline__ float bflo(unsigned w) { return __uint_as_float(w << 16); }
; __device__ __forceinline__ float bfhi(unsigned w) { return __uint_as_float(w & 0xffff0000u); }
; __device__ __forceinline__ u32x4 pack8(const f32x4 a, const f32x4 b) { u32x4 w; w.x = cvt_pk_bf16(a[0], a[1]); w.y = cvt_pk_bf16(a[2], a[3]); w.z = cvt_pk_bf16(b[0], b[1]); w.w = cvt_pk_bf16(b[2], b[3]); return w; }
;     __device__ __forceinline__ void operator()(const f32x4 (&acc)[2][2][4][2], const Unit& u, int wr, int wc, int fr, int fq) const {
;     ...
;             if ((q & 1) == 0 && q + 2 < 8) {
; #pragma unroll
;                 for (int h2 = 0; h2 < 2; ++h2)
; #pragma unroll
;                     for (int bj = 0; bj < 2; ++bj) { const int qn = q + 2 + h2; xnxt[h2][bj] = *(const u32x4*)(X + (size_t)(row0 + (qn >> 2) * HALF + (qn & 3) * 16) * 1024 + col0 + bj * HALF); } }
; #pragma unroll
;                 for (int bj = 0; bj < 2; ++bj) { bf16_t* p = X + (size_t)row * 1024 + col0 + bj * HALF; const u32x4 xv = xcur[q & 1][bj];
;                     f32x4 a = acc[ai][bj][m][0] * scale, b = acc[ai][bj][m][1] * scale;
;                     a[0] += bflo(xv.x); a[1] += bfhi(xv.x); a[2] += bflo(xv.y); a[3] += bfhi(xv.y); b[0] += bflo(xv.z); b[1] += bfhi(xv.z); b[2] += bflo(xv.w); b[3] += bfhi(xv.w);
;                     const u32x4 w = pack8(a, b); *(u32x4*)p = w;
;                     if constexpr (WX8) { unsigned q0 = 0u, q1 = 0u; q0 = __builtin_amdgcn_cvt_pk_fp8_f32(bflo(w.x), bfhi(w.x), q0, false); q0 = __builtin_amdgcn_cvt_pk_fp8_f32(bflo(w.y), bfhi(w.y), q0, true); q1 = __builtin_amdgcn_cvt_pk_fp8_f32(bflo(w.z), bfhi(w.z), q1, false); q1 = __builtin_amdgcn_cvt_pk_fp8_f32(bflo(w.w), bfhi(w.w), q1, true);
;                         *(u32x2*)((unsigned char*)X + (WS_X8 - WS_X) + (size_t)row * 1024 + col0 + bj * HALF) = (u32x2){q0, q1}; }
;                     s += (bflo(w.x) * bflo(w.x) + bfhi(w.x) * bfhi(w.x)) + (bflo(w.y) * bflo(w.y) + bfhi(w.y) * bfhi(w.y)) + (bflo(w.z) * bflo(w.z) + bfhi(w.z) * bfhi(w.z)) + (bflo(w.w) * bflo(w.w) + bfhi(w.w) * bfhi(w.w)); }
;                 s += __shfl_xor(s, 16); s += __shfl_xor(s, 32);
;                 if (fq == 0) ssn[(size_t)row * 16 + u.pn * 4 + wc] = s;
.LBB0_1420:
	s_or_b64 exec, exec, s[4:5]
	v_lshlrev_b32_e32 v90, 16, v128
	v_add_f32_e32 v80, v80, v90
	v_and_b32_e32 v90, 0xffff0000, v128
	v_add_f32_e32 v81, v81, v90
	v_lshlrev_b32_e32 v90, 16, v129
	v_add_f32_e32 v82, v82, v90
	v_and_b32_e32 v90, 0xffff0000, v129
	v_add_f32_e32 v83, v83, v90
	v_lshlrev_b32_e32 v90, 16, v130
	v_add_f32_e32 v90, v76, v90
	v_and_b32_e32 v76, 0xffff0000, v130
	v_add_f32_e32 v91, v77, v76
	v_lshlrev_b32_e32 v76, 16, v131
	v_add_f32_e32 v92, v78, v76
	v_and_b32_e32 v76, 0xffff0000, v131
	v_add_f32_e32 v79, v79, v76
	v_cvt_pk_bf16_f32 v76, v80, v81
	v_cvt_pk_bf16_f32 v77, v82, v83
	v_cvt_pk_bf16_f32 v78, v90, v91
	v_cvt_pk_bf16_f32 v79, v92, v79
	v_mov_b32_e32 v80, v3
	v_lshlrev_b32_e32 v82, 16, v76
	v_and_b32_e32 v83, 0xffff0000, v76
	v_lshlrev_b32_e32 v92, 16, v78
	v_and_b32_e32 v93, 0xffff0000, v78
	v_mov_b32_e32 v81, v3
	v_cvt_pk_fp8_f32 v80, v82, v83
	v_cvt_pk_fp8_f32 v81, v92, v93
	v_lshlrev_b32_e32 v90, 16, v77
	v_and_b32_e32 v91, 0xffff0000, v77
	v_lshlrev_b32_e32 v94, 16, v79
	v_and_b32_e32 v95, 0xffff0000, v79
	v_lshl_add_u64 v[86:87], s[44:45], 0, v[178:179]
	v_cvt_pk_fp8_f32 v80, v90, v91 op_sel:[0,0,1]
	v_cvt_pk_fp8_f32 v81, v94, v95 op_sel:[0,0,1]
	s_waitcnt lgkmcnt(0)
	v_lshlrev_b64 v[84:85], 10, v[176:177]
	v_lshl_add_u64 v[88:89], v[170:171], 1, v[86:87]
	global_store_dwordx4 v[88:89], v[76:79], off
	s_nop 1
	v_lshl_add_u64 v[76:77], s[48:49], 0, v[84:85]
	v_lshl_add_u64 v[76:77], v[76:77], 0, v[170:171]
	global_store_dwordx2 v[76:77], v[80:81], off
	v_mul_f32_e32 v76, v83, v83
	v_mul_f32_e32 v77, v91, v91
	v_fmac_f32_e32 v76, v82, v82
	v_fmac_f32_e32 v77, v90, v90
	v_add_f32_e32 v76, v76, v77
	v_mul_f32_e32 v77, v93, v93
	v_fmac_f32_e32 v77, v92, v92
	v_add_f32_e32 v76, v76, v77
	v_mul_f32_e32 v77, v95, v95
	v_fmac_f32_e32 v77, v94, v94
	v_add_f32_e32 v76, v76, v77
	v_lshlrev_b32_e32 v77, 16, v124
	v_add_f32_e32 v72, v72, v77
	v_and_b32_e32 v77, 0xffff0000, v124
	v_add_f32_e32 v73, v73, v77
	v_lshlrev_b32_e32 v77, 16, v125
	v_add_f32_e32 v74, v74, v77
	v_and_b32_e32 v77, 0xffff0000, v125
	v_add_f32_e32 v75, v75, v77
	v_lshlrev_b32_e32 v77, 16, v126
	v_add_f32_e32 v77, v68, v77
	v_and_b32_e32 v68, 0xffff0000, v126
	v_add_f32_e32 v78, v69, v68
	v_lshlrev_b32_e32 v68, 16, v127
	v_add_f32_e32 v79, v70, v68
	v_and_b32_e32 v68, 0xffff0000, v127
	v_add_f32_e32 v71, v71, v68
	v_cvt_pk_bf16_f32 v68, v72, v73
	v_cvt_pk_bf16_f32 v69, v74, v75
	v_cvt_pk_bf16_f32 v70, v77, v78
	v_cvt_pk_bf16_f32 v71, v79, v71
	global_store_dwordx4 v[88:89], v[68:71], off offset:256
	v_lshlrev_b32_e32 v74, 16, v68
	v_mov_b32_e32 v72, v3
	v_and_b32_e32 v68, 0xffff0000, v68
	v_cvt_pk_fp8_f32 v72, v74, v68
	v_lshlrev_b32_e32 v75, 16, v69
	v_and_b32_e32 v69, 0xffff0000, v69
	v_mul_f32_e32 v68, v68, v68
	v_cvt_pk_fp8_f32 v72, v75, v69 op_sel:[0,0,1]
	v_mul_f32_e32 v69, v69, v69
	v_lshlrev_b32_e32 v77, 16, v70
	v_and_b32_e32 v70, 0xffff0000, v70
	v_fmac_f32_e32 v68, v74, v74
	v_fmac_f32_e32 v69, v75, v75
	v_add_f32_e32 v68, v68, v69
	v_mul_f32_e32 v69, v70, v70
	v_lshlrev_b32_e32 v78, 16, v71
	v_and_b32_e32 v71, 0xffff0000, v71
	v_fmac_f32_e32 v69, v77, v77
	v_add_f32_e32 v68, v68, v69
	v_mul_f32_e32 v69, v71, v71
	v_fmac_f32_e32 v69, v78, v78
	v_add_f32_e32 v68, v68, v69
	v_add_f32_e32 v74, v76, v68
	v_mov_b32_e32 v73, v3
	v_mov_b32_e32 v75, v74
	s_nop 1
	v_permlane16_swap_b32_e32 v75, v74
	v_cvt_pk_fp8_f32 v73, v77, v70
	v_sub_co_u32_e64 v68, s[42:43], 0, v84
	v_cvt_pk_fp8_f32 v73, v78, v71 op_sel:[0,0,1]
	s_nop 0
	v_subb_co_u32_e64 v69, s[42:43], 0, v85, s[42:43]
	v_lshl_add_u64 v[68:69], v[86:87], 0, v[68:69]
	v_lshl_add_u64 v[70:71], v[68:69], 0, v[170:171]
	s_waitcnt lgkmcnt(0)
	v_add_f32_e32 v68, v74, v75
	v_mov_b32_e32 v69, v68
	s_nop 1
	v_permlane32_swap_b32_e32 v69, v68
	v_add_co_u32_e64 v70, s[42:43], s15, v70
	s_nop 1
	v_addc_co_u32_e64 v71, s[42:43], 0, v71, s[42:43]
	global_store_dwordx2 v[70:71], v[72:73], off offset:128
	s_and_saveexec_b64 s[4:5], vcc
	s_cbranch_execz .LBB0_1422
	v_lshlrev_b64 v[70:71], 6, v[176:177]
	v_lshl_add_u64 v[70:71], s[46:47], 0, v[70:71]
	v_lshl_add_u64 v[70:71], s[60:61], 2, v[70:71]
	s_lshl_b32 s92, s22, 2
	v_lshl_add_u64 v[70:71], v[70:71], 0, s[92:93]
	s_waitcnt lgkmcnt(0)
	v_add_f32_e32 v68, v68, v69
	global_store_dword v[70:71], v68, off
; __device__ __forceinline__ float bflo(unsigned w) { return __uint_as_float(w << 16); }
; __device__ __forceinline__ float bfhi(unsigned w) { return __uint_as_float(w & 0xffff0000u); }
; __device__ __forceinline__ u32x4 pack8(const f32x4 a, const f32x4 b) { u32x4 w; w.x = cvt_pk_bf16(a[0], a[1]); w.y = cvt_pk_bf16(a[2], a[3]); w.z = cvt_pk_bf16(b[0], b[1]); w.w = cvt_pk_bf16(b[2], b[3]); return w; }
;     __device__ __forceinline__ void operator()(const f32x4 (&acc)[2][2][4][2], const Unit& u, int wr, int wc, int fr, int fq) const {
;     ...
;             if ((q & 1) == 0 && q + 2 < 8) {
; #pragma unroll
;                 for (int h2 = 0; h2 < 2; ++h2)
; #pragma unroll
;                     for (int bj = 0; bj < 2; ++bj) { const int qn = q + 2 + h2; xnxt[h2][bj] = *(const u32x4*)(X + (size_t)(row0 + (qn >> 2) * HALF + (qn & 3) * 16) * 1024 + col0 + bj * HALF); } }
; #pragma unroll
;                 for (int bj = 0; bj < 2; ++bj) { bf16_t* p = X + (size_t)row * 1024 + col0 + bj * HALF; const u32x4 xv = xcur[q & 1][bj];
;                     f32x4 a = acc[ai][bj][m][0] * scale, b = acc[ai][bj][m][1] * scale;
;                     a[0] += bflo(xv.x); a[1] += bfhi(xv.x); a[2] += bflo(xv.y); a[3] += bfhi(xv.y); b[0] += bflo(xv.z); b[1] += bfhi(xv.z); b[2] += bflo(xv.w); b[3] += bfhi(xv.w);
;                     const u32x4 w = pack8(a, b); *(u32x4*)p = w;
;                     if constexpr (WX8) { unsigned q0 = 0u, q1 = 0u; q0 = __builtin_amdgcn_cvt_pk_fp8_f32(bflo(w.x), bfhi(w.x), q0, false); q0 = __builtin_amdgcn_cvt_pk_fp8_f32(bflo(w.y), bfhi(w.y), q0, true); q1 = __builtin_amdgcn_cvt_pk_fp8_f32(bflo(w.z), bfhi(w.z), q1, false); q1 = __builtin_amdgcn_cvt_pk_fp8_f32(bflo(w.w), bfhi(w.w), q1, true);
;                         *(u32x2*)((unsigned char*)X + (WS_X8 - WS_X) + (size_t)row * 1024 + col0 + bj * HALF) = (u32x2){q0, q1}; }
;                     s += (bflo(w.x) * bflo(w.x) + bfhi(w.x) * bfhi(w.x)) + (bflo(w.y) * bflo(w.y) + bfhi(w.y) * bfhi(w.y)) + (bflo(w.z) * bflo(w.z) + bfhi(w.z) * bfhi(w.z)) + (bflo(w.w) * bflo(w.w) + bfhi(w.w) * bfhi(w.w)); }
;                 s += __shfl_xor(s, 16); s += __shfl_xor(s, 32);
;                 if (fq == 0) ssn[(size_t)row * 16 + u.pn * 4 + wc] = s;
.LBB0_1422:
	s_or_b64 exec, exec, s[4:5]
	v_add_u32_e32 v86, 0xa0, v172
	v_ashrrev_i32_e32 v87, 31, v86
	v_add_u32_e32 v84, 0xb0, v172
	v_lshlrev_b64 v[90:91], 11, v[86:87]
	v_ashrrev_i32_e32 v85, 31, v84
	s_waitcnt lgkmcnt(0)
	v_lshl_add_u64 v[68:69], v[174:175], 0, v[90:91]
	v_lshlrev_b64 v[88:89], 11, v[84:85]
	global_load_dwordx4 v[80:83], v[68:69], off
	global_load_dwordx4 v[76:79], v[68:69], off offset:256
	v_lshl_add_u64 v[68:69], v[174:175], 0, v[88:89]
	global_load_dwordx4 v[72:75], v[68:69], off
	s_nop 0
	global_load_dwordx4 v[68:71], v[68:69], off offset:256
	s_waitcnt vmcnt(15)
	v_lshlrev_b32_e32 v98, 16, v112
	v_add_f32_e32 v64, v64, v98
	v_and_b32_e32 v98, 0xffff0000, v112
	v_add_f32_e32 v65, v65, v98
	v_lshlrev_b32_e32 v98, 16, v113
	v_add_f32_e32 v66, v66, v98
	v_and_b32_e32 v98, 0xffff0000, v113
	v_add_f32_e32 v67, v67, v98
	v_lshlrev_b32_e32 v98, 16, v114
	v_add_f32_e32 v98, v60, v98
	v_and_b32_e32 v60, 0xffff0000, v114
	v_add_f32_e32 v99, v61, v60
	v_lshlrev_b32_e32 v60, 16, v115
	v_add_f32_e32 v112, v62, v60
	v_and_b32_e32 v60, 0xffff0000, v115
	v_add_f32_e32 v63, v63, v60
	v_cvt_pk_bf16_f32 v60, v64, v65
	v_cvt_pk_bf16_f32 v61, v66, v67
	v_cvt_pk_bf16_f32 v62, v98, v99
	v_cvt_pk_bf16_f32 v63, v112, v63
	v_mov_b32_e32 v64, v3
	v_lshlrev_b32_e32 v66, 16, v60
	v_and_b32_e32 v67, 0xffff0000, v60
	v_lshlrev_b32_e32 v112, 16, v62
	v_and_b32_e32 v113, 0xffff0000, v62
	v_mov_b32_e32 v65, v3
	v_cvt_pk_fp8_f32 v64, v66, v67
	v_cvt_pk_fp8_f32 v65, v112, v113
	v_lshlrev_b32_e32 v98, 16, v61
	v_and_b32_e32 v99, 0xffff0000, v61
	v_lshlrev_b32_e32 v114, 16, v63
	v_and_b32_e32 v115, 0xffff0000, v63
	v_lshl_add_u64 v[94:95], s[44:45], 0, v[122:123]
	v_cvt_pk_fp8_f32 v64, v98, v99 op_sel:[0,0,1]
	v_cvt_pk_fp8_f32 v65, v114, v115 op_sel:[0,0,1]
	v_lshlrev_b64 v[92:93], 10, v[118:119]
	v_lshl_add_u64 v[96:97], v[170:171], 1, v[94:95]
	global_store_dwordx4 v[96:97], v[60:63], off
	s_nop 1
	v_lshl_add_u64 v[60:61], s[48:49], 0, v[92:93]
	v_lshl_add_u64 v[60:61], v[60:61], 0, v[170:171]
	global_store_dwordx2 v[60:61], v[64:65], off
	v_mul_f32_e32 v60, v67, v67
	v_mul_f32_e32 v61, v99, v99
	v_fmac_f32_e32 v60, v66, v66
	v_fmac_f32_e32 v61, v98, v98
	v_add_f32_e32 v60, v60, v61
	v_mul_f32_e32 v61, v113, v113
	v_fmac_f32_e32 v61, v112, v112
	v_add_f32_e32 v60, v60, v61
	v_mul_f32_e32 v61, v115, v115
	v_fmac_f32_e32 v61, v114, v114
	v_add_f32_e32 v60, v60, v61
	s_waitcnt vmcnt(16)
	v_lshlrev_b32_e32 v61, 16, v108
	v_add_f32_e32 v56, v56, v61
	v_and_b32_e32 v61, 0xffff0000, v108
	v_add_f32_e32 v57, v57, v61
	v_lshlrev_b32_e32 v61, 16, v109
	v_add_f32_e32 v58, v58, v61
	v_and_b32_e32 v61, 0xffff0000, v109
	v_add_f32_e32 v59, v59, v61
	v_lshlrev_b32_e32 v61, 16, v110
	v_add_f32_e32 v61, v52, v61
	v_and_b32_e32 v52, 0xffff0000, v110
	v_add_f32_e32 v62, v53, v52
	v_lshlrev_b32_e32 v52, 16, v111
	v_add_f32_e32 v63, v54, v52
	v_and_b32_e32 v52, 0xffff0000, v111
	v_add_f32_e32 v55, v55, v52
	v_cvt_pk_bf16_f32 v52, v56, v57
	v_cvt_pk_bf16_f32 v53, v58, v59
	v_cvt_pk_bf16_f32 v54, v61, v62
	v_cvt_pk_bf16_f32 v55, v63, v55
	global_store_dwordx4 v[96:97], v[52:55], off offset:256
	v_lshlrev_b32_e32 v58, 16, v52
	v_mov_b32_e32 v56, v3
	v_and_b32_e32 v52, 0xffff0000, v52
	v_cvt_pk_fp8_f32 v56, v58, v52
	v_lshlrev_b32_e32 v59, 16, v53
	v_and_b32_e32 v53, 0xffff0000, v53
	v_mul_f32_e32 v52, v52, v52
	v_cvt_pk_fp8_f32 v56, v59, v53 op_sel:[0,0,1]
	v_mul_f32_e32 v53, v53, v53
	v_lshlrev_b32_e32 v61, 16, v54
	v_and_b32_e32 v54, 0xffff0000, v54
	v_fmac_f32_e32 v52, v58, v58
	v_fmac_f32_e32 v53, v59, v59
	v_add_f32_e32 v52, v52, v53
	v_mul_f32_e32 v53, v54, v54
	v_lshlrev_b32_e32 v62, 16, v55
	v_and_b32_e32 v55, 0xffff0000, v55
	v_fmac_f32_e32 v53, v61, v61
	v_add_f32_e32 v52, v52, v53
	v_mul_f32_e32 v53, v55, v55
	v_fmac_f32_e32 v53, v62, v62
	v_add_f32_e32 v52, v52, v53
	v_add_f32_e32 v58, v60, v52
	v_mov_b32_e32 v57, v3
	v_mov_b32_e32 v59, v58
	s_nop 1
	v_permlane16_swap_b32_e32 v59, v58
	v_cvt_pk_fp8_f32 v57, v61, v54
	v_sub_co_u32_e64 v52, s[42:43], 0, v92
	v_cvt_pk_fp8_f32 v57, v62, v55 op_sel:[0,0,1]
	s_nop 0
	v_subb_co_u32_e64 v53, s[42:43], 0, v93, s[42:43]
	v_lshl_add_u64 v[52:53], v[94:95], 0, v[52:53]
	v_lshl_add_u64 v[54:55], v[52:53], 0, v[170:171]
	s_waitcnt lgkmcnt(0)
	v_add_f32_e32 v52, v58, v59
	v_mov_b32_e32 v53, v52
	s_nop 1
	v_permlane32_swap_b32_e32 v53, v52
	v_add_co_u32_e64 v54, s[42:43], s15, v54
	s_nop 1
	v_addc_co_u32_e64 v55, s[42:43], 0, v55, s[42:43]
	global_store_dwordx2 v[54:55], v[56:57], off offset:128
	s_and_saveexec_b64 s[4:5], vcc
	s_cbranch_execz .LBB0_1424
	v_lshlrev_b64 v[54:55], 6, v[118:119]
	v_lshl_add_u64 v[54:55], s[46:47], 0, v[54:55]
	v_lshl_add_u64 v[54:55], s[60:61], 2, v[54:55]
	s_lshl_b32 s92, s22, 2
	v_lshl_add_u64 v[54:55], v[54:55], 0, s[92:93]
	s_waitcnt lgkmcnt(0)
	v_add_f32_e32 v52, v52, v53
	global_store_dword v[54:55], v52, off
; __device__ __forceinline__ float bflo(unsigned w) { return __uint_as_float(w << 16); }
; __device__ __forceinline__ float bfhi(unsigned w) { return __uint_as_float(w & 0xffff0000u); }
; __device__ __forceinline__ u32x4 pack8(const f32x4 a, const f32x4 b) { u32x4 w; w.x = cvt_pk_bf16(a[0], a[1]); w.y = cvt_pk_bf16(a[2], a[3]); w.z = cvt_pk_bf16(b[0], b[1]); w.w = cvt_pk_bf16(b[2], b[3]); return w; }
;     __device__ __forceinline__ void operator()(const f32x4 (&acc)[2][2][4][2], const Unit& u, int wr, int wc, int fr, int fq) const {
;     ...
;             if ((q & 1) == 0 && q + 2 < 8) {
; #pragma unroll
;                 for (int h2 = 0; h2 < 2; ++h2)
; #pragma unroll
;                     for (int bj = 0; bj < 2; ++bj) { const int qn = q + 2 + h2; xnxt[h2][bj] = *(const u32x4*)(X + (size_t)(row0 + (qn >> 2) * HALF + (qn & 3) * 16) * 1024 + col0 + bj * HALF); } }
; #pragma unroll
;                 for (int bj = 0; bj < 2; ++bj) { bf16_t* p = X + (size_t)row * 1024 + col0 + bj * HALF; const u32x4 xv = xcur[q & 1][bj];
;                     f32x4 a = acc[ai][bj][m][0] * scale, b = acc[ai][bj][m][1] * scale;
;                     a[0] += bflo(xv.x); a[1] += bfhi(xv.x); a[2] += bflo(xv.y); a[3] += bfhi(xv.y); b[0] += bflo(xv.z); b[1] += bfhi(xv.z); b[2] += bflo(xv.w); b[3] += bfhi(xv.w);
;                     const u32x4 w = pack8(a, b); *(u32x4*)p = w;
;                     if constexpr (WX8) { unsigned q0 = 0u, q1 = 0u; q0 = __builtin_amdgcn_cvt_pk_fp8_f32(bflo(w.x), bfhi(w.x), q0, false); q0 = __builtin_amdgcn_cvt_pk_fp8_f32(bflo(w.y), bfhi(w.y), q0, true); q1 = __builtin_amdgcn_cvt_pk_fp8_f32(bflo(w.z), bfhi(w.z), q1, false); q1 = __builtin_amdgcn_cvt_pk_fp8_f32(bflo(w.w), bfhi(w.w), q1, true);
;                         *(u32x2*)((unsigned char*)X + (WS_X8 - WS_X) + (size_t)row * 1024 + col0 + bj * HALF) = (u32x2){q0, q1}; }
;                     s += (bflo(w.x) * bflo(w.x) + bfhi(w.x) * bfhi(w.x)) + (bflo(w.y) * bflo(w.y) + bfhi(w.y) * bfhi(w.y)) + (bflo(w.z) * bflo(w.z) + bfhi(w.z) * bfhi(w.z)) + (bflo(w.w) * bflo(w.w) + bfhi(w.w) * bfhi(w.w)); }
;                 s += __shfl_xor(s, 16); s += __shfl_xor(s, 32);
;                 if (fq == 0) ssn[(size_t)row * 16 + u.pn * 4 + wc] = s;
.LBB0_1424:
	s_or_b64 exec, exec, s[4:5]
	s_waitcnt vmcnt(17)
	v_lshlrev_b32_e32 v58, 16, v104
	v_add_f32_e32 v48, v48, v58
	v_and_b32_e32 v58, 0xffff0000, v104
	v_add_f32_e32 v49, v49, v58
	v_lshlrev_b32_e32 v58, 16, v105
	v_add_f32_e32 v50, v50, v58
	v_and_b32_e32 v58, 0xffff0000, v105
	v_add_f32_e32 v51, v51, v58
	v_lshlrev_b32_e32 v58, 16, v106
	v_add_f32_e32 v58, v44, v58
	v_and_b32_e32 v44, 0xffff0000, v106
	v_add_f32_e32 v59, v45, v44
	v_lshlrev_b32_e32 v44, 16, v107
	v_add_f32_e32 v60, v46, v44
	v_and_b32_e32 v44, 0xffff0000, v107
	v_add_f32_e32 v47, v47, v44
	v_cvt_pk_bf16_f32 v44, v48, v49
	v_cvt_pk_bf16_f32 v45, v50, v51
	v_cvt_pk_bf16_f32 v46, v58, v59
	v_cvt_pk_bf16_f32 v47, v60, v47
	v_mov_b32_e32 v48, v3
	v_lshlrev_b32_e32 v50, 16, v44
	v_and_b32_e32 v51, 0xffff0000, v44
	v_lshlrev_b32_e32 v60, 16, v46
	v_and_b32_e32 v61, 0xffff0000, v46
	v_mov_b32_e32 v49, v3
	v_cvt_pk_fp8_f32 v48, v50, v51
	v_cvt_pk_fp8_f32 v49, v60, v61
	v_lshlrev_b32_e32 v58, 16, v45
	v_and_b32_e32 v59, 0xffff0000, v45
	v_lshlrev_b32_e32 v62, 16, v47
	v_and_b32_e32 v63, 0xffff0000, v47
	v_lshl_add_u64 v[54:55], s[44:45], 0, v[120:121]
	v_cvt_pk_fp8_f32 v48, v58, v59 op_sel:[0,0,1]
	v_cvt_pk_fp8_f32 v49, v62, v63 op_sel:[0,0,1]
	s_waitcnt lgkmcnt(0)
	v_lshlrev_b64 v[52:53], 10, v[116:117]
	v_lshl_add_u64 v[56:57], v[170:171], 1, v[54:55]
	global_store_dwordx4 v[56:57], v[44:47], off
	s_nop 1
	v_lshl_add_u64 v[44:45], s[48:49], 0, v[52:53]
	v_lshl_add_u64 v[44:45], v[44:45], 0, v[170:171]
	global_store_dwordx2 v[44:45], v[48:49], off
	v_mul_f32_e32 v44, v51, v51
	v_mul_f32_e32 v45, v59, v59
	v_fmac_f32_e32 v44, v50, v50
	v_fmac_f32_e32 v45, v58, v58
	v_add_f32_e32 v44, v44, v45
	v_mul_f32_e32 v45, v61, v61
	v_fmac_f32_e32 v45, v60, v60
	v_add_f32_e32 v44, v44, v45
	v_mul_f32_e32 v45, v63, v63
	v_fmac_f32_e32 v45, v62, v62
	v_add_f32_e32 v44, v44, v45
	s_waitcnt vmcnt(18)
	v_lshlrev_b32_e32 v45, 16, v100
	v_add_f32_e32 v40, v40, v45
	v_and_b32_e32 v45, 0xffff0000, v100
	v_add_f32_e32 v41, v41, v45
	v_lshlrev_b32_e32 v45, 16, v101
	v_add_f32_e32 v42, v42, v45
	v_and_b32_e32 v45, 0xffff0000, v101
	v_add_f32_e32 v43, v43, v45
	v_lshlrev_b32_e32 v45, 16, v102
	v_add_f32_e32 v45, v36, v45
	v_and_b32_e32 v36, 0xffff0000, v102
	v_add_f32_e32 v46, v37, v36
	v_lshlrev_b32_e32 v36, 16, v103
	v_add_f32_e32 v47, v38, v36
	v_and_b32_e32 v36, 0xffff0000, v103
	v_add_f32_e32 v39, v39, v36
	v_cvt_pk_bf16_f32 v36, v40, v41
	v_cvt_pk_bf16_f32 v37, v42, v43
	v_cvt_pk_bf16_f32 v38, v45, v46
	v_cvt_pk_bf16_f32 v39, v47, v39
	global_store_dwordx4 v[56:57], v[36:39], off offset:256
	v_lshlrev_b32_e32 v42, 16, v36
	v_mov_b32_e32 v40, v3
	v_and_b32_e32 v36, 0xffff0000, v36
	v_cvt_pk_fp8_f32 v40, v42, v36
	v_lshlrev_b32_e32 v43, 16, v37
	v_and_b32_e32 v37, 0xffff0000, v37
	v_mul_f32_e32 v36, v36, v36
	v_cvt_pk_fp8_f32 v40, v43, v37 op_sel:[0,0,1]
	v_mul_f32_e32 v37, v37, v37
	v_lshlrev_b32_e32 v45, 16, v38
	v_and_b32_e32 v38, 0xffff0000, v38
	v_fmac_f32_e32 v36, v42, v42
	v_fmac_f32_e32 v37, v43, v43
	v_add_f32_e32 v36, v36, v37
	v_mul_f32_e32 v37, v38, v38
	v_lshlrev_b32_e32 v46, 16, v39
	v_and_b32_e32 v39, 0xffff0000, v39
	v_fmac_f32_e32 v37, v45, v45
	v_add_f32_e32 v36, v36, v37
	v_mul_f32_e32 v37, v39, v39
	v_fmac_f32_e32 v37, v46, v46
	v_add_f32_e32 v36, v36, v37
	v_add_f32_e32 v42, v44, v36
	v_mov_b32_e32 v41, v3
	v_mov_b32_e32 v43, v42
	s_nop 1
	v_permlane16_swap_b32_e32 v43, v42
	v_cvt_pk_fp8_f32 v41, v45, v38
	v_sub_co_u32_e64 v36, s[42:43], 0, v52
	v_cvt_pk_fp8_f32 v41, v46, v39 op_sel:[0,0,1]
	s_nop 0
	v_subb_co_u32_e64 v37, s[42:43], 0, v53, s[42:43]
	v_lshl_add_u64 v[36:37], v[54:55], 0, v[36:37]
	v_lshl_add_u64 v[38:39], v[36:37], 0, v[170:171]
	s_waitcnt lgkmcnt(0)
	v_add_f32_e32 v36, v42, v43
	v_mov_b32_e32 v37, v36
	s_nop 1
	v_permlane32_swap_b32_e32 v37, v36
	v_add_co_u32_e64 v38, s[42:43], s15, v38
	s_nop 1
	v_addc_co_u32_e64 v39, s[42:43], 0, v39, s[42:43]
	global_store_dwordx2 v[38:39], v[40:41], off offset:128
	s_and_saveexec_b64 s[4:5], vcc
	s_cbranch_execz .LBB0_1426
	v_lshlrev_b64 v[38:39], 6, v[116:117]
	v_lshl_add_u64 v[38:39], s[46:47], 0, v[38:39]
	v_lshl_add_u64 v[38:39], s[60:61], 2, v[38:39]
	s_lshl_b32 s92, s22, 2
	v_lshl_add_u64 v[38:39], v[38:39], 0, s[92:93]
	s_waitcnt lgkmcnt(0)
	v_add_f32_e32 v36, v36, v37
	global_store_dword v[38:39], v36, off
; __device__ __forceinline__ float bflo(unsigned w) { return __uint_as_float(w << 16); }
; __device__ __forceinline__ float bfhi(unsigned w) { return __uint_as_float(w & 0xffff0000u); }
; __device__ __forceinline__ u32x4 pack8(const f32x4 a, const f32x4 b) { u32x4 w; w.x = cvt_pk_bf16(a[0], a[1]); w.y = cvt_pk_bf16(a[2], a[3]); w.z = cvt_pk_bf16(b[0], b[1]); w.w = cvt_pk_bf16(b[2], b[3]); return w; }
;     __device__ __forceinline__ void operator()(const f32x4 (&acc)[2][2][4][2], const Unit& u, int wr, int wc, int fr, int fq) const {
;     ...
;             if ((q & 1) == 0 && q + 2 < 8) {
; #pragma unroll
;                 for (int h2 = 0; h2 < 2; ++h2)
; #pragma unroll
;                     for (int bj = 0; bj < 2; ++bj) { const int qn = q + 2 + h2; xnxt[h2][bj] = *(const u32x4*)(X + (size_t)(row0 + (qn >> 2) * HALF + (qn & 3) * 16) * 1024 + col0 + bj * HALF); } }
; #pragma unroll
;                 for (int bj = 0; bj < 2; ++bj) { bf16_t* p = X + (size_t)row * 1024 + col0 + bj * HALF; const u32x4 xv = xcur[q & 1][bj];
;                     f32x4 a = acc[ai][bj][m][0] * scale, b = acc[ai][bj][m][1] * scale;
;                     a[0] += bflo(xv.x); a[1] += bfhi(xv.x); a[2] += bflo(xv.y); a[3] += bfhi(xv.y); b[0] += bflo(xv.z); b[1] += bfhi(xv.z); b[2] += bflo(xv.w); b[3] += bfhi(xv.w);
;                     const u32x4 w = pack8(a, b); *(u32x4*)p = w;
;                     if constexpr (WX8) { unsigned q0 = 0u, q1 = 0u; q0 = __builtin_amdgcn_cvt_pk_fp8_f32(bflo(w.x), bfhi(w.x), q0, false); q0 = __builtin_amdgcn_cvt_pk_fp8_f32(bflo(w.y), bfhi(w.y), q0, true); q1 = __builtin_amdgcn_cvt_pk_fp8_f32(bflo(w.z), bfhi(w.z), q1, false); q1 = __builtin_amdgcn_cvt_pk_fp8_f32(bflo(w.w), bfhi(w.w), q1, true);
;                         *(u32x2*)((unsigned char*)X + (WS_X8 - WS_X) + (size_t)row * 1024 + col0 + bj * HALF) = (u32x2){q0, q1}; }
;                     s += (bflo(w.x) * bflo(w.x) + bfhi(w.x) * bfhi(w.x)) + (bflo(w.y) * bflo(w.y) + bfhi(w.y) * bfhi(w.y)) + (bflo(w.z) * bflo(w.z) + bfhi(w.z) * bfhi(w.z)) + (bflo(w.w) * bflo(w.w) + bfhi(w.w) * bfhi(w.w)); }
;                 s += __shfl_xor(s, 16); s += __shfl_xor(s, 32);
;                 if (fq == 0) ssn[(size_t)row * 16 + u.pn * 4 + wc] = s;
.LBB0_1426:
	s_or_b64 exec, exec, s[4:5]
	s_waitcnt vmcnt(11)
	v_lshlrev_b32_e32 v42, 16, v80
	v_add_f32_e32 v32, v32, v42
	v_and_b32_e32 v42, 0xffff0000, v80
	v_add_f32_e32 v33, v33, v42
	v_lshlrev_b32_e32 v42, 16, v81
	v_add_f32_e32 v34, v34, v42
	v_and_b32_e32 v42, 0xffff0000, v81
	v_add_f32_e32 v35, v35, v42
	v_lshlrev_b32_e32 v42, 16, v82
	v_add_f32_e32 v42, v28, v42
	v_and_b32_e32 v28, 0xffff0000, v82
	v_add_f32_e32 v43, v29, v28
	v_lshlrev_b32_e32 v28, 16, v83
	v_add_f32_e32 v44, v30, v28
	v_and_b32_e32 v28, 0xffff0000, v83
	v_add_f32_e32 v31, v31, v28
	v_cvt_pk_bf16_f32 v28, v32, v33
	v_cvt_pk_bf16_f32 v29, v34, v35
	v_cvt_pk_bf16_f32 v30, v42, v43
	v_cvt_pk_bf16_f32 v31, v44, v31
	v_mov_b32_e32 v32, v3
	v_lshlrev_b32_e32 v34, 16, v28
	v_and_b32_e32 v35, 0xffff0000, v28
	v_lshlrev_b32_e32 v44, 16, v30
	v_and_b32_e32 v45, 0xffff0000, v30
	v_mov_b32_e32 v33, v3
	v_cvt_pk_fp8_f32 v32, v34, v35
	v_cvt_pk_fp8_f32 v33, v44, v45
	v_lshlrev_b32_e32 v42, 16, v29
	v_and_b32_e32 v43, 0xffff0000, v29
	v_lshlrev_b32_e32 v46, 16, v31
	v_and_b32_e32 v47, 0xffff0000, v31
	v_lshl_add_u64 v[38:39], s[44:45], 0, v[90:91]
	v_cvt_pk_fp8_f32 v32, v42, v43 op_sel:[0,0,1]
	v_cvt_pk_fp8_f32 v33, v46, v47 op_sel:[0,0,1]
	s_waitcnt lgkmcnt(0)
	v_lshlrev_b64 v[36:37], 10, v[86:87]
	v_lshl_add_u64 v[40:41], v[170:171], 1, v[38:39]
	global_store_dwordx4 v[40:41], v[28:31], off
	s_nop 1
	v_lshl_add_u64 v[28:29], s[48:49], 0, v[36:37]
	v_lshl_add_u64 v[28:29], v[28:29], 0, v[170:171]
	global_store_dwordx2 v[28:29], v[32:33], off
	v_mul_f32_e32 v28, v35, v35
	v_mul_f32_e32 v29, v43, v43
	v_fmac_f32_e32 v28, v34, v34
	v_fmac_f32_e32 v29, v42, v42
	v_add_f32_e32 v28, v28, v29
	v_mul_f32_e32 v29, v45, v45
	v_fmac_f32_e32 v29, v44, v44
	v_add_f32_e32 v28, v28, v29
	v_mul_f32_e32 v29, v47, v47
	v_fmac_f32_e32 v29, v46, v46
	v_add_f32_e32 v28, v28, v29
	s_waitcnt vmcnt(12)
	v_lshlrev_b32_e32 v29, 16, v76
	v_add_f32_e32 v24, v24, v29
	v_and_b32_e32 v29, 0xffff0000, v76
	v_add_f32_e32 v25, v25, v29
	v_lshlrev_b32_e32 v29, 16, v77
	v_add_f32_e32 v26, v26, v29
	v_and_b32_e32 v29, 0xffff0000, v77
	v_add_f32_e32 v27, v27, v29
	v_lshlrev_b32_e32 v29, 16, v78
	v_add_f32_e32 v29, v20, v29
	v_and_b32_e32 v20, 0xffff0000, v78
	v_add_f32_e32 v30, v21, v20
	v_lshlrev_b32_e32 v20, 16, v79
	v_add_f32_e32 v31, v22, v20
	v_and_b32_e32 v20, 0xffff0000, v79
	v_add_f32_e32 v23, v23, v20
	v_cvt_pk_bf16_f32 v20, v24, v25
	v_cvt_pk_bf16_f32 v21, v26, v27
	v_cvt_pk_bf16_f32 v22, v29, v30
	v_cvt_pk_bf16_f32 v23, v31, v23
	global_store_dwordx4 v[40:41], v[20:23], off offset:256
	v_lshlrev_b32_e32 v26, 16, v20
	v_mov_b32_e32 v24, v3
	v_and_b32_e32 v20, 0xffff0000, v20
	v_cvt_pk_fp8_f32 v24, v26, v20
	v_lshlrev_b32_e32 v27, 16, v21
	v_and_b32_e32 v21, 0xffff0000, v21
	v_mul_f32_e32 v20, v20, v20
	v_cvt_pk_fp8_f32 v24, v27, v21 op_sel:[0,0,1]
	v_mul_f32_e32 v21, v21, v21
	v_lshlrev_b32_e32 v29, 16, v22
	v_and_b32_e32 v22, 0xffff0000, v22
	v_fmac_f32_e32 v20, v26, v26
	v_fmac_f32_e32 v21, v27, v27
	v_add_f32_e32 v20, v20, v21
	v_mul_f32_e32 v21, v22, v22
	v_lshlrev_b32_e32 v30, 16, v23
	v_and_b32_e32 v23, 0xffff0000, v23
	v_fmac_f32_e32 v21, v29, v29
	v_add_f32_e32 v20, v20, v21
	v_mul_f32_e32 v21, v23, v23
	v_fmac_f32_e32 v21, v30, v30
	v_add_f32_e32 v20, v20, v21
	v_add_f32_e32 v26, v28, v20
	v_mov_b32_e32 v25, v3
	v_mov_b32_e32 v27, v26
	s_nop 1
	v_permlane16_swap_b32_e32 v27, v26
	v_cvt_pk_fp8_f32 v25, v29, v22
	v_sub_co_u32_e64 v20, s[42:43], 0, v36
	v_cvt_pk_fp8_f32 v25, v30, v23 op_sel:[0,0,1]
	s_nop 0
	v_subb_co_u32_e64 v21, s[42:43], 0, v37, s[42:43]
	v_lshl_add_u64 v[20:21], v[38:39], 0, v[20:21]
	v_lshl_add_u64 v[22:23], v[20:21], 0, v[170:171]
	s_waitcnt lgkmcnt(0)
	v_add_f32_e32 v20, v26, v27
	v_mov_b32_e32 v21, v20
	s_nop 1
	v_permlane32_swap_b32_e32 v21, v20
	v_add_co_u32_e64 v22, s[42:43], s15, v22
	s_nop 1
	v_addc_co_u32_e64 v23, s[42:43], 0, v23, s[42:43]
	global_store_dwordx2 v[22:23], v[24:25], off offset:128
	s_and_saveexec_b64 s[4:5], vcc
	s_cbranch_execz .LBB0_1428
	v_lshlrev_b64 v[22:23], 6, v[86:87]
	v_lshl_add_u64 v[22:23], s[46:47], 0, v[22:23]
	v_lshl_add_u64 v[22:23], s[60:61], 2, v[22:23]
	s_lshl_b32 s92, s22, 2
	v_lshl_add_u64 v[22:23], v[22:23], 0, s[92:93]
	s_waitcnt lgkmcnt(0)
	v_add_f32_e32 v20, v20, v21
	global_store_dword v[22:23], v20, off
; __device__ __forceinline__ float bflo(unsigned w) { return __uint_as_float(w << 16); }
; __device__ __forceinline__ float bfhi(unsigned w) { return __uint_as_float(w & 0xffff0000u); }
; __device__ __forceinline__ u32x4 pack8(const f32x4 a, const f32x4 b) { u32x4 w; w.x = cvt_pk_bf16(a[0], a[1]); w.y = cvt_pk_bf16(a[2], a[3]); w.z = cvt_pk_bf16(b[0], b[1]); w.w = cvt_pk_bf16(b[2], b[3]); return w; }
;     __device__ __forceinline__ void operator()(const f32x4 (&acc)[2][2][4][2], const Unit& u, int wr, int wc, int fr, int fq) const {
;     ...
;             if ((q & 1) == 0 && q + 2 < 8) {
; #pragma unroll
;                 for (int h2 = 0; h2 < 2; ++h2)
; #pragma unroll
;                     for (int bj = 0; bj < 2; ++bj) { const int qn = q + 2 + h2; xnxt[h2][bj] = *(const u32x4*)(X + (size_t)(row0 + (qn >> 2) * HALF + (qn & 3) * 16) * 1024 + col0 + bj * HALF); } }
; #pragma unroll
;                 for (int bj = 0; bj < 2; ++bj) { bf16_t* p = X + (size_t)row * 1024 + col0 + bj * HALF; const u32x4 xv = xcur[q & 1][bj];
;                     f32x4 a = acc[ai][bj][m][0] * scale, b = acc[ai][bj][m][1] * scale;
;                     a[0] += bflo(xv.x); a[1] += bfhi(xv.x); a[2] += bflo(xv.y); a[3] += bfhi(xv.y); b[0] += bflo(xv.z); b[1] += bfhi(xv.z); b[2] += bflo(xv.w); b[3] += bfhi(xv.w);
;                     const u32x4 w = pack8(a, b); *(u32x4*)p = w;
;                     if constexpr (WX8) { unsigned q0 = 0u, q1 = 0u; q0 = __builtin_amdgcn_cvt_pk_fp8_f32(bflo(w.x), bfhi(w.x), q0, false); q0 = __builtin_amdgcn_cvt_pk_fp8_f32(bflo(w.y), bfhi(w.y), q0, true); q1 = __builtin_amdgcn_cvt_pk_fp8_f32(bflo(w.z), bfhi(w.z), q1, false); q1 = __builtin_amdgcn_cvt_pk_fp8_f32(bflo(w.w), bfhi(w.w), q1, true);
;                         *(u32x2*)((unsigned char*)X + (WS_X8 - WS_X) + (size_t)row * 1024 + col0 + bj * HALF) = (u32x2){q0, q1}; }
;                     s += (bflo(w.x) * bflo(w.x) + bfhi(w.x) * bfhi(w.x)) + (bflo(w.y) * bflo(w.y) + bfhi(w.y) * bfhi(w.y)) + (bflo(w.z) * bflo(w.z) + bfhi(w.z) * bfhi(w.z)) + (bflo(w.w) * bflo(w.w) + bfhi(w.w) * bfhi(w.w)); }
;                 s += __shfl_xor(s, 16); s += __shfl_xor(s, 32);
;                 if (fq == 0) ssn[(size_t)row * 16 + u.pn * 4 + wc] = s;
.LBB0_1428:
	s_or_b64 exec, exec, s[4:5]
	s_waitcnt vmcnt(13)
	v_lshlrev_b32_e32 v26, 16, v72
	v_add_f32_e32 v16, v16, v26
	v_and_b32_e32 v26, 0xffff0000, v72
	v_add_f32_e32 v17, v17, v26
	v_lshlrev_b32_e32 v26, 16, v73
	v_add_f32_e32 v18, v18, v26
	v_and_b32_e32 v26, 0xffff0000, v73
	v_add_f32_e32 v19, v19, v26
	v_lshlrev_b32_e32 v26, 16, v74
	v_add_f32_e32 v26, v12, v26
	v_and_b32_e32 v12, 0xffff0000, v74
	v_add_f32_e32 v27, v13, v12
	v_lshlrev_b32_e32 v12, 16, v75
	v_add_f32_e32 v28, v14, v12
	v_and_b32_e32 v12, 0xffff0000, v75
	v_add_f32_e32 v15, v15, v12
	v_cvt_pk_bf16_f32 v12, v16, v17
	v_cvt_pk_bf16_f32 v13, v18, v19
	v_cvt_pk_bf16_f32 v14, v26, v27
	v_cvt_pk_bf16_f32 v15, v28, v15
	v_mov_b32_e32 v16, v3
	v_lshlrev_b32_e32 v18, 16, v12
	v_and_b32_e32 v19, 0xffff0000, v12
	v_lshlrev_b32_e32 v28, 16, v14
	v_and_b32_e32 v29, 0xffff0000, v14
	v_mov_b32_e32 v17, v3
	v_cvt_pk_fp8_f32 v16, v18, v19
	v_cvt_pk_fp8_f32 v17, v28, v29
	v_lshlrev_b32_e32 v26, 16, v13
	v_and_b32_e32 v27, 0xffff0000, v13
	v_lshlrev_b32_e32 v30, 16, v15
	v_and_b32_e32 v31, 0xffff0000, v15
	v_lshl_add_u64 v[22:23], s[44:45], 0, v[88:89]
	v_cvt_pk_fp8_f32 v16, v26, v27 op_sel:[0,0,1]
	v_cvt_pk_fp8_f32 v17, v30, v31 op_sel:[0,0,1]
	s_waitcnt lgkmcnt(0)
	v_lshlrev_b64 v[20:21], 10, v[84:85]
	v_lshl_add_u64 v[24:25], v[170:171], 1, v[22:23]
	global_store_dwordx4 v[24:25], v[12:15], off
	s_nop 1
	v_lshl_add_u64 v[12:13], s[48:49], 0, v[20:21]
	v_lshl_add_u64 v[12:13], v[12:13], 0, v[170:171]
	global_store_dwordx2 v[12:13], v[16:17], off
	v_mul_f32_e32 v12, v19, v19
	v_mul_f32_e32 v13, v27, v27
	v_fmac_f32_e32 v12, v18, v18
	v_fmac_f32_e32 v13, v26, v26
	v_add_f32_e32 v12, v12, v13
	v_mul_f32_e32 v13, v29, v29
	v_fmac_f32_e32 v13, v28, v28
	v_add_f32_e32 v12, v12, v13
	v_mul_f32_e32 v13, v31, v31
	v_fmac_f32_e32 v13, v30, v30
	v_add_f32_e32 v12, v12, v13
	s_waitcnt vmcnt(14)
	v_lshlrev_b32_e32 v13, 16, v68
	v_add_f32_e32 v8, v8, v13
	v_and_b32_e32 v13, 0xffff0000, v68
	v_add_f32_e32 v9, v9, v13
	v_lshlrev_b32_e32 v13, 16, v69
	v_add_f32_e32 v10, v10, v13
	v_and_b32_e32 v13, 0xffff0000, v69
	v_add_f32_e32 v11, v11, v13
	v_lshlrev_b32_e32 v13, 16, v70
	v_add_f32_e32 v13, v4, v13
	v_and_b32_e32 v4, 0xffff0000, v70
	v_add_f32_e32 v14, v5, v4
	v_lshlrev_b32_e32 v4, 16, v71
	v_add_f32_e32 v15, v6, v4
	v_and_b32_e32 v4, 0xffff0000, v71
	v_add_f32_e32 v7, v7, v4
	v_cvt_pk_bf16_f32 v4, v8, v9
	v_cvt_pk_bf16_f32 v5, v10, v11
	v_cvt_pk_bf16_f32 v6, v13, v14
	v_cvt_pk_bf16_f32 v7, v15, v7
	global_store_dwordx4 v[24:25], v[4:7], off offset:256
	v_lshlrev_b32_e32 v10, 16, v4
	v_mov_b32_e32 v8, v3
	v_and_b32_e32 v4, 0xffff0000, v4
	v_cvt_pk_fp8_f32 v8, v10, v4
	v_lshlrev_b32_e32 v11, 16, v5
	v_and_b32_e32 v5, 0xffff0000, v5
	v_mul_f32_e32 v4, v4, v4
	v_cvt_pk_fp8_f32 v8, v11, v5 op_sel:[0,0,1]
	v_mul_f32_e32 v5, v5, v5
	v_lshlrev_b32_e32 v13, 16, v6
	v_and_b32_e32 v6, 0xffff0000, v6
	v_fmac_f32_e32 v4, v10, v10
	v_fmac_f32_e32 v5, v11, v11
	v_add_f32_e32 v4, v4, v5
	v_mul_f32_e32 v5, v6, v6
	v_lshlrev_b32_e32 v14, 16, v7
	v_and_b32_e32 v7, 0xffff0000, v7
	v_fmac_f32_e32 v5, v13, v13
	v_add_f32_e32 v4, v4, v5
	v_mul_f32_e32 v5, v7, v7
	v_fmac_f32_e32 v5, v14, v14
	v_add_f32_e32 v4, v4, v5
	v_add_f32_e32 v10, v12, v4
	v_mov_b32_e32 v9, v3
	v_mov_b32_e32 v11, v10
	s_nop 1
	v_permlane16_swap_b32_e32 v11, v10
	v_cvt_pk_fp8_f32 v9, v13, v6
	v_sub_co_u32_e64 v4, s[42:43], 0, v20
	v_cvt_pk_fp8_f32 v9, v14, v7 op_sel:[0,0,1]
	s_nop 0
	v_subb_co_u32_e64 v5, s[42:43], 0, v21, s[42:43]
	v_lshl_add_u64 v[4:5], v[22:23], 0, v[4:5]
	v_lshl_add_u64 v[6:7], v[4:5], 0, v[170:171]
	s_waitcnt lgkmcnt(0)
	v_add_f32_e32 v4, v10, v11
	v_mov_b32_e32 v5, v4
	s_nop 1
	v_permlane32_swap_b32_e32 v5, v4
	v_add_co_u32_e64 v6, s[42:43], s15, v6
	s_nop 1
	v_addc_co_u32_e64 v7, s[42:43], 0, v7, s[42:43]
	global_store_dwordx2 v[6:7], v[8:9], off offset:128
	s_and_saveexec_b64 s[4:5], vcc
	s_cbranch_execz .LBB0_1430
	v_lshlrev_b64 v[6:7], 6, v[84:85]
	v_lshl_add_u64 v[6:7], s[46:47], 0, v[6:7]
	v_lshl_add_u64 v[6:7], s[60:61], 2, v[6:7]
	s_lshl_b32 s92, s22, 2
	v_lshl_add_u64 v[6:7], v[6:7], 0, s[92:93]
	s_waitcnt lgkmcnt(0)
	v_add_f32_e32 v4, v4, v5
	global_store_dword v[6:7], v4, off

; __device__ __forceinline__ u32x4 pack8(const f32x4 a, const f32x4 b) { u32x4 w; w.x = cvt_pk_bf16(a[0], a[1]); w.y = cvt_pk_bf16(a[2], a[3]); w.z = cvt_pk_bf16(b[0], b[1]); w.w = cvt_pk_bf16(b[2], b[3]); return w; }
; __device__ __forceinline__ float rstd_of4(const float* ss, int row, int fq) { const f32x4 a = *(const f32x4*)(ss + (size_t)row * 16 + fq * 4); float s = (a[0] + a[1]) + (a[2] + a[3]);
;     s += __shfl_xor(s, 16); s += __shfl_xor(s, 32); return __builtin_amdgcn_rsqf(s * (1.f / 1024.f) + 1e-6f); }
;     __device__ __forceinline__ void operator()(const f32x4 (&acc)[2][2][4][2], const Unit& u, int wr, int wc, int fr, int fq) const {
;         asm volatile("" : "+v"(fr), "+v"(fq));
;         const int row0 = u.pm * BM + wr * 64 + fr, col0 = u.pn * BM + wc * 32 + fq * 8;
; #pragma unroll
;         for (int ai = 0; ai < 2; ++ai)
; #pragma unroll
;             for (int m = 0; m < 4; ++m) { const int row = row0 + ai * HALF + m * 16; const float rs = rstd_of4(ss, row, fq) * scale;
; #pragma unroll
;                 for (int bj = 0; bj < 2; ++bj) *(u32x4*)(O + (size_t)row * ldc + col0 + bj * HALF) = pack8(acc[ai][bj][m][0] * rs, acc[ai][bj][m][1] * rs); asm volatile("" ::: "memory"); }
.LBB0_1501:
	s_lshl_b32 s4, s66, 8
	v_mov_b32_e32 v5, v182
	v_mov_b32_e32 v4, v1
	s_add_i32 s4, s4, s22
	v_and_b32_e32 v7, 64, v246
	v_add_u32_e32 v6, s4, v4
	s_lshl_b32 s4, s65, 8
	s_or_b32 s4, s4, s23
	v_lshl_add_u32 v4, v5, 3, s4
	v_lshlrev_b32_e32 v8, 2, v5
	v_xor_b32_e32 v5, 16, v246
	v_add_u32_e32 v7, 64, v7
	v_cmp_lt_i32_e32 vcc, v5, v7
	v_ashrrev_i32_e32 v9, 31, v8
	v_lshlrev_b64 v[8:9], 2, v[8:9]
	v_cndmask_b32_e32 v5, v246, v5, vcc
	v_lshlrev_b32_e32 v10, 2, v5
	v_xor_b32_e32 v5, 32, v246
	v_cmp_lt_i32_e32 vcc, v5, v7
	v_ashrrev_i32_e32 v7, 31, v6
	v_lshlrev_b64 v[12:13], 6, v[6:7]
	v_lshl_add_u64 v[12:13], s[44:45], 0, v[12:13]
	v_lshl_add_u64 v[12:13], v[12:13], 0, v[8:9]
	global_load_dwordx4 v[12:15], v[12:13], off
	v_add_u32_e32 v24, 16, v6
	v_ashrrev_i32_e32 v25, 31, v24
	v_lshlrev_b64 v[24:25], 6, v[24:25]
	v_lshl_add_u64 v[24:25], s[44:45], 0, v[24:25]
	v_lshl_add_u64 v[24:25], v[24:25], 0, v[8:9]
	global_load_dwordx4 v[24:27], v[24:25], off
	v_add_u32_e32 v28, 32, v6
	v_ashrrev_i32_e32 v29, 31, v28
	v_lshlrev_b64 v[28:29], 6, v[28:29]
	v_lshl_add_u64 v[28:29], s[44:45], 0, v[28:29]
	v_lshl_add_u64 v[28:29], v[28:29], 0, v[8:9]
	global_load_dwordx4 v[28:31], v[28:29], off
	v_add_u32_e32 v32, 48, v6
	v_ashrrev_i32_e32 v33, 31, v32
	v_lshlrev_b64 v[32:33], 6, v[32:33]
	v_lshl_add_u64 v[32:33], s[44:45], 0, v[32:33]
	v_lshl_add_u64 v[32:33], v[32:33], 0, v[8:9]
	global_load_dwordx4 v[32:35], v[32:33], off
	v_add_u32_e32 v208, 0x80, v6
	v_ashrrev_i32_e32 v209, 31, v208
	v_lshlrev_b64 v[208:209], 6, v[208:209]
	v_lshl_add_u64 v[208:209], s[44:45], 0, v[208:209]
	v_lshl_add_u64 v[208:209], v[208:209], 0, v[8:9]
	global_load_dwordx4 v[208:211], v[208:209], off
	v_add_u32_e32 v212, 0x90, v6
	v_ashrrev_i32_e32 v213, 31, v212
	v_lshlrev_b64 v[212:213], 6, v[212:213]
	v_lshl_add_u64 v[212:213], s[44:45], 0, v[212:213]
	v_lshl_add_u64 v[212:213], v[212:213], 0, v[8:9]
	global_load_dwordx4 v[212:215], v[212:213], off
	v_add_u32_e32 v216, 0xa0, v6
	v_ashrrev_i32_e32 v217, 31, v216
	v_lshlrev_b64 v[216:217], 6, v[216:217]
	v_lshl_add_u64 v[216:217], s[44:45], 0, v[216:217]
	v_lshl_add_u64 v[216:217], v[216:217], 0, v[8:9]
	global_load_dwordx4 v[216:219], v[216:217], off
	v_add_u32_e32 v220, 0xb0, v6
	v_ashrrev_i32_e32 v221, 31, v220
	v_lshlrev_b64 v[220:221], 6, v[220:221]
	v_lshl_add_u64 v[220:221], s[44:45], 0, v[220:221]
	v_lshl_add_u64 v[220:221], v[220:221], 0, v[8:9]
	global_load_dwordx4 v[220:223], v[220:221], off
	v_cndmask_b32_e32 v5, v246, v5, vcc
	v_lshlrev_b32_e32 v11, 2, v5
	v_ashrrev_i32_e32 v5, 31, v4
	v_lshlrev_b64 v[4:5], 1, v[4:5]
	s_mov_b64 s[4:5], -1
	s_andn2_b64 vcc, exec, s[40:41]
	s_waitcnt vmcnt(0)
	v_mov_b32_e32 v16, v13
	v_mov_b32_e32 v17, v14
	v_mov_b32_e32 v13, v15
	v_pk_add_f32 v[12:13], v[16:17], v[12:13]
	s_nop 0
	v_add_f32_e32 v12, v12, v13
	v_mov_b32_e32 v13, v12
	s_nop 1
	v_permlane16_swap_b32_e32 v13, v12
	s_waitcnt lgkmcnt(0)
	v_add_f32_e32 v12, v12, v13
	v_mov_b32_e32 v13, v12
	s_nop 1
	v_permlane32_swap_b32_e32 v13, v12
	s_waitcnt lgkmcnt(0)
	v_add_f32_e32 v12, v12, v13
	v_fmamk_f32 v12, v12, 0x3a800000, v227
	v_rsq_f32_e32 v12, v12
	s_nop 0
	v_mul_f32_e32 v16, 0x3ab8aa3b, v12
	v_pk_mul_f32 v[14:15], v[162:163], v[16:17] op_sel_hi:[1,0]
	v_pk_mul_f32 v[12:13], v[160:161], v[16:17] op_sel_hi:[1,0]
	v_pk_mul_f32 v[18:19], v[158:159], v[16:17] op_sel_hi:[1,0]
	v_pk_mul_f32 v[20:21], v[156:157], v[16:17] op_sel_hi:[1,0]
	v_cvt_pk_bf16_f32 v12, v12, v13
	v_cvt_pk_bf16_f32 v13, v14, v15
	s_nop 0
	v_cvt_pk_bf16_f32 v14, v20, v21
	v_cvt_pk_bf16_f32 v15, v18, v19
	v_lshlrev_b64 v[18:19], 11, v[6:7]
	v_lshl_add_u64 v[18:19], s[42:43], 0, v[18:19]
	v_lshl_add_u64 v[18:19], v[18:19], 0, v[4:5]
	global_store_dwordx4 v[18:19], v[12:15], off
	v_pk_mul_f32 v[20:21], v[150:151], v[16:17] op_sel_hi:[1,0]
	s_nop 0
	v_pk_mul_f32 v[14:15], v[154:155], v[16:17] op_sel_hi:[1,0]
	v_pk_mul_f32 v[12:13], v[152:153], v[16:17] op_sel_hi:[1,0]
	v_pk_mul_f32 v[16:17], v[148:149], v[16:17] op_sel_hi:[1,0]
	v_cvt_pk_bf16_f32 v12, v12, v13
	v_cvt_pk_bf16_f32 v13, v14, v15
	s_nop 0
	v_cvt_pk_bf16_f32 v14, v16, v17
	v_add_u32_e32 v16, 16, v6
	v_ashrrev_i32_e32 v17, 31, v16
	v_cvt_pk_bf16_f32 v15, v20, v21
	global_store_dwordx4 v[18:19], v[12:15], off offset:256
	s_nop 1
	v_lshlrev_b64 v[12:13], 6, v[16:17]
	v_lshl_add_u64 v[12:13], s[44:45], 0, v[12:13]
	v_lshl_add_u64 v[12:13], v[12:13], 0, v[8:9]
	v_mov_b64_e32 v[12:13], v[24:25]
	v_mov_b64_e32 v[14:15], v[26:27]
	v_lshlrev_b64 v[16:17], 11, v[16:17]
	v_lshl_add_u64 v[16:17], s[42:43], 0, v[16:17]
	v_lshl_add_u64 v[16:17], v[16:17], 0, v[4:5]
	v_mov_b32_e32 v18, v13
	v_mov_b32_e32 v19, v14
	v_mov_b32_e32 v13, v15
	v_pk_add_f32 v[12:13], v[18:19], v[12:13]
	s_nop 0
	v_add_f32_e32 v7, v12, v13
	v_mov_b32_e32 v12, v7
	s_nop 1
	v_permlane16_swap_b32_e32 v12, v7
	s_waitcnt lgkmcnt(0)
	v_add_f32_e32 v7, v7, v12
	v_mov_b32_e32 v12, v7
	s_nop 1
	v_permlane32_swap_b32_e32 v12, v7
	s_waitcnt lgkmcnt(0)
; __device__ __forceinline__ u32x4 pack8(const f32x4 a, const f32x4 b) { u32x4 w; w.x = cvt_pk_bf16(a[0], a[1]); w.y = cvt_pk_bf16(a[2], a[3]); w.z = cvt_pk_bf16(b[0], b[1]); w.w = cvt_pk_bf16(b[2], b[3]); return w; }
; __device__ __forceinline__ float rstd_of4(const float* ss, int row, int fq) { const f32x4 a = *(const f32x4*)(ss + (size_t)row * 16 + fq * 4); float s = (a[0] + a[1]) + (a[2] + a[3]);
;     s += __shfl_xor(s, 16); s += __shfl_xor(s, 32); return __builtin_amdgcn_rsqf(s * (1.f / 1024.f) + 1e-6f); }
;     __device__ __forceinline__ void operator()(const f32x4 (&acc)[2][2][4][2], const Unit& u, int wr, int wc, int fr, int fq) const {
;         asm volatile("" : "+v"(fr), "+v"(fq));
;         const int row0 = u.pm * BM + wr * 64 + fr, col0 = u.pn * BM + wc * 32 + fq * 8;
; #pragma unroll
;         for (int ai = 0; ai < 2; ++ai)
; #pragma unroll
;             for (int m = 0; m < 4; ++m) { const int row = row0 + ai * HALF + m * 16; const float rs = rstd_of4(ss, row, fq) * scale;
; #pragma unroll
;                 for (int bj = 0; bj < 2; ++bj) *(u32x4*)(O + (size_t)row * ldc + col0 + bj * HALF) = pack8(acc[ai][bj][m][0] * rs, acc[ai][bj][m][1] * rs); asm volatile("" ::: "memory"); }
	v_add_f32_e32 v7, v7, v12
	v_fmamk_f32 v7, v7, 0x3a800000, v227
	v_rsq_f32_e32 v7, v7
	s_nop 0
	v_mul_f32_e32 v18, 0x3ab8aa3b, v7
	v_pk_mul_f32 v[14:15], v[146:147], v[18:19] op_sel_hi:[1,0]
	v_pk_mul_f32 v[12:13], v[144:145], v[18:19] op_sel_hi:[1,0]
	v_pk_mul_f32 v[20:21], v[142:143], v[18:19] op_sel_hi:[1,0]
	v_pk_mul_f32 v[22:23], v[140:141], v[18:19] op_sel_hi:[1,0]
	v_cvt_pk_bf16_f32 v12, v12, v13
	v_cvt_pk_bf16_f32 v13, v14, v15
	s_nop 0
	v_cvt_pk_bf16_f32 v14, v22, v23
	v_cvt_pk_bf16_f32 v15, v20, v21
	global_store_dwordx4 v[16:17], v[12:15], off
	v_pk_mul_f32 v[20:21], v[134:135], v[18:19] op_sel_hi:[1,0]
	s_nop 0
	v_pk_mul_f32 v[14:15], v[138:139], v[18:19] op_sel_hi:[1,0]
	v_pk_mul_f32 v[12:13], v[136:137], v[18:19] op_sel_hi:[1,0]
	v_pk_mul_f32 v[18:19], v[132:133], v[18:19] op_sel_hi:[1,0]
	v_cvt_pk_bf16_f32 v12, v12, v13
	v_cvt_pk_bf16_f32 v13, v14, v15
	s_nop 0
	v_cvt_pk_bf16_f32 v14, v18, v19
	v_cvt_pk_bf16_f32 v15, v20, v21
	global_store_dwordx4 v[16:17], v[12:15], off offset:256
	v_add_u32_e32 v16, 32, v6
	v_ashrrev_i32_e32 v17, 31, v16
	v_lshlrev_b64 v[12:13], 6, v[16:17]
	v_lshl_add_u64 v[12:13], s[44:45], 0, v[12:13]
	v_lshl_add_u64 v[12:13], v[12:13], 0, v[8:9]
	v_mov_b64_e32 v[12:13], v[28:29]
	v_mov_b64_e32 v[14:15], v[30:31]
	v_lshlrev_b64 v[16:17], 11, v[16:17]
	v_lshl_add_u64 v[16:17], s[42:43], 0, v[16:17]
	v_lshl_add_u64 v[16:17], v[16:17], 0, v[4:5]
	v_mov_b32_e32 v18, v13
	v_mov_b32_e32 v19, v14
	v_mov_b32_e32 v13, v15
	v_pk_add_f32 v[12:13], v[18:19], v[12:13]
	s_nop 0
	v_add_f32_e32 v7, v12, v13
	v_mov_b32_e32 v12, v7
	s_nop 1
	v_permlane16_swap_b32_e32 v12, v7
	s_waitcnt lgkmcnt(0)
	v_add_f32_e32 v7, v7, v12
	v_mov_b32_e32 v12, v7
	s_nop 1
	v_permlane32_swap_b32_e32 v12, v7
	s_waitcnt lgkmcnt(0)
	v_add_f32_e32 v7, v7, v12
	v_fmamk_f32 v7, v7, 0x3a800000, v227
	v_rsq_f32_e32 v7, v7
	s_nop 0
	v_mul_f32_e32 v18, 0x3ab8aa3b, v7
	v_pk_mul_f32 v[14:15], v[130:131], v[18:19] op_sel_hi:[1,0]
	v_pk_mul_f32 v[12:13], v[128:129], v[18:19] op_sel_hi:[1,0]
	v_pk_mul_f32 v[20:21], v[126:127], v[18:19] op_sel_hi:[1,0]
	v_pk_mul_f32 v[22:23], v[124:125], v[18:19] op_sel_hi:[1,0]
	v_cvt_pk_bf16_f32 v12, v12, v13
	v_cvt_pk_bf16_f32 v13, v14, v15
	s_nop 0
	v_cvt_pk_bf16_f32 v14, v22, v23
	v_cvt_pk_bf16_f32 v15, v20, v21
	global_store_dwordx4 v[16:17], v[12:15], off
	v_pk_mul_f32 v[20:21], v[118:119], v[18:19] op_sel_hi:[1,0]
	s_nop 0
	v_pk_mul_f32 v[14:15], v[122:123], v[18:19] op_sel_hi:[1,0]
	v_pk_mul_f32 v[12:13], v[120:121], v[18:19] op_sel_hi:[1,0]
	v_pk_mul_f32 v[18:19], v[116:117], v[18:19] op_sel_hi:[1,0]
	v_cvt_pk_bf16_f32 v12, v12, v13
	v_cvt_pk_bf16_f32 v13, v14, v15
	s_nop 0
	v_cvt_pk_bf16_f32 v14, v18, v19
	v_cvt_pk_bf16_f32 v15, v20, v21
	global_store_dwordx4 v[16:17], v[12:15], off offset:256
	v_add_u32_e32 v16, 48, v6
	v_ashrrev_i32_e32 v17, 31, v16
	v_lshlrev_b64 v[12:13], 6, v[16:17]
	v_lshl_add_u64 v[12:13], s[44:45], 0, v[12:13]
	v_lshl_add_u64 v[12:13], v[12:13], 0, v[8:9]
	v_mov_b64_e32 v[12:13], v[32:33]
	v_mov_b64_e32 v[14:15], v[34:35]
	v_lshlrev_b64 v[16:17], 11, v[16:17]
	v_lshl_add_u64 v[16:17], s[42:43], 0, v[16:17]
	v_lshl_add_u64 v[16:17], v[16:17], 0, v[4:5]
	v_mov_b32_e32 v18, v13
	v_mov_b32_e32 v19, v14
	v_mov_b32_e32 v13, v15
	v_pk_add_f32 v[12:13], v[18:19], v[12:13]
	s_nop 0
	v_add_f32_e32 v7, v12, v13
	v_mov_b32_e32 v12, v7
	s_nop 1
	v_permlane16_swap_b32_e32 v12, v7
	s_waitcnt lgkmcnt(0)
	v_add_f32_e32 v7, v7, v12
	v_mov_b32_e32 v12, v7
	s_nop 1
	v_permlane32_swap_b32_e32 v12, v7
	s_waitcnt lgkmcnt(0)
	v_add_f32_e32 v7, v7, v12
	v_fmamk_f32 v7, v7, 0x3a800000, v227
	v_rsq_f32_e32 v7, v7
	s_nop 0
	v_mul_f32_e32 v18, 0x3ab8aa3b, v7
	v_pk_mul_f32 v[14:15], v[114:115], v[18:19] op_sel_hi:[1,0]
	v_pk_mul_f32 v[12:13], v[112:113], v[18:19] op_sel_hi:[1,0]
	v_pk_mul_f32 v[20:21], v[110:111], v[18:19] op_sel_hi:[1,0]
	v_pk_mul_f32 v[22:23], v[108:109], v[18:19] op_sel_hi:[1,0]
	v_cvt_pk_bf16_f32 v12, v12, v13
	v_cvt_pk_bf16_f32 v13, v14, v15
	s_nop 0
	v_cvt_pk_bf16_f32 v14, v22, v23
	v_cvt_pk_bf16_f32 v15, v20, v21
	global_store_dwordx4 v[16:17], v[12:15], off
	v_pk_mul_f32 v[20:21], v[102:103], v[18:19] op_sel_hi:[1,0]
	s_nop 0
	v_pk_mul_f32 v[14:15], v[106:107], v[18:19] op_sel_hi:[1,0]
	v_pk_mul_f32 v[12:13], v[104:105], v[18:19] op_sel_hi:[1,0]
	v_pk_mul_f32 v[18:19], v[100:101], v[18:19] op_sel_hi:[1,0]
	v_cvt_pk_bf16_f32 v12, v12, v13
	v_cvt_pk_bf16_f32 v13, v14, v15
	s_nop 0
	v_cvt_pk_bf16_f32 v14, v18, v19
	v_cvt_pk_bf16_f32 v15, v20, v21
	global_store_dwordx4 v[16:17], v[12:15], off offset:256
	v_add_u32_e32 v16, 0x80, v6
	v_ashrrev_i32_e32 v17, 31, v16
	v_lshlrev_b64 v[12:13], 6, v[16:17]
	v_lshl_add_u64 v[12:13], s[44:45], 0, v[12:13]
	v_lshl_add_u64 v[12:13], v[12:13], 0, v[8:9]
	v_mov_b64_e32 v[12:13], v[208:209]
	v_mov_b64_e32 v[14:15], v[210:211]
	v_lshlrev_b64 v[16:17], 11, v[16:17]
	v_lshl_add_u64 v[16:17], s[42:43], 0, v[16:17]
	v_lshl_add_u64 v[16:17], v[16:17], 0, v[4:5]
	v_mov_b32_e32 v18, v13
	v_mov_b32_e32 v19, v14
	v_mov_b32_e32 v13, v15
	v_pk_add_f32 v[12:13], v[18:19], v[12:13]
	s_nop 0
	v_add_f32_e32 v7, v12, v13
	v_mov_b32_e32 v12, v7
	s_nop 1
	v_permlane16_swap_b32_e32 v12, v7
	s_waitcnt lgkmcnt(0)
	v_add_f32_e32 v7, v7, v12
	v_mov_b32_e32 v12, v7
	s_nop 1
	v_permlane32_swap_b32_e32 v12, v7
	s_waitcnt lgkmcnt(0)
; __device__ __forceinline__ u32x4 pack8(const f32x4 a, const f32x4 b) { u32x4 w; w.x = cvt_pk_bf16(a[0], a[1]); w.y = cvt_pk_bf16(a[2], a[3]); w.z = cvt_pk_bf16(b[0], b[1]); w.w = cvt_pk_bf16(b[2], b[3]); return w; }
; __device__ __forceinline__ float rstd_of4(const float* ss, int row, int fq) { const f32x4 a = *(const f32x4*)(ss + (size_t)row * 16 + fq * 4); float s = (a[0] + a[1]) + (a[2] + a[3]);
;     s += __shfl_xor(s, 16); s += __shfl_xor(s, 32); return __builtin_amdgcn_rsqf(s * (1.f / 1024.f) + 1e-6f); }
;     __device__ __forceinline__ void operator()(const f32x4 (&acc)[2][2][4][2], const Unit& u, int wr, int wc, int fr, int fq) const {
;         asm volatile("" : "+v"(fr), "+v"(fq));
;         const int row0 = u.pm * BM + wr * 64 + fr, col0 = u.pn * BM + wc * 32 + fq * 8;
; #pragma unroll
;         for (int ai = 0; ai < 2; ++ai)
; #pragma unroll
;             for (int m = 0; m < 4; ++m) { const int row = row0 + ai * HALF + m * 16; const float rs = rstd_of4(ss, row, fq) * scale;
; #pragma unroll
;                 for (int bj = 0; bj < 2; ++bj) *(u32x4*)(O + (size_t)row * ldc + col0 + bj * HALF) = pack8(acc[ai][bj][m][0] * rs, acc[ai][bj][m][1] * rs); asm volatile("" ::: "memory"); }
	v_add_f32_e32 v7, v7, v12
	v_fmamk_f32 v7, v7, 0x3a800000, v227
	v_rsq_f32_e32 v7, v7
	s_nop 0
	v_mul_f32_e32 v18, 0x3ab8aa3b, v7
	v_pk_mul_f32 v[14:15], v[98:99], v[18:19] op_sel_hi:[1,0]
	v_pk_mul_f32 v[12:13], v[96:97], v[18:19] op_sel_hi:[1,0]
	v_pk_mul_f32 v[20:21], v[94:95], v[18:19] op_sel_hi:[1,0]
	v_pk_mul_f32 v[22:23], v[92:93], v[18:19] op_sel_hi:[1,0]
	v_cvt_pk_bf16_f32 v12, v12, v13
	v_cvt_pk_bf16_f32 v13, v14, v15
	s_nop 0
	v_cvt_pk_bf16_f32 v14, v22, v23
	v_cvt_pk_bf16_f32 v15, v20, v21
	global_store_dwordx4 v[16:17], v[12:15], off
	v_pk_mul_f32 v[20:21], v[86:87], v[18:19] op_sel_hi:[1,0]
	s_nop 0
	v_pk_mul_f32 v[14:15], v[90:91], v[18:19] op_sel_hi:[1,0]
	v_pk_mul_f32 v[12:13], v[88:89], v[18:19] op_sel_hi:[1,0]
	v_pk_mul_f32 v[18:19], v[84:85], v[18:19] op_sel_hi:[1,0]
	v_cvt_pk_bf16_f32 v12, v12, v13
	v_cvt_pk_bf16_f32 v13, v14, v15
	s_nop 0
	v_cvt_pk_bf16_f32 v14, v18, v19
	v_cvt_pk_bf16_f32 v15, v20, v21
	global_store_dwordx4 v[16:17], v[12:15], off offset:256
	v_add_u32_e32 v16, 0x90, v6
	v_ashrrev_i32_e32 v17, 31, v16
	v_lshlrev_b64 v[12:13], 6, v[16:17]
	v_lshl_add_u64 v[12:13], s[44:45], 0, v[12:13]
	v_lshl_add_u64 v[12:13], v[12:13], 0, v[8:9]
	v_mov_b64_e32 v[12:13], v[212:213]
	v_mov_b64_e32 v[14:15], v[214:215]
	v_lshlrev_b64 v[16:17], 11, v[16:17]
	v_lshl_add_u64 v[16:17], s[42:43], 0, v[16:17]
	v_lshl_add_u64 v[16:17], v[16:17], 0, v[4:5]
	v_mov_b32_e32 v18, v13
	v_mov_b32_e32 v19, v14
	v_mov_b32_e32 v13, v15
	v_pk_add_f32 v[12:13], v[18:19], v[12:13]
	s_nop 0
	v_add_f32_e32 v7, v12, v13
	v_mov_b32_e32 v12, v7
	s_nop 1
	v_permlane16_swap_b32_e32 v12, v7
	s_waitcnt lgkmcnt(0)
	v_add_f32_e32 v7, v7, v12
	v_mov_b32_e32 v12, v7
	s_nop 1
	v_permlane32_swap_b32_e32 v12, v7
	s_waitcnt lgkmcnt(0)
	v_add_f32_e32 v7, v7, v12
	v_fmamk_f32 v7, v7, 0x3a800000, v227
	v_rsq_f32_e32 v7, v7
	s_nop 0
	v_mul_f32_e32 v18, 0x3ab8aa3b, v7
	v_pk_mul_f32 v[14:15], v[82:83], v[18:19] op_sel_hi:[1,0]
	v_pk_mul_f32 v[12:13], v[80:81], v[18:19] op_sel_hi:[1,0]
	v_pk_mul_f32 v[20:21], v[78:79], v[18:19] op_sel_hi:[1,0]
	v_pk_mul_f32 v[22:23], v[76:77], v[18:19] op_sel_hi:[1,0]
	v_cvt_pk_bf16_f32 v12, v12, v13
	v_cvt_pk_bf16_f32 v13, v14, v15
	s_nop 0
	v_cvt_pk_bf16_f32 v14, v22, v23
	v_cvt_pk_bf16_f32 v15, v20, v21
	global_store_dwordx4 v[16:17], v[12:15], off
	v_pk_mul_f32 v[20:21], v[70:71], v[18:19] op_sel_hi:[1,0]
	s_nop 0
	v_pk_mul_f32 v[14:15], v[74:75], v[18:19] op_sel_hi:[1,0]
	v_pk_mul_f32 v[12:13], v[72:73], v[18:19] op_sel_hi:[1,0]
	v_pk_mul_f32 v[18:19], v[68:69], v[18:19] op_sel_hi:[1,0]
	v_cvt_pk_bf16_f32 v12, v12, v13
	v_cvt_pk_bf16_f32 v13, v14, v15
	s_nop 0
	v_cvt_pk_bf16_f32 v14, v18, v19
	v_cvt_pk_bf16_f32 v15, v20, v21
	global_store_dwordx4 v[16:17], v[12:15], off offset:256
	v_add_u32_e32 v16, 0xa0, v6
	v_ashrrev_i32_e32 v17, 31, v16
	v_lshlrev_b64 v[12:13], 6, v[16:17]
	v_lshl_add_u64 v[12:13], s[44:45], 0, v[12:13]
	v_lshl_add_u64 v[12:13], v[12:13], 0, v[8:9]
	v_mov_b64_e32 v[12:13], v[216:217]
	v_mov_b64_e32 v[14:15], v[218:219]
	v_lshlrev_b64 v[16:17], 11, v[16:17]
	v_lshl_add_u64 v[16:17], s[42:43], 0, v[16:17]
	v_lshl_add_u64 v[16:17], v[16:17], 0, v[4:5]
	v_mov_b32_e32 v18, v13
	v_mov_b32_e32 v19, v14
	v_mov_b32_e32 v13, v15
	v_pk_add_f32 v[12:13], v[18:19], v[12:13]
	s_nop 0
	v_add_f32_e32 v7, v12, v13
	v_mov_b32_e32 v12, v7
	s_nop 1
	v_permlane16_swap_b32_e32 v12, v7
	s_waitcnt lgkmcnt(0)
	v_add_f32_e32 v7, v7, v12
	v_mov_b32_e32 v12, v7
	s_nop 1
	v_permlane32_swap_b32_e32 v12, v7
	s_waitcnt lgkmcnt(0)
	v_add_f32_e32 v7, v7, v12
	v_fmamk_f32 v7, v7, 0x3a800000, v227
	v_rsq_f32_e32 v7, v7
	s_nop 0
	v_mul_f32_e32 v18, 0x3ab8aa3b, v7
	v_pk_mul_f32 v[12:13], v[64:65], v[18:19] op_sel_hi:[1,0]
	v_pk_mul_f32 v[14:15], v[66:67], v[18:19] op_sel_hi:[1,0]
	v_cvt_pk_bf16_f32 v12, v12, v13
	v_pk_mul_f32 v[20:21], v[62:63], v[18:19] op_sel_hi:[1,0]
	v_cvt_pk_bf16_f32 v13, v14, v15
	v_pk_mul_f32 v[22:23], v[60:61], v[18:19] op_sel_hi:[1,0]
	s_nop 0
	v_cvt_pk_bf16_f32 v14, v22, v23
	v_cvt_pk_bf16_f32 v15, v20, v21
	global_store_dwordx4 v[16:17], v[12:15], off
	v_pk_mul_f32 v[20:21], v[54:55], v[18:19] op_sel_hi:[1,0]
	s_nop 0
	v_pk_mul_f32 v[12:13], v[56:57], v[18:19] op_sel_hi:[1,0]
	v_pk_mul_f32 v[14:15], v[58:59], v[18:19] op_sel_hi:[1,0]
	v_cvt_pk_bf16_f32 v12, v12, v13
	v_pk_mul_f32 v[18:19], v[52:53], v[18:19] op_sel_hi:[1,0]
	v_cvt_pk_bf16_f32 v13, v14, v15
	s_nop 0
	v_cvt_pk_bf16_f32 v14, v18, v19
	v_cvt_pk_bf16_f32 v15, v20, v21
	global_store_dwordx4 v[16:17], v[12:15], off offset:256
	s_nop 1
	v_add_u32_e32 v12, 0xb0, v6
	v_ashrrev_i32_e32 v13, 31, v12
	v_lshlrev_b64 v[6:7], 6, v[12:13]
	v_lshl_add_u64 v[6:7], s[44:45], 0, v[6:7]
	v_lshl_add_u64 v[6:7], v[6:7], 0, v[8:9]
	v_mov_b64_e32 v[6:7], v[220:221]
	v_mov_b64_e32 v[8:9], v[222:223]
	v_lshlrev_b64 v[12:13], 11, v[12:13]
	v_lshl_add_u64 v[12:13], s[42:43], 0, v[12:13]
	v_lshl_add_u64 v[12:13], v[12:13], 0, v[4:5]
	v_mov_b32_e32 v14, v7
	v_mov_b32_e32 v15, v8
	v_mov_b32_e32 v7, v9
	v_pk_add_f32 v[6:7], v[14:15], v[6:7]
	s_nop 0
	v_add_f32_e32 v6, v6, v7
	v_mov_b32_e32 v7, v6
	s_nop 1
	v_permlane16_swap_b32_e32 v7, v6
	s_waitcnt lgkmcnt(0)
	v_add_f32_e32 v6, v6, v7
	v_mov_b32_e32 v7, v6
	s_nop 1
	v_permlane32_swap_b32_e32 v7, v6
	s_waitcnt lgkmcnt(0)
	v_add_f32_e32 v6, v6, v7
	v_fmamk_f32 v6, v6, 0x3a800000, v227
	v_rsq_f32_e32 v6, v6
	s_nop 0
	v_mul_f32_e32 v10, 0x3ab8aa3b, v6
	v_pk_mul_f32 v[6:7], v[48:49], v[10:11] op_sel_hi:[1,0]
	v_pk_mul_f32 v[8:9], v[50:51], v[10:11] op_sel_hi:[1,0]
	v_cvt_pk_bf16_f32 v6, v6, v7
	v_pk_mul_f32 v[14:15], v[46:47], v[10:11] op_sel_hi:[1,0]
	v_cvt_pk_bf16_f32 v7, v8, v9
	v_pk_mul_f32 v[16:17], v[44:45], v[10:11] op_sel_hi:[1,0]
	v_pk_mul_f32 v[4:5], v[40:41], v[10:11] op_sel_hi:[1,0]
	v_cvt_pk_bf16_f32 v8, v16, v17
	v_cvt_pk_bf16_f32 v9, v14, v15
	global_store_dwordx4 v[12:13], v[6:9], off
	v_cvt_pk_bf16_f32 v4, v4, v5
	s_nop 1
	v_pk_mul_f32 v[6:7], v[42:43], v[10:11] op_sel_hi:[1,0]
	v_pk_mul_f32 v[8:9], v[38:39], v[10:11] op_sel_hi:[1,0]
	v_pk_mul_f32 v[10:11], v[36:37], v[10:11] op_sel_hi:[1,0]
	v_cvt_pk_bf16_f32 v5, v6, v7
	s_nop 0
	v_cvt_pk_bf16_f32 v6, v10, v11
	v_cvt_pk_bf16_f32 v7, v8, v9
	global_store_dwordx4 v[12:13], v[4:7], off offset:256
	s_cbranch_vccnz .LBB0_1490
	s_andn2_b64 vcc, exec, s[38:39]
	s_cbranch_vccnz .LBB0_1489
	s_barrier
	s_branch .LBB0_1489

; __device__ __forceinline__ float bflo(unsigned w) { return __uint_as_float(w << 16); }
;     __device__ __forceinline__ void operator()(const f32x4 (&acc)[2][2][4][2], const Unit& u, int wr, int wc, int fr, int fq) const {
;     ...
;         const int row0 = u.pm * BM + wr * 64 + fr, col0 = u.pn * BM + wc * 32 + fq * 8;
;         u32x4 xcur[2][2], xnxt[2][2];
; #pragma unroll
;         for (int h2 = 0; h2 < 2; ++h2)
; #pragma unroll
;             for (int bj = 0; bj < 2; ++bj) xcur[h2][bj] = *(const u32x4*)(X + (size_t)(row0 + h2 * 16) * 1024 + col0 + bj * HALF);
; #pragma unroll
;         for (int q = 0; q < 8; ++q) { const int ai = q >> 2, m = q & 3; const int row = row0 + ai * HALF + m * 16; float s = 0.f;
;             if ((q & 1) == 0 && q + 2 < 8) {
; #pragma unroll
;                 for (int h2 = 0; h2 < 2; ++h2)
; #pragma unroll
;                     for (int bj = 0; bj < 2; ++bj) { const int qn = q + 2 + h2; xnxt[h2][bj] = *(const u32x4*)(X + (size_t)(row0 + (qn >> 2) * HALF + (qn & 3) * 16) * 1024 + col0 + bj * HALF); } }
; #pragma unroll
;                 for (int bj = 0; bj < 2; ++bj) { bf16_t* p = X + (size_t)row * 1024 + col0 + bj * HALF; const u32x4 xv = xcur[q & 1][bj];
;                     f32x4 a = acc[ai][bj][m][0] * scale, b = acc[ai][bj][m][1] * scale;
;                     a[0] += bflo(xv.x); a[1] += bfhi(xv.x); a[2] += bflo(xv.y); a[3] += bfhi(xv.y); b[0] += bflo(xv.z); b[1] += bfhi(xv.z); b[2] += bflo(xv.w); b[3] += bfhi(xv.w);
;                     const u32x4 w = pack8(a, b); *(u32x4*)p = w;
;                     if constexpr (WX8) { unsigned q0 = 0u, q1 = 0u; q0 = __builtin_amdgcn_cvt_pk_fp8_f32(bflo(w.x), bfhi(w.x), q0, false); q0 = __builtin_amdgcn_cvt_pk_fp8_f32(bflo(w.y), bfhi(w.y), q0, true); q1 = __builtin_amdgcn_cvt_pk_fp8_f32(bflo(w.z), bfhi(w.z), q1, false); q1 = __builtin_amdgcn_cvt_pk_fp8_f32(bflo(w.w), bfhi(w.w), q1, true);
;                         *(u32x2*)((unsigned char*)X + (WS_X8 - WS_X) + (size_t)row * 1024 + col0 + bj * HALF) = (u32x2){q0, q1}; }
;                     s += (bflo(w.x) * bflo(w.x) + bfhi(w.x) * bfhi(w.x)) + (bflo(w.y) * bflo(w.y) + bfhi(w.y) * bfhi(w.y)) + (bflo(w.z) * bflo(w.z) + bfhi(w.z) * bfhi(w.z)) + (bflo(w.w) * bflo(w.w) + bfhi(w.w) * bfhi(w.w)); }
;                 s += __shfl_xor(s, 16); s += __shfl_xor(s, 32);
;                 if (fq == 0) ssn[(size_t)row * 16 + u.pn * 4 + wc] = s;
.LBB0_1590:
	s_lshl_b32 s4, s69, 8
	v_mov_b32_e32 v6, v194
	v_mov_b32_e32 v4, v1
	s_add_i32 s4, s4, s23
	v_pk_mul_f32 v[160:161], v[160:161], s[80:81] op_sel_hi:[1,0]
	v_add_u32_e32 v176, s4, v4
	s_lshl_b32 s4, s68, 8
	s_or_b32 s4, s4, s64
	v_lshl_add_u32 v174, v6, 3, s4
	v_ashrrev_i32_e32 v175, 31, v174
	v_lshlrev_b64 v[192:193], 1, v[174:175]
	v_ashrrev_i32_e32 v177, 31, v176
	v_lshl_add_u64 v[178:179], s[44:45], 0, v[192:193]
	v_lshlrev_b64 v[190:191], 11, v[176:177]
	v_lshl_add_u64 v[4:5], v[178:179], 0, v[190:191]
	global_load_dwordx4 v[210:213], v[4:5], off
	global_load_dwordx4 v[28:31], v[4:5], off offset:256
	v_add_u32_e32 v32, 16, v176
	v_ashrrev_i32_e32 v33, 31, v32
	v_add_u32_e32 v184, 32, v176
	v_lshlrev_b64 v[34:35], 11, v[32:33]
	v_ashrrev_i32_e32 v185, 31, v184
	v_add_u32_e32 v180, 48, v176
	v_lshl_add_u64 v[4:5], v[178:179], 0, v[34:35]
	v_lshlrev_b64 v[186:187], 11, v[184:185]
	v_ashrrev_i32_e32 v181, 31, v180
	global_load_dwordx4 v[24:27], v[4:5], off
	global_load_dwordx4 v[20:23], v[4:5], off offset:256
	v_lshl_add_u64 v[4:5], v[178:179], 0, v[186:187]
	v_lshlrev_b64 v[182:183], 11, v[180:181]
	global_load_dwordx4 v[16:19], v[4:5], off
	global_load_dwordx4 v[12:15], v[4:5], off offset:256
	v_lshl_add_u64 v[4:5], v[178:179], 0, v[182:183]
	v_cmp_eq_u32_e32 vcc, 0, v6
	global_load_dwordx4 v[8:11], v[4:5], off
	s_nop 0
	global_load_dwordx4 v[4:7], v[4:5], off offset:256
	v_pk_mul_f32 v[162:163], v[162:163], s[80:81] op_sel_hi:[1,0]
	v_pk_mul_f32 v[156:157], v[156:157], s[80:81] op_sel_hi:[1,0]
	v_pk_mul_f32 v[158:159], v[158:159], s[80:81] op_sel_hi:[1,0]
	v_lshl_add_u64 v[190:191], s[44:45], 0, v[190:191]
	v_lshl_add_u64 v[192:193], v[190:191], 0, v[192:193]
	v_lshlrev_b64 v[188:189], 10, v[176:177]
	v_pk_mul_f32 v[152:153], v[152:153], s[80:81] op_sel_hi:[1,0]
	v_pk_mul_f32 v[154:155], v[154:155], s[80:81] op_sel_hi:[1,0]
	v_pk_mul_f32 v[148:149], v[148:149], s[80:81] op_sel_hi:[1,0]
	v_pk_mul_f32 v[150:151], v[150:151], s[80:81] op_sel_hi:[1,0]
	s_lshl_b32 s60, s68, 2
	s_ashr_i32 s61, s60, 31
	s_waitcnt vmcnt(0)
	v_lshlrev_b32_e32 v204, 16, v210
	v_add_f32_e32 v160, v160, v204
	v_and_b32_e32 v204, 0xffff0000, v210
	v_add_f32_e32 v161, v161, v204
	v_lshlrev_b32_e32 v204, 16, v211
	v_add_f32_e32 v162, v162, v204
	v_and_b32_e32 v204, 0xffff0000, v211
	v_add_f32_e32 v163, v163, v204
	v_lshlrev_b32_e32 v204, 16, v212
	v_add_f32_e32 v204, v156, v204
	v_and_b32_e32 v156, 0xffff0000, v212
	v_add_f32_e32 v205, v157, v156
	v_lshlrev_b32_e32 v156, 16, v213
	v_add_f32_e32 v206, v158, v156
	v_and_b32_e32 v156, 0xffff0000, v213
	v_add_f32_e32 v159, v159, v156
	v_cvt_pk_bf16_f32 v156, v160, v161
	v_cvt_pk_bf16_f32 v157, v162, v163
	v_cvt_pk_bf16_f32 v158, v204, v205
	v_cvt_pk_bf16_f32 v159, v206, v159
	global_store_dwordx4 v[192:193], v[156:159], off
	v_lshlrev_b32_e32 v160, 16, v156
	v_and_b32_e32 v161, 0xffff0000, v156
	v_mov_b32_e32 v156, v3
	v_lshlrev_b32_e32 v162, 16, v157
	v_and_b32_e32 v163, 0xffff0000, v157
	v_lshlrev_b32_e32 v204, 16, v158
	v_and_b32_e32 v205, 0xffff0000, v158
	v_mov_b32_e32 v157, v3
	v_cvt_pk_fp8_f32 v156, v160, v161
	v_cvt_pk_fp8_f32 v157, v204, v205
	v_lshlrev_b32_e32 v206, 16, v159
	v_and_b32_e32 v207, 0xffff0000, v159
	v_cvt_pk_fp8_f32 v156, v162, v163 op_sel:[0,0,1]
	v_cvt_pk_fp8_f32 v157, v206, v207 op_sel:[0,0,1]
	v_lshl_add_u64 v[158:159], s[48:49], 0, v[188:189]
	v_lshl_add_u64 v[158:159], v[158:159], 0, v[174:175]
	global_store_dwordx2 v[158:159], v[156:157], off
	v_mul_f32_e32 v156, v161, v161
	v_mul_f32_e32 v157, v163, v163
	v_fmac_f32_e32 v156, v160, v160
	v_fmac_f32_e32 v157, v162, v162
	v_add_f32_e32 v156, v156, v157
	v_mul_f32_e32 v157, v205, v205
	v_fmac_f32_e32 v157, v204, v204
	v_add_f32_e32 v156, v156, v157
	v_mul_f32_e32 v157, v207, v207
	v_fmac_f32_e32 v157, v206, v206
	v_add_f32_e32 v156, v156, v157
	v_lshlrev_b32_e32 v157, 16, v28
	v_and_b32_e32 v28, 0xffff0000, v28
	v_add_f32_e32 v28, v153, v28
	v_lshlrev_b32_e32 v153, 16, v29
	v_add_f32_e32 v153, v154, v153
	v_and_b32_e32 v29, 0xffff0000, v29
	v_lshlrev_b32_e32 v154, 16, v30
	v_and_b32_e32 v30, 0xffff0000, v30
	v_add_f32_e32 v29, v155, v29
	v_add_f32_e32 v30, v149, v30
	v_lshlrev_b32_e32 v149, 16, v31
	v_and_b32_e32 v31, 0xffff0000, v31
	v_add_f32_e32 v152, v152, v157
	v_add_f32_e32 v148, v148, v154
	v_add_f32_e32 v149, v150, v149
	v_add_f32_e32 v31, v151, v31
	v_cvt_pk_bf16_f32 v28, v152, v28
	v_cvt_pk_bf16_f32 v29, v153, v29
	v_cvt_pk_bf16_f32 v30, v148, v30
	v_cvt_pk_bf16_f32 v31, v149, v31
	global_store_dwordx4 v[192:193], v[28:31], off offset:256
	v_lshlrev_b32_e32 v148, 16, v28
	v_and_b32_e32 v149, 0xffff0000, v28
	v_mov_b32_e32 v28, v3
	v_lshlrev_b32_e32 v150, 16, v29
	v_and_b32_e32 v151, 0xffff0000, v29
	v_lshlrev_b32_e32 v152, 16, v30
	v_and_b32_e32 v153, 0xffff0000, v30
	v_mov_b32_e32 v29, v3
	v_cvt_pk_fp8_f32 v28, v148, v149
	v_cvt_pk_fp8_f32 v29, v152, v153
	v_sub_co_u32_e64 v30, s[42:43], 0, v188
	v_lshlrev_b32_e32 v154, 16, v31
	v_and_b32_e32 v155, 0xffff0000, v31
	v_subb_co_u32_e64 v31, s[42:43], 0, v189, s[42:43]
	v_cvt_pk_fp8_f32 v28, v150, v151 op_sel:[0,0,1]
	v_cvt_pk_fp8_f32 v29, v154, v155 op_sel:[0,0,1]
	v_lshl_add_u64 v[30:31], v[190:191], 0, v[30:31]
	v_lshl_add_u64 v[30:31], v[30:31], 0, v[174:175]
	v_add_co_u32_e64 v30, s[42:43], s15, v30
	s_nop 1
	v_addc_co_u32_e64 v31, s[42:43], 0, v31, s[42:43]
	global_store_dwordx2 v[30:31], v[28:29], off offset:128
	v_mul_f32_e32 v28, v149, v149
	v_mul_f32_e32 v29, v151, v151
	v_fmac_f32_e32 v28, v148, v148
	v_fmac_f32_e32 v29, v150, v150
	v_add_f32_e32 v28, v28, v29
	v_mul_f32_e32 v29, v153, v153
	v_fmac_f32_e32 v29, v152, v152
	v_add_f32_e32 v28, v28, v29
	v_mul_f32_e32 v29, v155, v155
	v_fmac_f32_e32 v29, v154, v154
	v_and_b32_e32 v30, 64, v246
	v_add_f32_e32 v28, v28, v29
	v_xor_b32_e32 v29, 16, v246
	v_add_u32_e32 v30, 64, v30
	v_cmp_lt_i32_e64 s[42:43], v29, v30
	v_add_f32_e32 v28, v156, v28
	s_nop 0
	v_cndmask_b32_e64 v29, v246, v29, s[42:43]
	v_lshlrev_b32_e32 v148, 2, v29
	v_mov_b32_e32 v29, v28
	s_nop 1
	v_permlane16_swap_b32_e32 v29, v28
	s_waitcnt lgkmcnt(0)
	v_add_f32_e32 v28, v28, v29
	v_xor_b32_e32 v29, 32, v246
	v_cmp_lt_i32_e64 s[42:43], v29, v30
	s_nop 1
	v_cndmask_b32_e64 v29, v246, v29, s[42:43]
	v_lshlrev_b32_e32 v149, 2, v29
	v_mov_b32_e32 v29, v28
	s_nop 1
	v_permlane32_swap_b32_e32 v29, v28
	s_and_saveexec_b64 s[4:5], vcc
	s_cbranch_execz .LBB0_1592
	v_lshlrev_b64 v[30:31], 6, v[176:177]
	v_lshl_add_u64 v[30:31], s[46:47], 0, v[30:31]
	v_lshl_add_u64 v[30:31], s[60:61], 2, v[30:31]
	s_lshl_b32 s92, s22, 2
	v_lshl_add_u64 v[30:31], v[30:31], 0, s[92:93]
	s_waitcnt lgkmcnt(0)
	v_add_f32_e32 v28, v28, v29
	global_store_dword v[30:31], v28, off
; __device__ __forceinline__ float bflo(unsigned w) { return __uint_as_float(w << 16); }
; __device__ __forceinline__ float bfhi(unsigned w) { return __uint_as_float(w & 0xffff0000u); }
; __device__ __forceinline__ u32x4 pack8(const f32x4 a, const f32x4 b) { u32x4 w; w.x = cvt_pk_bf16(a[0], a[1]); w.y = cvt_pk_bf16(a[2], a[3]); w.z = cvt_pk_bf16(b[0], b[1]); w.w = cvt_pk_bf16(b[2], b[3]); return w; }
;     __device__ __forceinline__ void operator()(const f32x4 (&acc)[2][2][4][2], const Unit& u, int wr, int wc, int fr, int fq) const {
;     ...
;             if ((q & 1) == 0 && q + 2 < 8) {
; #pragma unroll
;                 for (int h2 = 0; h2 < 2; ++h2)
; #pragma unroll
;                     for (int bj = 0; bj < 2; ++bj) { const int qn = q + 2 + h2; xnxt[h2][bj] = *(const u32x4*)(X + (size_t)(row0 + (qn >> 2) * HALF + (qn & 3) * 16) * 1024 + col0 + bj * HALF); } }
; #pragma unroll
;                 for (int bj = 0; bj < 2; ++bj) { bf16_t* p = X + (size_t)row * 1024 + col0 + bj * HALF; const u32x4 xv = xcur[q & 1][bj];
;                     f32x4 a = acc[ai][bj][m][0] * scale, b = acc[ai][bj][m][1] * scale;
;                     a[0] += bflo(xv.x); a[1] += bfhi(xv.x); a[2] += bflo(xv.y); a[3] += bfhi(xv.y); b[0] += bflo(xv.z); b[1] += bfhi(xv.z); b[2] += bflo(xv.w); b[3] += bfhi(xv.w);
;                     const u32x4 w = pack8(a, b); *(u32x4*)p = w;
;                     if constexpr (WX8) { unsigned q0 = 0u, q1 = 0u; q0 = __builtin_amdgcn_cvt_pk_fp8_f32(bflo(w.x), bfhi(w.x), q0, false); q0 = __builtin_amdgcn_cvt_pk_fp8_f32(bflo(w.y), bfhi(w.y), q0, true); q1 = __builtin_amdgcn_cvt_pk_fp8_f32(bflo(w.z), bfhi(w.z), q1, false); q1 = __builtin_amdgcn_cvt_pk_fp8_f32(bflo(w.w), bfhi(w.w), q1, true);
;                         *(u32x2*)((unsigned char*)X + (WS_X8 - WS_X) + (size_t)row * 1024 + col0 + bj * HALF) = (u32x2){q0, q1}; }
;                     s += (bflo(w.x) * bflo(w.x) + bfhi(w.x) * bfhi(w.x)) + (bflo(w.y) * bflo(w.y) + bfhi(w.y) * bfhi(w.y)) + (bflo(w.z) * bflo(w.z) + bfhi(w.z) * bfhi(w.z)) + (bflo(w.w) * bflo(w.w) + bfhi(w.w) * bfhi(w.w)); }
;                 s += __shfl_xor(s, 16); s += __shfl_xor(s, 32);
;                 if (fq == 0) ssn[(size_t)row * 16 + u.pn * 4 + wc] = s;
.LBB0_1592:
	s_or_b64 exec, exec, s[4:5]
	v_pk_mul_f32 v[144:145], v[144:145], s[80:81] op_sel_hi:[1,0]
	v_lshlrev_b32_e32 v150, 16, v24
	v_and_b32_e32 v24, 0xffff0000, v24
	v_pk_mul_f32 v[146:147], v[146:147], s[80:81] op_sel_hi:[1,0]
	v_add_f32_e32 v24, v145, v24
	v_lshlrev_b32_e32 v145, 16, v25
	v_pk_mul_f32 v[140:141], v[140:141], s[80:81] op_sel_hi:[1,0]
	v_add_f32_e32 v145, v146, v145
	v_lshlrev_b32_e32 v146, 16, v26
	v_and_b32_e32 v26, 0xffff0000, v26
	v_pk_mul_f32 v[142:143], v[142:143], s[80:81] op_sel_hi:[1,0]
	v_and_b32_e32 v25, 0xffff0000, v25
	v_add_f32_e32 v26, v141, v26
	v_lshlrev_b32_e32 v141, 16, v27
	v_and_b32_e32 v27, 0xffff0000, v27
	v_add_f32_e32 v25, v147, v25
	v_add_f32_e32 v140, v140, v146
	v_add_f32_e32 v141, v142, v141
	v_add_f32_e32 v27, v143, v27
	v_add_f32_e32 v144, v144, v150
	v_cvt_pk_bf16_f32 v24, v144, v24
	v_cvt_pk_bf16_f32 v25, v145, v25
	v_cvt_pk_bf16_f32 v26, v140, v26
	v_cvt_pk_bf16_f32 v27, v141, v27
	v_mov_b32_e32 v140, v3
	v_lshlrev_b32_e32 v142, 16, v24
	v_and_b32_e32 v143, 0xffff0000, v24
	v_lshlrev_b32_e32 v146, 16, v26
	v_and_b32_e32 v147, 0xffff0000, v26
	v_mov_b32_e32 v141, v3
	v_cvt_pk_fp8_f32 v140, v142, v143
	v_cvt_pk_fp8_f32 v141, v146, v147
	v_lshlrev_b32_e32 v144, 16, v25
	v_and_b32_e32 v145, 0xffff0000, v25
	v_lshlrev_b32_e32 v150, 16, v27
	v_and_b32_e32 v151, 0xffff0000, v27
	v_lshl_add_u64 v[30:31], s[44:45], 0, v[34:35]
	v_cvt_pk_fp8_f32 v140, v144, v145 op_sel:[0,0,1]
	v_cvt_pk_fp8_f32 v141, v150, v151 op_sel:[0,0,1]
	s_waitcnt lgkmcnt(0)
	v_lshlrev_b64 v[28:29], 10, v[32:33]
	v_lshl_add_u64 v[34:35], v[174:175], 1, v[30:31]
	global_store_dwordx4 v[34:35], v[24:27], off
	v_pk_mul_f32 v[134:135], v[134:135], s[80:81] op_sel_hi:[1,0]
	v_pk_mul_f32 v[132:133], v[132:133], s[80:81] op_sel_hi:[1,0]
	v_lshl_add_u64 v[24:25], s[48:49], 0, v[28:29]
	v_lshl_add_u64 v[24:25], v[24:25], 0, v[174:175]
	global_store_dwordx2 v[24:25], v[140:141], off
	v_mul_f32_e32 v24, v143, v143
	v_mul_f32_e32 v25, v145, v145
	v_fmac_f32_e32 v24, v142, v142
	v_fmac_f32_e32 v25, v144, v144
	v_add_f32_e32 v24, v24, v25
	v_mul_f32_e32 v25, v147, v147
	v_fmac_f32_e32 v25, v146, v146
	v_add_f32_e32 v24, v24, v25
	v_mul_f32_e32 v25, v151, v151
	v_fmac_f32_e32 v25, v150, v150
	v_pk_mul_f32 v[26:27], v[136:137], s[80:81] op_sel_hi:[1,0]
	v_lshlrev_b32_e32 v136, 16, v20
	v_and_b32_e32 v20, 0xffff0000, v20
	v_add_f32_e32 v140, v24, v25
	v_pk_mul_f32 v[24:25], v[138:139], s[80:81] op_sel_hi:[1,0]
	v_add_f32_e32 v20, v27, v20
	v_lshlrev_b32_e32 v27, 16, v21
	v_and_b32_e32 v21, 0xffff0000, v21
	v_add_f32_e32 v24, v24, v27
	v_add_f32_e32 v21, v25, v21
	v_lshlrev_b32_e32 v25, 16, v22
	v_and_b32_e32 v22, 0xffff0000, v22
	v_lshlrev_b32_e32 v27, 16, v23
	v_and_b32_e32 v23, 0xffff0000, v23
	v_add_f32_e32 v26, v26, v136
	v_add_f32_e32 v22, v133, v22
	v_add_f32_e32 v23, v135, v23
	v_cvt_pk_bf16_f32 v20, v26, v20
	v_add_f32_e32 v25, v132, v25
	v_add_f32_e32 v27, v134, v27
	v_cvt_pk_bf16_f32 v21, v24, v21
	v_cvt_pk_bf16_f32 v22, v25, v22
	v_cvt_pk_bf16_f32 v23, v27, v23
	global_store_dwordx4 v[34:35], v[20:23], off offset:256
	v_lshlrev_b32_e32 v26, 16, v20
	v_mov_b32_e32 v24, v3
	v_and_b32_e32 v20, 0xffff0000, v20
	v_cvt_pk_fp8_f32 v24, v26, v20
	v_lshlrev_b32_e32 v27, 16, v21
	v_and_b32_e32 v21, 0xffff0000, v21
	v_mul_f32_e32 v20, v20, v20
	v_cvt_pk_fp8_f32 v24, v27, v21 op_sel:[0,0,1]
	v_mul_f32_e32 v21, v21, v21
	v_lshlrev_b32_e32 v34, 16, v22
	v_and_b32_e32 v22, 0xffff0000, v22
	v_fmac_f32_e32 v20, v26, v26
	v_fmac_f32_e32 v21, v27, v27
	v_add_f32_e32 v20, v20, v21
	v_mul_f32_e32 v21, v22, v22
	v_lshlrev_b32_e32 v35, 16, v23
	v_and_b32_e32 v23, 0xffff0000, v23
	v_fmac_f32_e32 v21, v34, v34
	v_add_f32_e32 v20, v20, v21
	v_mul_f32_e32 v21, v23, v23
	v_fmac_f32_e32 v21, v35, v35
	v_add_f32_e32 v20, v20, v21
	v_add_f32_e32 v26, v140, v20
	v_mov_b32_e32 v25, v3
	v_mov_b32_e32 v27, v26
	s_nop 1
	v_permlane16_swap_b32_e32 v27, v26
	v_cvt_pk_fp8_f32 v25, v34, v22
	v_sub_co_u32_e64 v20, s[42:43], 0, v28
	v_cvt_pk_fp8_f32 v25, v35, v23 op_sel:[0,0,1]
	s_nop 0
	v_subb_co_u32_e64 v21, s[42:43], 0, v29, s[42:43]
	v_lshl_add_u64 v[20:21], v[30:31], 0, v[20:21]
	v_lshl_add_u64 v[22:23], v[20:21], 0, v[174:175]
	s_waitcnt lgkmcnt(0)
	v_add_f32_e32 v20, v26, v27
	v_mov_b32_e32 v21, v20
	s_nop 1
	v_permlane32_swap_b32_e32 v21, v20
	v_add_co_u32_e64 v22, s[42:43], s15, v22
	s_nop 1
	v_addc_co_u32_e64 v23, s[42:43], 0, v23, s[42:43]
	global_store_dwordx2 v[22:23], v[24:25], off offset:128
	s_and_saveexec_b64 s[4:5], vcc
	s_cbranch_execz .LBB0_1594
	v_lshlrev_b64 v[22:23], 6, v[32:33]
	v_lshl_add_u64 v[22:23], s[46:47], 0, v[22:23]
	v_lshl_add_u64 v[22:23], s[60:61], 2, v[22:23]
	s_lshl_b32 s92, s22, 2
	v_lshl_add_u64 v[22:23], v[22:23], 0, s[92:93]
	s_waitcnt lgkmcnt(0)
	v_add_f32_e32 v20, v20, v21
	global_store_dword v[22:23], v20, off
; __device__ __forceinline__ float bflo(unsigned w) { return __uint_as_float(w << 16); }
; __device__ __forceinline__ float bfhi(unsigned w) { return __uint_as_float(w & 0xffff0000u); }
; __device__ __forceinline__ u32x4 pack8(const f32x4 a, const f32x4 b) { u32x4 w; w.x = cvt_pk_bf16(a[0], a[1]); w.y = cvt_pk_bf16(a[2], a[3]); w.z = cvt_pk_bf16(b[0], b[1]); w.w = cvt_pk_bf16(b[2], b[3]); return w; }
;     __device__ __forceinline__ void operator()(const f32x4 (&acc)[2][2][4][2], const Unit& u, int wr, int wc, int fr, int fq) const {
;     ...
;             if ((q & 1) == 0 && q + 2 < 8) {
; #pragma unroll
;                 for (int h2 = 0; h2 < 2; ++h2)
; #pragma unroll
;                     for (int bj = 0; bj < 2; ++bj) { const int qn = q + 2 + h2; xnxt[h2][bj] = *(const u32x4*)(X + (size_t)(row0 + (qn >> 2) * HALF + (qn & 3) * 16) * 1024 + col0 + bj * HALF); } }
; #pragma unroll
;                 for (int bj = 0; bj < 2; ++bj) { bf16_t* p = X + (size_t)row * 1024 + col0 + bj * HALF; const u32x4 xv = xcur[q & 1][bj];
;                     f32x4 a = acc[ai][bj][m][0] * scale, b = acc[ai][bj][m][1] * scale;
;                     a[0] += bflo(xv.x); a[1] += bfhi(xv.x); a[2] += bflo(xv.y); a[3] += bfhi(xv.y); b[0] += bflo(xv.z); b[1] += bfhi(xv.z); b[2] += bflo(xv.w); b[3] += bfhi(xv.w);
;                     const u32x4 w = pack8(a, b); *(u32x4*)p = w;
;                     if constexpr (WX8) { unsigned q0 = 0u, q1 = 0u; q0 = __builtin_amdgcn_cvt_pk_fp8_f32(bflo(w.x), bfhi(w.x), q0, false); q0 = __builtin_amdgcn_cvt_pk_fp8_f32(bflo(w.y), bfhi(w.y), q0, true); q1 = __builtin_amdgcn_cvt_pk_fp8_f32(bflo(w.z), bfhi(w.z), q1, false); q1 = __builtin_amdgcn_cvt_pk_fp8_f32(bflo(w.w), bfhi(w.w), q1, true);
;                         *(u32x2*)((unsigned char*)X + (WS_X8 - WS_X) + (size_t)row * 1024 + col0 + bj * HALF) = (u32x2){q0, q1}; }
;                     s += (bflo(w.x) * bflo(w.x) + bfhi(w.x) * bfhi(w.x)) + (bflo(w.y) * bflo(w.y) + bfhi(w.y) * bfhi(w.y)) + (bflo(w.z) * bflo(w.z) + bfhi(w.z) * bfhi(w.z)) + (bflo(w.w) * bflo(w.w) + bfhi(w.w) * bfhi(w.w)); }
;                 s += __shfl_xor(s, 16); s += __shfl_xor(s, 32);
;                 if (fq == 0) ssn[(size_t)row * 16 + u.pn * 4 + wc] = s;
.LBB0_1594:
	s_or_b64 exec, exec, s[4:5]
	v_add_u32_e32 v134, 0x80, v176
	v_ashrrev_i32_e32 v135, 31, v134
	v_add_u32_e32 v132, 0x90, v176
	v_lshlrev_b64 v[138:139], 11, v[134:135]
	v_ashrrev_i32_e32 v133, 31, v132
	s_waitcnt lgkmcnt(0)
	v_lshl_add_u64 v[20:21], v[178:179], 0, v[138:139]
	v_lshlrev_b64 v[136:137], 11, v[132:133]
	global_load_dwordx4 v[32:35], v[20:21], off
	global_load_dwordx4 v[28:31], v[20:21], off offset:256
	v_lshl_add_u64 v[20:21], v[178:179], 0, v[136:137]
	global_load_dwordx4 v[24:27], v[20:21], off
	s_nop 0
	global_load_dwordx4 v[20:23], v[20:21], off offset:256
	v_pk_mul_f32 v[128:129], v[128:129], s[80:81] op_sel_hi:[1,0]
	v_lshlrev_b32_e32 v146, 16, v16
	v_and_b32_e32 v16, 0xffff0000, v16
	v_pk_mul_f32 v[130:131], v[130:131], s[80:81] op_sel_hi:[1,0]
	v_add_f32_e32 v16, v129, v16
	v_lshlrev_b32_e32 v129, 16, v17
	v_pk_mul_f32 v[124:125], v[124:125], s[80:81] op_sel_hi:[1,0]
	v_add_f32_e32 v129, v130, v129
	v_lshlrev_b32_e32 v130, 16, v18
	v_and_b32_e32 v18, 0xffff0000, v18
	v_pk_mul_f32 v[126:127], v[126:127], s[80:81] op_sel_hi:[1,0]
	v_and_b32_e32 v17, 0xffff0000, v17
	v_add_f32_e32 v18, v125, v18
	v_lshlrev_b32_e32 v125, 16, v19
	v_and_b32_e32 v19, 0xffff0000, v19
	v_add_f32_e32 v17, v131, v17
	v_add_f32_e32 v124, v124, v130
	v_add_f32_e32 v125, v126, v125
	v_add_f32_e32 v19, v127, v19
	v_add_f32_e32 v128, v128, v146
	v_cvt_pk_bf16_f32 v16, v128, v16
	v_cvt_pk_bf16_f32 v17, v129, v17
	v_cvt_pk_bf16_f32 v18, v124, v18
	v_cvt_pk_bf16_f32 v19, v125, v19
	v_mov_b32_e32 v124, v3
	v_lshlrev_b32_e32 v126, 16, v16
	v_and_b32_e32 v127, 0xffff0000, v16
	v_lshlrev_b32_e32 v130, 16, v18
	v_and_b32_e32 v131, 0xffff0000, v18
	v_mov_b32_e32 v125, v3
	v_cvt_pk_fp8_f32 v124, v126, v127
	v_cvt_pk_fp8_f32 v125, v130, v131
	v_lshlrev_b32_e32 v128, 16, v17
	v_and_b32_e32 v129, 0xffff0000, v17
	v_lshlrev_b32_e32 v146, 16, v19
	v_and_b32_e32 v147, 0xffff0000, v19
	v_lshl_add_u64 v[142:143], s[44:45], 0, v[186:187]
	v_cvt_pk_fp8_f32 v124, v128, v129 op_sel:[0,0,1]
	v_cvt_pk_fp8_f32 v125, v146, v147 op_sel:[0,0,1]
	v_lshlrev_b64 v[140:141], 10, v[184:185]
	v_lshl_add_u64 v[144:145], v[174:175], 1, v[142:143]
	global_store_dwordx4 v[144:145], v[16:19], off
	v_pk_mul_f32 v[118:119], v[118:119], s[80:81] op_sel_hi:[1,0]
	v_pk_mul_f32 v[116:117], v[116:117], s[80:81] op_sel_hi:[1,0]
	v_lshl_add_u64 v[16:17], s[48:49], 0, v[140:141]
	v_lshl_add_u64 v[16:17], v[16:17], 0, v[174:175]
	global_store_dwordx2 v[16:17], v[124:125], off
	v_mul_f32_e32 v16, v127, v127
	v_mul_f32_e32 v17, v129, v129
	v_fmac_f32_e32 v16, v126, v126
	v_fmac_f32_e32 v17, v128, v128
	v_add_f32_e32 v16, v16, v17
	v_mul_f32_e32 v17, v131, v131
	v_fmac_f32_e32 v17, v130, v130
	v_add_f32_e32 v16, v16, v17
	v_mul_f32_e32 v17, v147, v147
	v_fmac_f32_e32 v17, v146, v146
	v_pk_mul_f32 v[18:19], v[120:121], s[80:81] op_sel_hi:[1,0]
	v_lshlrev_b32_e32 v120, 16, v12
	v_and_b32_e32 v12, 0xffff0000, v12
	v_add_f32_e32 v124, v16, v17
	v_pk_mul_f32 v[16:17], v[122:123], s[80:81] op_sel_hi:[1,0]
	v_add_f32_e32 v12, v19, v12
	v_lshlrev_b32_e32 v19, 16, v13
	v_and_b32_e32 v13, 0xffff0000, v13
	v_add_f32_e32 v16, v16, v19
	v_add_f32_e32 v13, v17, v13
	v_lshlrev_b32_e32 v17, 16, v14
	v_and_b32_e32 v14, 0xffff0000, v14
	v_lshlrev_b32_e32 v19, 16, v15
	v_and_b32_e32 v15, 0xffff0000, v15
	v_add_f32_e32 v18, v18, v120
	v_add_f32_e32 v14, v117, v14
	v_add_f32_e32 v15, v119, v15
	v_cvt_pk_bf16_f32 v12, v18, v12
	v_add_f32_e32 v17, v116, v17
	v_add_f32_e32 v19, v118, v19
	v_cvt_pk_bf16_f32 v13, v16, v13
	v_cvt_pk_bf16_f32 v14, v17, v14
	v_cvt_pk_bf16_f32 v15, v19, v15
	global_store_dwordx4 v[144:145], v[12:15], off offset:256
	v_lshlrev_b32_e32 v18, 16, v12
	v_mov_b32_e32 v16, v3
	v_and_b32_e32 v12, 0xffff0000, v12
	v_cvt_pk_fp8_f32 v16, v18, v12
	v_lshlrev_b32_e32 v19, 16, v13
	v_and_b32_e32 v13, 0xffff0000, v13
	v_mul_f32_e32 v12, v12, v12
	v_cvt_pk_fp8_f32 v16, v19, v13 op_sel:[0,0,1]
	v_mul_f32_e32 v13, v13, v13
	v_lshlrev_b32_e32 v116, 16, v14
	v_and_b32_e32 v14, 0xffff0000, v14
	v_fmac_f32_e32 v12, v18, v18
	v_fmac_f32_e32 v13, v19, v19
	v_add_f32_e32 v12, v12, v13
	v_mul_f32_e32 v13, v14, v14
	v_lshlrev_b32_e32 v117, 16, v15
	v_and_b32_e32 v15, 0xffff0000, v15
	v_fmac_f32_e32 v13, v116, v116
	v_add_f32_e32 v12, v12, v13
	v_mul_f32_e32 v13, v15, v15
	v_fmac_f32_e32 v13, v117, v117
	v_add_f32_e32 v12, v12, v13
	v_add_f32_e32 v18, v124, v12
	v_mov_b32_e32 v17, v3
	v_mov_b32_e32 v19, v18
	s_nop 1
	v_permlane16_swap_b32_e32 v19, v18
	v_cvt_pk_fp8_f32 v17, v116, v14
	v_sub_co_u32_e64 v12, s[42:43], 0, v140
	v_cvt_pk_fp8_f32 v17, v117, v15 op_sel:[0,0,1]
	s_nop 0
	v_subb_co_u32_e64 v13, s[42:43], 0, v141, s[42:43]
	v_lshl_add_u64 v[12:13], v[142:143], 0, v[12:13]
	v_lshl_add_u64 v[14:15], v[12:13], 0, v[174:175]
	s_waitcnt lgkmcnt(0)
	v_add_f32_e32 v12, v18, v19
	v_mov_b32_e32 v13, v12
	s_nop 1
	v_permlane32_swap_b32_e32 v13, v12
	v_add_co_u32_e64 v14, s[42:43], s15, v14
	s_nop 1
	v_addc_co_u32_e64 v15, s[42:43], 0, v15, s[42:43]
	global_store_dwordx2 v[14:15], v[16:17], off offset:128
	s_and_saveexec_b64 s[4:5], vcc
	s_cbranch_execz .LBB0_1596
	v_lshlrev_b64 v[14:15], 6, v[184:185]
	v_lshl_add_u64 v[14:15], s[46:47], 0, v[14:15]
	v_lshl_add_u64 v[14:15], s[60:61], 2, v[14:15]
	s_lshl_b32 s92, s22, 2
	v_lshl_add_u64 v[14:15], v[14:15], 0, s[92:93]
	s_waitcnt lgkmcnt(0)
	v_add_f32_e32 v12, v12, v13
	global_store_dword v[14:15], v12, off
; __device__ __forceinline__ float bflo(unsigned w) { return __uint_as_float(w << 16); }
; __device__ __forceinline__ float bfhi(unsigned w) { return __uint_as_float(w & 0xffff0000u); }
; __device__ __forceinline__ u32x4 pack8(const f32x4 a, const f32x4 b) { u32x4 w; w.x = cvt_pk_bf16(a[0], a[1]); w.y = cvt_pk_bf16(a[2], a[3]); w.z = cvt_pk_bf16(b[0], b[1]); w.w = cvt_pk_bf16(b[2], b[3]); return w; }
;     __device__ __forceinline__ void operator()(const f32x4 (&acc)[2][2][4][2], const Unit& u, int wr, int wc, int fr, int fq) const {
;     ...
;             if ((q & 1) == 0 && q + 2 < 8) {
; #pragma unroll
;                 for (int h2 = 0; h2 < 2; ++h2)
; #pragma unroll
;                     for (int bj = 0; bj < 2; ++bj) { const int qn = q + 2 + h2; xnxt[h2][bj] = *(const u32x4*)(X + (size_t)(row0 + (qn >> 2) * HALF + (qn & 3) * 16) * 1024 + col0 + bj * HALF); } }
; #pragma unroll
;                 for (int bj = 0; bj < 2; ++bj) { bf16_t* p = X + (size_t)row * 1024 + col0 + bj * HALF; const u32x4 xv = xcur[q & 1][bj];
;                     f32x4 a = acc[ai][bj][m][0] * scale, b = acc[ai][bj][m][1] * scale;
;                     a[0] += bflo(xv.x); a[1] += bfhi(xv.x); a[2] += bflo(xv.y); a[3] += bfhi(xv.y); b[0] += bflo(xv.z); b[1] += bfhi(xv.z); b[2] += bflo(xv.w); b[3] += bfhi(xv.w);
;                     const u32x4 w = pack8(a, b); *(u32x4*)p = w;
;                     if constexpr (WX8) { unsigned q0 = 0u, q1 = 0u; q0 = __builtin_amdgcn_cvt_pk_fp8_f32(bflo(w.x), bfhi(w.x), q0, false); q0 = __builtin_amdgcn_cvt_pk_fp8_f32(bflo(w.y), bfhi(w.y), q0, true); q1 = __builtin_amdgcn_cvt_pk_fp8_f32(bflo(w.z), bfhi(w.z), q1, false); q1 = __builtin_amdgcn_cvt_pk_fp8_f32(bflo(w.w), bfhi(w.w), q1, true);
;                         *(u32x2*)((unsigned char*)X + (WS_X8 - WS_X) + (size_t)row * 1024 + col0 + bj * HALF) = (u32x2){q0, q1}; }
;                     s += (bflo(w.x) * bflo(w.x) + bfhi(w.x) * bfhi(w.x)) + (bflo(w.y) * bflo(w.y) + bfhi(w.y) * bfhi(w.y)) + (bflo(w.z) * bflo(w.z) + bfhi(w.z) * bfhi(w.z)) + (bflo(w.w) * bflo(w.w) + bfhi(w.w) * bfhi(w.w)); }
;                 s += __shfl_xor(s, 16); s += __shfl_xor(s, 32);
;                 if (fq == 0) ssn[(size_t)row * 16 + u.pn * 4 + wc] = s;
.LBB0_1596:
	s_or_b64 exec, exec, s[4:5]
	v_pk_mul_f32 v[18:19], v[114:115], s[80:81] op_sel_hi:[1,0]
	v_pk_mul_f32 v[112:113], v[112:113], s[80:81] op_sel_hi:[1,0]
	v_lshlrev_b32_e32 v114, 16, v8
	v_and_b32_e32 v8, 0xffff0000, v8
	v_add_f32_e32 v8, v113, v8
	v_lshlrev_b32_e32 v113, 16, v9
	v_and_b32_e32 v9, 0xffff0000, v9
	v_pk_mul_f32 v[108:109], v[108:109], s[80:81] op_sel_hi:[1,0]
	v_add_f32_e32 v9, v19, v9
	v_lshlrev_b32_e32 v19, 16, v10
	v_pk_mul_f32 v[110:111], v[110:111], s[80:81] op_sel_hi:[1,0]
	v_add_f32_e32 v19, v108, v19
	v_and_b32_e32 v10, 0xffff0000, v10
	v_lshlrev_b32_e32 v108, 16, v11
	v_and_b32_e32 v11, 0xffff0000, v11
	v_add_f32_e32 v112, v112, v114
	v_add_f32_e32 v18, v18, v113
	v_add_f32_e32 v10, v109, v10
	v_add_f32_e32 v108, v110, v108
	v_add_f32_e32 v11, v111, v11
	v_cvt_pk_bf16_f32 v8, v112, v8
	v_cvt_pk_bf16_f32 v9, v18, v9
	v_cvt_pk_bf16_f32 v10, v19, v10
	v_cvt_pk_bf16_f32 v11, v108, v11
	v_mov_b32_e32 v18, v3
	v_lshlrev_b32_e32 v108, 16, v8
	v_and_b32_e32 v109, 0xffff0000, v8
	v_lshlrev_b32_e32 v112, 16, v10
	v_and_b32_e32 v113, 0xffff0000, v10
	v_mov_b32_e32 v19, v3
	v_cvt_pk_fp8_f32 v18, v108, v109
	v_cvt_pk_fp8_f32 v19, v112, v113
	v_lshlrev_b32_e32 v110, 16, v9
	v_and_b32_e32 v111, 0xffff0000, v9
	v_lshlrev_b32_e32 v114, 16, v11
	v_and_b32_e32 v115, 0xffff0000, v11
	v_lshl_add_u64 v[14:15], s[44:45], 0, v[182:183]
	v_cvt_pk_fp8_f32 v18, v110, v111 op_sel:[0,0,1]
	v_cvt_pk_fp8_f32 v19, v114, v115 op_sel:[0,0,1]
	s_waitcnt lgkmcnt(0)
	v_lshlrev_b64 v[12:13], 10, v[180:181]
	v_lshl_add_u64 v[16:17], v[174:175], 1, v[14:15]
	global_store_dwordx4 v[16:17], v[8:11], off
	v_pk_mul_f32 v[100:101], v[100:101], s[80:81] op_sel_hi:[1,0]
	s_nop 0
	v_lshl_add_u64 v[8:9], s[48:49], 0, v[12:13]
	v_lshl_add_u64 v[8:9], v[8:9], 0, v[174:175]
	global_store_dwordx2 v[8:9], v[18:19], off
	v_mul_f32_e32 v8, v109, v109
	v_mul_f32_e32 v9, v111, v111
	v_fmac_f32_e32 v8, v108, v108
	v_fmac_f32_e32 v9, v110, v110
	v_add_f32_e32 v8, v8, v9
	v_mul_f32_e32 v9, v113, v113
	v_fmac_f32_e32 v9, v112, v112
	v_add_f32_e32 v8, v8, v9
	v_mul_f32_e32 v9, v115, v115
	v_fmac_f32_e32 v9, v114, v114
	v_pk_mul_f32 v[10:11], v[104:105], s[80:81] op_sel_hi:[1,0]
	v_pk_mul_f32 v[18:19], v[102:103], s[80:81] op_sel_hi:[1,0]
	v_lshlrev_b32_e32 v102, 16, v4
	v_and_b32_e32 v4, 0xffff0000, v4
	v_add_f32_e32 v108, v8, v9
	v_pk_mul_f32 v[8:9], v[106:107], s[80:81] op_sel_hi:[1,0]
	v_add_f32_e32 v4, v11, v4
	v_lshlrev_b32_e32 v11, 16, v5
	v_and_b32_e32 v5, 0xffff0000, v5
	v_add_f32_e32 v8, v8, v11
	v_add_f32_e32 v5, v9, v5
	v_lshlrev_b32_e32 v9, 16, v6
	v_and_b32_e32 v6, 0xffff0000, v6
	v_lshlrev_b32_e32 v11, 16, v7
	v_and_b32_e32 v7, 0xffff0000, v7
	v_add_f32_e32 v10, v10, v102
	v_add_f32_e32 v6, v101, v6
	v_add_f32_e32 v7, v19, v7
	v_cvt_pk_bf16_f32 v4, v10, v4
	v_add_f32_e32 v9, v100, v9
	v_add_f32_e32 v11, v18, v11
	v_cvt_pk_bf16_f32 v5, v8, v5
	v_cvt_pk_bf16_f32 v6, v9, v6
	v_cvt_pk_bf16_f32 v7, v11, v7
	global_store_dwordx4 v[16:17], v[4:7], off offset:256
	v_lshlrev_b32_e32 v10, 16, v4
	v_mov_b32_e32 v8, v3
	v_and_b32_e32 v4, 0xffff0000, v4
	v_cvt_pk_fp8_f32 v8, v10, v4
	v_lshlrev_b32_e32 v11, 16, v5
	v_and_b32_e32 v5, 0xffff0000, v5
	v_mul_f32_e32 v4, v4, v4
	v_cvt_pk_fp8_f32 v8, v11, v5 op_sel:[0,0,1]
	v_mul_f32_e32 v5, v5, v5
	v_lshlrev_b32_e32 v16, 16, v6
	v_and_b32_e32 v6, 0xffff0000, v6
	v_fmac_f32_e32 v4, v10, v10
	v_fmac_f32_e32 v5, v11, v11
	v_add_f32_e32 v4, v4, v5
	v_mul_f32_e32 v5, v6, v6
	v_lshlrev_b32_e32 v17, 16, v7
	v_and_b32_e32 v7, 0xffff0000, v7
	v_fmac_f32_e32 v5, v16, v16
	v_add_f32_e32 v4, v4, v5
	v_mul_f32_e32 v5, v7, v7
	v_fmac_f32_e32 v5, v17, v17
	v_add_f32_e32 v4, v4, v5
	v_add_f32_e32 v10, v108, v4
	v_mov_b32_e32 v9, v3
	v_mov_b32_e32 v11, v10
	s_nop 1
	v_permlane16_swap_b32_e32 v11, v10
	v_cvt_pk_fp8_f32 v9, v16, v6
	v_sub_co_u32_e64 v4, s[42:43], 0, v12
	v_cvt_pk_fp8_f32 v9, v17, v7 op_sel:[0,0,1]
	s_nop 0
	v_subb_co_u32_e64 v5, s[42:43], 0, v13, s[42:43]
	v_lshl_add_u64 v[4:5], v[14:15], 0, v[4:5]
	v_lshl_add_u64 v[6:7], v[4:5], 0, v[174:175]
	s_waitcnt lgkmcnt(0)
	v_add_f32_e32 v4, v10, v11
	v_mov_b32_e32 v5, v4
	s_nop 1
	v_permlane32_swap_b32_e32 v5, v4
	v_add_co_u32_e64 v6, s[42:43], s15, v6
	s_nop 1
	v_addc_co_u32_e64 v7, s[42:43], 0, v7, s[42:43]
	global_store_dwordx2 v[6:7], v[8:9], off offset:128
	s_and_saveexec_b64 s[4:5], vcc
	s_cbranch_execz .LBB0_1598
	v_lshlrev_b64 v[6:7], 6, v[180:181]
	v_lshl_add_u64 v[6:7], s[46:47], 0, v[6:7]
	v_lshl_add_u64 v[6:7], s[60:61], 2, v[6:7]
	s_lshl_b32 s92, s22, 2
	v_lshl_add_u64 v[6:7], v[6:7], 0, s[92:93]
	s_waitcnt lgkmcnt(0)
	v_add_f32_e32 v4, v4, v5
	global_store_dword v[6:7], v4, off
; __device__ __forceinline__ float bflo(unsigned w) { return __uint_as_float(w << 16); }
; __device__ __forceinline__ float bfhi(unsigned w) { return __uint_as_float(w & 0xffff0000u); }
; __device__ __forceinline__ u32x4 pack8(const f32x4 a, const f32x4 b) { u32x4 w; w.x = cvt_pk_bf16(a[0], a[1]); w.y = cvt_pk_bf16(a[2], a[3]); w.z = cvt_pk_bf16(b[0], b[1]); w.w = cvt_pk_bf16(b[2], b[3]); return w; }
;     __device__ __forceinline__ void operator()(const f32x4 (&acc)[2][2][4][2], const Unit& u, int wr, int wc, int fr, int fq) const {
;     ...
;             if ((q & 1) == 0 && q + 2 < 8) {
; #pragma unroll
;                 for (int h2 = 0; h2 < 2; ++h2)
; #pragma unroll
;                     for (int bj = 0; bj < 2; ++bj) { const int qn = q + 2 + h2; xnxt[h2][bj] = *(const u32x4*)(X + (size_t)(row0 + (qn >> 2) * HALF + (qn & 3) * 16) * 1024 + col0 + bj * HALF); } }
; #pragma unroll
;                 for (int bj = 0; bj < 2; ++bj) { bf16_t* p = X + (size_t)row * 1024 + col0 + bj * HALF; const u32x4 xv = xcur[q & 1][bj];
;                     f32x4 a = acc[ai][bj][m][0] * scale, b = acc[ai][bj][m][1] * scale;
;                     a[0] += bflo(xv.x); a[1] += bfhi(xv.x); a[2] += bflo(xv.y); a[3] += bfhi(xv.y); b[0] += bflo(xv.z); b[1] += bfhi(xv.z); b[2] += bflo(xv.w); b[3] += bfhi(xv.w);
;                     const u32x4 w = pack8(a, b); *(u32x4*)p = w;
;                     if constexpr (WX8) { unsigned q0 = 0u, q1 = 0u; q0 = __builtin_amdgcn_cvt_pk_fp8_f32(bflo(w.x), bfhi(w.x), q0, false); q0 = __builtin_amdgcn_cvt_pk_fp8_f32(bflo(w.y), bfhi(w.y), q0, true); q1 = __builtin_amdgcn_cvt_pk_fp8_f32(bflo(w.z), bfhi(w.z), q1, false); q1 = __builtin_amdgcn_cvt_pk_fp8_f32(bflo(w.w), bfhi(w.w), q1, true);
;                         *(u32x2*)((unsigned char*)X + (WS_X8 - WS_X) + (size_t)row * 1024 + col0 + bj * HALF) = (u32x2){q0, q1}; }
;                     s += (bflo(w.x) * bflo(w.x) + bfhi(w.x) * bfhi(w.x)) + (bflo(w.y) * bflo(w.y) + bfhi(w.y) * bfhi(w.y)) + (bflo(w.z) * bflo(w.z) + bfhi(w.z) * bfhi(w.z)) + (bflo(w.w) * bflo(w.w) + bfhi(w.w) * bfhi(w.w)); }
;                 s += __shfl_xor(s, 16); s += __shfl_xor(s, 32);
;                 if (fq == 0) ssn[(size_t)row * 16 + u.pn * 4 + wc] = s;
.LBB0_1598:
	s_or_b64 exec, exec, s[4:5]
	v_add_u32_e32 v102, 0xa0, v176
	v_ashrrev_i32_e32 v103, 31, v102
	v_add_u32_e32 v100, 0xb0, v176
	v_lshlrev_b64 v[106:107], 11, v[102:103]
	v_ashrrev_i32_e32 v101, 31, v100
	s_waitcnt lgkmcnt(0)
	v_lshl_add_u64 v[4:5], v[178:179], 0, v[106:107]
	v_lshlrev_b64 v[104:105], 11, v[100:101]
	global_load_dwordx4 v[16:19], v[4:5], off
	global_load_dwordx4 v[12:15], v[4:5], off offset:256
	v_lshl_add_u64 v[4:5], v[178:179], 0, v[104:105]
	global_load_dwordx4 v[8:11], v[4:5], off
	s_nop 0
	global_load_dwordx4 v[4:7], v[4:5], off offset:256
	v_pk_mul_f32 v[96:97], v[96:97], s[80:81] op_sel_hi:[1,0]
	s_waitcnt vmcnt(15)
	v_lshlrev_b32_e32 v114, 16, v32
	v_and_b32_e32 v32, 0xffff0000, v32
	v_pk_mul_f32 v[98:99], v[98:99], s[80:81] op_sel_hi:[1,0]
	v_add_f32_e32 v32, v97, v32
	v_lshlrev_b32_e32 v97, 16, v33
	v_pk_mul_f32 v[92:93], v[92:93], s[80:81] op_sel_hi:[1,0]
	v_add_f32_e32 v97, v98, v97
	v_lshlrev_b32_e32 v98, 16, v34
	v_and_b32_e32 v34, 0xffff0000, v34
	v_pk_mul_f32 v[94:95], v[94:95], s[80:81] op_sel_hi:[1,0]
	v_and_b32_e32 v33, 0xffff0000, v33
	v_add_f32_e32 v34, v93, v34
	v_lshlrev_b32_e32 v93, 16, v35
	v_and_b32_e32 v35, 0xffff0000, v35
	v_add_f32_e32 v33, v99, v33
	v_add_f32_e32 v92, v92, v98
	v_add_f32_e32 v93, v94, v93
	v_add_f32_e32 v35, v95, v35
	v_add_f32_e32 v96, v96, v114
	v_cvt_pk_bf16_f32 v32, v96, v32
	v_cvt_pk_bf16_f32 v33, v97, v33
	v_cvt_pk_bf16_f32 v34, v92, v34
	v_cvt_pk_bf16_f32 v35, v93, v35
	v_mov_b32_e32 v92, v3
	v_lshlrev_b32_e32 v94, 16, v32
	v_and_b32_e32 v95, 0xffff0000, v32
	v_lshlrev_b32_e32 v98, 16, v34
	v_and_b32_e32 v99, 0xffff0000, v34
	v_mov_b32_e32 v93, v3
	v_cvt_pk_fp8_f32 v92, v94, v95
	v_cvt_pk_fp8_f32 v93, v98, v99
	v_lshlrev_b32_e32 v96, 16, v33
	v_and_b32_e32 v97, 0xffff0000, v33
	v_lshlrev_b32_e32 v114, 16, v35
	v_and_b32_e32 v115, 0xffff0000, v35
	v_lshl_add_u64 v[110:111], s[44:45], 0, v[138:139]
	v_cvt_pk_fp8_f32 v92, v96, v97 op_sel:[0,0,1]
	v_cvt_pk_fp8_f32 v93, v114, v115 op_sel:[0,0,1]
	v_lshlrev_b64 v[108:109], 10, v[134:135]
	v_lshl_add_u64 v[112:113], v[174:175], 1, v[110:111]
	global_store_dwordx4 v[112:113], v[32:35], off
	v_pk_mul_f32 v[86:87], v[86:87], s[80:81] op_sel_hi:[1,0]
	v_pk_mul_f32 v[84:85], v[84:85], s[80:81] op_sel_hi:[1,0]
	v_lshl_add_u64 v[32:33], s[48:49], 0, v[108:109]
	v_lshl_add_u64 v[32:33], v[32:33], 0, v[174:175]
	global_store_dwordx2 v[32:33], v[92:93], off
	v_mul_f32_e32 v32, v95, v95
	v_mul_f32_e32 v33, v97, v97
	v_fmac_f32_e32 v32, v94, v94
	v_fmac_f32_e32 v33, v96, v96
	v_add_f32_e32 v32, v32, v33
	v_mul_f32_e32 v33, v99, v99
	v_fmac_f32_e32 v33, v98, v98
	v_add_f32_e32 v32, v32, v33
	v_mul_f32_e32 v33, v115, v115
	v_fmac_f32_e32 v33, v114, v114
	v_pk_mul_f32 v[34:35], v[88:89], s[80:81] op_sel_hi:[1,0]
	s_waitcnt vmcnt(16)
	v_lshlrev_b32_e32 v88, 16, v28
	v_and_b32_e32 v28, 0xffff0000, v28
	v_add_f32_e32 v92, v32, v33
	v_pk_mul_f32 v[32:33], v[90:91], s[80:81] op_sel_hi:[1,0]
	v_add_f32_e32 v28, v35, v28
	v_lshlrev_b32_e32 v35, 16, v29
	v_and_b32_e32 v29, 0xffff0000, v29
	v_add_f32_e32 v32, v32, v35
	v_add_f32_e32 v29, v33, v29
	v_lshlrev_b32_e32 v33, 16, v30
	v_and_b32_e32 v30, 0xffff0000, v30
	v_lshlrev_b32_e32 v35, 16, v31
	v_and_b32_e32 v31, 0xffff0000, v31
	v_add_f32_e32 v34, v34, v88
	v_add_f32_e32 v30, v85, v30
	v_add_f32_e32 v31, v87, v31
	v_cvt_pk_bf16_f32 v28, v34, v28
	v_add_f32_e32 v33, v84, v33
	v_add_f32_e32 v35, v86, v35
	v_cvt_pk_bf16_f32 v29, v32, v29
	v_cvt_pk_bf16_f32 v30, v33, v30
	v_cvt_pk_bf16_f32 v31, v35, v31
	global_store_dwordx4 v[112:113], v[28:31], off offset:256
	v_lshlrev_b32_e32 v34, 16, v28
	v_mov_b32_e32 v32, v3
	v_and_b32_e32 v28, 0xffff0000, v28
	v_cvt_pk_fp8_f32 v32, v34, v28
	v_lshlrev_b32_e32 v35, 16, v29
	v_and_b32_e32 v29, 0xffff0000, v29
	v_mul_f32_e32 v28, v28, v28
	v_cvt_pk_fp8_f32 v32, v35, v29 op_sel:[0,0,1]
	v_mul_f32_e32 v29, v29, v29
	v_lshlrev_b32_e32 v84, 16, v30
	v_and_b32_e32 v30, 0xffff0000, v30
	v_fmac_f32_e32 v28, v34, v34
	v_fmac_f32_e32 v29, v35, v35
	v_add_f32_e32 v28, v28, v29
	v_mul_f32_e32 v29, v30, v30
	v_lshlrev_b32_e32 v85, 16, v31
	v_and_b32_e32 v31, 0xffff0000, v31
	v_fmac_f32_e32 v29, v84, v84
	v_add_f32_e32 v28, v28, v29
	v_mul_f32_e32 v29, v31, v31
	v_fmac_f32_e32 v29, v85, v85
	v_add_f32_e32 v28, v28, v29
	v_add_f32_e32 v34, v92, v28
	v_mov_b32_e32 v33, v3
	v_mov_b32_e32 v35, v34
	s_nop 1
	v_permlane16_swap_b32_e32 v35, v34
	v_cvt_pk_fp8_f32 v33, v84, v30
	v_sub_co_u32_e64 v28, s[42:43], 0, v108
	v_cvt_pk_fp8_f32 v33, v85, v31 op_sel:[0,0,1]
	s_nop 0
	v_subb_co_u32_e64 v29, s[42:43], 0, v109, s[42:43]
	v_lshl_add_u64 v[28:29], v[110:111], 0, v[28:29]
	v_lshl_add_u64 v[30:31], v[28:29], 0, v[174:175]
	s_waitcnt lgkmcnt(0)
	v_add_f32_e32 v28, v34, v35
	v_mov_b32_e32 v29, v28
	s_nop 1
	v_permlane32_swap_b32_e32 v29, v28
	v_add_co_u32_e64 v30, s[42:43], s15, v30
	s_nop 1
	v_addc_co_u32_e64 v31, s[42:43], 0, v31, s[42:43]
	global_store_dwordx2 v[30:31], v[32:33], off offset:128
	s_and_saveexec_b64 s[4:5], vcc
	s_cbranch_execz .LBB0_1600
	v_lshlrev_b64 v[30:31], 6, v[134:135]
	v_lshl_add_u64 v[30:31], s[46:47], 0, v[30:31]
	v_lshl_add_u64 v[30:31], s[60:61], 2, v[30:31]
	s_lshl_b32 s92, s22, 2
	v_lshl_add_u64 v[30:31], v[30:31], 0, s[92:93]
	s_waitcnt lgkmcnt(0)
	v_add_f32_e32 v28, v28, v29
	global_store_dword v[30:31], v28, off
; __device__ __forceinline__ float bflo(unsigned w) { return __uint_as_float(w << 16); }
; __device__ __forceinline__ float bfhi(unsigned w) { return __uint_as_float(w & 0xffff0000u); }
; __device__ __forceinline__ u32x4 pack8(const f32x4 a, const f32x4 b) { u32x4 w; w.x = cvt_pk_bf16(a[0], a[1]); w.y = cvt_pk_bf16(a[2], a[3]); w.z = cvt_pk_bf16(b[0], b[1]); w.w = cvt_pk_bf16(b[2], b[3]); return w; }
;     __device__ __forceinline__ void operator()(const f32x4 (&acc)[2][2][4][2], const Unit& u, int wr, int wc, int fr, int fq) const {
;     ...
;             if ((q & 1) == 0 && q + 2 < 8) {
; #pragma unroll
;                 for (int h2 = 0; h2 < 2; ++h2)
; #pragma unroll
;                     for (int bj = 0; bj < 2; ++bj) { const int qn = q + 2 + h2; xnxt[h2][bj] = *(const u32x4*)(X + (size_t)(row0 + (qn >> 2) * HALF + (qn & 3) * 16) * 1024 + col0 + bj * HALF); } }
; #pragma unroll
;                 for (int bj = 0; bj < 2; ++bj) { bf16_t* p = X + (size_t)row * 1024 + col0 + bj * HALF; const u32x4 xv = xcur[q & 1][bj];
;                     f32x4 a = acc[ai][bj][m][0] * scale, b = acc[ai][bj][m][1] * scale;
;                     a[0] += bflo(xv.x); a[1] += bfhi(xv.x); a[2] += bflo(xv.y); a[3] += bfhi(xv.y); b[0] += bflo(xv.z); b[1] += bfhi(xv.z); b[2] += bflo(xv.w); b[3] += bfhi(xv.w);
;                     const u32x4 w = pack8(a, b); *(u32x4*)p = w;
;                     if constexpr (WX8) { unsigned q0 = 0u, q1 = 0u; q0 = __builtin_amdgcn_cvt_pk_fp8_f32(bflo(w.x), bfhi(w.x), q0, false); q0 = __builtin_amdgcn_cvt_pk_fp8_f32(bflo(w.y), bfhi(w.y), q0, true); q1 = __builtin_amdgcn_cvt_pk_fp8_f32(bflo(w.z), bfhi(w.z), q1, false); q1 = __builtin_amdgcn_cvt_pk_fp8_f32(bflo(w.w), bfhi(w.w), q1, true);
;                         *(u32x2*)((unsigned char*)X + (WS_X8 - WS_X) + (size_t)row * 1024 + col0 + bj * HALF) = (u32x2){q0, q1}; }
;                     s += (bflo(w.x) * bflo(w.x) + bfhi(w.x) * bfhi(w.x)) + (bflo(w.y) * bflo(w.y) + bfhi(w.y) * bfhi(w.y)) + (bflo(w.z) * bflo(w.z) + bfhi(w.z) * bfhi(w.z)) + (bflo(w.w) * bflo(w.w) + bfhi(w.w) * bfhi(w.w)); }
;                 s += __shfl_xor(s, 16); s += __shfl_xor(s, 32);
;                 if (fq == 0) ssn[(size_t)row * 16 + u.pn * 4 + wc] = s;
.LBB0_1600:
	s_or_b64 exec, exec, s[4:5]
	v_pk_mul_f32 v[34:35], v[82:83], s[80:81] op_sel_hi:[1,0]
	v_pk_mul_f32 v[80:81], v[80:81], s[80:81] op_sel_hi:[1,0]
	s_waitcnt vmcnt(17)
	v_lshlrev_b32_e32 v82, 16, v24
	v_and_b32_e32 v24, 0xffff0000, v24
	v_add_f32_e32 v24, v81, v24
	v_lshlrev_b32_e32 v81, 16, v25
	v_and_b32_e32 v25, 0xffff0000, v25
	v_pk_mul_f32 v[76:77], v[76:77], s[80:81] op_sel_hi:[1,0]
	v_add_f32_e32 v25, v35, v25
	v_lshlrev_b32_e32 v35, 16, v26
	v_pk_mul_f32 v[78:79], v[78:79], s[80:81] op_sel_hi:[1,0]
	v_add_f32_e32 v35, v76, v35
	v_and_b32_e32 v26, 0xffff0000, v26
	v_lshlrev_b32_e32 v76, 16, v27
	v_and_b32_e32 v27, 0xffff0000, v27
	v_add_f32_e32 v80, v80, v82
	v_add_f32_e32 v34, v34, v81
	v_add_f32_e32 v26, v77, v26
	v_add_f32_e32 v76, v78, v76
	v_add_f32_e32 v27, v79, v27
	v_cvt_pk_bf16_f32 v24, v80, v24
	v_cvt_pk_bf16_f32 v25, v34, v25
	v_cvt_pk_bf16_f32 v26, v35, v26
	v_cvt_pk_bf16_f32 v27, v76, v27
	v_mov_b32_e32 v34, v3
	v_lshlrev_b32_e32 v76, 16, v24
	v_and_b32_e32 v77, 0xffff0000, v24
	v_lshlrev_b32_e32 v80, 16, v26
	v_and_b32_e32 v81, 0xffff0000, v26
	v_mov_b32_e32 v35, v3
	v_cvt_pk_fp8_f32 v34, v76, v77
	v_cvt_pk_fp8_f32 v35, v80, v81
	v_lshlrev_b32_e32 v78, 16, v25
	v_and_b32_e32 v79, 0xffff0000, v25
	v_lshlrev_b32_e32 v82, 16, v27
	v_and_b32_e32 v83, 0xffff0000, v27
	v_lshl_add_u64 v[30:31], s[44:45], 0, v[136:137]
	v_cvt_pk_fp8_f32 v34, v78, v79 op_sel:[0,0,1]
	v_cvt_pk_fp8_f32 v35, v82, v83 op_sel:[0,0,1]
	s_waitcnt lgkmcnt(0)
	v_lshlrev_b64 v[28:29], 10, v[132:133]
	v_lshl_add_u64 v[32:33], v[174:175], 1, v[30:31]
	global_store_dwordx4 v[32:33], v[24:27], off
	v_pk_mul_f32 v[68:69], v[68:69], s[80:81] op_sel_hi:[1,0]
	s_nop 0
	v_lshl_add_u64 v[24:25], s[48:49], 0, v[28:29]
	v_lshl_add_u64 v[24:25], v[24:25], 0, v[174:175]
	global_store_dwordx2 v[24:25], v[34:35], off
	v_mul_f32_e32 v24, v77, v77
	v_mul_f32_e32 v25, v79, v79
	v_fmac_f32_e32 v24, v76, v76
	v_fmac_f32_e32 v25, v78, v78
	v_add_f32_e32 v24, v24, v25
	v_mul_f32_e32 v25, v81, v81
	v_fmac_f32_e32 v25, v80, v80
	v_add_f32_e32 v24, v24, v25
	v_mul_f32_e32 v25, v83, v83
	v_fmac_f32_e32 v25, v82, v82
	v_pk_mul_f32 v[26:27], v[72:73], s[80:81] op_sel_hi:[1,0]
	v_pk_mul_f32 v[34:35], v[70:71], s[80:81] op_sel_hi:[1,0]
	s_waitcnt vmcnt(18)
	v_lshlrev_b32_e32 v70, 16, v20
	v_and_b32_e32 v20, 0xffff0000, v20
	v_add_f32_e32 v76, v24, v25
	v_pk_mul_f32 v[24:25], v[74:75], s[80:81] op_sel_hi:[1,0]
	v_add_f32_e32 v20, v27, v20
	v_lshlrev_b32_e32 v27, 16, v21
	v_and_b32_e32 v21, 0xffff0000, v21
	v_add_f32_e32 v24, v24, v27
	v_add_f32_e32 v21, v25, v21
	v_lshlrev_b32_e32 v25, 16, v22
	v_and_b32_e32 v22, 0xffff0000, v22
	v_lshlrev_b32_e32 v27, 16, v23
	v_and_b32_e32 v23, 0xffff0000, v23
	v_add_f32_e32 v26, v26, v70
	v_add_f32_e32 v22, v69, v22
	v_add_f32_e32 v23, v35, v23
	v_cvt_pk_bf16_f32 v20, v26, v20
	v_add_f32_e32 v25, v68, v25
	v_add_f32_e32 v27, v34, v27
	v_cvt_pk_bf16_f32 v21, v24, v21
	v_cvt_pk_bf16_f32 v22, v25, v22
	v_cvt_pk_bf16_f32 v23, v27, v23
	global_store_dwordx4 v[32:33], v[20:23], off offset:256
	v_lshlrev_b32_e32 v26, 16, v20
	v_mov_b32_e32 v24, v3
	v_and_b32_e32 v20, 0xffff0000, v20
	v_cvt_pk_fp8_f32 v24, v26, v20
	v_lshlrev_b32_e32 v27, 16, v21
	v_and_b32_e32 v21, 0xffff0000, v21
	v_mul_f32_e32 v20, v20, v20
	v_cvt_pk_fp8_f32 v24, v27, v21 op_sel:[0,0,1]
	v_mul_f32_e32 v21, v21, v21
	v_lshlrev_b32_e32 v32, 16, v22
	v_and_b32_e32 v22, 0xffff0000, v22
	v_fmac_f32_e32 v20, v26, v26
	v_fmac_f32_e32 v21, v27, v27
	v_add_f32_e32 v20, v20, v21
	v_mul_f32_e32 v21, v22, v22
	v_lshlrev_b32_e32 v33, 16, v23
	v_and_b32_e32 v23, 0xffff0000, v23
	v_fmac_f32_e32 v21, v32, v32
	v_add_f32_e32 v20, v20, v21
	v_mul_f32_e32 v21, v23, v23
	v_fmac_f32_e32 v21, v33, v33
	v_add_f32_e32 v20, v20, v21
	v_add_f32_e32 v26, v76, v20
	v_mov_b32_e32 v25, v3
	v_mov_b32_e32 v27, v26
	s_nop 1
	v_permlane16_swap_b32_e32 v27, v26
	v_cvt_pk_fp8_f32 v25, v32, v22
	v_sub_co_u32_e64 v20, s[42:43], 0, v28
	v_cvt_pk_fp8_f32 v25, v33, v23 op_sel:[0,0,1]
	s_nop 0
	v_subb_co_u32_e64 v21, s[42:43], 0, v29, s[42:43]
	v_lshl_add_u64 v[20:21], v[30:31], 0, v[20:21]
	v_lshl_add_u64 v[22:23], v[20:21], 0, v[174:175]
	s_waitcnt lgkmcnt(0)
	v_add_f32_e32 v20, v26, v27
	v_mov_b32_e32 v21, v20
	s_nop 1
	v_permlane32_swap_b32_e32 v21, v20
	v_add_co_u32_e64 v22, s[42:43], s15, v22
	s_nop 1
	v_addc_co_u32_e64 v23, s[42:43], 0, v23, s[42:43]
	global_store_dwordx2 v[22:23], v[24:25], off offset:128
	s_and_saveexec_b64 s[4:5], vcc
	s_cbranch_execz .LBB0_1602
	v_lshlrev_b64 v[22:23], 6, v[132:133]
	v_lshl_add_u64 v[22:23], s[46:47], 0, v[22:23]
	v_lshl_add_u64 v[22:23], s[60:61], 2, v[22:23]
	s_lshl_b32 s92, s22, 2
	v_lshl_add_u64 v[22:23], v[22:23], 0, s[92:93]
	s_waitcnt lgkmcnt(0)
	v_add_f32_e32 v20, v20, v21
	global_store_dword v[22:23], v20, off
; __device__ __forceinline__ float bflo(unsigned w) { return __uint_as_float(w << 16); }
; __device__ __forceinline__ float bfhi(unsigned w) { return __uint_as_float(w & 0xffff0000u); }
; __device__ __forceinline__ u32x4 pack8(const f32x4 a, const f32x4 b) { u32x4 w; w.x = cvt_pk_bf16(a[0], a[1]); w.y = cvt_pk_bf16(a[2], a[3]); w.z = cvt_pk_bf16(b[0], b[1]); w.w = cvt_pk_bf16(b[2], b[3]); return w; }
;     __device__ __forceinline__ void operator()(const f32x4 (&acc)[2][2][4][2], const Unit& u, int wr, int wc, int fr, int fq) const {
;     ...
;             if ((q & 1) == 0 && q + 2 < 8) {
; #pragma unroll
;                 for (int h2 = 0; h2 < 2; ++h2)
; #pragma unroll
;                     for (int bj = 0; bj < 2; ++bj) { const int qn = q + 2 + h2; xnxt[h2][bj] = *(const u32x4*)(X + (size_t)(row0 + (qn >> 2) * HALF + (qn & 3) * 16) * 1024 + col0 + bj * HALF); } }
; #pragma unroll
;                 for (int bj = 0; bj < 2; ++bj) { bf16_t* p = X + (size_t)row * 1024 + col0 + bj * HALF; const u32x4 xv = xcur[q & 1][bj];
;                     f32x4 a = acc[ai][bj][m][0] * scale, b = acc[ai][bj][m][1] * scale;
;                     a[0] += bflo(xv.x); a[1] += bfhi(xv.x); a[2] += bflo(xv.y); a[3] += bfhi(xv.y); b[0] += bflo(xv.z); b[1] += bfhi(xv.z); b[2] += bflo(xv.w); b[3] += bfhi(xv.w);
;                     const u32x4 w = pack8(a, b); *(u32x4*)p = w;
;                     if constexpr (WX8) { unsigned q0 = 0u, q1 = 0u; q0 = __builtin_amdgcn_cvt_pk_fp8_f32(bflo(w.x), bfhi(w.x), q0, false); q0 = __builtin_amdgcn_cvt_pk_fp8_f32(bflo(w.y), bfhi(w.y), q0, true); q1 = __builtin_amdgcn_cvt_pk_fp8_f32(bflo(w.z), bfhi(w.z), q1, false); q1 = __builtin_amdgcn_cvt_pk_fp8_f32(bflo(w.w), bfhi(w.w), q1, true);
;                         *(u32x2*)((unsigned char*)X + (WS_X8 - WS_X) + (size_t)row * 1024 + col0 + bj * HALF) = (u32x2){q0, q1}; }
;                     s += (bflo(w.x) * bflo(w.x) + bfhi(w.x) * bfhi(w.x)) + (bflo(w.y) * bflo(w.y) + bfhi(w.y) * bfhi(w.y)) + (bflo(w.z) * bflo(w.z) + bfhi(w.z) * bfhi(w.z)) + (bflo(w.w) * bflo(w.w) + bfhi(w.w) * bfhi(w.w)); }
;                 s += __shfl_xor(s, 16); s += __shfl_xor(s, 32);
;                 if (fq == 0) ssn[(size_t)row * 16 + u.pn * 4 + wc] = s;
.LBB0_1602:
	s_or_b64 exec, exec, s[4:5]
	v_pk_mul_f32 v[28:29], v[64:65], s[80:81] op_sel_hi:[1,0]
	s_waitcnt vmcnt(11)
	v_lshlrev_b32_e32 v34, 16, v16
	v_and_b32_e32 v16, 0xffff0000, v16
	v_pk_mul_f32 v[26:27], v[66:67], s[80:81] op_sel_hi:[1,0]
	v_add_f32_e32 v16, v29, v16
	v_lshlrev_b32_e32 v29, 16, v17
	v_and_b32_e32 v17, 0xffff0000, v17
	v_pk_mul_f32 v[30:31], v[62:63], s[80:81] op_sel_hi:[1,0]
	v_pk_mul_f32 v[32:33], v[60:61], s[80:81] op_sel_hi:[1,0]
	v_add_f32_e32 v26, v26, v29
	v_add_f32_e32 v17, v27, v17
	v_lshlrev_b32_e32 v27, 16, v18
	v_and_b32_e32 v18, 0xffff0000, v18
	v_lshlrev_b32_e32 v29, 16, v19
	v_and_b32_e32 v19, 0xffff0000, v19
	v_add_f32_e32 v28, v28, v34
	v_add_f32_e32 v27, v32, v27
	v_add_f32_e32 v18, v33, v18
	v_add_f32_e32 v29, v30, v29
	v_add_f32_e32 v19, v31, v19
	v_cvt_pk_bf16_f32 v16, v28, v16
	v_cvt_pk_bf16_f32 v17, v26, v17
	v_cvt_pk_bf16_f32 v18, v27, v18
	v_cvt_pk_bf16_f32 v19, v29, v19
	v_mov_b32_e32 v26, v3
	v_lshlrev_b32_e32 v28, 16, v16
	v_and_b32_e32 v29, 0xffff0000, v16
	v_lshlrev_b32_e32 v32, 16, v18
	v_and_b32_e32 v33, 0xffff0000, v18
	v_mov_b32_e32 v27, v3
	v_cvt_pk_fp8_f32 v26, v28, v29
	v_cvt_pk_fp8_f32 v27, v32, v33
	v_lshlrev_b32_e32 v30, 16, v17
	v_and_b32_e32 v31, 0xffff0000, v17
	v_lshlrev_b32_e32 v34, 16, v19
	v_and_b32_e32 v35, 0xffff0000, v19
	v_lshl_add_u64 v[22:23], s[44:45], 0, v[106:107]
	v_cvt_pk_fp8_f32 v26, v30, v31 op_sel:[0,0,1]
	v_cvt_pk_fp8_f32 v27, v34, v35 op_sel:[0,0,1]
	s_waitcnt lgkmcnt(0)
	v_lshlrev_b64 v[20:21], 10, v[102:103]
	v_lshl_add_u64 v[24:25], v[174:175], 1, v[22:23]
	global_store_dwordx4 v[24:25], v[16:19], off
	s_nop 1
	v_lshl_add_u64 v[16:17], s[48:49], 0, v[20:21]
	v_lshl_add_u64 v[16:17], v[16:17], 0, v[174:175]
	global_store_dwordx2 v[16:17], v[26:27], off
	v_mul_f32_e32 v16, v29, v29
	v_mul_f32_e32 v17, v31, v31
	v_fmac_f32_e32 v16, v28, v28
	v_fmac_f32_e32 v17, v30, v30
	v_add_f32_e32 v16, v16, v17
	v_mul_f32_e32 v17, v33, v33
	v_fmac_f32_e32 v17, v32, v32
	v_add_f32_e32 v16, v16, v17
	v_mul_f32_e32 v17, v35, v35
	v_fmac_f32_e32 v17, v34, v34
	v_pk_mul_f32 v[18:19], v[56:57], s[80:81] op_sel_hi:[1,0]
	s_waitcnt vmcnt(12)
	v_lshlrev_b32_e32 v31, 16, v12
	v_and_b32_e32 v12, 0xffff0000, v12
	v_add_f32_e32 v30, v16, v17
	v_pk_mul_f32 v[16:17], v[58:59], s[80:81] op_sel_hi:[1,0]
	v_add_f32_e32 v12, v19, v12
	v_lshlrev_b32_e32 v19, 16, v13
	v_and_b32_e32 v13, 0xffff0000, v13
	v_pk_mul_f32 v[26:27], v[54:55], s[80:81] op_sel_hi:[1,0]
	v_pk_mul_f32 v[28:29], v[52:53], s[80:81] op_sel_hi:[1,0]
	v_add_f32_e32 v16, v16, v19
	v_add_f32_e32 v13, v17, v13
	v_lshlrev_b32_e32 v17, 16, v14
	v_and_b32_e32 v14, 0xffff0000, v14
	v_lshlrev_b32_e32 v19, 16, v15
	v_and_b32_e32 v15, 0xffff0000, v15
	v_add_f32_e32 v18, v18, v31
	v_add_f32_e32 v14, v29, v14
	v_add_f32_e32 v15, v27, v15
	v_cvt_pk_bf16_f32 v12, v18, v12
	v_add_f32_e32 v17, v28, v17
	v_add_f32_e32 v19, v26, v19
	v_cvt_pk_bf16_f32 v13, v16, v13
	v_cvt_pk_bf16_f32 v14, v17, v14
	v_cvt_pk_bf16_f32 v15, v19, v15
	global_store_dwordx4 v[24:25], v[12:15], off offset:256
	v_lshlrev_b32_e32 v18, 16, v12
	v_mov_b32_e32 v16, v3
	v_and_b32_e32 v12, 0xffff0000, v12
	v_cvt_pk_fp8_f32 v16, v18, v12
	v_lshlrev_b32_e32 v19, 16, v13
	v_and_b32_e32 v13, 0xffff0000, v13
	v_mul_f32_e32 v12, v12, v12
	v_cvt_pk_fp8_f32 v16, v19, v13 op_sel:[0,0,1]
	v_mul_f32_e32 v13, v13, v13
	v_lshlrev_b32_e32 v24, 16, v14
	v_and_b32_e32 v14, 0xffff0000, v14
	v_fmac_f32_e32 v12, v18, v18
	v_fmac_f32_e32 v13, v19, v19
	v_add_f32_e32 v12, v12, v13
	v_mul_f32_e32 v13, v14, v14
	v_lshlrev_b32_e32 v25, 16, v15
	v_and_b32_e32 v15, 0xffff0000, v15
	v_fmac_f32_e32 v13, v24, v24
	v_add_f32_e32 v12, v12, v13
	v_mul_f32_e32 v13, v15, v15
	v_fmac_f32_e32 v13, v25, v25
	v_add_f32_e32 v12, v12, v13
	v_add_f32_e32 v18, v30, v12
	v_mov_b32_e32 v17, v3
	v_mov_b32_e32 v19, v18
	s_nop 1
	v_permlane16_swap_b32_e32 v19, v18
	v_cvt_pk_fp8_f32 v17, v24, v14
	v_sub_co_u32_e64 v12, s[42:43], 0, v20
	v_cvt_pk_fp8_f32 v17, v25, v15 op_sel:[0,0,1]
	s_nop 0
	v_subb_co_u32_e64 v13, s[42:43], 0, v21, s[42:43]
	v_lshl_add_u64 v[12:13], v[22:23], 0, v[12:13]
	v_lshl_add_u64 v[14:15], v[12:13], 0, v[174:175]
	s_waitcnt lgkmcnt(0)
	v_add_f32_e32 v12, v18, v19
	v_mov_b32_e32 v13, v12
	s_nop 1
	v_permlane32_swap_b32_e32 v13, v12
	v_add_co_u32_e64 v14, s[42:43], s15, v14
	s_nop 1
	v_addc_co_u32_e64 v15, s[42:43], 0, v15, s[42:43]
	global_store_dwordx2 v[14:15], v[16:17], off offset:128
	s_and_saveexec_b64 s[4:5], vcc
	s_cbranch_execz .LBB0_1604
	v_lshlrev_b64 v[14:15], 6, v[102:103]
	v_lshl_add_u64 v[14:15], s[46:47], 0, v[14:15]
	v_lshl_add_u64 v[14:15], s[60:61], 2, v[14:15]
	s_lshl_b32 s92, s22, 2
	v_lshl_add_u64 v[14:15], v[14:15], 0, s[92:93]
	s_waitcnt lgkmcnt(0)
	v_add_f32_e32 v12, v12, v13
	global_store_dword v[14:15], v12, off
; __device__ __forceinline__ float bflo(unsigned w) { return __uint_as_float(w << 16); }
; __device__ __forceinline__ float bfhi(unsigned w) { return __uint_as_float(w & 0xffff0000u); }
; __device__ __forceinline__ u32x4 pack8(const f32x4 a, const f32x4 b) { u32x4 w; w.x = cvt_pk_bf16(a[0], a[1]); w.y = cvt_pk_bf16(a[2], a[3]); w.z = cvt_pk_bf16(b[0], b[1]); w.w = cvt_pk_bf16(b[2], b[3]); return w; }
;     __device__ __forceinline__ void operator()(const f32x4 (&acc)[2][2][4][2], const Unit& u, int wr, int wc, int fr, int fq) const {
;     ...
;             if ((q & 1) == 0 && q + 2 < 8) {
; #pragma unroll
;                 for (int h2 = 0; h2 < 2; ++h2)
; #pragma unroll
;                     for (int bj = 0; bj < 2; ++bj) { const int qn = q + 2 + h2; xnxt[h2][bj] = *(const u32x4*)(X + (size_t)(row0 + (qn >> 2) * HALF + (qn & 3) * 16) * 1024 + col0 + bj * HALF); } }
; #pragma unroll
;                 for (int bj = 0; bj < 2; ++bj) { bf16_t* p = X + (size_t)row * 1024 + col0 + bj * HALF; const u32x4 xv = xcur[q & 1][bj];
;                     f32x4 a = acc[ai][bj][m][0] * scale, b = acc[ai][bj][m][1] * scale;
;                     a[0] += bflo(xv.x); a[1] += bfhi(xv.x); a[2] += bflo(xv.y); a[3] += bfhi(xv.y); b[0] += bflo(xv.z); b[1] += bfhi(xv.z); b[2] += bflo(xv.w); b[3] += bfhi(xv.w);
;                     const u32x4 w = pack8(a, b); *(u32x4*)p = w;
;                     if constexpr (WX8) { unsigned q0 = 0u, q1 = 0u; q0 = __builtin_amdgcn_cvt_pk_fp8_f32(bflo(w.x), bfhi(w.x), q0, false); q0 = __builtin_amdgcn_cvt_pk_fp8_f32(bflo(w.y), bfhi(w.y), q0, true); q1 = __builtin_amdgcn_cvt_pk_fp8_f32(bflo(w.z), bfhi(w.z), q1, false); q1 = __builtin_amdgcn_cvt_pk_fp8_f32(bflo(w.w), bfhi(w.w), q1, true);
;                         *(u32x2*)((unsigned char*)X + (WS_X8 - WS_X) + (size_t)row * 1024 + col0 + bj * HALF) = (u32x2){q0, q1}; }
;                     s += (bflo(w.x) * bflo(w.x) + bfhi(w.x) * bfhi(w.x)) + (bflo(w.y) * bflo(w.y) + bfhi(w.y) * bfhi(w.y)) + (bflo(w.z) * bflo(w.z) + bfhi(w.z) * bfhi(w.z)) + (bflo(w.w) * bflo(w.w) + bfhi(w.w) * bfhi(w.w)); }
;                 s += __shfl_xor(s, 16); s += __shfl_xor(s, 32);
;                 if (fq == 0) ssn[(size_t)row * 16 + u.pn * 4 + wc] = s;
.LBB0_1604:
	s_or_b64 exec, exec, s[4:5]
	v_pk_mul_f32 v[20:21], v[48:49], s[80:81] op_sel_hi:[1,0]
	s_waitcnt vmcnt(13)
	v_lshlrev_b32_e32 v26, 16, v8
	v_and_b32_e32 v8, 0xffff0000, v8
	v_pk_mul_f32 v[18:19], v[50:51], s[80:81] op_sel_hi:[1,0]
	v_add_f32_e32 v8, v21, v8
	v_lshlrev_b32_e32 v21, 16, v9
	v_and_b32_e32 v9, 0xffff0000, v9
	v_pk_mul_f32 v[22:23], v[46:47], s[80:81] op_sel_hi:[1,0]
	v_pk_mul_f32 v[24:25], v[44:45], s[80:81] op_sel_hi:[1,0]
	v_add_f32_e32 v18, v18, v21
	v_add_f32_e32 v9, v19, v9
	v_lshlrev_b32_e32 v19, 16, v10
	v_and_b32_e32 v10, 0xffff0000, v10
	v_lshlrev_b32_e32 v21, 16, v11
	v_and_b32_e32 v11, 0xffff0000, v11
	v_add_f32_e32 v20, v20, v26
	v_add_f32_e32 v19, v24, v19
	v_add_f32_e32 v10, v25, v10
	v_add_f32_e32 v21, v22, v21
	v_add_f32_e32 v11, v23, v11
	v_cvt_pk_bf16_f32 v8, v20, v8
	v_cvt_pk_bf16_f32 v9, v18, v9
	v_cvt_pk_bf16_f32 v10, v19, v10
	v_cvt_pk_bf16_f32 v11, v21, v11
	v_mov_b32_e32 v18, v3
	v_lshlrev_b32_e32 v20, 16, v8
	v_and_b32_e32 v21, 0xffff0000, v8
	v_lshlrev_b32_e32 v24, 16, v10
	v_and_b32_e32 v25, 0xffff0000, v10
	v_mov_b32_e32 v19, v3
	v_cvt_pk_fp8_f32 v18, v20, v21
	v_cvt_pk_fp8_f32 v19, v24, v25
	v_lshlrev_b32_e32 v22, 16, v9
	v_and_b32_e32 v23, 0xffff0000, v9
	v_lshlrev_b32_e32 v26, 16, v11
	v_and_b32_e32 v27, 0xffff0000, v11
	v_lshl_add_u64 v[14:15], s[44:45], 0, v[104:105]
	v_cvt_pk_fp8_f32 v18, v22, v23 op_sel:[0,0,1]
	v_cvt_pk_fp8_f32 v19, v26, v27 op_sel:[0,0,1]
	s_waitcnt lgkmcnt(0)
	v_lshlrev_b64 v[12:13], 10, v[100:101]
	v_lshl_add_u64 v[16:17], v[174:175], 1, v[14:15]
	global_store_dwordx4 v[16:17], v[8:11], off
	s_nop 1
	v_lshl_add_u64 v[8:9], s[48:49], 0, v[12:13]
	v_lshl_add_u64 v[8:9], v[8:9], 0, v[174:175]
	global_store_dwordx2 v[8:9], v[18:19], off
	v_mul_f32_e32 v8, v21, v21
	v_mul_f32_e32 v9, v23, v23
	v_fmac_f32_e32 v8, v20, v20
	v_fmac_f32_e32 v9, v22, v22
	v_add_f32_e32 v8, v8, v9
	v_mul_f32_e32 v9, v25, v25
	v_fmac_f32_e32 v9, v24, v24
	v_add_f32_e32 v8, v8, v9
	v_mul_f32_e32 v9, v27, v27
	v_fmac_f32_e32 v9, v26, v26
	v_pk_mul_f32 v[10:11], v[40:41], s[80:81] op_sel_hi:[1,0]
	s_waitcnt vmcnt(14)
	v_lshlrev_b32_e32 v23, 16, v4
	v_and_b32_e32 v4, 0xffff0000, v4
	v_add_f32_e32 v22, v8, v9
	v_pk_mul_f32 v[8:9], v[42:43], s[80:81] op_sel_hi:[1,0]
	v_add_f32_e32 v4, v11, v4
	v_lshlrev_b32_e32 v11, 16, v5
	v_and_b32_e32 v5, 0xffff0000, v5
	v_pk_mul_f32 v[18:19], v[38:39], s[80:81] op_sel_hi:[1,0]
	v_pk_mul_f32 v[20:21], v[36:37], s[80:81] op_sel_hi:[1,0]
	v_add_f32_e32 v8, v8, v11
	v_add_f32_e32 v5, v9, v5
	v_lshlrev_b32_e32 v9, 16, v6
	v_and_b32_e32 v6, 0xffff0000, v6
	v_lshlrev_b32_e32 v11, 16, v7
	v_and_b32_e32 v7, 0xffff0000, v7
	v_add_f32_e32 v10, v10, v23
	v_add_f32_e32 v6, v21, v6
	v_add_f32_e32 v7, v19, v7
	v_cvt_pk_bf16_f32 v4, v10, v4
	v_add_f32_e32 v9, v20, v9
	v_add_f32_e32 v11, v18, v11
	v_cvt_pk_bf16_f32 v5, v8, v5
	v_cvt_pk_bf16_f32 v6, v9, v6
	v_cvt_pk_bf16_f32 v7, v11, v7
	global_store_dwordx4 v[16:17], v[4:7], off offset:256
	v_lshlrev_b32_e32 v10, 16, v4
	v_mov_b32_e32 v8, v3
	v_and_b32_e32 v4, 0xffff0000, v4
	v_cvt_pk_fp8_f32 v8, v10, v4
	v_lshlrev_b32_e32 v11, 16, v5
	v_and_b32_e32 v5, 0xffff0000, v5
	v_mul_f32_e32 v4, v4, v4
	v_cvt_pk_fp8_f32 v8, v11, v5 op_sel:[0,0,1]
	v_mul_f32_e32 v5, v5, v5
	v_lshlrev_b32_e32 v16, 16, v6
	v_and_b32_e32 v6, 0xffff0000, v6
	v_fmac_f32_e32 v4, v10, v10
	v_fmac_f32_e32 v5, v11, v11
	v_add_f32_e32 v4, v4, v5
	v_mul_f32_e32 v5, v6, v6
	v_lshlrev_b32_e32 v17, 16, v7
	v_and_b32_e32 v7, 0xffff0000, v7
	v_fmac_f32_e32 v5, v16, v16
	v_add_f32_e32 v4, v4, v5
	v_mul_f32_e32 v5, v7, v7
	v_fmac_f32_e32 v5, v17, v17
	v_add_f32_e32 v4, v4, v5
	v_add_f32_e32 v10, v22, v4
	v_mov_b32_e32 v9, v3
	v_mov_b32_e32 v11, v10
	s_nop 1
	v_permlane16_swap_b32_e32 v11, v10
	v_cvt_pk_fp8_f32 v9, v16, v6
	v_sub_co_u32_e64 v4, s[42:43], 0, v12
	v_cvt_pk_fp8_f32 v9, v17, v7 op_sel:[0,0,1]
	s_nop 0
	v_subb_co_u32_e64 v5, s[42:43], 0, v13, s[42:43]
	v_lshl_add_u64 v[4:5], v[14:15], 0, v[4:5]
	v_lshl_add_u64 v[6:7], v[4:5], 0, v[174:175]
	s_waitcnt lgkmcnt(0)
	v_add_f32_e32 v4, v10, v11
	v_mov_b32_e32 v5, v4
	s_nop 1
	v_permlane32_swap_b32_e32 v5, v4
	v_add_co_u32_e64 v6, s[42:43], s15, v6
	s_nop 1
	v_addc_co_u32_e64 v7, s[42:43], 0, v7, s[42:43]
	global_store_dwordx2 v[6:7], v[8:9], off offset:128
	s_and_saveexec_b64 s[4:5], vcc
	s_cbranch_execz .LBB0_1606
	v_lshlrev_b64 v[6:7], 6, v[100:101]
	v_lshl_add_u64 v[6:7], s[46:47], 0, v[6:7]
	v_lshl_add_u64 v[6:7], s[60:61], 2, v[6:7]
	s_lshl_b32 s92, s22, 2
	v_lshl_add_u64 v[6:7], v[6:7], 0, s[92:93]
	s_waitcnt lgkmcnt(0)
	v_add_f32_e32 v4, v4, v5
	global_store_dword v[6:7], v4, off

; __device__ __forceinline__ float rstd_fin4(const f32x4 a) { float s = (a[0] + a[1]) + (a[2] + a[3]); s += __shfl_xor(s, 16); s += __shfl_xor(s, 32); return __builtin_amdgcn_rsqf(s * (1.f / 1024.f) + 1e-6f); }
;     __device__ __forceinline__ void operator()(const f32x4 (&acc)[2][2][4][2], const Unit& u, int wr, int wc, int fr, int fq) const {
;     ...
;         const int row0 = u.pm * BM + wr * 64 + fr;
;         unsigned char* const hb = (unsigned char*)H + (size_t)(u.pm * (FFH / 128) + u.pn + pn0) * 32768 + (((wr * 4 + wc) * 8) * 64 + (fq >> 1) * 32 + fr * 2 + (fq & 1)) * 8;
;         f32x4 pa[2][4];
; #pragma unroll
;         for (int ai = 0; ai < 2; ++ai)
; #pragma unroll
;             for (int m = 0; m < 4; ++m) pa[ai][m] = rstd_ld4(ss, row0 + ai * HALF + m * 16, fq);
; #pragma unroll
;         for (int ai = 0; ai < 2; ++ai)
; #pragma unroll
;             for (int m = 0; m < 4; ++m) { const float rs = rstd_fin4(pa[ai][m]) * sc;
;                 const float rsl = rs * 1.4426950408889634f, rsu = rs * 0.6931471805599453f;
;                 f32x4 h0, h1;
; #pragma unroll
;                 for (int n = 0; n < 2; ++n) { const f32x4 G = acc[ai][0][m][n], U = acc[ai][1][m][n]; f32x4 hv;
; #pragma unroll
;                     for (int q = 0; q < 2; ++q) { const f32x2 g2 = (f32x2){G[2 * q], G[2 * q + 1]} * rsl, u2 = (f32x2){U[2 * q], U[2 * q + 1]} * rsu;
;                         f32x2 r2; r2.x = __builtin_amdgcn_rcpf(1.f + __builtin_amdgcn_exp2f(-g2.x)); r2.y = __builtin_amdgcn_rcpf(1.f + __builtin_amdgcn_exp2f(-g2.y));
;                         const f32x2 o2 = g2 * u2 * r2; hv[2 * q] = o2.x; hv[2 * q + 1] = o2.y; }
;                     if (n == 0) h0 = hv; else h1 = hv; }
;                 unsigned w0 = 0u, w1 = 0u;
;                 w0 = __builtin_amdgcn_cvt_pk_fp8_f32(h0[0], h0[1], w0, false); w0 = __builtin_amdgcn_cvt_pk_fp8_f32(h0[2], h0[3], w0, true); w1 = __builtin_amdgcn_cvt_pk_fp8_f32(h1[0], h1[1], w1, false); w1 = __builtin_amdgcn_cvt_pk_fp8_f32(h1[2], h1[3], w1, true);
;                 *(u32x2*)(hb + (ai * 4 + m) * 512) = (u32x2){w0, w1}; asm volatile("" ::: "memory"); }
.LBB0_1674:
	s_lshl_b32 s4, s72, 8
	v_mov_b32_e32 v14, v1
	v_mov_b32_e32 v15, v182
	s_add_i32 s4, s4, s66
	v_and_b32_e32 v17, 64, v246
	v_add_u32_e32 v4, s4, v14
	v_lshlrev_b32_e32 v6, 2, v15
	v_ashrrev_i32_e32 v7, 31, v6
	v_ashrrev_i32_e32 v5, 31, v4
	v_lshl_add_u64 v[6:7], v[6:7], 2, s[44:45]
	v_lshlrev_b64 v[4:5], 6, v[4:5]
	v_lshl_add_u64 v[12:13], v[6:7], 0, v[4:5]
	global_load_dwordx4 v[4:7], v[12:13], off
	global_load_dwordx4 v[8:11], v[12:13], off offset:1024
	global_load_dwordx4 v[28:31], v[12:13], off offset:2048
	global_load_dwordx4 v[20:23], v[12:13], off offset:3072
	v_xor_b32_e32 v16, 16, v246
	v_add_u32_e32 v17, 64, v17
	v_xor_b32_e32 v18, 32, v246
	v_cmp_lt_i32_e32 vcc, v16, v17
	v_mov_b32_e32 v32, v3
	v_mov_b32_e32 v33, v3
	v_cndmask_b32_e32 v16, v246, v16, vcc
	v_cmp_lt_i32_e32 vcc, v18, v17
	v_lshlrev_b32_e32 v27, 2, v16
	s_mul_i32 s4, s72, 22
	v_cndmask_b32_e32 v17, v246, v18, vcc
	v_lshlrev_b32_e32 v26, 2, v17
	s_add_i32 s4, s4, s71
	s_ashr_i32 s5, s4, 31
	v_lshlrev_b32_e32 v19, 4, v15
	v_lshl_add_u32 v14, v14, 1, s69
	s_lshl_b64 s[4:5], s[4:5], 15
	v_and_b32_e32 v18, 0x1fffffe0, v19
	v_and_or_b32 v14, v15, 1, v14
	v_add_lshl_u32 v14, v14, v18, 3
	s_add_u32 s4, s6, s4
	v_ashrrev_i32_e32 v15, 31, v14
	s_addc_u32 s5, s7, s5
	v_lshl_add_u64 v[24:25], s[4:5], 0, v[14:15]
	s_mov_b64 s[4:5], -1
	s_waitcnt vmcnt(0)
	v_mov_b32_e32 v16, v5
	v_mov_b32_e32 v17, v6
	v_mov_b32_e32 v5, v7
	v_mov_b32_e32 v6, v9
	v_mov_b32_e32 v7, v10
	v_mov_b32_e32 v9, v11
	v_pk_add_f32 v[4:5], v[16:17], v[4:5]
	v_pk_add_f32 v[6:7], v[6:7], v[8:9]
	v_add_f32_e32 v8, v4, v5
	v_add_f32_e32 v6, v6, v7
	v_mov_b32_e32 v7, v8
	s_nop 1
	v_permlane16_swap_b32_e32 v7, v8
	v_mov_b32_e32 v9, v6
	s_nop 1
	v_permlane16_swap_b32_e32 v9, v6
	v_add_co_u32_e32 v4, vcc, s88, v12
	s_waitcnt lgkmcnt(1)
	v_add_f32_e32 v7, v8, v7
	s_waitcnt lgkmcnt(0)
	v_add_f32_e32 v6, v6, v9
	v_mov_b32_e32 v8, v7
	s_nop 1
	v_permlane32_swap_b32_e32 v8, v7
	v_mov_b32_e32 v9, v6
	s_nop 1
	v_permlane32_swap_b32_e32 v9, v6
	v_addc_co_u32_e32 v5, vcc, 0, v13, vcc
	global_load_dwordx4 v[16:19], v[4:5], off
	global_load_dwordx4 v[12:15], v[4:5], off offset:1024
	s_waitcnt lgkmcnt(1)
	v_add_f32_e32 v7, v7, v8
	s_waitcnt lgkmcnt(0)
	v_add_f32_e32 v6, v6, v9
	v_fmamk_f32 v7, v7, 0x3a800000, v227
	v_fmamk_f32 v6, v6, 0x3a800000, v227
	v_rsq_f32_e32 v34, v7
	v_rsq_f32_e32 v35, v6
	global_load_dwordx4 v[8:11], v[4:5], off offset:2048
	s_nop 0
	global_load_dwordx4 v[4:7], v[4:5], off offset:3072
	s_andn2_b64 vcc, exec, s[40:41]
	v_mul_f32_e32 v174, 0x3c800000, v34
	v_mul_f32_e32 v35, 0x3c800000, v35
	v_mul_f32_e32 v34, 0x3fb8aa3b, v174
	v_mul_f32_e32 v174, 0x3f317218, v174
	v_pk_mul_f32 v[160:161], v[160:161], v[34:35] op_sel_hi:[1,0]
	v_pk_mul_f32 v[152:153], v[152:153], v[174:175] op_sel_hi:[1,0]
	v_pk_mul_f32 v[162:163], v[162:163], v[34:35] op_sel_hi:[1,0]
	v_pk_mul_f32 v[154:155], v[154:155], v[174:175] op_sel_hi:[1,0]
	v_pk_mul_f32 v[156:157], v[156:157], v[34:35] op_sel_hi:[1,0]
	v_mul_f32_e32 v176, 0x3fb8aa3b, v35
	v_mul_f32_e32 v178, 0x3f317218, v35
	v_pk_mul_f32 v[148:149], v[148:149], v[174:175] op_sel_hi:[1,0]
	v_pk_mul_f32 v[34:35], v[158:159], v[34:35] op_sel_hi:[1,0]
	v_exp_f32_e64 v158, -v160
	v_exp_f32_e64 v159, -v161
	v_pk_mul_f32 v[152:153], v[160:161], v[152:153]
	v_exp_f32_e64 v160, -v162
	v_exp_f32_e64 v161, -v163
	v_pk_mul_f32 v[154:155], v[162:163], v[154:155]
	v_exp_f32_e64 v162, -v156
	v_exp_f32_e64 v163, -v157
	v_pk_mul_f32 v[148:149], v[156:157], v[148:149]
	v_exp_f32_e64 v156, -v34
	v_exp_f32_e64 v157, -v35
	v_pk_mul_f32 v[150:151], v[150:151], v[174:175] op_sel_hi:[1,0]
	v_pk_mul_f32 v[144:145], v[144:145], v[176:177] op_sel_hi:[1,0]
	v_pk_mul_f32 v[34:35], v[34:35], v[150:151]
	v_add_f32_e32 v150, 1.0, v158
	v_add_f32_e32 v151, 1.0, v159
	v_add_f32_e32 v158, 1.0, v160
	v_add_f32_e32 v159, 1.0, v161
	v_add_f32_e32 v160, 1.0, v162
	v_add_f32_e32 v161, 1.0, v163
	v_add_f32_e32 v162, 1.0, v156
	v_add_f32_e32 v163, 1.0, v157
	v_rcp_f32_e32 v150, v150
	v_rcp_f32_e32 v151, v151
	v_rcp_f32_e32 v156, v158
	v_rcp_f32_e32 v157, v159
	v_rcp_f32_e32 v158, v160
	v_rcp_f32_e32 v159, v161
	v_rcp_f32_e32 v160, v162
	v_rcp_f32_e32 v161, v163
	v_pk_mul_f32 v[150:151], v[152:153], v[150:151]
	v_pk_mul_f32 v[148:149], v[148:149], v[158:159]
	v_cvt_pk_fp8_f32 v32, v150, v151
	v_cvt_pk_fp8_f32 v33, v148, v149
	v_pk_mul_f32 v[148:149], v[154:155], v[156:157]
	v_pk_mul_f32 v[34:35], v[34:35], v[160:161]
	v_cvt_pk_fp8_f32 v32, v148, v149 op_sel:[0,0,1]
	v_cvt_pk_fp8_f32 v33, v34, v35 op_sel:[0,0,1]
	v_exp_f32_e64 v35, -v145
	v_exp_f32_e64 v174, -v144
	v_pk_mul_f32 v[136:137], v[136:137], v[178:179] op_sel_hi:[1,0]
	global_store_dwordx2 v[24:25], v[32:33], off
	v_add_f32_e32 v32, 1.0, v35
	v_add_f32_e32 v34, 1.0, v174
	v_rcp_f32_e32 v35, v32
	v_pk_mul_f32 v[32:33], v[144:145], v[136:137]
	v_pk_mul_f32 v[136:137], v[146:147], v[176:177] op_sel_hi:[1,0]
	v_rcp_f32_e32 v34, v34
	v_exp_f32_e64 v144, -v136
	v_exp_f32_e64 v145, -v137
	v_pk_mul_f32 v[132:133], v[132:133], v[178:179] op_sel_hi:[1,0]
	v_pk_mul_f32 v[32:33], v[32:33], v[34:35]
	v_pk_mul_f32 v[34:35], v[138:139], v[178:179] op_sel_hi:[1,0]
	v_add_f32_e32 v138, 1.0, v144
	v_add_f32_e32 v139, 1.0, v145
	v_rcp_f32_e32 v138, v138
	v_rcp_f32_e32 v139, v139
	v_pk_mul_f32 v[34:35], v[136:137], v[34:35]
	v_pk_mul_f32 v[136:137], v[140:141], v[176:177] op_sel_hi:[1,0]
	v_pk_mul_f32 v[134:135], v[134:135], v[178:179] op_sel_hi:[1,0]
	v_exp_f32_e64 v140, -v136
	v_pk_mul_f32 v[34:35], v[34:35], v[138:139]
	v_exp_f32_e64 v139, -v137
	v_pk_mul_f32 v[132:133], v[136:137], v[132:133]
	v_mov_b32_e32 v136, v29
	v_mov_b32_e32 v137, v30
	v_mov_b32_e32 v29, v31
	v_pk_add_f32 v[28:29], v[136:137], v[28:29]
	v_add_f32_e32 v138, 1.0, v140
	v_add_f32_e32 v136, v28, v29
	v_mov_b32_e32 v137, v136
	s_nop 1
	v_permlane16_swap_b32_e32 v137, v136
	v_add_f32_e32 v139, 1.0, v139
	v_rcp_f32_e32 v138, v138
	v_rcp_f32_e32 v139, v139
	v_pk_mul_f32 v[140:141], v[142:143], v[176:177] op_sel_hi:[1,0]
	s_waitcnt lgkmcnt(0)
; __device__ __forceinline__ float rstd_fin4(const f32x4 a) { float s = (a[0] + a[1]) + (a[2] + a[3]); s += __shfl_xor(s, 16); s += __shfl_xor(s, 32); return __builtin_amdgcn_rsqf(s * (1.f / 1024.f) + 1e-6f); }
;     __device__ __forceinline__ void operator()(const f32x4 (&acc)[2][2][4][2], const Unit& u, int wr, int wc, int fr, int fq) const {
;     ...
;         const int row0 = u.pm * BM + wr * 64 + fr;
;         unsigned char* const hb = (unsigned char*)H + (size_t)(u.pm * (FFH / 128) + u.pn + pn0) * 32768 + (((wr * 4 + wc) * 8) * 64 + (fq >> 1) * 32 + fr * 2 + (fq & 1)) * 8;
;         f32x4 pa[2][4];
; #pragma unroll
;         for (int ai = 0; ai < 2; ++ai)
; #pragma unroll
;             for (int m = 0; m < 4; ++m) pa[ai][m] = rstd_ld4(ss, row0 + ai * HALF + m * 16, fq);
; #pragma unroll
;         for (int ai = 0; ai < 2; ++ai)
; #pragma unroll
;             for (int m = 0; m < 4; ++m) { const float rs = rstd_fin4(pa[ai][m]) * sc;
;                 const float rsl = rs * 1.4426950408889634f, rsu = rs * 0.6931471805599453f;
;                 f32x4 h0, h1;
; #pragma unroll
;                 for (int n = 0; n < 2; ++n) { const f32x4 G = acc[ai][0][m][n], U = acc[ai][1][m][n]; f32x4 hv;
; #pragma unroll
;                     for (int q = 0; q < 2; ++q) { const f32x2 g2 = (f32x2){G[2 * q], G[2 * q + 1]} * rsl, u2 = (f32x2){U[2 * q], U[2 * q + 1]} * rsu;
;                         f32x2 r2; r2.x = __builtin_amdgcn_rcpf(1.f + __builtin_amdgcn_exp2f(-g2.x)); r2.y = __builtin_amdgcn_rcpf(1.f + __builtin_amdgcn_exp2f(-g2.y));
;                         const f32x2 o2 = g2 * u2 * r2; hv[2 * q] = o2.x; hv[2 * q + 1] = o2.y; }
;                     if (n == 0) h0 = hv; else h1 = hv; }
;                 unsigned w0 = 0u, w1 = 0u;
;                 w0 = __builtin_amdgcn_cvt_pk_fp8_f32(h0[0], h0[1], w0, false); w0 = __builtin_amdgcn_cvt_pk_fp8_f32(h0[2], h0[3], w0, true); w1 = __builtin_amdgcn_cvt_pk_fp8_f32(h1[0], h1[1], w1, false); w1 = __builtin_amdgcn_cvt_pk_fp8_f32(h1[2], h1[3], w1, true);
;                 *(u32x2*)(hb + (ai * 4 + m) * 512) = (u32x2){w0, w1}; asm volatile("" ::: "memory"); }
	v_add_f32_e32 v136, v136, v137
	v_mov_b32_e32 v137, v136
	s_nop 1
	v_permlane32_swap_b32_e32 v137, v136
	v_exp_f32_e64 v142, -v140
	v_pk_mul_f32 v[132:133], v[132:133], v[138:139]
	v_exp_f32_e64 v139, -v141
	v_pk_mul_f32 v[30:31], v[140:141], v[134:135]
	v_mov_b32_e32 v134, v3
	v_add_f32_e32 v138, 1.0, v142
	v_add_f32_e32 v29, 1.0, v139
	v_cvt_pk_fp8_f32 v134, v32, v33
	s_waitcnt lgkmcnt(0)
	v_add_f32_e32 v32, v136, v137
	v_rcp_f32_e32 v28, v138
	v_rcp_f32_e32 v29, v29
	v_mov_b32_e32 v135, v3
	v_fmamk_f32 v32, v32, 0x3a800000, v227
	v_cvt_pk_fp8_f32 v135, v132, v133
	v_rsq_f32_e32 v32, v32
	v_pk_mul_f32 v[28:29], v[30:31], v[28:29]
	v_cvt_pk_fp8_f32 v134, v34, v35 op_sel:[0,0,1]
	v_cvt_pk_fp8_f32 v135, v28, v29 op_sel:[0,0,1]
	v_mul_f32_e32 v29, 0x3c800000, v32
	v_mul_f32_e32 v28, 0x3fb8aa3b, v29
	v_pk_mul_f32 v[30:31], v[128:129], v[28:29] op_sel_hi:[1,0]
	v_mul_f32_e32 v32, 0x3f317218, v29
	v_exp_f32_e64 v33, -v30
	v_exp_f32_e64 v29, -v31
	global_store_dwordx2 v[24:25], v[134:135], off offset:512
	v_pk_mul_f32 v[34:35], v[120:121], v[32:33] op_sel_hi:[1,0]
	v_add_f32_e32 v29, 1.0, v29
	v_pk_mul_f32 v[30:31], v[30:31], v[34:35]
	v_pk_mul_f32 v[34:35], v[130:131], v[28:29] op_sel_hi:[1,0]
	v_add_f32_e32 v33, 1.0, v33
	v_rcp_f32_e32 v121, v29
	v_exp_f32_e64 v29, -v34
	v_rcp_f32_e32 v120, v33
	v_exp_f32_e64 v33, -v35
	v_add_f32_e32 v29, 1.0, v29
	v_pk_mul_f32 v[30:31], v[30:31], v[120:121]
	v_pk_mul_f32 v[120:121], v[122:123], v[32:33] op_sel_hi:[1,0]
	v_rcp_f32_e32 v122, v29
	v_add_f32_e32 v29, 1.0, v33
	v_pk_mul_f32 v[34:35], v[34:35], v[120:121]
	v_pk_mul_f32 v[120:121], v[124:125], v[28:29] op_sel_hi:[1,0]
	v_rcp_f32_e32 v123, v29
	v_exp_f32_e64 v29, -v120
	v_exp_f32_e64 v33, -v121
	v_pk_mul_f32 v[34:35], v[34:35], v[122:123]
	v_add_f32_e32 v29, 1.0, v29
	v_rcp_f32_e32 v122, v29
	v_add_f32_e32 v29, 1.0, v33
	v_pk_mul_f32 v[116:117], v[116:117], v[32:33] op_sel_hi:[1,0]
	v_rcp_f32_e32 v123, v29
	v_pk_mul_f32 v[28:29], v[126:127], v[28:29] op_sel_hi:[1,0]
	v_pk_mul_f32 v[116:117], v[120:121], v[116:117]
	v_exp_f32_e64 v120, -v28
	v_exp_f32_e64 v121, -v29
	v_pk_mul_f32 v[32:33], v[118:119], v[32:33] op_sel_hi:[1,0]
	v_pk_mul_f32 v[116:117], v[116:117], v[122:123]
	v_add_f32_e32 v118, 1.0, v120
	v_add_f32_e32 v119, 1.0, v121
	v_mov_b32_e32 v120, v21
	v_mov_b32_e32 v121, v22
	v_mov_b32_e32 v21, v23
	v_pk_add_f32 v[20:21], v[120:121], v[20:21]
	v_rcp_f32_e32 v118, v118
	v_add_f32_e32 v22, v20, v21
	v_mov_b32_e32 v23, v22
	s_nop 1
	v_permlane16_swap_b32_e32 v23, v22
	v_mov_b32_e32 v20, v3
	v_cvt_pk_fp8_f32 v20, v30, v31
	v_rcp_f32_e32 v119, v119
	v_mov_b32_e32 v21, v3
	s_waitcnt lgkmcnt(0)
	v_add_f32_e32 v30, v22, v23
	v_mov_b32_e32 v31, v30
	s_nop 1
	v_permlane32_swap_b32_e32 v31, v30
	v_cvt_pk_fp8_f32 v21, v116, v117
	v_pk_mul_f32 v[22:23], v[28:29], v[32:33]
	v_cvt_pk_fp8_f32 v20, v34, v35 op_sel:[0,0,1]
	v_pk_mul_f32 v[22:23], v[22:23], v[118:119]
	s_nop 0
	v_cvt_pk_fp8_f32 v21, v22, v23 op_sel:[0,0,1]
	s_waitcnt lgkmcnt(0)
	v_add_f32_e32 v22, v30, v31
	v_fmamk_f32 v22, v22, 0x3a800000, v227
	v_rsq_f32_e32 v22, v22
	global_store_dwordx2 v[24:25], v[20:21], off offset:1024
	v_mul_f32_e32 v21, 0x3c800000, v22
	v_mul_f32_e32 v20, 0x3fb8aa3b, v21
	v_pk_mul_f32 v[22:23], v[112:113], v[20:21] op_sel_hi:[1,0]
	v_mul_f32_e32 v28, 0x3f317218, v21
	v_exp_f32_e64 v29, -v22
	v_exp_f32_e64 v21, -v23
	v_pk_mul_f32 v[30:31], v[104:105], v[28:29] op_sel_hi:[1,0]
	v_add_f32_e32 v21, 1.0, v21
	v_pk_mul_f32 v[22:23], v[22:23], v[30:31]
	v_pk_mul_f32 v[30:31], v[114:115], v[20:21] op_sel_hi:[1,0]
	v_add_f32_e32 v29, 1.0, v29
	v_rcp_f32_e32 v33, v21
	v_exp_f32_e64 v21, -v30
	v_rcp_f32_e32 v32, v29
	v_exp_f32_e64 v29, -v31
	v_add_f32_e32 v21, 1.0, v21
	v_pk_mul_f32 v[22:23], v[22:23], v[32:33]
	v_pk_mul_f32 v[32:33], v[106:107], v[28:29] op_sel_hi:[1,0]
	v_rcp_f32_e32 v34, v21
	v_add_f32_e32 v21, 1.0, v29
	v_pk_mul_f32 v[30:31], v[30:31], v[32:33]
	v_pk_mul_f32 v[32:33], v[108:109], v[20:21] op_sel_hi:[1,0]
	v_rcp_f32_e32 v35, v21
	v_exp_f32_e64 v21, -v32
	v_exp_f32_e64 v29, -v33
	v_pk_mul_f32 v[30:31], v[30:31], v[34:35]
	v_add_f32_e32 v21, 1.0, v21
	v_pk_mul_f32 v[34:35], v[100:101], v[28:29] op_sel_hi:[1,0]
	v_rcp_f32_e32 v100, v21
	v_add_f32_e32 v21, 1.0, v29
	v_rcp_f32_e32 v101, v21
	v_pk_mul_f32 v[32:33], v[32:33], v[34:35]
	v_pk_mul_f32 v[20:21], v[110:111], v[20:21] op_sel_hi:[1,0]
	v_pk_mul_f32 v[28:29], v[102:103], v[28:29] op_sel_hi:[1,0]
	v_pk_mul_f32 v[32:33], v[32:33], v[100:101]
	s_waitcnt vmcnt(6)
	v_mov_b32_e32 v100, v17
	v_mov_b32_e32 v101, v18
	v_mov_b32_e32 v17, v19
	v_pk_add_f32 v[16:17], v[100:101], v[16:17]
	v_exp_f32_e64 v34, -v20
	v_add_f32_e32 v18, v16, v17
	v_mov_b32_e32 v19, v18
	s_nop 1
	v_permlane16_swap_b32_e32 v19, v18
	v_exp_f32_e64 v35, -v21
	v_mov_b32_e32 v16, v3
	v_add_f32_e32 v34, 1.0, v34
	v_cvt_pk_fp8_f32 v16, v22, v23
	v_add_f32_e32 v35, 1.0, v35
	s_waitcnt lgkmcnt(0)
	v_add_f32_e32 v22, v18, v19
	v_rcp_f32_e32 v34, v34
	v_rcp_f32_e32 v35, v35
	v_mov_b32_e32 v17, v3
	v_mov_b32_e32 v23, v22
	s_nop 1
	v_permlane32_swap_b32_e32 v23, v22
	v_cvt_pk_fp8_f32 v17, v32, v33
	v_pk_mul_f32 v[18:19], v[20:21], v[28:29]
	v_cvt_pk_fp8_f32 v16, v30, v31 op_sel:[0,0,1]
	v_pk_mul_f32 v[18:19], v[18:19], v[34:35]
	s_nop 0
	v_cvt_pk_fp8_f32 v17, v18, v19 op_sel:[0,0,1]
	s_waitcnt lgkmcnt(0)
; __device__ __forceinline__ float rstd_fin4(const f32x4 a) { float s = (a[0] + a[1]) + (a[2] + a[3]); s += __shfl_xor(s, 16); s += __shfl_xor(s, 32); return __builtin_amdgcn_rsqf(s * (1.f / 1024.f) + 1e-6f); }
;     __device__ __forceinline__ void operator()(const f32x4 (&acc)[2][2][4][2], const Unit& u, int wr, int wc, int fr, int fq) const {
;     ...
;         const int row0 = u.pm * BM + wr * 64 + fr;
;         unsigned char* const hb = (unsigned char*)H + (size_t)(u.pm * (FFH / 128) + u.pn + pn0) * 32768 + (((wr * 4 + wc) * 8) * 64 + (fq >> 1) * 32 + fr * 2 + (fq & 1)) * 8;
;         f32x4 pa[2][4];
; #pragma unroll
;         for (int ai = 0; ai < 2; ++ai)
; #pragma unroll
;             for (int m = 0; m < 4; ++m) pa[ai][m] = rstd_ld4(ss, row0 + ai * HALF + m * 16, fq);
; #pragma unroll
;         for (int ai = 0; ai < 2; ++ai)
; #pragma unroll
;             for (int m = 0; m < 4; ++m) { const float rs = rstd_fin4(pa[ai][m]) * sc;
;                 const float rsl = rs * 1.4426950408889634f, rsu = rs * 0.6931471805599453f;
;                 f32x4 h0, h1;
; #pragma unroll
;                 for (int n = 0; n < 2; ++n) { const f32x4 G = acc[ai][0][m][n], U = acc[ai][1][m][n]; f32x4 hv;
; #pragma unroll
;                     for (int q = 0; q < 2; ++q) { const f32x2 g2 = (f32x2){G[2 * q], G[2 * q + 1]} * rsl, u2 = (f32x2){U[2 * q], U[2 * q + 1]} * rsu;
;                         f32x2 r2; r2.x = __builtin_amdgcn_rcpf(1.f + __builtin_amdgcn_exp2f(-g2.x)); r2.y = __builtin_amdgcn_rcpf(1.f + __builtin_amdgcn_exp2f(-g2.y));
;                         const f32x2 o2 = g2 * u2 * r2; hv[2 * q] = o2.x; hv[2 * q + 1] = o2.y; }
;                     if (n == 0) h0 = hv; else h1 = hv; }
;                 unsigned w0 = 0u, w1 = 0u;
;                 w0 = __builtin_amdgcn_cvt_pk_fp8_f32(h0[0], h0[1], w0, false); w0 = __builtin_amdgcn_cvt_pk_fp8_f32(h0[2], h0[3], w0, true); w1 = __builtin_amdgcn_cvt_pk_fp8_f32(h1[0], h1[1], w1, false); w1 = __builtin_amdgcn_cvt_pk_fp8_f32(h1[2], h1[3], w1, true);
;                 *(u32x2*)(hb + (ai * 4 + m) * 512) = (u32x2){w0, w1}; asm volatile("" ::: "memory"); }
	v_add_f32_e32 v18, v22, v23
	v_fmamk_f32 v18, v18, 0x3a800000, v227
	v_rsq_f32_e32 v18, v18
	global_store_dwordx2 v[24:25], v[16:17], off offset:1536
	v_mul_f32_e32 v17, 0x3c800000, v18
	v_mul_f32_e32 v16, 0x3fb8aa3b, v17
	v_pk_mul_f32 v[18:19], v[96:97], v[16:17] op_sel_hi:[1,0]
	v_mul_f32_e32 v20, 0x3f317218, v17
	v_exp_f32_e64 v21, -v18
	v_exp_f32_e64 v17, -v19
	v_pk_mul_f32 v[22:23], v[88:89], v[20:21] op_sel_hi:[1,0]
	v_add_f32_e32 v17, 1.0, v17
	v_pk_mul_f32 v[18:19], v[18:19], v[22:23]
	v_pk_mul_f32 v[22:23], v[98:99], v[16:17] op_sel_hi:[1,0]
	v_add_f32_e32 v21, 1.0, v21
	v_rcp_f32_e32 v29, v17
	v_exp_f32_e64 v17, -v22
	v_rcp_f32_e32 v28, v21
	v_exp_f32_e64 v21, -v23
	v_add_f32_e32 v17, 1.0, v17
	v_pk_mul_f32 v[18:19], v[18:19], v[28:29]
	v_pk_mul_f32 v[28:29], v[90:91], v[20:21] op_sel_hi:[1,0]
	v_rcp_f32_e32 v30, v17
	v_add_f32_e32 v17, 1.0, v21
	v_pk_mul_f32 v[22:23], v[22:23], v[28:29]
	v_pk_mul_f32 v[28:29], v[92:93], v[16:17] op_sel_hi:[1,0]
	v_rcp_f32_e32 v31, v17
	v_exp_f32_e64 v21, -v29
	v_exp_f32_e64 v17, -v28
	v_pk_mul_f32 v[22:23], v[22:23], v[30:31]
	v_pk_mul_f32 v[30:31], v[84:85], v[20:21] op_sel_hi:[1,0]
	v_add_f32_e32 v17, 1.0, v17
	v_pk_mul_f32 v[28:29], v[28:29], v[30:31]
	s_waitcnt vmcnt(6)
	v_mov_b32_e32 v30, v13
	v_mov_b32_e32 v31, v14
	v_mov_b32_e32 v13, v15
	v_pk_add_f32 v[12:13], v[30:31], v[12:13]
	v_rcp_f32_e32 v32, v17
	v_add_f32_e32 v30, v12, v13
	v_mov_b32_e32 v31, v30
	s_nop 1
	v_permlane16_swap_b32_e32 v31, v30
	v_add_f32_e32 v17, 1.0, v21
	v_rcp_f32_e32 v33, v17
	v_pk_mul_f32 v[16:17], v[94:95], v[16:17] op_sel_hi:[1,0]
	v_pk_mul_f32 v[20:21], v[86:87], v[20:21] op_sel_hi:[1,0]
	v_exp_f32_e64 v34, -v16
	v_pk_mul_f32 v[14:15], v[16:17], v[20:21]
	s_waitcnt lgkmcnt(0)
	v_add_f32_e32 v20, v30, v31
	v_mov_b32_e32 v21, v20
	s_nop 1
	v_permlane32_swap_b32_e32 v21, v20
	v_pk_mul_f32 v[28:29], v[28:29], v[32:33]
	v_exp_f32_e64 v33, -v17
	v_mov_b32_e32 v16, v3
	v_add_f32_e32 v32, 1.0, v34
	v_cvt_pk_fp8_f32 v16, v18, v19
	v_add_f32_e32 v13, 1.0, v33
	s_waitcnt lgkmcnt(0)
	v_add_f32_e32 v18, v20, v21
	v_rcp_f32_e32 v12, v32
	v_rcp_f32_e32 v13, v13
	v_mov_b32_e32 v17, v3
	v_fmamk_f32 v18, v18, 0x3a800000, v227
	v_cvt_pk_fp8_f32 v17, v28, v29
	v_rsq_f32_e32 v18, v18
	v_pk_mul_f32 v[12:13], v[14:15], v[12:13]
	v_cvt_pk_fp8_f32 v16, v22, v23 op_sel:[0,0,1]
	v_cvt_pk_fp8_f32 v17, v12, v13 op_sel:[0,0,1]
	v_mul_f32_e32 v13, 0x3c800000, v18
	v_mul_f32_e32 v12, 0x3fb8aa3b, v13
	v_pk_mul_f32 v[14:15], v[80:81], v[12:13] op_sel_hi:[1,0]
	v_mul_f32_e32 v18, 0x3f317218, v13
	v_exp_f32_e64 v19, -v14
	v_exp_f32_e64 v13, -v15
	global_store_dwordx2 v[24:25], v[16:17], off offset:2048
	v_pk_mul_f32 v[20:21], v[72:73], v[18:19] op_sel_hi:[1,0]
	v_add_f32_e32 v13, 1.0, v13
	v_pk_mul_f32 v[14:15], v[14:15], v[20:21]
	v_pk_mul_f32 v[20:21], v[82:83], v[12:13] op_sel_hi:[1,0]
	v_add_f32_e32 v19, 1.0, v19
	v_rcp_f32_e32 v23, v13
	v_exp_f32_e64 v13, -v20
	v_rcp_f32_e32 v22, v19
	v_exp_f32_e64 v19, -v21
	v_add_f32_e32 v13, 1.0, v13
	v_pk_mul_f32 v[14:15], v[14:15], v[22:23]
	v_pk_mul_f32 v[22:23], v[74:75], v[18:19] op_sel_hi:[1,0]
	v_rcp_f32_e32 v28, v13
	v_add_f32_e32 v13, 1.0, v19
	v_pk_mul_f32 v[20:21], v[20:21], v[22:23]
	v_pk_mul_f32 v[22:23], v[76:77], v[12:13] op_sel_hi:[1,0]
	v_rcp_f32_e32 v29, v13
	v_exp_f32_e64 v13, -v22
	v_exp_f32_e64 v19, -v23
	v_pk_mul_f32 v[20:21], v[20:21], v[28:29]
	v_add_f32_e32 v13, 1.0, v13
	v_rcp_f32_e32 v30, v13
	v_add_f32_e32 v13, 1.0, v19
	v_rcp_f32_e32 v31, v13
	v_pk_mul_f32 v[28:29], v[68:69], v[18:19] op_sel_hi:[1,0]
	v_pk_mul_f32 v[12:13], v[78:79], v[12:13] op_sel_hi:[1,0]
	v_pk_mul_f32 v[22:23], v[22:23], v[28:29]
	v_exp_f32_e64 v28, -v12
	v_pk_mul_f32 v[22:23], v[22:23], v[30:31]
	s_waitcnt vmcnt(6)
	v_mov_b32_e32 v30, v9
	v_mov_b32_e32 v31, v10
	v_mov_b32_e32 v9, v11
	v_pk_add_f32 v[8:9], v[30:31], v[8:9]
	v_exp_f32_e64 v29, -v13
	v_add_f32_e32 v10, v8, v9
	v_mov_b32_e32 v11, v10
	s_nop 1
	v_permlane16_swap_b32_e32 v11, v10
	v_mov_b32_e32 v8, v3
	v_add_f32_e32 v28, 1.0, v28
	v_add_f32_e32 v29, 1.0, v29
	v_cvt_pk_fp8_f32 v8, v14, v15
	s_waitcnt lgkmcnt(0)
	v_add_f32_e32 v14, v10, v11
	v_rcp_f32_e32 v28, v28
	v_rcp_f32_e32 v29, v29
	v_mov_b32_e32 v9, v3
	v_mov_b32_e32 v15, v14
	s_nop 1
	v_permlane32_swap_b32_e32 v15, v14
	v_cvt_pk_fp8_f32 v9, v22, v23
	v_pk_mul_f32 v[18:19], v[70:71], v[18:19] op_sel_hi:[1,0]
	v_cvt_pk_fp8_f32 v8, v20, v21 op_sel:[0,0,1]
	v_pk_mul_f32 v[10:11], v[12:13], v[18:19]
	s_nop 0
	v_pk_mul_f32 v[10:11], v[10:11], v[28:29]
	s_nop 0
	v_cvt_pk_fp8_f32 v9, v10, v11 op_sel:[0,0,1]
	s_waitcnt lgkmcnt(0)
; __device__ __forceinline__ float rstd_fin4(const f32x4 a) { float s = (a[0] + a[1]) + (a[2] + a[3]); s += __shfl_xor(s, 16); s += __shfl_xor(s, 32); return __builtin_amdgcn_rsqf(s * (1.f / 1024.f) + 1e-6f); }
;     __device__ __forceinline__ void operator()(const f32x4 (&acc)[2][2][4][2], const Unit& u, int wr, int wc, int fr, int fq) const {
;     ...
;         const int row0 = u.pm * BM + wr * 64 + fr;
;         unsigned char* const hb = (unsigned char*)H + (size_t)(u.pm * (FFH / 128) + u.pn + pn0) * 32768 + (((wr * 4 + wc) * 8) * 64 + (fq >> 1) * 32 + fr * 2 + (fq & 1)) * 8;
;         f32x4 pa[2][4];
; #pragma unroll
;         for (int ai = 0; ai < 2; ++ai)
; #pragma unroll
;             for (int m = 0; m < 4; ++m) pa[ai][m] = rstd_ld4(ss, row0 + ai * HALF + m * 16, fq);
; #pragma unroll
;         for (int ai = 0; ai < 2; ++ai)
; #pragma unroll
;             for (int m = 0; m < 4; ++m) { const float rs = rstd_fin4(pa[ai][m]) * sc;
;                 const float rsl = rs * 1.4426950408889634f, rsu = rs * 0.6931471805599453f;
;                 f32x4 h0, h1;
; #pragma unroll
;                 for (int n = 0; n < 2; ++n) { const f32x4 G = acc[ai][0][m][n], U = acc[ai][1][m][n]; f32x4 hv;
; #pragma unroll
;                     for (int q = 0; q < 2; ++q) { const f32x2 g2 = (f32x2){G[2 * q], G[2 * q + 1]} * rsl, u2 = (f32x2){U[2 * q], U[2 * q + 1]} * rsu;
;                         f32x2 r2; r2.x = __builtin_amdgcn_rcpf(1.f + __builtin_amdgcn_exp2f(-g2.x)); r2.y = __builtin_amdgcn_rcpf(1.f + __builtin_amdgcn_exp2f(-g2.y));
;                         const f32x2 o2 = g2 * u2 * r2; hv[2 * q] = o2.x; hv[2 * q + 1] = o2.y; }
;                     if (n == 0) h0 = hv; else h1 = hv; }
;                 unsigned w0 = 0u, w1 = 0u;
;                 w0 = __builtin_amdgcn_cvt_pk_fp8_f32(h0[0], h0[1], w0, false); w0 = __builtin_amdgcn_cvt_pk_fp8_f32(h0[2], h0[3], w0, true); w1 = __builtin_amdgcn_cvt_pk_fp8_f32(h1[0], h1[1], w1, false); w1 = __builtin_amdgcn_cvt_pk_fp8_f32(h1[2], h1[3], w1, true);
;                 *(u32x2*)(hb + (ai * 4 + m) * 512) = (u32x2){w0, w1}; asm volatile("" ::: "memory"); }
	v_add_f32_e32 v10, v14, v15
	v_fmamk_f32 v10, v10, 0x3a800000, v227
	v_rsq_f32_e32 v10, v10
	global_store_dwordx2 v[24:25], v[8:9], off offset:2560
	v_mul_f32_e32 v9, 0x3c800000, v10
	v_mul_f32_e32 v8, 0x3fb8aa3b, v9
	v_pk_mul_f32 v[10:11], v[64:65], v[8:9] op_sel_hi:[1,0]
	v_mul_f32_e32 v12, 0x3f317218, v9
	v_exp_f32_e64 v13, -v10
	v_exp_f32_e64 v9, -v11
	v_pk_mul_f32 v[14:15], v[56:57], v[12:13] op_sel_hi:[1,0]
	v_add_f32_e32 v9, 1.0, v9
	v_pk_mul_f32 v[10:11], v[10:11], v[14:15]
	v_pk_mul_f32 v[14:15], v[66:67], v[8:9] op_sel_hi:[1,0]
	v_add_f32_e32 v13, 1.0, v13
	v_rcp_f32_e32 v17, v9
	v_exp_f32_e64 v9, -v14
	v_rcp_f32_e32 v16, v13
	v_exp_f32_e64 v13, -v15
	v_add_f32_e32 v9, 1.0, v9
	v_pk_mul_f32 v[10:11], v[10:11], v[16:17]
	v_pk_mul_f32 v[16:17], v[58:59], v[12:13] op_sel_hi:[1,0]
	v_rcp_f32_e32 v18, v9
	v_add_f32_e32 v9, 1.0, v13
	v_pk_mul_f32 v[14:15], v[14:15], v[16:17]
	v_pk_mul_f32 v[16:17], v[60:61], v[8:9] op_sel_hi:[1,0]
	v_rcp_f32_e32 v19, v9
	v_exp_f32_e64 v13, -v17
	v_exp_f32_e64 v9, -v16
	v_pk_mul_f32 v[14:15], v[14:15], v[18:19]
	v_pk_mul_f32 v[18:19], v[52:53], v[12:13] op_sel_hi:[1,0]
	v_add_f32_e32 v9, 1.0, v9
	v_pk_mul_f32 v[16:17], v[16:17], v[18:19]
	s_waitcnt vmcnt(6)
	v_mov_b32_e32 v18, v5
	v_mov_b32_e32 v19, v6
	v_mov_b32_e32 v5, v7
	v_pk_add_f32 v[4:5], v[18:19], v[4:5]
	v_rcp_f32_e32 v20, v9
	v_add_f32_e32 v18, v4, v5
	v_mov_b32_e32 v19, v18
	s_nop 1
	v_permlane16_swap_b32_e32 v19, v18
	v_add_f32_e32 v9, 1.0, v13
	v_rcp_f32_e32 v21, v9
	v_pk_mul_f32 v[8:9], v[62:63], v[8:9] op_sel_hi:[1,0]
	v_pk_mul_f32 v[12:13], v[54:55], v[12:13] op_sel_hi:[1,0]
	v_exp_f32_e64 v22, -v8
	v_pk_mul_f32 v[6:7], v[8:9], v[12:13]
	s_waitcnt lgkmcnt(0)
	v_add_f32_e32 v12, v18, v19
	v_mov_b32_e32 v13, v12
	s_nop 1
	v_permlane32_swap_b32_e32 v13, v12
	v_pk_mul_f32 v[16:17], v[16:17], v[20:21]
	v_exp_f32_e64 v21, -v9
	v_mov_b32_e32 v8, v3
	v_add_f32_e32 v20, 1.0, v22
	v_cvt_pk_fp8_f32 v8, v10, v11
	v_add_f32_e32 v5, 1.0, v21
	s_waitcnt lgkmcnt(0)
	v_add_f32_e32 v10, v12, v13
	v_rcp_f32_e32 v4, v20
	v_rcp_f32_e32 v5, v5
	v_mov_b32_e32 v9, v3
	v_fmamk_f32 v10, v10, 0x3a800000, v227
	v_cvt_pk_fp8_f32 v9, v16, v17
	v_rsq_f32_e32 v10, v10
	v_pk_mul_f32 v[4:5], v[6:7], v[4:5]
	v_cvt_pk_fp8_f32 v8, v14, v15 op_sel:[0,0,1]
	v_cvt_pk_fp8_f32 v9, v4, v5 op_sel:[0,0,1]
	v_mul_f32_e32 v5, 0x3c800000, v10
	v_mul_f32_e32 v4, 0x3fb8aa3b, v5
	v_pk_mul_f32 v[6:7], v[48:49], v[4:5] op_sel_hi:[1,0]
	v_mul_f32_e32 v10, 0x3f317218, v5
	v_exp_f32_e64 v11, -v6
	v_exp_f32_e64 v5, -v7
	global_store_dwordx2 v[24:25], v[8:9], off offset:3072
	v_pk_mul_f32 v[12:13], v[40:41], v[10:11] op_sel_hi:[1,0]
	v_add_f32_e32 v5, 1.0, v5
	v_pk_mul_f32 v[6:7], v[6:7], v[12:13]
	v_pk_mul_f32 v[12:13], v[50:51], v[4:5] op_sel_hi:[1,0]
	v_add_f32_e32 v11, 1.0, v11
	v_rcp_f32_e32 v15, v5
	v_exp_f32_e64 v5, -v12
	v_rcp_f32_e32 v14, v11
	v_exp_f32_e64 v11, -v13
	v_add_f32_e32 v5, 1.0, v5
	v_pk_mul_f32 v[6:7], v[6:7], v[14:15]
	v_pk_mul_f32 v[14:15], v[42:43], v[10:11] op_sel_hi:[1,0]
	v_rcp_f32_e32 v16, v5
	v_add_f32_e32 v5, 1.0, v11
	v_pk_mul_f32 v[12:13], v[12:13], v[14:15]
	v_pk_mul_f32 v[14:15], v[44:45], v[4:5] op_sel_hi:[1,0]
	v_rcp_f32_e32 v17, v5
	v_exp_f32_e64 v5, -v14
	v_exp_f32_e64 v11, -v15
	v_pk_mul_f32 v[12:13], v[12:13], v[16:17]
	v_add_f32_e32 v5, 1.0, v5
	v_rcp_f32_e32 v18, v5
	v_add_f32_e32 v5, 1.0, v11
	v_pk_mul_f32 v[16:17], v[36:37], v[10:11] op_sel_hi:[1,0]
	v_rcp_f32_e32 v19, v5
	v_pk_mul_f32 v[4:5], v[46:47], v[4:5] op_sel_hi:[1,0]
	v_pk_mul_f32 v[14:15], v[14:15], v[16:17]
	v_exp_f32_e64 v16, -v4
	v_exp_f32_e64 v17, -v5
	v_pk_mul_f32 v[14:15], v[14:15], v[18:19]
	v_mov_b32_e32 v18, v3
	v_add_f32_e32 v16, 1.0, v16
	v_add_f32_e32 v17, 1.0, v17
	v_rcp_f32_e32 v16, v16
	v_rcp_f32_e32 v17, v17
	v_mov_b32_e32 v19, v3
	v_cvt_pk_fp8_f32 v18, v6, v7
	v_cvt_pk_fp8_f32 v19, v14, v15
	v_pk_mul_f32 v[10:11], v[38:39], v[10:11] op_sel_hi:[1,0]
	v_cvt_pk_fp8_f32 v18, v12, v13 op_sel:[0,0,1]
	v_pk_mul_f32 v[4:5], v[4:5], v[10:11]
	s_nop 0
	v_pk_mul_f32 v[4:5], v[4:5], v[16:17]
	s_nop 0
	v_cvt_pk_fp8_f32 v19, v4, v5 op_sel:[0,0,1]
	global_store_dwordx2 v[24:25], v[18:19], off offset:3584
	s_cbranch_vccnz .LBB0_1667
	s_andn2_b64 vcc, exec, s[48:49]
	s_cbranch_vccnz .LBB0_1666
	s_barrier
	s_branch .LBB0_1666

; __device__ __forceinline__ float rstd_fin4(const f32x4 a) { float s = (a[0] + a[1]) + (a[2] + a[3]); s += __shfl_xor(s, 16); s += __shfl_xor(s, 32); return __builtin_amdgcn_rsqf(s * (1.f / 1024.f) + 1e-6f); }
;     __device__ __forceinline__ void operator()(const f32x4 (&acc)[2][2][4][2], const Unit& u, int wr, int wc, int fr, int fq) const {
;     ...
;         const int row0 = u.pm * BM + wr * 64 + fr;
;         unsigned char* const hb = (unsigned char*)H + (size_t)(u.pm * (FFH / 128) + u.pn + pn0) * 32768 + (((wr * 4 + wc) * 8) * 64 + (fq >> 1) * 32 + fr * 2 + (fq & 1)) * 8;
;         f32x4 pa[2][4];
; #pragma unroll
;         for (int ai = 0; ai < 2; ++ai)
; #pragma unroll
;             for (int m = 0; m < 4; ++m) pa[ai][m] = rstd_ld4(ss, row0 + ai * HALF + m * 16, fq);
; #pragma unroll
;         for (int ai = 0; ai < 2; ++ai)
; #pragma unroll
;             for (int m = 0; m < 4; ++m) { const float rs = rstd_fin4(pa[ai][m]) * sc;
;                 const float rsl = rs * 1.4426950408889634f, rsu = rs * 0.6931471805599453f;
;                 f32x4 h0, h1;
; #pragma unroll
;                 for (int n = 0; n < 2; ++n) { const f32x4 G = acc[ai][0][m][n], U = acc[ai][1][m][n]; f32x4 hv;
; #pragma unroll
;                     for (int q = 0; q < 2; ++q) { const f32x2 g2 = (f32x2){G[2 * q], G[2 * q + 1]} * rsl, u2 = (f32x2){U[2 * q], U[2 * q + 1]} * rsu;
;                         f32x2 r2; r2.x = __builtin_amdgcn_rcpf(1.f + __builtin_amdgcn_exp2f(-g2.x)); r2.y = __builtin_amdgcn_rcpf(1.f + __builtin_amdgcn_exp2f(-g2.y));
;                         const f32x2 o2 = g2 * u2 * r2; hv[2 * q] = o2.x; hv[2 * q + 1] = o2.y; }
;                     if (n == 0) h0 = hv; else h1 = hv; }
;                 unsigned w0 = 0u, w1 = 0u;
;                 w0 = __builtin_amdgcn_cvt_pk_fp8_f32(h0[0], h0[1], w0, false); w0 = __builtin_amdgcn_cvt_pk_fp8_f32(h0[2], h0[3], w0, true); w1 = __builtin_amdgcn_cvt_pk_fp8_f32(h1[0], h1[1], w1, false); w1 = __builtin_amdgcn_cvt_pk_fp8_f32(h1[2], h1[3], w1, true);
;                 *(u32x2*)(hb + (ai * 4 + m) * 512) = (u32x2){w0, w1}; asm volatile("" ::: "memory"); }
.LBB0_1692:
	s_lshl_b32 s4, s68, 8
	v_mov_b32_e32 v14, v1
	v_mov_b32_e32 v15, v182
	s_add_i32 s4, s4, s62
	v_and_b32_e32 v17, 64, v246
	v_add_u32_e32 v4, s4, v14
	v_lshlrev_b32_e32 v6, 2, v15
	v_ashrrev_i32_e32 v7, 31, v6
	v_ashrrev_i32_e32 v5, 31, v4
	v_lshl_add_u64 v[6:7], v[6:7], 2, s[42:43]
	v_lshlrev_b64 v[4:5], 6, v[4:5]
	v_lshl_add_u64 v[12:13], v[6:7], 0, v[4:5]
	global_load_dwordx4 v[4:7], v[12:13], off
	global_load_dwordx4 v[8:11], v[12:13], off offset:1024
	global_load_dwordx4 v[28:31], v[12:13], off offset:2048
	global_load_dwordx4 v[20:23], v[12:13], off offset:3072
	v_xor_b32_e32 v16, 16, v246
	v_add_u32_e32 v17, 64, v17
	v_xor_b32_e32 v18, 32, v246
	v_cmp_lt_i32_e32 vcc, v16, v17
	v_mov_b32_e32 v32, v3
	v_mov_b32_e32 v33, v3
	v_cndmask_b32_e32 v16, v246, v16, vcc
	v_cmp_lt_i32_e32 vcc, v18, v17
	v_lshlrev_b32_e32 v27, 2, v16
	s_mul_i32 s4, s68, 22
	v_cndmask_b32_e32 v17, v246, v18, vcc
	v_lshlrev_b32_e32 v26, 2, v17
	s_add_i32 s4, s4, s67
	s_ashr_i32 s5, s4, 31
	v_lshlrev_b32_e32 v19, 4, v15
	v_lshl_add_u32 v14, v14, 1, s65
	s_lshl_b64 s[4:5], s[4:5], 15
	v_and_b32_e32 v18, 0x1fffffe0, v19
	v_and_or_b32 v14, v15, 1, v14
	v_add_lshl_u32 v14, v14, v18, 3
	s_add_u32 s4, s22, s4
	v_ashrrev_i32_e32 v15, 31, v14
	s_addc_u32 s5, s23, s5
	v_lshl_add_u64 v[24:25], s[4:5], 0, v[14:15]
	s_mov_b64 s[4:5], -1
	s_waitcnt vmcnt(0)
	v_mov_b32_e32 v16, v5
	v_mov_b32_e32 v17, v6
	v_mov_b32_e32 v5, v7
	v_mov_b32_e32 v6, v9
	v_mov_b32_e32 v7, v10
	v_mov_b32_e32 v9, v11
	v_pk_add_f32 v[4:5], v[16:17], v[4:5]
	v_pk_add_f32 v[6:7], v[6:7], v[8:9]
	v_add_f32_e32 v8, v4, v5
	v_add_f32_e32 v6, v6, v7
	v_mov_b32_e32 v7, v8
	s_nop 1
	v_permlane16_swap_b32_e32 v7, v8
	v_mov_b32_e32 v9, v6
	s_nop 1
	v_permlane16_swap_b32_e32 v9, v6
	v_add_co_u32_e32 v4, vcc, s88, v12
	s_waitcnt lgkmcnt(1)
	v_add_f32_e32 v7, v8, v7
	s_waitcnt lgkmcnt(0)
	v_add_f32_e32 v6, v6, v9
	v_mov_b32_e32 v8, v7
	s_nop 1
	v_permlane32_swap_b32_e32 v8, v7
	v_mov_b32_e32 v9, v6
	s_nop 1
	v_permlane32_swap_b32_e32 v9, v6
	v_addc_co_u32_e32 v5, vcc, 0, v13, vcc
	global_load_dwordx4 v[16:19], v[4:5], off
	global_load_dwordx4 v[12:15], v[4:5], off offset:1024
	s_waitcnt lgkmcnt(1)
	v_add_f32_e32 v7, v7, v8
	s_waitcnt lgkmcnt(0)
	v_add_f32_e32 v6, v6, v9
	v_fmamk_f32 v7, v7, 0x3a800000, v227
	v_fmamk_f32 v6, v6, 0x3a800000, v227
	v_rsq_f32_e32 v34, v7
	v_rsq_f32_e32 v35, v6
	global_load_dwordx4 v[8:11], v[4:5], off offset:2048
	s_nop 0
	global_load_dwordx4 v[4:7], v[4:5], off offset:3072
	s_andn2_b64 vcc, exec, s[40:41]
	v_mul_f32_e32 v174, 0x3c800000, v34
	v_mul_f32_e32 v35, 0x3c800000, v35
	v_mul_f32_e32 v34, 0x3fb8aa3b, v174
	v_mul_f32_e32 v174, 0x3f317218, v174
	v_pk_mul_f32 v[160:161], v[160:161], v[34:35] op_sel_hi:[1,0]
	v_pk_mul_f32 v[152:153], v[152:153], v[174:175] op_sel_hi:[1,0]
	v_pk_mul_f32 v[162:163], v[162:163], v[34:35] op_sel_hi:[1,0]
	v_pk_mul_f32 v[154:155], v[154:155], v[174:175] op_sel_hi:[1,0]
	v_pk_mul_f32 v[156:157], v[156:157], v[34:35] op_sel_hi:[1,0]
	v_mul_f32_e32 v176, 0x3fb8aa3b, v35
	v_mul_f32_e32 v178, 0x3f317218, v35
	v_pk_mul_f32 v[148:149], v[148:149], v[174:175] op_sel_hi:[1,0]
	v_pk_mul_f32 v[34:35], v[158:159], v[34:35] op_sel_hi:[1,0]
	v_exp_f32_e64 v158, -v160
	v_exp_f32_e64 v159, -v161
	v_pk_mul_f32 v[152:153], v[160:161], v[152:153]
	v_exp_f32_e64 v160, -v162
	v_exp_f32_e64 v161, -v163
	v_pk_mul_f32 v[154:155], v[162:163], v[154:155]
	v_exp_f32_e64 v162, -v156
	v_exp_f32_e64 v163, -v157
	v_pk_mul_f32 v[148:149], v[156:157], v[148:149]
	v_exp_f32_e64 v156, -v34
	v_exp_f32_e64 v157, -v35
	v_pk_mul_f32 v[150:151], v[150:151], v[174:175] op_sel_hi:[1,0]
	v_pk_mul_f32 v[144:145], v[144:145], v[176:177] op_sel_hi:[1,0]
	v_pk_mul_f32 v[34:35], v[34:35], v[150:151]
	v_add_f32_e32 v150, 1.0, v158
	v_add_f32_e32 v151, 1.0, v159
	v_add_f32_e32 v158, 1.0, v160
	v_add_f32_e32 v159, 1.0, v161
	v_add_f32_e32 v160, 1.0, v162
	v_add_f32_e32 v161, 1.0, v163
	v_add_f32_e32 v162, 1.0, v156
	v_add_f32_e32 v163, 1.0, v157
	v_rcp_f32_e32 v150, v150
	v_rcp_f32_e32 v151, v151
	v_rcp_f32_e32 v156, v158
	v_rcp_f32_e32 v157, v159
	v_rcp_f32_e32 v158, v160
	v_rcp_f32_e32 v159, v161
	v_rcp_f32_e32 v160, v162
	v_rcp_f32_e32 v161, v163
	v_pk_mul_f32 v[150:151], v[152:153], v[150:151]
	v_pk_mul_f32 v[148:149], v[148:149], v[158:159]
	v_cvt_pk_fp8_f32 v32, v150, v151
	v_cvt_pk_fp8_f32 v33, v148, v149
	v_pk_mul_f32 v[148:149], v[154:155], v[156:157]
	v_pk_mul_f32 v[34:35], v[34:35], v[160:161]
	v_cvt_pk_fp8_f32 v32, v148, v149 op_sel:[0,0,1]
	v_cvt_pk_fp8_f32 v33, v34, v35 op_sel:[0,0,1]
	v_exp_f32_e64 v35, -v145
	v_exp_f32_e64 v174, -v144
	v_pk_mul_f32 v[136:137], v[136:137], v[178:179] op_sel_hi:[1,0]
	global_store_dwordx2 v[24:25], v[32:33], off
	v_add_f32_e32 v32, 1.0, v35
	v_add_f32_e32 v34, 1.0, v174
	v_rcp_f32_e32 v35, v32
	v_pk_mul_f32 v[32:33], v[144:145], v[136:137]
	v_pk_mul_f32 v[136:137], v[146:147], v[176:177] op_sel_hi:[1,0]
	v_rcp_f32_e32 v34, v34
	v_exp_f32_e64 v144, -v136
	v_exp_f32_e64 v145, -v137
	v_pk_mul_f32 v[132:133], v[132:133], v[178:179] op_sel_hi:[1,0]
	v_pk_mul_f32 v[32:33], v[32:33], v[34:35]
	v_pk_mul_f32 v[34:35], v[138:139], v[178:179] op_sel_hi:[1,0]
	v_add_f32_e32 v138, 1.0, v144
	v_add_f32_e32 v139, 1.0, v145
	v_rcp_f32_e32 v138, v138
	v_rcp_f32_e32 v139, v139
	v_pk_mul_f32 v[34:35], v[136:137], v[34:35]
	v_pk_mul_f32 v[136:137], v[140:141], v[176:177] op_sel_hi:[1,0]
	v_pk_mul_f32 v[134:135], v[134:135], v[178:179] op_sel_hi:[1,0]
	v_exp_f32_e64 v140, -v136
	v_pk_mul_f32 v[34:35], v[34:35], v[138:139]
	v_exp_f32_e64 v139, -v137
	v_pk_mul_f32 v[132:133], v[136:137], v[132:133]
	v_mov_b32_e32 v136, v29
	v_mov_b32_e32 v137, v30
	v_mov_b32_e32 v29, v31
	v_pk_add_f32 v[28:29], v[136:137], v[28:29]
	v_add_f32_e32 v138, 1.0, v140
	v_add_f32_e32 v136, v28, v29
	v_mov_b32_e32 v137, v136
	s_nop 1
	v_permlane16_swap_b32_e32 v137, v136
	v_add_f32_e32 v139, 1.0, v139
	v_rcp_f32_e32 v138, v138
	v_rcp_f32_e32 v139, v139
	v_pk_mul_f32 v[140:141], v[142:143], v[176:177] op_sel_hi:[1,0]
	s_waitcnt lgkmcnt(0)
; __device__ __forceinline__ float rstd_fin4(const f32x4 a) { float s = (a[0] + a[1]) + (a[2] + a[3]); s += __shfl_xor(s, 16); s += __shfl_xor(s, 32); return __builtin_amdgcn_rsqf(s * (1.f / 1024.f) + 1e-6f); }
;     __device__ __forceinline__ void operator()(const f32x4 (&acc)[2][2][4][2], const Unit& u, int wr, int wc, int fr, int fq) const {
;     ...
;         const int row0 = u.pm * BM + wr * 64 + fr;
;         unsigned char* const hb = (unsigned char*)H + (size_t)(u.pm * (FFH / 128) + u.pn + pn0) * 32768 + (((wr * 4 + wc) * 8) * 64 + (fq >> 1) * 32 + fr * 2 + (fq & 1)) * 8;
;         f32x4 pa[2][4];
; #pragma unroll
;         for (int ai = 0; ai < 2; ++ai)
; #pragma unroll
;             for (int m = 0; m < 4; ++m) pa[ai][m] = rstd_ld4(ss, row0 + ai * HALF + m * 16, fq);
; #pragma unroll
;         for (int ai = 0; ai < 2; ++ai)
; #pragma unroll
;             for (int m = 0; m < 4; ++m) { const float rs = rstd_fin4(pa[ai][m]) * sc;
;                 const float rsl = rs * 1.4426950408889634f, rsu = rs * 0.6931471805599453f;
;                 f32x4 h0, h1;
; #pragma unroll
;                 for (int n = 0; n < 2; ++n) { const f32x4 G = acc[ai][0][m][n], U = acc[ai][1][m][n]; f32x4 hv;
; #pragma unroll
;                     for (int q = 0; q < 2; ++q) { const f32x2 g2 = (f32x2){G[2 * q], G[2 * q + 1]} * rsl, u2 = (f32x2){U[2 * q], U[2 * q + 1]} * rsu;
;                         f32x2 r2; r2.x = __builtin_amdgcn_rcpf(1.f + __builtin_amdgcn_exp2f(-g2.x)); r2.y = __builtin_amdgcn_rcpf(1.f + __builtin_amdgcn_exp2f(-g2.y));
;                         const f32x2 o2 = g2 * u2 * r2; hv[2 * q] = o2.x; hv[2 * q + 1] = o2.y; }
;                     if (n == 0) h0 = hv; else h1 = hv; }
;                 unsigned w0 = 0u, w1 = 0u;
;                 w0 = __builtin_amdgcn_cvt_pk_fp8_f32(h0[0], h0[1], w0, false); w0 = __builtin_amdgcn_cvt_pk_fp8_f32(h0[2], h0[3], w0, true); w1 = __builtin_amdgcn_cvt_pk_fp8_f32(h1[0], h1[1], w1, false); w1 = __builtin_amdgcn_cvt_pk_fp8_f32(h1[2], h1[3], w1, true);
;                 *(u32x2*)(hb + (ai * 4 + m) * 512) = (u32x2){w0, w1}; asm volatile("" ::: "memory"); }
	v_add_f32_e32 v136, v136, v137
	v_mov_b32_e32 v137, v136
	s_nop 1
	v_permlane32_swap_b32_e32 v137, v136
	v_exp_f32_e64 v142, -v140
	v_pk_mul_f32 v[132:133], v[132:133], v[138:139]
	v_exp_f32_e64 v139, -v141
	v_pk_mul_f32 v[30:31], v[140:141], v[134:135]
	v_mov_b32_e32 v134, v3
	v_add_f32_e32 v138, 1.0, v142
	v_add_f32_e32 v29, 1.0, v139
	v_cvt_pk_fp8_f32 v134, v32, v33
	s_waitcnt lgkmcnt(0)
	v_add_f32_e32 v32, v136, v137
	v_rcp_f32_e32 v28, v138
	v_rcp_f32_e32 v29, v29
	v_mov_b32_e32 v135, v3
	v_fmamk_f32 v32, v32, 0x3a800000, v227
	v_cvt_pk_fp8_f32 v135, v132, v133
	v_rsq_f32_e32 v32, v32
	v_pk_mul_f32 v[28:29], v[30:31], v[28:29]
	v_cvt_pk_fp8_f32 v134, v34, v35 op_sel:[0,0,1]
	v_cvt_pk_fp8_f32 v135, v28, v29 op_sel:[0,0,1]
	v_mul_f32_e32 v29, 0x3c800000, v32
	v_mul_f32_e32 v28, 0x3fb8aa3b, v29
	v_pk_mul_f32 v[30:31], v[128:129], v[28:29] op_sel_hi:[1,0]
	v_mul_f32_e32 v32, 0x3f317218, v29
	v_exp_f32_e64 v33, -v30
	v_exp_f32_e64 v29, -v31
	global_store_dwordx2 v[24:25], v[134:135], off offset:512
	v_pk_mul_f32 v[34:35], v[120:121], v[32:33] op_sel_hi:[1,0]
	v_add_f32_e32 v29, 1.0, v29
	v_pk_mul_f32 v[30:31], v[30:31], v[34:35]
	v_pk_mul_f32 v[34:35], v[130:131], v[28:29] op_sel_hi:[1,0]
	v_add_f32_e32 v33, 1.0, v33
	v_rcp_f32_e32 v121, v29
	v_exp_f32_e64 v29, -v34
	v_rcp_f32_e32 v120, v33
	v_exp_f32_e64 v33, -v35
	v_add_f32_e32 v29, 1.0, v29
	v_pk_mul_f32 v[30:31], v[30:31], v[120:121]
	v_pk_mul_f32 v[120:121], v[122:123], v[32:33] op_sel_hi:[1,0]
	v_rcp_f32_e32 v122, v29
	v_add_f32_e32 v29, 1.0, v33
	v_pk_mul_f32 v[34:35], v[34:35], v[120:121]
	v_pk_mul_f32 v[120:121], v[124:125], v[28:29] op_sel_hi:[1,0]
	v_rcp_f32_e32 v123, v29
	v_exp_f32_e64 v29, -v120
	v_exp_f32_e64 v33, -v121
	v_pk_mul_f32 v[34:35], v[34:35], v[122:123]
	v_add_f32_e32 v29, 1.0, v29
	v_rcp_f32_e32 v122, v29
	v_add_f32_e32 v29, 1.0, v33
	v_pk_mul_f32 v[116:117], v[116:117], v[32:33] op_sel_hi:[1,0]
	v_rcp_f32_e32 v123, v29
	v_pk_mul_f32 v[28:29], v[126:127], v[28:29] op_sel_hi:[1,0]
	v_pk_mul_f32 v[116:117], v[120:121], v[116:117]
	v_exp_f32_e64 v120, -v28
	v_exp_f32_e64 v121, -v29
	v_pk_mul_f32 v[32:33], v[118:119], v[32:33] op_sel_hi:[1,0]
	v_pk_mul_f32 v[116:117], v[116:117], v[122:123]
	v_add_f32_e32 v118, 1.0, v120
	v_add_f32_e32 v119, 1.0, v121
	v_mov_b32_e32 v120, v21
	v_mov_b32_e32 v121, v22
	v_mov_b32_e32 v21, v23
	v_pk_add_f32 v[20:21], v[120:121], v[20:21]
	v_rcp_f32_e32 v118, v118
	v_add_f32_e32 v22, v20, v21
	v_mov_b32_e32 v23, v22
	s_nop 1
	v_permlane16_swap_b32_e32 v23, v22
	v_mov_b32_e32 v20, v3
	v_cvt_pk_fp8_f32 v20, v30, v31
	v_rcp_f32_e32 v119, v119
	v_mov_b32_e32 v21, v3
	s_waitcnt lgkmcnt(0)
	v_add_f32_e32 v30, v22, v23
	v_mov_b32_e32 v31, v30
	s_nop 1
	v_permlane32_swap_b32_e32 v31, v30
	v_cvt_pk_fp8_f32 v21, v116, v117
	v_pk_mul_f32 v[22:23], v[28:29], v[32:33]
	v_cvt_pk_fp8_f32 v20, v34, v35 op_sel:[0,0,1]
	v_pk_mul_f32 v[22:23], v[22:23], v[118:119]
	s_nop 0
	v_cvt_pk_fp8_f32 v21, v22, v23 op_sel:[0,0,1]
	s_waitcnt lgkmcnt(0)
	v_add_f32_e32 v22, v30, v31
	v_fmamk_f32 v22, v22, 0x3a800000, v227
	v_rsq_f32_e32 v22, v22
	global_store_dwordx2 v[24:25], v[20:21], off offset:1024
	v_mul_f32_e32 v21, 0x3c800000, v22
	v_mul_f32_e32 v20, 0x3fb8aa3b, v21
	v_pk_mul_f32 v[22:23], v[112:113], v[20:21] op_sel_hi:[1,0]
	v_mul_f32_e32 v28, 0x3f317218, v21
	v_exp_f32_e64 v29, -v22
	v_exp_f32_e64 v21, -v23
	v_pk_mul_f32 v[30:31], v[104:105], v[28:29] op_sel_hi:[1,0]
	v_add_f32_e32 v21, 1.0, v21
	v_pk_mul_f32 v[22:23], v[22:23], v[30:31]
	v_pk_mul_f32 v[30:31], v[114:115], v[20:21] op_sel_hi:[1,0]
	v_add_f32_e32 v29, 1.0, v29
	v_rcp_f32_e32 v33, v21
	v_exp_f32_e64 v21, -v30
	v_rcp_f32_e32 v32, v29
	v_exp_f32_e64 v29, -v31
	v_add_f32_e32 v21, 1.0, v21
	v_pk_mul_f32 v[22:23], v[22:23], v[32:33]
	v_pk_mul_f32 v[32:33], v[106:107], v[28:29] op_sel_hi:[1,0]
	v_rcp_f32_e32 v34, v21
	v_add_f32_e32 v21, 1.0, v29
	v_pk_mul_f32 v[30:31], v[30:31], v[32:33]
	v_pk_mul_f32 v[32:33], v[108:109], v[20:21] op_sel_hi:[1,0]
	v_rcp_f32_e32 v35, v21
	v_exp_f32_e64 v21, -v32
	v_exp_f32_e64 v29, -v33
	v_pk_mul_f32 v[30:31], v[30:31], v[34:35]
	v_add_f32_e32 v21, 1.0, v21
	v_pk_mul_f32 v[34:35], v[100:101], v[28:29] op_sel_hi:[1,0]
	v_rcp_f32_e32 v100, v21
	v_add_f32_e32 v21, 1.0, v29
	v_rcp_f32_e32 v101, v21
	v_pk_mul_f32 v[32:33], v[32:33], v[34:35]
	v_pk_mul_f32 v[20:21], v[110:111], v[20:21] op_sel_hi:[1,0]
	v_pk_mul_f32 v[28:29], v[102:103], v[28:29] op_sel_hi:[1,0]
	v_pk_mul_f32 v[32:33], v[32:33], v[100:101]
	s_waitcnt vmcnt(6)
	v_mov_b32_e32 v100, v17
	v_mov_b32_e32 v101, v18
	v_mov_b32_e32 v17, v19
	v_pk_add_f32 v[16:17], v[100:101], v[16:17]
	v_exp_f32_e64 v34, -v20
	v_add_f32_e32 v18, v16, v17
	v_mov_b32_e32 v19, v18
	s_nop 1
	v_permlane16_swap_b32_e32 v19, v18
	v_exp_f32_e64 v35, -v21
	v_mov_b32_e32 v16, v3
	v_add_f32_e32 v34, 1.0, v34
	v_cvt_pk_fp8_f32 v16, v22, v23
	v_add_f32_e32 v35, 1.0, v35
	s_waitcnt lgkmcnt(0)
	v_add_f32_e32 v22, v18, v19
	v_rcp_f32_e32 v34, v34
	v_rcp_f32_e32 v35, v35
	v_mov_b32_e32 v17, v3
	v_mov_b32_e32 v23, v22
	s_nop 1
	v_permlane32_swap_b32_e32 v23, v22
	v_cvt_pk_fp8_f32 v17, v32, v33
	v_pk_mul_f32 v[18:19], v[20:21], v[28:29]
	v_cvt_pk_fp8_f32 v16, v30, v31 op_sel:[0,0,1]
	v_pk_mul_f32 v[18:19], v[18:19], v[34:35]
	s_nop 0
	v_cvt_pk_fp8_f32 v17, v18, v19 op_sel:[0,0,1]
	s_waitcnt lgkmcnt(0)
; __device__ __forceinline__ float rstd_fin4(const f32x4 a) { float s = (a[0] + a[1]) + (a[2] + a[3]); s += __shfl_xor(s, 16); s += __shfl_xor(s, 32); return __builtin_amdgcn_rsqf(s * (1.f / 1024.f) + 1e-6f); }
;     __device__ __forceinline__ void operator()(const f32x4 (&acc)[2][2][4][2], const Unit& u, int wr, int wc, int fr, int fq) const {
;     ...
;         const int row0 = u.pm * BM + wr * 64 + fr;
;         unsigned char* const hb = (unsigned char*)H + (size_t)(u.pm * (FFH / 128) + u.pn + pn0) * 32768 + (((wr * 4 + wc) * 8) * 64 + (fq >> 1) * 32 + fr * 2 + (fq & 1)) * 8;
;         f32x4 pa[2][4];
; #pragma unroll
;         for (int ai = 0; ai < 2; ++ai)
; #pragma unroll
;             for (int m = 0; m < 4; ++m) pa[ai][m] = rstd_ld4(ss, row0 + ai * HALF + m * 16, fq);
; #pragma unroll
;         for (int ai = 0; ai < 2; ++ai)
; #pragma unroll
;             for (int m = 0; m < 4; ++m) { const float rs = rstd_fin4(pa[ai][m]) * sc;
;                 const float rsl = rs * 1.4426950408889634f, rsu = rs * 0.6931471805599453f;
;                 f32x4 h0, h1;
; #pragma unroll
;                 for (int n = 0; n < 2; ++n) { const f32x4 G = acc[ai][0][m][n], U = acc[ai][1][m][n]; f32x4 hv;
; #pragma unroll
;                     for (int q = 0; q < 2; ++q) { const f32x2 g2 = (f32x2){G[2 * q], G[2 * q + 1]} * rsl, u2 = (f32x2){U[2 * q], U[2 * q + 1]} * rsu;
;                         f32x2 r2; r2.x = __builtin_amdgcn_rcpf(1.f + __builtin_amdgcn_exp2f(-g2.x)); r2.y = __builtin_amdgcn_rcpf(1.f + __builtin_amdgcn_exp2f(-g2.y));
;                         const f32x2 o2 = g2 * u2 * r2; hv[2 * q] = o2.x; hv[2 * q + 1] = o2.y; }
;                     if (n == 0) h0 = hv; else h1 = hv; }
;                 unsigned w0 = 0u, w1 = 0u;
;                 w0 = __builtin_amdgcn_cvt_pk_fp8_f32(h0[0], h0[1], w0, false); w0 = __builtin_amdgcn_cvt_pk_fp8_f32(h0[2], h0[3], w0, true); w1 = __builtin_amdgcn_cvt_pk_fp8_f32(h1[0], h1[1], w1, false); w1 = __builtin_amdgcn_cvt_pk_fp8_f32(h1[2], h1[3], w1, true);
;                 *(u32x2*)(hb + (ai * 4 + m) * 512) = (u32x2){w0, w1}; asm volatile("" ::: "memory"); }
	v_add_f32_e32 v18, v22, v23
	v_fmamk_f32 v18, v18, 0x3a800000, v227
	v_rsq_f32_e32 v18, v18
	global_store_dwordx2 v[24:25], v[16:17], off offset:1536
	v_mul_f32_e32 v17, 0x3c800000, v18
	v_mul_f32_e32 v16, 0x3fb8aa3b, v17
	v_pk_mul_f32 v[18:19], v[96:97], v[16:17] op_sel_hi:[1,0]
	v_mul_f32_e32 v20, 0x3f317218, v17
	v_exp_f32_e64 v21, -v18
	v_exp_f32_e64 v17, -v19
	v_pk_mul_f32 v[22:23], v[88:89], v[20:21] op_sel_hi:[1,0]
	v_add_f32_e32 v17, 1.0, v17
	v_pk_mul_f32 v[18:19], v[18:19], v[22:23]
	v_pk_mul_f32 v[22:23], v[98:99], v[16:17] op_sel_hi:[1,0]
	v_add_f32_e32 v21, 1.0, v21
	v_rcp_f32_e32 v29, v17
	v_exp_f32_e64 v17, -v22
	v_rcp_f32_e32 v28, v21
	v_exp_f32_e64 v21, -v23
	v_add_f32_e32 v17, 1.0, v17
	v_pk_mul_f32 v[18:19], v[18:19], v[28:29]
	v_pk_mul_f32 v[28:29], v[90:91], v[20:21] op_sel_hi:[1,0]
	v_rcp_f32_e32 v30, v17
	v_add_f32_e32 v17, 1.0, v21
	v_pk_mul_f32 v[22:23], v[22:23], v[28:29]
	v_pk_mul_f32 v[28:29], v[92:93], v[16:17] op_sel_hi:[1,0]
	v_rcp_f32_e32 v31, v17
	v_exp_f32_e64 v21, -v29
	v_exp_f32_e64 v17, -v28
	v_pk_mul_f32 v[22:23], v[22:23], v[30:31]
	v_pk_mul_f32 v[30:31], v[84:85], v[20:21] op_sel_hi:[1,0]
	v_add_f32_e32 v17, 1.0, v17
	v_pk_mul_f32 v[28:29], v[28:29], v[30:31]
	s_waitcnt vmcnt(6)
	v_mov_b32_e32 v30, v13
	v_mov_b32_e32 v31, v14
	v_mov_b32_e32 v13, v15
	v_pk_add_f32 v[12:13], v[30:31], v[12:13]
	v_rcp_f32_e32 v32, v17
	v_add_f32_e32 v30, v12, v13
	v_mov_b32_e32 v31, v30
	s_nop 1
	v_permlane16_swap_b32_e32 v31, v30
	v_add_f32_e32 v17, 1.0, v21
	v_rcp_f32_e32 v33, v17
	v_pk_mul_f32 v[16:17], v[94:95], v[16:17] op_sel_hi:[1,0]
	v_pk_mul_f32 v[20:21], v[86:87], v[20:21] op_sel_hi:[1,0]
	v_exp_f32_e64 v34, -v16
	v_pk_mul_f32 v[14:15], v[16:17], v[20:21]
	s_waitcnt lgkmcnt(0)
	v_add_f32_e32 v20, v30, v31
	v_mov_b32_e32 v21, v20
	s_nop 1
	v_permlane32_swap_b32_e32 v21, v20
	v_pk_mul_f32 v[28:29], v[28:29], v[32:33]
	v_exp_f32_e64 v33, -v17
	v_mov_b32_e32 v16, v3
	v_add_f32_e32 v32, 1.0, v34
	v_cvt_pk_fp8_f32 v16, v18, v19
	v_add_f32_e32 v13, 1.0, v33
	s_waitcnt lgkmcnt(0)
	v_add_f32_e32 v18, v20, v21
	v_rcp_f32_e32 v12, v32
	v_rcp_f32_e32 v13, v13
	v_mov_b32_e32 v17, v3
	v_fmamk_f32 v18, v18, 0x3a800000, v227
	v_cvt_pk_fp8_f32 v17, v28, v29
	v_rsq_f32_e32 v18, v18
	v_pk_mul_f32 v[12:13], v[14:15], v[12:13]
	v_cvt_pk_fp8_f32 v16, v22, v23 op_sel:[0,0,1]
	v_cvt_pk_fp8_f32 v17, v12, v13 op_sel:[0,0,1]
	v_mul_f32_e32 v13, 0x3c800000, v18
	v_mul_f32_e32 v12, 0x3fb8aa3b, v13
	v_pk_mul_f32 v[14:15], v[80:81], v[12:13] op_sel_hi:[1,0]
	v_mul_f32_e32 v18, 0x3f317218, v13
	v_exp_f32_e64 v19, -v14
	v_exp_f32_e64 v13, -v15
	global_store_dwordx2 v[24:25], v[16:17], off offset:2048
	v_pk_mul_f32 v[20:21], v[72:73], v[18:19] op_sel_hi:[1,0]
	v_add_f32_e32 v13, 1.0, v13
	v_pk_mul_f32 v[14:15], v[14:15], v[20:21]
	v_pk_mul_f32 v[20:21], v[82:83], v[12:13] op_sel_hi:[1,0]
	v_add_f32_e32 v19, 1.0, v19
	v_rcp_f32_e32 v23, v13
	v_exp_f32_e64 v13, -v20
	v_rcp_f32_e32 v22, v19
	v_exp_f32_e64 v19, -v21
	v_add_f32_e32 v13, 1.0, v13
	v_pk_mul_f32 v[14:15], v[14:15], v[22:23]
	v_pk_mul_f32 v[22:23], v[74:75], v[18:19] op_sel_hi:[1,0]
	v_rcp_f32_e32 v28, v13
	v_add_f32_e32 v13, 1.0, v19
	v_pk_mul_f32 v[20:21], v[20:21], v[22:23]
	v_pk_mul_f32 v[22:23], v[76:77], v[12:13] op_sel_hi:[1,0]
	v_rcp_f32_e32 v29, v13
	v_exp_f32_e64 v13, -v22
	v_exp_f32_e64 v19, -v23
	v_pk_mul_f32 v[20:21], v[20:21], v[28:29]
	v_add_f32_e32 v13, 1.0, v13
	v_rcp_f32_e32 v30, v13
	v_add_f32_e32 v13, 1.0, v19
	v_rcp_f32_e32 v31, v13
	v_pk_mul_f32 v[28:29], v[68:69], v[18:19] op_sel_hi:[1,0]
	v_pk_mul_f32 v[12:13], v[78:79], v[12:13] op_sel_hi:[1,0]
	v_pk_mul_f32 v[22:23], v[22:23], v[28:29]
	v_exp_f32_e64 v28, -v12
	v_pk_mul_f32 v[22:23], v[22:23], v[30:31]
	s_waitcnt vmcnt(6)
	v_mov_b32_e32 v30, v9
	v_mov_b32_e32 v31, v10
	v_mov_b32_e32 v9, v11
	v_pk_add_f32 v[8:9], v[30:31], v[8:9]
	v_exp_f32_e64 v29, -v13
	v_add_f32_e32 v10, v8, v9
	v_mov_b32_e32 v11, v10
	s_nop 1
	v_permlane16_swap_b32_e32 v11, v10
	v_mov_b32_e32 v8, v3
	v_add_f32_e32 v28, 1.0, v28
	v_add_f32_e32 v29, 1.0, v29
	v_cvt_pk_fp8_f32 v8, v14, v15
	s_waitcnt lgkmcnt(0)
	v_add_f32_e32 v14, v10, v11
	v_rcp_f32_e32 v28, v28
	v_rcp_f32_e32 v29, v29
	v_mov_b32_e32 v9, v3
	v_mov_b32_e32 v15, v14
	s_nop 1
	v_permlane32_swap_b32_e32 v15, v14
	v_cvt_pk_fp8_f32 v9, v22, v23
	v_pk_mul_f32 v[18:19], v[70:71], v[18:19] op_sel_hi:[1,0]
	v_cvt_pk_fp8_f32 v8, v20, v21 op_sel:[0,0,1]
	v_pk_mul_f32 v[10:11], v[12:13], v[18:19]
	s_nop 0
	v_pk_mul_f32 v[10:11], v[10:11], v[28:29]
	s_nop 0
	v_cvt_pk_fp8_f32 v9, v10, v11 op_sel:[0,0,1]
	s_waitcnt lgkmcnt(0)
; __device__ __forceinline__ float rstd_fin4(const f32x4 a) { float s = (a[0] + a[1]) + (a[2] + a[3]); s += __shfl_xor(s, 16); s += __shfl_xor(s, 32); return __builtin_amdgcn_rsqf(s * (1.f / 1024.f) + 1e-6f); }
;     __device__ __forceinline__ void operator()(const f32x4 (&acc)[2][2][4][2], const Unit& u, int wr, int wc, int fr, int fq) const {
;     ...
;             for (int m = 0; m < 4; ++m) pa[ai][m] = rstd_ld4(ss, row0 + ai * HALF + m * 16, fq);
; #pragma unroll
;         for (int ai = 0; ai < 2; ++ai)
; #pragma unroll
;             for (int m = 0; m < 4; ++m) { const float rs = rstd_fin4(pa[ai][m]) * sc;
;                 const float rsl = rs * 1.4426950408889634f, rsu = rs * 0.6931471805599453f;
;                 f32x4 h0, h1;
; #pragma unroll
;                 for (int n = 0; n < 2; ++n) { const f32x4 G = acc[ai][0][m][n], U = acc[ai][1][m][n]; f32x4 hv;
; #pragma unroll
;                     for (int q = 0; q < 2; ++q) { const f32x2 g2 = (f32x2){G[2 * q], G[2 * q + 1]} * rsl, u2 = (f32x2){U[2 * q], U[2 * q + 1]} * rsu;
;                         f32x2 r2; r2.x = __builtin_amdgcn_rcpf(1.f + __builtin_amdgcn_exp2f(-g2.x)); r2.y = __builtin_amdgcn_rcpf(1.f + __builtin_amdgcn_exp2f(-g2.y));
;                         const f32x2 o2 = g2 * u2 * r2; hv[2 * q] = o2.x; hv[2 * q + 1] = o2.y; }
;                     if (n == 0) h0 = hv; else h1 = hv; }
;                 unsigned w0 = 0u, w1 = 0u;
;                 w0 = __builtin_amdgcn_cvt_pk_fp8_f32(h0[0], h0[1], w0, false); w0 = __builtin_amdgcn_cvt_pk_fp8_f32(h0[2], h0[3], w0, true); w1 = __builtin_amdgcn_cvt_pk_fp8_f32(h1[0], h1[1], w1, false); w1 = __builtin_amdgcn_cvt_pk_fp8_f32(h1[2], h1[3], w1, true);
;                 *(u32x2*)(hb + (ai * 4 + m) * 512) = (u32x2){w0, w1}; asm volatile("" ::: "memory"); }
	v_add_f32_e32 v10, v14, v15
	v_fmamk_f32 v10, v10, 0x3a800000, v227
	v_rsq_f32_e32 v10, v10
	global_store_dwordx2 v[24:25], v[8:9], off offset:2560
	v_mul_f32_e32 v9, 0x3c800000, v10
	v_mul_f32_e32 v8, 0x3fb8aa3b, v9
	v_pk_mul_f32 v[10:11], v[64:65], v[8:9] op_sel_hi:[1,0]
	v_mul_f32_e32 v12, 0x3f317218, v9
	v_exp_f32_e64 v13, -v10
	v_exp_f32_e64 v9, -v11
	v_pk_mul_f32 v[14:15], v[56:57], v[12:13] op_sel_hi:[1,0]
	v_add_f32_e32 v9, 1.0, v9
	v_pk_mul_f32 v[10:11], v[10:11], v[14:15]
	v_pk_mul_f32 v[14:15], v[66:67], v[8:9] op_sel_hi:[1,0]
	v_add_f32_e32 v13, 1.0, v13
	v_rcp_f32_e32 v17, v9
	v_exp_f32_e64 v9, -v14
	v_rcp_f32_e32 v16, v13
	v_exp_f32_e64 v13, -v15
	v_add_f32_e32 v9, 1.0, v9
	v_pk_mul_f32 v[10:11], v[10:11], v[16:17]
	v_pk_mul_f32 v[16:17], v[58:59], v[12:13] op_sel_hi:[1,0]
	v_rcp_f32_e32 v18, v9
	v_add_f32_e32 v9, 1.0, v13
	v_pk_mul_f32 v[14:15], v[14:15], v[16:17]
	v_pk_mul_f32 v[16:17], v[60:61], v[8:9] op_sel_hi:[1,0]
	v_rcp_f32_e32 v19, v9
	v_exp_f32_e64 v13, -v17
	v_exp_f32_e64 v9, -v16
	v_pk_mul_f32 v[14:15], v[14:15], v[18:19]
	v_pk_mul_f32 v[18:19], v[52:53], v[12:13] op_sel_hi:[1,0]
	v_add_f32_e32 v9, 1.0, v9
	v_pk_mul_f32 v[16:17], v[16:17], v[18:19]
	s_waitcnt vmcnt(6)
	v_mov_b32_e32 v18, v5
	v_mov_b32_e32 v19, v6
	v_mov_b32_e32 v5, v7
	v_pk_add_f32 v[4:5], v[18:19], v[4:5]
	v_rcp_f32_e32 v20, v9
	v_add_f32_e32 v18, v4, v5
	v_mov_b32_e32 v19, v18
	s_nop 1
	v_permlane16_swap_b32_e32 v19, v18
	v_add_f32_e32 v9, 1.0, v13
	v_rcp_f32_e32 v21, v9
	v_pk_mul_f32 v[8:9], v[62:63], v[8:9] op_sel_hi:[1,0]
	v_pk_mul_f32 v[12:13], v[54:55], v[12:13] op_sel_hi:[1,0]
	v_exp_f32_e64 v22, -v8
	v_pk_mul_f32 v[6:7], v[8:9], v[12:13]
	s_waitcnt lgkmcnt(0)
	v_add_f32_e32 v12, v18, v19
	v_mov_b32_e32 v13, v12
	s_nop 1
	v_permlane32_swap_b32_e32 v13, v12
	v_pk_mul_f32 v[16:17], v[16:17], v[20:21]
	v_exp_f32_e64 v21, -v9
	v_mov_b32_e32 v8, v3
	v_add_f32_e32 v20, 1.0, v22
	v_cvt_pk_fp8_f32 v8, v10, v11
	v_add_f32_e32 v5, 1.0, v21
	s_waitcnt lgkmcnt(0)
	v_add_f32_e32 v10, v12, v13
	v_rcp_f32_e32 v4, v20
	v_rcp_f32_e32 v5, v5
	v_mov_b32_e32 v9, v3
	v_fmamk_f32 v10, v10, 0x3a800000, v227
	v_cvt_pk_fp8_f32 v9, v16, v17
	v_rsq_f32_e32 v10, v10
	v_pk_mul_f32 v[4:5], v[6:7], v[4:5]
	v_cvt_pk_fp8_f32 v8, v14, v15 op_sel:[0,0,1]
	v_cvt_pk_fp8_f32 v9, v4, v5 op_sel:[0,0,1]
	v_mul_f32_e32 v5, 0x3c800000, v10
	v_mul_f32_e32 v4, 0x3fb8aa3b, v5
	v_pk_mul_f32 v[6:7], v[48:49], v[4:5] op_sel_hi:[1,0]
	v_mul_f32_e32 v10, 0x3f317218, v5
	v_exp_f32_e64 v11, -v6
	v_exp_f32_e64 v5, -v7
	global_store_dwordx2 v[24:25], v[8:9], off offset:3072
	v_pk_mul_f32 v[12:13], v[40:41], v[10:11] op_sel_hi:[1,0]
	v_add_f32_e32 v5, 1.0, v5
	v_pk_mul_f32 v[6:7], v[6:7], v[12:13]
	v_pk_mul_f32 v[12:13], v[50:51], v[4:5] op_sel_hi:[1,0]
	v_add_f32_e32 v11, 1.0, v11
	v_rcp_f32_e32 v15, v5
	v_exp_f32_e64 v5, -v12
	v_rcp_f32_e32 v14, v11
	v_exp_f32_e64 v11, -v13
	v_add_f32_e32 v5, 1.0, v5
	v_pk_mul_f32 v[6:7], v[6:7], v[14:15]
	v_pk_mul_f32 v[14:15], v[42:43], v[10:11] op_sel_hi:[1,0]
	v_rcp_f32_e32 v16, v5
	v_add_f32_e32 v5, 1.0, v11
	v_pk_mul_f32 v[12:13], v[12:13], v[14:15]
	v_pk_mul_f32 v[14:15], v[44:45], v[4:5] op_sel_hi:[1,0]
	v_rcp_f32_e32 v17, v5
	v_exp_f32_e64 v5, -v14
	v_exp_f32_e64 v11, -v15
	v_pk_mul_f32 v[12:13], v[12:13], v[16:17]
	v_add_f32_e32 v5, 1.0, v5
	v_rcp_f32_e32 v18, v5
	v_add_f32_e32 v5, 1.0, v11
	v_pk_mul_f32 v[16:17], v[36:37], v[10:11] op_sel_hi:[1,0]
	v_rcp_f32_e32 v19, v5
	v_pk_mul_f32 v[4:5], v[46:47], v[4:5] op_sel_hi:[1,0]
	v_pk_mul_f32 v[14:15], v[14:15], v[16:17]
	v_exp_f32_e64 v16, -v4
	v_exp_f32_e64 v17, -v5
	v_pk_mul_f32 v[14:15], v[14:15], v[18:19]
	v_mov_b32_e32 v18, v3
	v_add_f32_e32 v16, 1.0, v16
	v_add_f32_e32 v17, 1.0, v17
	v_rcp_f32_e32 v16, v16
	v_rcp_f32_e32 v17, v17
	v_mov_b32_e32 v19, v3
	v_cvt_pk_fp8_f32 v18, v6, v7
	v_cvt_pk_fp8_f32 v19, v14, v15
	v_pk_mul_f32 v[10:11], v[38:39], v[10:11] op_sel_hi:[1,0]
	v_cvt_pk_fp8_f32 v18, v12, v13 op_sel:[0,0,1]
	v_pk_mul_f32 v[4:5], v[4:5], v[10:11]
	s_nop 0
	v_pk_mul_f32 v[4:5], v[4:5], v[16:17]
	s_nop 0
	v_cvt_pk_fp8_f32 v19, v4, v5 op_sel:[0,0,1]
	global_store_dwordx2 v[24:25], v[18:19], off offset:3584
	s_cbranch_vccnz .LBB0_1685
	s_andn2_b64 vcc, exec, s[38:39]
	s_cbranch_vccnz .LBB0_1684
	s_barrier
	s_branch .LBB0_1684

; __device__ __forceinline__ float rstd_fin4(const f32x4 a) { float s = (a[0] + a[1]) + (a[2] + a[3]); s += __shfl_xor(s, 16); s += __shfl_xor(s, 32); return __builtin_amdgcn_rsqf(s * (1.f / 1024.f) + 1e-6f); }
;     __device__ __forceinline__ void operator()(const f32x4 (&acc)[2][2][4][2], const Unit& u, int wr, int wc, int fr, int fq) const {
;         asm volatile("" : "+v"(fr), "+v"(fq));
;         const int row0 = u.pm * BM + wr * 64 + fr;
;         unsigned char* const hb = (unsigned char*)H + (size_t)(u.pm * (FFH / 128) + u.pn + pn0) * 32768 + (((wr * 4 + wc) * 8) * 64 + (fq >> 1) * 32 + fr * 2 + (fq & 1)) * 8;
;         f32x4 pa[2][4];
; #pragma unroll
;         for (int ai = 0; ai < 2; ++ai)
; #pragma unroll
;             for (int m = 0; m < 4; ++m) pa[ai][m] = rstd_ld4(ss, row0 + ai * HALF + m * 16, fq);
; #pragma unroll
;         for (int ai = 0; ai < 2; ++ai)
; #pragma unroll
;             for (int m = 0; m < 4; ++m) { const float rs = rstd_fin4(pa[ai][m]) * sc;
;                 const float rsl = rs * 1.4426950408889634f, rsu = rs * 0.6931471805599453f;
;                 f32x4 h0, h1;
; #pragma unroll
;                 for (int n = 0; n < 2; ++n) { const f32x4 G = acc[ai][0][m][n], U = acc[ai][1][m][n]; f32x4 hv;
; #pragma unroll
;                     for (int q = 0; q < 2; ++q) { const f32x2 g2 = (f32x2){G[2 * q], G[2 * q + 1]} * rsl, u2 = (f32x2){U[2 * q], U[2 * q + 1]} * rsu;
;                         f32x2 r2; r2.x = __builtin_amdgcn_rcpf(1.f + __builtin_amdgcn_exp2f(-g2.x)); r2.y = __builtin_amdgcn_rcpf(1.f + __builtin_amdgcn_exp2f(-g2.y));
;                         const f32x2 o2 = g2 * u2 * r2; hv[2 * q] = o2.x; hv[2 * q + 1] = o2.y; }
;                     if (n == 0) h0 = hv; else h1 = hv; }
;                 unsigned w0 = 0u, w1 = 0u;
;                 w0 = __builtin_amdgcn_cvt_pk_fp8_f32(h0[0], h0[1], w0, false); w0 = __builtin_amdgcn_cvt_pk_fp8_f32(h0[2], h0[3], w0, true); w1 = __builtin_amdgcn_cvt_pk_fp8_f32(h1[0], h1[1], w1, false); w1 = __builtin_amdgcn_cvt_pk_fp8_f32(h1[2], h1[3], w1, true);
;                 *(u32x2*)(hb + (ai * 4 + m) * 512) = (u32x2){w0, w1}; asm volatile("" ::: "memory"); }
.LBB0_1712:
	s_lshl_b32 s4, s70, 8
	v_mov_b32_e32 v142, v168
	v_mov_b32_e32 v143, v1
	s_add_i32 s4, s4, s64
	v_and_b32_e32 v145, 64, v246
	v_add_u32_e32 v124, s4, v143
	v_lshlrev_b32_e32 v126, 2, v142
	v_ashrrev_i32_e32 v127, 31, v126
	v_ashrrev_i32_e32 v125, 31, v124
	v_lshl_add_u64 v[126:127], v[126:127], 2, s[44:45]
	v_lshlrev_b64 v[124:125], 6, v[124:125]
	v_lshl_add_u64 v[140:141], v[126:127], 0, v[124:125]
	global_load_dwordx4 v[136:139], v[140:141], off
	global_load_dwordx4 v[124:127], v[140:141], off offset:1024
	global_load_dwordx4 v[152:155], v[140:141], off offset:2048
	global_load_dwordx4 v[148:151], v[140:141], off offset:3072
	v_xor_b32_e32 v144, 16, v246
	v_add_u32_e32 v145, 64, v145
	v_xor_b32_e32 v146, 32, v246
	v_cmp_lt_i32_e32 vcc, v144, v145
	v_mov_b32_e32 v174, v3
	v_mov_b32_e32 v175, v3
	v_cndmask_b32_e32 v144, v246, v144, vcc
	v_cmp_lt_i32_e32 vcc, v146, v145
	v_lshlrev_b32_e32 v172, 2, v144
	s_mul_i32 s4, s70, 22
	v_cndmask_b32_e32 v145, v246, v146, vcc
	v_lshlrev_b32_e32 v171, 2, v145
	s_add_i32 s4, s69, s4
	s_add_i32 s4, s4, 18
	v_lshlrev_b32_e32 v147, 4, v142
	v_lshl_add_u32 v143, v143, 1, s67
	s_ashr_i32 s5, s4, 31
	v_and_b32_e32 v146, 0x1fffffe0, v147
	v_and_or_b32 v142, v142, 1, v143
	s_lshl_b64 s[4:5], s[4:5], 15
	v_add_lshl_u32 v142, v142, v146, 3
	s_add_u32 s4, s6, s4
	v_ashrrev_i32_e32 v143, 31, v142
	s_addc_u32 s5, s7, s5
	v_lshl_add_u64 v[166:167], s[4:5], 0, v[142:143]
	s_mov_b64 s[4:5], -1
	s_waitcnt vmcnt(0)
	v_mov_b32_e32 v144, v137
	v_mov_b32_e32 v145, v138
	v_mov_b32_e32 v137, v139
	v_mov_b32_e32 v138, v125
	v_mov_b32_e32 v139, v126
	v_mov_b32_e32 v125, v127
	v_pk_add_f32 v[126:127], v[144:145], v[136:137]
	v_pk_add_f32 v[124:125], v[138:139], v[124:125]
	v_add_f32_e32 v126, v126, v127
	v_add_f32_e32 v127, v124, v125
	v_mov_b32_e32 v136, v126
	s_nop 1
	v_permlane16_swap_b32_e32 v136, v126
	v_mov_b32_e32 v137, v127
	s_nop 1
	v_permlane16_swap_b32_e32 v137, v127
	v_add_co_u32_e32 v124, vcc, s88, v140
	s_waitcnt lgkmcnt(1)
	v_add_f32_e32 v126, v126, v136
	s_waitcnt lgkmcnt(0)
	v_add_f32_e32 v127, v127, v137
	v_mov_b32_e32 v136, v126
	s_nop 1
	v_permlane32_swap_b32_e32 v136, v126
	v_mov_b32_e32 v137, v127
	s_nop 1
	v_permlane32_swap_b32_e32 v137, v127
	v_addc_co_u32_e32 v125, vcc, 0, v141, vcc
	global_load_dwordx4 v[144:147], v[124:125], off
	global_load_dwordx4 v[140:143], v[124:125], off offset:1024
	s_waitcnt lgkmcnt(1)
	v_add_f32_e32 v126, v126, v136
	s_waitcnt lgkmcnt(0)
	v_add_f32_e32 v127, v127, v137
	v_fmamk_f32 v126, v126, 0x3a800000, v227
	v_fmamk_f32 v127, v127, 0x3a800000, v227
	v_rsq_f32_e32 v173, v126
	v_rsq_f32_e32 v177, v127
	global_load_dwordx4 v[136:139], v[124:125], off offset:2048
	s_nop 0
	global_load_dwordx4 v[124:127], v[124:125], off offset:3072
	s_andn2_b64 vcc, exec, s[40:41]
	v_mul_f32_e32 v176, 0x3fb8aa3b, v173
	v_mul_f32_e32 v178, 0x3f317218, v173
	v_pk_mul_f32 v[132:133], v[132:133], v[176:177] op_sel_hi:[1,0]
	v_pk_mul_f32 v[120:121], v[120:121], v[178:179] op_sel_hi:[1,0]
	v_pk_mul_f32 v[134:135], v[134:135], v[176:177] op_sel_hi:[1,0]
	v_pk_mul_f32 v[122:123], v[122:123], v[178:179] op_sel_hi:[1,0]
	v_pk_mul_f32 v[128:129], v[128:129], v[176:177] op_sel_hi:[1,0]
	v_pk_mul_f32 v[116:117], v[116:117], v[178:179] op_sel_hi:[1,0]
	v_pk_mul_f32 v[130:131], v[130:131], v[176:177] op_sel_hi:[1,0]
	v_exp_f32_e64 v173, -v132
	v_exp_f32_e64 v176, -v133
	v_pk_mul_f32 v[120:121], v[132:133], v[120:121]
	v_exp_f32_e64 v132, -v134
	v_exp_f32_e64 v133, -v135
	v_pk_mul_f32 v[122:123], v[134:135], v[122:123]
	v_exp_f32_e64 v134, -v128
	v_exp_f32_e64 v135, -v129
	v_pk_mul_f32 v[116:117], v[128:129], v[116:117]
	v_exp_f32_e64 v128, -v130
	v_exp_f32_e64 v129, -v131
	v_pk_mul_f32 v[118:119], v[118:119], v[178:179] op_sel_hi:[1,0]
	v_add_f32_e32 v132, 1.0, v132
	v_pk_mul_f32 v[118:119], v[130:131], v[118:119]
	v_add_f32_e32 v130, 1.0, v173
	v_add_f32_e32 v131, 1.0, v176
	v_add_f32_e32 v173, 1.0, v128
	v_add_f32_e32 v176, 1.0, v129
	v_rcp_f32_e32 v128, v130
	v_rcp_f32_e32 v129, v131
	v_add_f32_e32 v133, 1.0, v133
	v_add_f32_e32 v134, 1.0, v134
	v_add_f32_e32 v135, 1.0, v135
	v_rcp_f32_e32 v130, v132
	v_rcp_f32_e32 v131, v133
	v_rcp_f32_e32 v132, v134
	v_rcp_f32_e32 v133, v135
	v_pk_mul_f32 v[120:121], v[120:121], v[128:129]
	v_mul_f32_e32 v180, 0x3fb8aa3b, v177
	v_cvt_pk_fp8_f32 v174, v120, v121
	v_mul_f32_e32 v182, 0x3f317218, v177
	v_pk_mul_f32 v[116:117], v[116:117], v[132:133]
	v_pk_mul_f32 v[112:113], v[112:113], v[180:181] op_sel_hi:[1,0]
	v_pk_mul_f32 v[108:109], v[108:109], v[182:183] op_sel_hi:[1,0]
	v_cvt_pk_fp8_f32 v175, v116, v117
	v_pk_mul_f32 v[116:117], v[122:123], v[130:131]
	v_exp_f32_e64 v177, -v112
	v_cvt_pk_fp8_f32 v174, v116, v117 op_sel:[0,0,1]
	v_exp_f32_e64 v117, -v113
	v_pk_mul_f32 v[108:109], v[112:113], v[108:109]
	v_pk_mul_f32 v[112:113], v[114:115], v[180:181] op_sel_hi:[1,0]
	v_pk_mul_f32 v[110:111], v[110:111], v[182:183] op_sel_hi:[1,0]
	v_exp_f32_e64 v114, -v112
	v_exp_f32_e64 v115, -v113
	v_pk_mul_f32 v[104:105], v[104:105], v[180:181] op_sel_hi:[1,0]
	v_pk_mul_f32 v[110:111], v[112:113], v[110:111]
	v_add_f32_e32 v114, 1.0, v114
	v_add_f32_e32 v115, 1.0, v115
	v_exp_f32_e64 v112, -v104
	v_exp_f32_e64 v113, -v105
	v_rcp_f32_e32 v114, v114
	v_rcp_f32_e32 v115, v115
	v_add_f32_e32 v112, 1.0, v112
	v_add_f32_e32 v113, 1.0, v113
	v_pk_mul_f32 v[106:107], v[106:107], v[180:181] op_sel_hi:[1,0]
	v_pk_mul_f32 v[110:111], v[110:111], v[114:115]
	v_rcp_f32_e32 v112, v112
	v_rcp_f32_e32 v113, v113
	v_exp_f32_e64 v114, -v106
	v_pk_mul_f32 v[100:101], v[100:101], v[182:183] op_sel_hi:[1,0]
	v_add_f32_e32 v116, 1.0, v177
	v_pk_mul_f32 v[100:101], v[104:105], v[100:101]
	v_mov_b32_e32 v104, v153
	v_mov_b32_e32 v105, v154
	v_mov_b32_e32 v153, v155
	v_pk_add_f32 v[104:105], v[104:105], v[152:153]
	v_pk_mul_f32 v[100:101], v[100:101], v[112:113]
	v_add_f32_e32 v112, 1.0, v114
	v_add_f32_e32 v114, v104, v105
	v_mov_b32_e32 v115, v114
	s_nop 1
	v_permlane16_swap_b32_e32 v115, v114
	v_exp_f32_e64 v113, -v107
	v_rcp_f32_e32 v104, v112
	v_add_f32_e32 v117, 1.0, v117
	v_rcp_f32_e32 v116, v116
	s_waitcnt lgkmcnt(0)
; __device__ __forceinline__ float rstd_fin4(const f32x4 a) { float s = (a[0] + a[1]) + (a[2] + a[3]); s += __shfl_xor(s, 16); s += __shfl_xor(s, 32); return __builtin_amdgcn_rsqf(s * (1.f / 1024.f) + 1e-6f); }
;     __device__ __forceinline__ void operator()(const f32x4 (&acc)[2][2][4][2], const Unit& u, int wr, int wc, int fr, int fq) const {
;     ...
;             for (int m = 0; m < 4; ++m) { const float rs = rstd_fin4(pa[ai][m]) * sc;
;                 const float rsl = rs * 1.4426950408889634f, rsu = rs * 0.6931471805599453f;
;                 f32x4 h0, h1;
; #pragma unroll
;                 for (int n = 0; n < 2; ++n) { const f32x4 G = acc[ai][0][m][n], U = acc[ai][1][m][n]; f32x4 hv;
; #pragma unroll
;                     for (int q = 0; q < 2; ++q) { const f32x2 g2 = (f32x2){G[2 * q], G[2 * q + 1]} * rsl, u2 = (f32x2){U[2 * q], U[2 * q + 1]} * rsu;
;                         f32x2 r2; r2.x = __builtin_amdgcn_rcpf(1.f + __builtin_amdgcn_exp2f(-g2.x)); r2.y = __builtin_amdgcn_rcpf(1.f + __builtin_amdgcn_exp2f(-g2.y));
;                         const f32x2 o2 = g2 * u2 * r2; hv[2 * q] = o2.x; hv[2 * q + 1] = o2.y; }
;                     if (n == 0) h0 = hv; else h1 = hv; }
;                 unsigned w0 = 0u, w1 = 0u;
;                 w0 = __builtin_amdgcn_cvt_pk_fp8_f32(h0[0], h0[1], w0, false); w0 = __builtin_amdgcn_cvt_pk_fp8_f32(h0[2], h0[3], w0, true); w1 = __builtin_amdgcn_cvt_pk_fp8_f32(h1[0], h1[1], w1, false); w1 = __builtin_amdgcn_cvt_pk_fp8_f32(h1[2], h1[3], w1, true);
;                 *(u32x2*)(hb + (ai * 4 + m) * 512) = (u32x2){w0, w1}; asm volatile("" ::: "memory"); }
	v_add_f32_e32 v112, v114, v115
	v_add_f32_e32 v105, 1.0, v113
	v_mov_b32_e32 v113, v112
	s_nop 1
	v_permlane32_swap_b32_e32 v113, v112
	v_rcp_f32_e32 v117, v117
	v_pk_mul_f32 v[102:103], v[102:103], v[182:183] op_sel_hi:[1,0]
	v_rcp_f32_e32 v105, v105
	v_pk_mul_f32 v[102:103], v[106:107], v[102:103]
	v_mov_b32_e32 v107, v3
	v_cvt_pk_fp8_f32 v107, v100, v101
	s_waitcnt lgkmcnt(0)
	v_add_f32_e32 v100, v112, v113
	v_pk_mul_f32 v[108:109], v[108:109], v[116:117]
	v_mov_b32_e32 v106, v3
	v_fmamk_f32 v100, v100, 0x3a800000, v227
	v_cvt_pk_fp8_f32 v106, v108, v109
	v_rsq_f32_e32 v108, v100
	v_pk_mul_f32 v[100:101], v[102:103], v[104:105]
	v_rcp_f32_e32 v134, v173
	v_cvt_pk_fp8_f32 v107, v100, v101 op_sel:[0,0,1]
	v_mul_f32_e32 v100, 0x3fb8aa3b, v108
	v_pk_mul_f32 v[96:97], v[96:97], v[100:101] op_sel_hi:[1,0]
	v_mul_f32_e32 v102, 0x3f317218, v108
	v_exp_f32_e64 v101, -v96
	v_exp_f32_e64 v103, -v97
	v_rcp_f32_e32 v135, v176
	v_cvt_pk_fp8_f32 v106, v110, v111 op_sel:[0,0,1]
	v_add_f32_e32 v101, 1.0, v101
	v_pk_mul_f32 v[92:93], v[92:93], v[102:103] op_sel_hi:[1,0]
	v_rcp_f32_e32 v104, v101
	v_add_f32_e32 v101, 1.0, v103
	v_pk_mul_f32 v[92:93], v[96:97], v[92:93]
	v_pk_mul_f32 v[96:97], v[98:99], v[100:101] op_sel_hi:[1,0]
	v_pk_mul_f32 v[94:95], v[94:95], v[102:103] op_sel_hi:[1,0]
	v_pk_mul_f32 v[88:89], v[88:89], v[100:101] op_sel_hi:[1,0]
	v_exp_f32_e64 v98, -v96
	v_exp_f32_e64 v99, -v97
	v_pk_mul_f32 v[94:95], v[96:97], v[94:95]
	v_exp_f32_e64 v96, -v88
	v_exp_f32_e64 v97, -v89
	v_add_f32_e32 v98, 1.0, v98
	v_add_f32_e32 v99, 1.0, v99
	v_add_f32_e32 v96, 1.0, v96
	v_add_f32_e32 v97, 1.0, v97
	v_rcp_f32_e32 v96, v96
	v_rcp_f32_e32 v97, v97
	v_rcp_f32_e32 v98, v98
	v_rcp_f32_e32 v99, v99
	v_pk_mul_f32 v[84:85], v[84:85], v[102:103] op_sel_hi:[1,0]
	v_rcp_f32_e32 v105, v101
	v_pk_mul_f32 v[84:85], v[88:89], v[84:85]
	v_pk_mul_f32 v[94:95], v[94:95], v[98:99]
	v_pk_mul_f32 v[84:85], v[84:85], v[96:97]
	v_mov_b32_e32 v96, v149
	v_mov_b32_e32 v97, v150
	v_mov_b32_e32 v149, v151
	v_pk_add_f32 v[96:97], v[96:97], v[148:149]
	v_pk_mul_f32 v[88:89], v[90:91], v[100:101] op_sel_hi:[1,0]
	v_add_f32_e32 v98, v96, v97
	v_mov_b32_e32 v99, v98
	s_nop 1
	v_permlane16_swap_b32_e32 v99, v98
	v_exp_f32_e64 v90, -v88
	v_exp_f32_e64 v91, -v89
	v_pk_mul_f32 v[92:93], v[92:93], v[104:105]
	v_mov_b32_e32 v96, v3
	v_add_f32_e32 v90, 1.0, v90
	v_add_f32_e32 v91, 1.0, v91
	v_cvt_pk_fp8_f32 v96, v92, v93
	s_waitcnt lgkmcnt(0)
	v_add_f32_e32 v92, v98, v99
	v_rcp_f32_e32 v90, v90
	v_rcp_f32_e32 v91, v91
	v_mov_b32_e32 v97, v3
	v_mov_b32_e32 v93, v92
	s_nop 1
	v_permlane32_swap_b32_e32 v93, v92
	v_cvt_pk_fp8_f32 v97, v84, v85
	v_pk_mul_f32 v[86:87], v[86:87], v[102:103] op_sel_hi:[1,0]
	v_pk_mul_f32 v[118:119], v[118:119], v[134:135]
	v_pk_mul_f32 v[84:85], v[88:89], v[86:87]
	v_cvt_pk_fp8_f32 v175, v118, v119 op_sel:[0,0,1]
	v_pk_mul_f32 v[84:85], v[84:85], v[90:91]
	v_cvt_pk_fp8_f32 v96, v94, v95 op_sel:[0,0,1]
	v_cvt_pk_fp8_f32 v97, v84, v85 op_sel:[0,0,1]
	s_waitcnt lgkmcnt(0)
	v_add_f32_e32 v84, v92, v93
	v_fmamk_f32 v84, v84, 0x3a800000, v227
	v_rsq_f32_e32 v85, v84
	global_store_dwordx2 v[166:167], v[174:175], off
	global_store_dwordx2 v[166:167], v[106:107], off offset:512
	v_mul_f32_e32 v84, 0x3fb8aa3b, v85
	v_pk_mul_f32 v[80:81], v[80:81], v[84:85] op_sel_hi:[1,0]
	v_mul_f32_e32 v86, 0x3f317218, v85
	v_exp_f32_e64 v87, -v80
	v_exp_f32_e64 v85, -v81
	global_store_dwordx2 v[166:167], v[96:97], off offset:1024
	v_pk_mul_f32 v[76:77], v[76:77], v[86:87] op_sel_hi:[1,0]
	v_add_f32_e32 v87, 1.0, v87
	v_add_f32_e32 v85, 1.0, v85
	v_pk_mul_f32 v[76:77], v[80:81], v[76:77]
	v_pk_mul_f32 v[80:81], v[82:83], v[84:85] op_sel_hi:[1,0]
	v_pk_mul_f32 v[78:79], v[78:79], v[86:87] op_sel_hi:[1,0]
	v_pk_mul_f32 v[72:73], v[72:73], v[84:85] op_sel_hi:[1,0]
	v_exp_f32_e64 v82, -v80
	v_exp_f32_e64 v83, -v81
	v_pk_mul_f32 v[78:79], v[80:81], v[78:79]
	v_exp_f32_e64 v80, -v72
	v_exp_f32_e64 v81, -v73
	v_add_f32_e32 v82, 1.0, v82
	v_add_f32_e32 v83, 1.0, v83
	v_add_f32_e32 v80, 1.0, v80
	v_add_f32_e32 v81, 1.0, v81
	v_rcp_f32_e32 v80, v80
	v_rcp_f32_e32 v81, v81
	v_rcp_f32_e32 v82, v82
	v_rcp_f32_e32 v83, v83
	v_pk_mul_f32 v[68:69], v[68:69], v[86:87] op_sel_hi:[1,0]
	v_rcp_f32_e32 v88, v87
	v_pk_mul_f32 v[68:69], v[72:73], v[68:69]
	v_pk_mul_f32 v[78:79], v[78:79], v[82:83]
	v_pk_mul_f32 v[68:69], v[68:69], v[80:81]
	s_waitcnt vmcnt(6)
	v_mov_b32_e32 v80, v145
	v_mov_b32_e32 v81, v146
	v_mov_b32_e32 v145, v147
	v_pk_add_f32 v[80:81], v[80:81], v[144:145]
	v_rcp_f32_e32 v89, v85
	v_add_f32_e32 v82, v80, v81
	v_pk_mul_f32 v[72:73], v[74:75], v[84:85] op_sel_hi:[1,0]
	v_mov_b32_e32 v83, v82
	s_nop 1
	v_permlane16_swap_b32_e32 v83, v82
	v_exp_f32_e64 v74, -v72
	v_exp_f32_e64 v75, -v73
	v_pk_mul_f32 v[76:77], v[76:77], v[88:89]
	v_mov_b32_e32 v80, v3
	v_add_f32_e32 v74, 1.0, v74
	v_add_f32_e32 v75, 1.0, v75
	v_cvt_pk_fp8_f32 v80, v76, v77
	s_waitcnt lgkmcnt(0)
	v_add_f32_e32 v76, v82, v83
	v_rcp_f32_e32 v74, v74
	v_rcp_f32_e32 v75, v75
	v_mov_b32_e32 v81, v3
	v_mov_b32_e32 v77, v76
	s_nop 1
	v_permlane32_swap_b32_e32 v77, v76
	v_cvt_pk_fp8_f32 v81, v68, v69
	v_pk_mul_f32 v[70:71], v[70:71], v[86:87] op_sel_hi:[1,0]
	v_cvt_pk_fp8_f32 v80, v78, v79 op_sel:[0,0,1]
	v_pk_mul_f32 v[68:69], v[72:73], v[70:71]
	s_nop 0
	v_pk_mul_f32 v[68:69], v[68:69], v[74:75]
	s_nop 0
	v_cvt_pk_fp8_f32 v81, v68, v69 op_sel:[0,0,1]
	s_waitcnt lgkmcnt(0)
; __device__ __forceinline__ float rstd_fin4(const f32x4 a) { float s = (a[0] + a[1]) + (a[2] + a[3]); s += __shfl_xor(s, 16); s += __shfl_xor(s, 32); return __builtin_amdgcn_rsqf(s * (1.f / 1024.f) + 1e-6f); }
;     __device__ __forceinline__ void operator()(const f32x4 (&acc)[2][2][4][2], const Unit& u, int wr, int wc, int fr, int fq) const {
;     ...
;             for (int m = 0; m < 4; ++m) { const float rs = rstd_fin4(pa[ai][m]) * sc;
;                 const float rsl = rs * 1.4426950408889634f, rsu = rs * 0.6931471805599453f;
;                 f32x4 h0, h1;
; #pragma unroll
;                 for (int n = 0; n < 2; ++n) { const f32x4 G = acc[ai][0][m][n], U = acc[ai][1][m][n]; f32x4 hv;
; #pragma unroll
;                     for (int q = 0; q < 2; ++q) { const f32x2 g2 = (f32x2){G[2 * q], G[2 * q + 1]} * rsl, u2 = (f32x2){U[2 * q], U[2 * q + 1]} * rsu;
;                         f32x2 r2; r2.x = __builtin_amdgcn_rcpf(1.f + __builtin_amdgcn_exp2f(-g2.x)); r2.y = __builtin_amdgcn_rcpf(1.f + __builtin_amdgcn_exp2f(-g2.y));
;                         const f32x2 o2 = g2 * u2 * r2; hv[2 * q] = o2.x; hv[2 * q + 1] = o2.y; }
;                     if (n == 0) h0 = hv; else h1 = hv; }
;                 unsigned w0 = 0u, w1 = 0u;
;                 w0 = __builtin_amdgcn_cvt_pk_fp8_f32(h0[0], h0[1], w0, false); w0 = __builtin_amdgcn_cvt_pk_fp8_f32(h0[2], h0[3], w0, true); w1 = __builtin_amdgcn_cvt_pk_fp8_f32(h1[0], h1[1], w1, false); w1 = __builtin_amdgcn_cvt_pk_fp8_f32(h1[2], h1[3], w1, true);
;                 *(u32x2*)(hb + (ai * 4 + m) * 512) = (u32x2){w0, w1}; asm volatile("" ::: "memory"); }
	v_add_f32_e32 v68, v76, v77
	v_fmamk_f32 v68, v68, 0x3a800000, v227
	v_rsq_f32_e32 v69, v68
	global_store_dwordx2 v[166:167], v[80:81], off offset:1536
	v_mul_f32_e32 v68, 0x3fb8aa3b, v69
	v_pk_mul_f32 v[64:65], v[64:65], v[68:69] op_sel_hi:[1,0]
	v_mul_f32_e32 v70, 0x3f317218, v69
	v_exp_f32_e64 v71, -v64
	v_exp_f32_e64 v69, -v65
	v_pk_mul_f32 v[60:61], v[60:61], v[70:71] op_sel_hi:[1,0]
	v_add_f32_e32 v69, 1.0, v69
	v_pk_mul_f32 v[60:61], v[64:65], v[60:61]
	v_pk_mul_f32 v[64:65], v[66:67], v[68:69] op_sel_hi:[1,0]
	v_add_f32_e32 v71, 1.0, v71
	v_exp_f32_e64 v66, -v64
	v_exp_f32_e64 v67, -v65
	v_pk_mul_f32 v[62:63], v[62:63], v[70:71] op_sel_hi:[1,0]
	v_pk_mul_f32 v[56:57], v[56:57], v[68:69] op_sel_hi:[1,0]
	v_add_f32_e32 v66, 1.0, v66
	v_add_f32_e32 v67, 1.0, v67
	v_pk_mul_f32 v[62:63], v[64:65], v[62:63]
	v_exp_f32_e64 v64, -v56
	v_exp_f32_e64 v65, -v57
	v_rcp_f32_e32 v66, v66
	v_rcp_f32_e32 v67, v67
	v_add_f32_e32 v64, 1.0, v64
	v_add_f32_e32 v65, 1.0, v65
	v_pk_mul_f32 v[58:59], v[58:59], v[68:69] op_sel_hi:[1,0]
	v_pk_mul_f32 v[62:63], v[62:63], v[66:67]
	v_rcp_f32_e32 v64, v64
	v_rcp_f32_e32 v65, v65
	v_exp_f32_e64 v66, -v58
	v_pk_mul_f32 v[52:53], v[52:53], v[70:71] op_sel_hi:[1,0]
	v_rcp_f32_e32 v72, v71
	v_pk_mul_f32 v[52:53], v[56:57], v[52:53]
	s_waitcnt vmcnt(6)
	v_mov_b32_e32 v56, v141
	v_mov_b32_e32 v57, v142
	v_mov_b32_e32 v141, v143
	v_pk_add_f32 v[56:57], v[56:57], v[140:141]
	v_pk_mul_f32 v[52:53], v[52:53], v[64:65]
	v_add_f32_e32 v64, 1.0, v66
	v_add_f32_e32 v66, v56, v57
	v_mov_b32_e32 v67, v66
	s_nop 1
	v_permlane16_swap_b32_e32 v67, v66
	v_exp_f32_e64 v65, -v59
	v_rcp_f32_e32 v56, v64
	v_rcp_f32_e32 v73, v69
	v_pk_mul_f32 v[54:55], v[54:55], v[70:71] op_sel_hi:[1,0]
	s_waitcnt lgkmcnt(0)
	v_add_f32_e32 v64, v66, v67
	v_add_f32_e32 v57, 1.0, v65
	v_mov_b32_e32 v65, v64
	s_nop 1
	v_permlane32_swap_b32_e32 v65, v64
	v_pk_mul_f32 v[54:55], v[58:59], v[54:55]
	v_mov_b32_e32 v59, v3
	v_cvt_pk_fp8_f32 v59, v52, v53
	v_pk_mul_f32 v[60:61], v[60:61], v[72:73]
	s_waitcnt lgkmcnt(0)
	v_add_f32_e32 v52, v64, v65
	v_rcp_f32_e32 v57, v57
	v_mov_b32_e32 v58, v3
	v_fmamk_f32 v52, v52, 0x3a800000, v227
	v_cvt_pk_fp8_f32 v58, v60, v61
	v_rsq_f32_e32 v60, v52
	v_pk_mul_f32 v[52:53], v[54:55], v[56:57]
	v_cvt_pk_fp8_f32 v58, v62, v63 op_sel:[0,0,1]
	v_cvt_pk_fp8_f32 v59, v52, v53 op_sel:[0,0,1]
	v_mul_f32_e32 v52, 0x3fb8aa3b, v60
	v_pk_mul_f32 v[48:49], v[48:49], v[52:53] op_sel_hi:[1,0]
	v_mul_f32_e32 v54, 0x3f317218, v60
	v_exp_f32_e64 v53, -v48
	v_exp_f32_e64 v55, -v49
	global_store_dwordx2 v[166:167], v[58:59], off offset:2048
	v_add_f32_e32 v53, 1.0, v53
	v_pk_mul_f32 v[44:45], v[44:45], v[54:55] op_sel_hi:[1,0]
	v_rcp_f32_e32 v56, v53
	v_add_f32_e32 v53, 1.0, v55
	v_pk_mul_f32 v[44:45], v[48:49], v[44:45]
	v_pk_mul_f32 v[48:49], v[50:51], v[52:53] op_sel_hi:[1,0]
	v_pk_mul_f32 v[46:47], v[46:47], v[54:55] op_sel_hi:[1,0]
	v_pk_mul_f32 v[40:41], v[40:41], v[52:53] op_sel_hi:[1,0]
	v_exp_f32_e64 v50, -v48
	v_exp_f32_e64 v51, -v49
	v_pk_mul_f32 v[46:47], v[48:49], v[46:47]
	v_exp_f32_e64 v48, -v40
	v_exp_f32_e64 v49, -v41
	v_add_f32_e32 v50, 1.0, v50
	v_add_f32_e32 v51, 1.0, v51
	v_add_f32_e32 v48, 1.0, v48
	v_add_f32_e32 v49, 1.0, v49
	v_rcp_f32_e32 v48, v48
	v_rcp_f32_e32 v49, v49
	v_rcp_f32_e32 v50, v50
	v_rcp_f32_e32 v51, v51
	v_pk_mul_f32 v[36:37], v[36:37], v[54:55] op_sel_hi:[1,0]
	v_rcp_f32_e32 v57, v53
	v_pk_mul_f32 v[36:37], v[40:41], v[36:37]
	v_pk_mul_f32 v[46:47], v[46:47], v[50:51]
	v_pk_mul_f32 v[36:37], v[36:37], v[48:49]
	s_waitcnt vmcnt(6)
	v_mov_b32_e32 v48, v137
	v_mov_b32_e32 v49, v138
	v_mov_b32_e32 v137, v139
	v_pk_add_f32 v[48:49], v[48:49], v[136:137]
	v_pk_mul_f32 v[40:41], v[42:43], v[52:53] op_sel_hi:[1,0]
	v_add_f32_e32 v50, v48, v49
	v_mov_b32_e32 v51, v50
	s_nop 1
	v_permlane16_swap_b32_e32 v51, v50
	v_exp_f32_e64 v42, -v40
	v_exp_f32_e64 v43, -v41
	v_pk_mul_f32 v[44:45], v[44:45], v[56:57]
	v_mov_b32_e32 v48, v3
	v_add_f32_e32 v42, 1.0, v42
	v_add_f32_e32 v43, 1.0, v43
	v_cvt_pk_fp8_f32 v48, v44, v45
	s_waitcnt lgkmcnt(0)
	v_add_f32_e32 v44, v50, v51
	v_rcp_f32_e32 v42, v42
	v_rcp_f32_e32 v43, v43
	v_mov_b32_e32 v49, v3
	v_mov_b32_e32 v45, v44
	s_nop 1
	v_permlane32_swap_b32_e32 v45, v44
	v_cvt_pk_fp8_f32 v49, v36, v37
	v_pk_mul_f32 v[38:39], v[38:39], v[54:55] op_sel_hi:[1,0]
	v_cvt_pk_fp8_f32 v48, v46, v47 op_sel:[0,0,1]
	v_pk_mul_f32 v[36:37], v[40:41], v[38:39]
	s_nop 0
	v_pk_mul_f32 v[36:37], v[36:37], v[42:43]
	s_nop 0
	v_cvt_pk_fp8_f32 v49, v36, v37 op_sel:[0,0,1]
	s_waitcnt lgkmcnt(0)
; __device__ __forceinline__ float rstd_fin4(const f32x4 a) { float s = (a[0] + a[1]) + (a[2] + a[3]); s += __shfl_xor(s, 16); s += __shfl_xor(s, 32); return __builtin_amdgcn_rsqf(s * (1.f / 1024.f) + 1e-6f); }
;     __device__ __forceinline__ void operator()(const f32x4 (&acc)[2][2][4][2], const Unit& u, int wr, int wc, int fr, int fq) const {
;     ...
;             for (int m = 0; m < 4; ++m) { const float rs = rstd_fin4(pa[ai][m]) * sc;
;                 const float rsl = rs * 1.4426950408889634f, rsu = rs * 0.6931471805599453f;
;                 f32x4 h0, h1;
; #pragma unroll
;                 for (int n = 0; n < 2; ++n) { const f32x4 G = acc[ai][0][m][n], U = acc[ai][1][m][n]; f32x4 hv;
; #pragma unroll
;                     for (int q = 0; q < 2; ++q) { const f32x2 g2 = (f32x2){G[2 * q], G[2 * q + 1]} * rsl, u2 = (f32x2){U[2 * q], U[2 * q + 1]} * rsu;
;                         f32x2 r2; r2.x = __builtin_amdgcn_rcpf(1.f + __builtin_amdgcn_exp2f(-g2.x)); r2.y = __builtin_amdgcn_rcpf(1.f + __builtin_amdgcn_exp2f(-g2.y));
;                         const f32x2 o2 = g2 * u2 * r2; hv[2 * q] = o2.x; hv[2 * q + 1] = o2.y; }
;                     if (n == 0) h0 = hv; else h1 = hv; }
;                 unsigned w0 = 0u, w1 = 0u;
;                 w0 = __builtin_amdgcn_cvt_pk_fp8_f32(h0[0], h0[1], w0, false); w0 = __builtin_amdgcn_cvt_pk_fp8_f32(h0[2], h0[3], w0, true); w1 = __builtin_amdgcn_cvt_pk_fp8_f32(h1[0], h1[1], w1, false); w1 = __builtin_amdgcn_cvt_pk_fp8_f32(h1[2], h1[3], w1, true);
;                 *(u32x2*)(hb + (ai * 4 + m) * 512) = (u32x2){w0, w1}; asm volatile("" ::: "memory"); }
	v_add_f32_e32 v36, v44, v45
	v_fmamk_f32 v36, v36, 0x3a800000, v227
	v_rsq_f32_e32 v37, v36
	global_store_dwordx2 v[166:167], v[48:49], off offset:2560
	v_mul_f32_e32 v36, 0x3fb8aa3b, v37
	v_pk_mul_f32 v[32:33], v[32:33], v[36:37] op_sel_hi:[1,0]
	v_mul_f32_e32 v38, 0x3f317218, v37
	v_exp_f32_e64 v39, -v32
	v_exp_f32_e64 v37, -v33
	v_pk_mul_f32 v[28:29], v[28:29], v[38:39] op_sel_hi:[1,0]
	v_add_f32_e32 v37, 1.0, v37
	v_pk_mul_f32 v[28:29], v[32:33], v[28:29]
	v_pk_mul_f32 v[32:33], v[34:35], v[36:37] op_sel_hi:[1,0]
	v_add_f32_e32 v39, 1.0, v39
	v_exp_f32_e64 v34, -v32
	v_exp_f32_e64 v35, -v33
	v_pk_mul_f32 v[30:31], v[30:31], v[38:39] op_sel_hi:[1,0]
	v_pk_mul_f32 v[24:25], v[24:25], v[36:37] op_sel_hi:[1,0]
	v_add_f32_e32 v34, 1.0, v34
	v_add_f32_e32 v35, 1.0, v35
	v_pk_mul_f32 v[30:31], v[32:33], v[30:31]
	v_exp_f32_e64 v32, -v24
	v_exp_f32_e64 v33, -v25
	v_rcp_f32_e32 v34, v34
	v_rcp_f32_e32 v35, v35
	v_add_f32_e32 v32, 1.0, v32
	v_add_f32_e32 v33, 1.0, v33
	v_pk_mul_f32 v[26:27], v[26:27], v[36:37] op_sel_hi:[1,0]
	v_pk_mul_f32 v[30:31], v[30:31], v[34:35]
	v_rcp_f32_e32 v32, v32
	v_rcp_f32_e32 v33, v33
	v_exp_f32_e64 v34, -v26
	v_pk_mul_f32 v[20:21], v[20:21], v[38:39] op_sel_hi:[1,0]
	v_rcp_f32_e32 v40, v39
	v_pk_mul_f32 v[20:21], v[24:25], v[20:21]
	s_waitcnt vmcnt(6)
	v_mov_b32_e32 v24, v125
	v_mov_b32_e32 v25, v126
	v_mov_b32_e32 v125, v127
	v_pk_add_f32 v[24:25], v[24:25], v[124:125]
	v_pk_mul_f32 v[20:21], v[20:21], v[32:33]
	v_add_f32_e32 v32, 1.0, v34
	v_add_f32_e32 v34, v24, v25
	v_mov_b32_e32 v35, v34
	s_nop 1
	v_permlane16_swap_b32_e32 v35, v34
	v_exp_f32_e64 v33, -v27
	v_rcp_f32_e32 v24, v32
	v_rcp_f32_e32 v41, v37
	v_pk_mul_f32 v[22:23], v[22:23], v[38:39] op_sel_hi:[1,0]
	s_waitcnt lgkmcnt(0)
	v_add_f32_e32 v32, v34, v35
	v_add_f32_e32 v25, 1.0, v33
	v_mov_b32_e32 v33, v32
	s_nop 1
	v_permlane32_swap_b32_e32 v33, v32
	v_pk_mul_f32 v[22:23], v[26:27], v[22:23]
	v_mov_b32_e32 v27, v3
	v_cvt_pk_fp8_f32 v27, v20, v21
	v_pk_mul_f32 v[28:29], v[28:29], v[40:41]
	s_waitcnt lgkmcnt(0)
	v_add_f32_e32 v20, v32, v33
	v_rcp_f32_e32 v25, v25
	v_mov_b32_e32 v26, v3
	v_fmamk_f32 v20, v20, 0x3a800000, v227
	v_cvt_pk_fp8_f32 v26, v28, v29
	v_rsq_f32_e32 v28, v20
	v_pk_mul_f32 v[20:21], v[22:23], v[24:25]
	v_cvt_pk_fp8_f32 v26, v30, v31 op_sel:[0,0,1]
	v_cvt_pk_fp8_f32 v27, v20, v21 op_sel:[0,0,1]
	v_mul_f32_e32 v20, 0x3fb8aa3b, v28
	v_pk_mul_f32 v[16:17], v[16:17], v[20:21] op_sel_hi:[1,0]
	v_mul_f32_e32 v22, 0x3f317218, v28
	v_exp_f32_e64 v21, -v16
	v_exp_f32_e64 v23, -v17
	global_store_dwordx2 v[166:167], v[26:27], off offset:3072
	v_add_f32_e32 v21, 1.0, v21
	v_pk_mul_f32 v[12:13], v[12:13], v[22:23] op_sel_hi:[1,0]
	v_rcp_f32_e32 v24, v21
	v_add_f32_e32 v21, 1.0, v23
	v_pk_mul_f32 v[12:13], v[16:17], v[12:13]
	v_pk_mul_f32 v[16:17], v[18:19], v[20:21] op_sel_hi:[1,0]
	v_pk_mul_f32 v[14:15], v[14:15], v[22:23] op_sel_hi:[1,0]
	v_pk_mul_f32 v[8:9], v[8:9], v[20:21] op_sel_hi:[1,0]
	v_exp_f32_e64 v18, -v16
	v_exp_f32_e64 v19, -v17
	v_pk_mul_f32 v[14:15], v[16:17], v[14:15]
	v_exp_f32_e64 v16, -v8
	v_exp_f32_e64 v17, -v9
	v_pk_mul_f32 v[4:5], v[4:5], v[22:23] op_sel_hi:[1,0]
	v_rcp_f32_e32 v25, v21
	v_pk_mul_f32 v[4:5], v[8:9], v[4:5]
	v_pk_mul_f32 v[8:9], v[10:11], v[20:21] op_sel_hi:[1,0]
	v_add_f32_e32 v16, 1.0, v16
	v_add_f32_e32 v17, 1.0, v17
	v_exp_f32_e64 v10, -v8
	v_exp_f32_e64 v11, -v9
	v_rcp_f32_e32 v16, v16
	v_rcp_f32_e32 v17, v17
	v_add_f32_e32 v18, 1.0, v18
	v_add_f32_e32 v19, 1.0, v19
	v_add_f32_e32 v10, 1.0, v10
	v_add_f32_e32 v11, 1.0, v11
	v_pk_mul_f32 v[12:13], v[12:13], v[24:25]
	v_rcp_f32_e32 v18, v18
	v_rcp_f32_e32 v19, v19
	v_pk_mul_f32 v[4:5], v[4:5], v[16:17]
	v_rcp_f32_e32 v10, v10
	v_rcp_f32_e32 v11, v11
	v_mov_b32_e32 v16, v3
	v_mov_b32_e32 v17, v3
	v_cvt_pk_fp8_f32 v16, v12, v13
	v_cvt_pk_fp8_f32 v17, v4, v5
	v_pk_mul_f32 v[6:7], v[6:7], v[22:23] op_sel_hi:[1,0]
	v_pk_mul_f32 v[14:15], v[14:15], v[18:19]
	v_pk_mul_f32 v[4:5], v[8:9], v[6:7]
	v_cvt_pk_fp8_f32 v16, v14, v15 op_sel:[0,0,1]
	v_pk_mul_f32 v[4:5], v[4:5], v[10:11]
	s_nop 0
	v_cvt_pk_fp8_f32 v17, v4, v5 op_sel:[0,0,1]
	global_store_dwordx2 v[166:167], v[16:17], off offset:3584
	s_cbranch_vccnz .LBB0_1701
	s_andn2_b64 vcc, exec, s[46:47]
	s_cbranch_vccnz .LBB0_1700
	s_barrier
	s_branch .LBB0_1700

; __device__ __forceinline__ float bflo(unsigned w) { return __uint_as_float(w << 16); }
;     __device__ __forceinline__ void operator()(const f32x4 (&acc)[2][2][4][2], const Unit& u, int wr, int wc, int fr, int fq) const {
;     ...
;         const int row0 = u.pm * BM + wr * 64 + fr, col0 = u.pn * BM + wc * 32 + fq * 8;
;         u32x4 xcur[2][2], xnxt[2][2];
; #pragma unroll
;         for (int h2 = 0; h2 < 2; ++h2)
; #pragma unroll
;             for (int bj = 0; bj < 2; ++bj) xcur[h2][bj] = *(const u32x4*)(X + (size_t)(row0 + h2 * 16) * 1024 + col0 + bj * HALF);
; #pragma unroll
;         for (int q = 0; q < 8; ++q) { const int ai = q >> 2, m = q & 3; const int row = row0 + ai * HALF + m * 16; float s = 0.f;
;             if ((q & 1) == 0 && q + 2 < 8) {
; #pragma unroll
;                 for (int h2 = 0; h2 < 2; ++h2)
; #pragma unroll
;                     for (int bj = 0; bj < 2; ++bj) { const int qn = q + 2 + h2; xnxt[h2][bj] = *(const u32x4*)(X + (size_t)(row0 + (qn >> 2) * HALF + (qn & 3) * 16) * 1024 + col0 + bj * HALF); } }
; #pragma unroll
;                 for (int bj = 0; bj < 2; ++bj) { bf16_t* p = X + (size_t)row * 1024 + col0 + bj * HALF; const u32x4 xv = xcur[q & 1][bj];
;                     f32x4 a = acc[ai][bj][m][0] * scale, b = acc[ai][bj][m][1] * scale;
;                     a[0] += bflo(xv.x); a[1] += bfhi(xv.x); a[2] += bflo(xv.y); a[3] += bfhi(xv.y); b[0] += bflo(xv.z); b[1] += bfhi(xv.z); b[2] += bflo(xv.w); b[3] += bfhi(xv.w);
;                     const u32x4 w = pack8(a, b); *(u32x4*)p = w;
;                     if constexpr (WX8) { unsigned q0 = 0u, q1 = 0u; q0 = __builtin_amdgcn_cvt_pk_fp8_f32(bflo(w.x), bfhi(w.x), q0, false); q0 = __builtin_amdgcn_cvt_pk_fp8_f32(bflo(w.y), bfhi(w.y), q0, true); q1 = __builtin_amdgcn_cvt_pk_fp8_f32(bflo(w.z), bfhi(w.z), q1, false); q1 = __builtin_amdgcn_cvt_pk_fp8_f32(bflo(w.w), bfhi(w.w), q1, true);
;                         *(u32x2*)((unsigned char*)X + (WS_X8 - WS_X) + (size_t)row * 1024 + col0 + bj * HALF) = (u32x2){q0, q1}; }
;                     s += (bflo(w.x) * bflo(w.x) + bfhi(w.x) * bfhi(w.x)) + (bflo(w.y) * bflo(w.y) + bfhi(w.y) * bfhi(w.y)) + (bflo(w.z) * bflo(w.z) + bfhi(w.z) * bfhi(w.z)) + (bflo(w.w) * bflo(w.w) + bfhi(w.w) * bfhi(w.w)); }
;                 s += __shfl_xor(s, 16); s += __shfl_xor(s, 32);
;                 if (fq == 0) ssn[(size_t)row * 16 + u.pn * 4 + wc] = s;
.LBB0_1834:
	s_lshl_b32 s4, s69, 8
	v_mov_b32_e32 v4, v1
	v_mov_b32_e32 v185, v182
	s_add_i32 s4, s4, s23
	v_pk_mul_f32 v[190:191], v[152:153], s[28:29] op_sel_hi:[1,0]
	v_add_u32_e32 v176, s4, v4
	s_lshl_b32 s4, s68, 8
	s_or_b32 s4, s4, s62
	v_lshl_add_u32 v174, v185, 3, s4
	v_ashrrev_i32_e32 v175, 31, v174
	v_lshlrev_b64 v[4:5], 1, v[174:175]
	v_ashrrev_i32_e32 v177, 31, v176
	v_lshl_add_u64 v[178:179], s[44:45], 0, v[4:5]
	v_lshlrev_b64 v[6:7], 11, v[176:177]
	v_lshl_add_u64 v[8:9], v[178:179], 0, v[6:7]
	global_load_dwordx4 v[28:31], v[8:9], off
	global_load_dwordx4 v[186:189], v[8:9], off offset:256
	v_add_u32_e32 v20, 16, v176
	v_add_u32_e32 v152, 32, v176
	v_pk_mul_f32 v[194:195], v[148:149], s[28:29] op_sel_hi:[1,0]
	v_add_u32_e32 v148, 48, v176
	v_ashrrev_i32_e32 v21, 31, v20
	v_ashrrev_i32_e32 v153, 31, v152
	v_pk_mul_f32 v[180:181], v[154:155], s[28:29] op_sel_hi:[1,0]
	v_ashrrev_i32_e32 v149, 31, v148
	v_lshlrev_b64 v[22:23], 11, v[20:21]
	v_lshlrev_b64 v[154:155], 11, v[152:153]
	v_pk_mul_f32 v[192:193], v[150:151], s[28:29] op_sel_hi:[1,0]
	v_lshlrev_b64 v[150:151], 11, v[148:149]
	v_lshl_add_u64 v[6:7], s[44:45], 0, v[6:7]
	v_lshl_add_u64 v[8:9], v[178:179], 0, v[22:23]
	v_lshl_add_u64 v[10:11], v[178:179], 0, v[154:155]
	v_lshl_add_u64 v[204:205], v[178:179], 0, v[150:151]
	v_lshl_add_u64 v[206:207], v[6:7], 0, v[4:5]
	global_load_dwordx4 v[12:15], v[8:9], off
	global_load_dwordx4 v[4:7], v[8:9], off offset:256
	global_load_dwordx4 v[32:35], v[10:11], off
	global_load_dwordx4 v[24:27], v[10:11], off offset:256
	global_load_dwordx4 v[16:19], v[204:205], off
	s_nop 0
	global_load_dwordx4 v[8:11], v[204:205], off offset:256
	v_pk_mul_f32 v[162:163], v[162:163], s[28:29] op_sel_hi:[1,0]
	v_pk_mul_f32 v[160:161], v[160:161], s[28:29] op_sel_hi:[1,0]
	v_pk_mul_f32 v[158:159], v[158:159], s[28:29] op_sel_hi:[1,0]
	v_pk_mul_f32 v[156:157], v[156:157], s[28:29] op_sel_hi:[1,0]
	s_lshl_b32 s52, s68, 2
	s_ashr_i32 s53, s52, 31
	s_waitcnt vmcnt(0)
	v_lshlrev_b32_e32 v204, 16, v28
	v_and_b32_e32 v28, 0xffff0000, v28
	v_lshlrev_b32_e32 v205, 16, v29
	v_and_b32_e32 v29, 0xffff0000, v29
	v_lshlrev_b32_e32 v208, 16, v30
	v_and_b32_e32 v30, 0xffff0000, v30
	v_lshlrev_b32_e32 v209, 16, v31
	v_and_b32_e32 v31, 0xffff0000, v31
	v_add_f32_e32 v28, v161, v28
	v_add_f32_e32 v29, v163, v29
	v_add_f32_e32 v160, v160, v204
	v_add_f32_e32 v161, v162, v205
	v_add_f32_e32 v156, v156, v208
	v_add_f32_e32 v30, v157, v30
	v_add_f32_e32 v157, v158, v209
	v_add_f32_e32 v31, v159, v31
	v_cvt_pk_bf16_f32 v28, v160, v28
	v_cvt_pk_bf16_f32 v29, v161, v29
	v_cvt_pk_bf16_f32 v30, v156, v30
	v_cvt_pk_bf16_f32 v31, v157, v31
	global_store_dwordx4 v[206:207], v[28:31], off
	v_lshlrev_b32_e32 v156, 16, v28
	v_lshlrev_b32_e32 v157, 16, v29
	v_and_b32_e32 v28, 0xffff0000, v28
	v_and_b32_e32 v29, 0xffff0000, v29
	v_lshlrev_b32_e32 v160, 16, v30
	v_and_b32_e32 v30, 0xffff0000, v30
	v_mul_f32_e32 v28, v28, v28
	v_mul_f32_e32 v29, v29, v29
	v_lshlrev_b32_e32 v161, 16, v31
	v_and_b32_e32 v31, 0xffff0000, v31
	v_mul_f32_e32 v30, v30, v30
	v_fmac_f32_e32 v28, v156, v156
	v_fmac_f32_e32 v29, v157, v157
	v_mul_f32_e32 v31, v31, v31
	v_fmac_f32_e32 v30, v160, v160
	v_add_f32_e32 v28, v28, v29
	v_lshlrev_b32_e32 v210, 16, v186
	v_and_b32_e32 v186, 0xffff0000, v186
	v_fmac_f32_e32 v31, v161, v161
	v_add_f32_e32 v28, v28, v30
	v_lshlrev_b32_e32 v30, 16, v189
	v_lshlrev_b32_e32 v211, 16, v187
	v_and_b32_e32 v187, 0xffff0000, v187
	v_lshlrev_b32_e32 v212, 16, v188
	v_and_b32_e32 v188, 0xffff0000, v188
	v_add_f32_e32 v158, v190, v210
	v_add_f32_e32 v159, v191, v186
	v_add_f32_e32 v28, v28, v31
	v_add_f32_e32 v30, v192, v30
	v_and_b32_e32 v31, 0xffff0000, v189
	v_add_f32_e32 v162, v180, v211
	v_add_f32_e32 v163, v181, v187
	v_add_f32_e32 v180, v194, v212
	v_add_f32_e32 v29, v195, v188
	v_add_f32_e32 v31, v193, v31
	v_cvt_pk_bf16_f32 v158, v158, v159
	v_cvt_pk_bf16_f32 v159, v162, v163
	v_cvt_pk_bf16_f32 v160, v180, v29
	v_cvt_pk_bf16_f32 v161, v30, v31
	global_store_dwordx4 v[206:207], v[158:161], off offset:256
	v_and_b32_e32 v30, 0xffff0000, v158
	v_lshlrev_b32_e32 v29, 16, v158
	v_mul_f32_e32 v30, v30, v30
	v_and_b32_e32 v31, 0xffff0000, v159
	v_fmac_f32_e32 v30, v29, v29
	v_lshlrev_b32_e32 v29, 16, v159
	v_mul_f32_e32 v31, v31, v31
	v_fmac_f32_e32 v31, v29, v29
	v_add_f32_e32 v29, v30, v31
	v_and_b32_e32 v31, 0xffff0000, v160
	v_lshlrev_b32_e32 v30, 16, v160
	v_mul_f32_e32 v31, v31, v31
	v_fmac_f32_e32 v31, v30, v30
	v_add_f32_e32 v29, v29, v31
	v_and_b32_e32 v31, 0xffff0000, v161
	v_lshlrev_b32_e32 v30, 16, v161
	v_mul_f32_e32 v31, v31, v31
	v_fmac_f32_e32 v31, v30, v30
	v_add_f32_e32 v29, v29, v31
	v_and_b32_e32 v30, 64, v246
	v_add_f32_e32 v28, v28, v29
	v_xor_b32_e32 v29, 16, v246
	v_add_u32_e32 v30, 64, v30
	v_cmp_lt_i32_e32 vcc, v29, v30
	s_nop 1
	v_cndmask_b32_e32 v29, v246, v29, vcc
	v_lshlrev_b32_e32 v156, 2, v29
	v_mov_b32_e32 v29, v28
	s_nop 1
	v_permlane16_swap_b32_e32 v29, v28
	s_waitcnt lgkmcnt(0)
	v_add_f32_e32 v28, v28, v29
	v_xor_b32_e32 v29, 32, v246
	v_cmp_lt_i32_e32 vcc, v29, v30
	s_nop 1
	v_cndmask_b32_e32 v29, v246, v29, vcc
	v_lshlrev_b32_e32 v157, 2, v29
	v_mov_b32_e32 v29, v28
	s_nop 1
	v_permlane32_swap_b32_e32 v29, v28
	v_cmp_eq_u32_e32 vcc, 0, v185
	s_and_saveexec_b64 s[4:5], vcc
	s_cbranch_execz .LBB0_1836
	v_lshlrev_b64 v[30:31], 6, v[176:177]
	v_lshl_add_u64 v[30:31], s[46:47], 0, v[30:31]
	v_lshl_add_u64 v[30:31], s[52:53], 2, v[30:31]
	s_lshl_b32 s92, s22, 2
	v_lshl_add_u64 v[30:31], v[30:31], 0, s[92:93]
	s_waitcnt lgkmcnt(0)
	v_add_f32_e32 v28, v28, v29
	global_store_dword v[30:31], v28, off
; __device__ __forceinline__ float bflo(unsigned w) { return __uint_as_float(w << 16); }
; __device__ __forceinline__ float bfhi(unsigned w) { return __uint_as_float(w & 0xffff0000u); }
;     __device__ __forceinline__ void operator()(const f32x4 (&acc)[2][2][4][2], const Unit& u, int wr, int wc, int fr, int fq) const {
;     ...
;         for (int q = 0; q < 8; ++q) { const int ai = q >> 2, m = q & 3; const int row = row0 + ai * HALF + m * 16; float s = 0.f;
;             if ((q & 1) == 0 && q + 2 < 8) {
; #pragma unroll
;                 for (int h2 = 0; h2 < 2; ++h2)
; #pragma unroll
;                     for (int bj = 0; bj < 2; ++bj) { const int qn = q + 2 + h2; xnxt[h2][bj] = *(const u32x4*)(X + (size_t)(row0 + (qn >> 2) * HALF + (qn & 3) * 16) * 1024 + col0 + bj * HALF); } }
; #pragma unroll
;                 for (int bj = 0; bj < 2; ++bj) { bf16_t* p = X + (size_t)row * 1024 + col0 + bj * HALF; const u32x4 xv = xcur[q & 1][bj];
;                     f32x4 a = acc[ai][bj][m][0] * scale, b = acc[ai][bj][m][1] * scale;
;                     a[0] += bflo(xv.x); a[1] += bfhi(xv.x); a[2] += bflo(xv.y); a[3] += bfhi(xv.y); b[0] += bflo(xv.z); b[1] += bfhi(xv.z); b[2] += bflo(xv.w); b[3] += bfhi(xv.w);
;                     const u32x4 w = pack8(a, b); *(u32x4*)p = w;
;                     if constexpr (WX8) { unsigned q0 = 0u, q1 = 0u; q0 = __builtin_amdgcn_cvt_pk_fp8_f32(bflo(w.x), bfhi(w.x), q0, false); q0 = __builtin_amdgcn_cvt_pk_fp8_f32(bflo(w.y), bfhi(w.y), q0, true); q1 = __builtin_amdgcn_cvt_pk_fp8_f32(bflo(w.z), bfhi(w.z), q1, false); q1 = __builtin_amdgcn_cvt_pk_fp8_f32(bflo(w.w), bfhi(w.w), q1, true);
;                         *(u32x2*)((unsigned char*)X + (WS_X8 - WS_X) + (size_t)row * 1024 + col0 + bj * HALF) = (u32x2){q0, q1}; }
;                     s += (bflo(w.x) * bflo(w.x) + bfhi(w.x) * bfhi(w.x)) + (bflo(w.y) * bflo(w.y) + bfhi(w.y) * bfhi(w.y)) + (bflo(w.z) * bflo(w.z) + bfhi(w.z) * bfhi(w.z)) + (bflo(w.w) * bflo(w.w) + bfhi(w.w) * bfhi(w.w)); }
;                 s += __shfl_xor(s, 16); s += __shfl_xor(s, 32);
;                 if (fq == 0) ssn[(size_t)row * 16 + u.pn * 4 + wc] = s;
;             if (q & 1) { asm volatile("" ::: "memory");
; #pragma unroll
;                 for (int h2 = 0; h2 < 2; ++h2)
; #pragma unroll
;                     for (int bj = 0; bj < 2; ++bj) xcur[h2][bj] = xnxt[h2][bj]; } }
.LBB0_1836:
	s_or_b64 exec, exec, s[4:5]
	v_pk_mul_f32 v[30:31], v[144:145], s[28:29] op_sel_hi:[1,0]
	v_lshlrev_b32_e32 v144, 16, v12
	v_and_b32_e32 v12, 0xffff0000, v12
	s_waitcnt lgkmcnt(0)
	v_pk_mul_f32 v[28:29], v[146:147], s[28:29] op_sel_hi:[1,0]
	v_add_f32_e32 v12, v31, v12
	v_lshlrev_b32_e32 v31, 16, v13
	v_and_b32_e32 v13, 0xffff0000, v13
	v_lshl_add_u64 v[22:23], s[44:45], 0, v[22:23]
	v_pk_mul_f32 v[142:143], v[142:143], s[28:29] op_sel_hi:[1,0]
	v_pk_mul_f32 v[140:141], v[140:141], s[28:29] op_sel_hi:[1,0]
	v_add_f32_e32 v28, v28, v31
	v_add_f32_e32 v13, v29, v13
	v_lshlrev_b32_e32 v29, 16, v14
	v_and_b32_e32 v14, 0xffff0000, v14
	v_lshlrev_b32_e32 v31, 16, v15
	v_and_b32_e32 v15, 0xffff0000, v15
	v_lshl_add_u64 v[22:23], v[174:175], 1, v[22:23]
	v_add_f32_e32 v30, v30, v144
	v_add_f32_e32 v14, v141, v14
	v_add_f32_e32 v15, v143, v15
	v_cvt_pk_bf16_f32 v12, v30, v12
	v_add_f32_e32 v29, v140, v29
	v_add_f32_e32 v31, v142, v31
	v_cvt_pk_bf16_f32 v13, v28, v13
	v_cvt_pk_bf16_f32 v14, v29, v14
	v_cvt_pk_bf16_f32 v15, v31, v15
	global_store_dwordx4 v[22:23], v[12:15], off
	v_lshlrev_b32_e32 v28, 16, v12
	v_pk_mul_f32 v[30:31], v[132:133], s[28:29] op_sel_hi:[1,0]
	v_and_b32_e32 v12, 0xffff0000, v12
	v_mul_f32_e32 v12, v12, v12
	v_fmac_f32_e32 v12, v28, v28
	v_lshlrev_b32_e32 v28, 16, v13
	v_and_b32_e32 v13, 0xffff0000, v13
	v_mul_f32_e32 v13, v13, v13
	v_fmac_f32_e32 v13, v28, v28
	v_add_f32_e32 v12, v12, v13
	v_lshlrev_b32_e32 v13, 16, v14
	v_and_b32_e32 v14, 0xffff0000, v14
	v_mul_f32_e32 v14, v14, v14
	v_fmac_f32_e32 v14, v13, v13
	v_add_f32_e32 v12, v12, v14
	v_and_b32_e32 v14, 0xffff0000, v15
	v_lshlrev_b32_e32 v13, 16, v15
	v_mul_f32_e32 v14, v14, v14
	v_fmac_f32_e32 v14, v13, v13
	v_add_f32_e32 v140, v12, v14
	v_pk_mul_f32 v[14:15], v[136:137], s[28:29] op_sel_hi:[1,0]
	v_lshlrev_b32_e32 v132, 16, v4
	v_and_b32_e32 v4, 0xffff0000, v4
	v_pk_mul_f32 v[12:13], v[138:139], s[28:29] op_sel_hi:[1,0]
	v_add_f32_e32 v4, v15, v4
	v_lshlrev_b32_e32 v15, 16, v5
	v_add_f32_e32 v15, v12, v15
	v_and_b32_e32 v5, 0xffff0000, v5
	v_lshlrev_b32_e32 v12, 16, v6
	v_pk_mul_f32 v[28:29], v[134:135], s[28:29] op_sel_hi:[1,0]
	v_add_f32_e32 v5, v13, v5
	v_add_f32_e32 v30, v30, v12
	v_and_b32_e32 v6, 0xffff0000, v6
	v_lshlrev_b32_e32 v12, 16, v7
	v_add_f32_e32 v14, v14, v132
	v_add_f32_e32 v6, v31, v6
	v_add_f32_e32 v28, v28, v12
	v_cvt_pk_bf16_f32 v12, v14, v4
	v_cvt_pk_bf16_f32 v13, v15, v5
	v_cvt_pk_bf16_f32 v14, v30, v6
	v_and_b32_e32 v7, 0xffff0000, v7
	v_and_b32_e32 v5, 0xffff0000, v12
	v_lshlrev_b32_e32 v4, 16, v12
	v_mul_f32_e32 v5, v5, v5
	v_and_b32_e32 v6, 0xffff0000, v13
	v_fmac_f32_e32 v5, v4, v4
	v_lshlrev_b32_e32 v4, 16, v13
	v_mul_f32_e32 v6, v6, v6
	v_fmac_f32_e32 v6, v4, v4
	v_add_f32_e32 v4, v5, v6
	v_and_b32_e32 v6, 0xffff0000, v14
	v_lshlrev_b32_e32 v5, 16, v14
	v_mul_f32_e32 v6, v6, v6
	v_fmac_f32_e32 v6, v5, v5
	v_add_f32_e32 v7, v29, v7
	v_cvt_pk_bf16_f32 v15, v28, v7
	v_add_f32_e32 v4, v4, v6
	v_and_b32_e32 v6, 0xffff0000, v15
	v_lshlrev_b32_e32 v5, 16, v15
	v_mul_f32_e32 v6, v6, v6
	v_fmac_f32_e32 v6, v5, v5
	v_add_f32_e32 v4, v4, v6
	v_add_f32_e32 v4, v140, v4
	v_mov_b32_e32 v5, v4
	s_nop 1
	v_permlane16_swap_b32_e32 v5, v4
	global_store_dwordx4 v[22:23], v[12:15], off offset:256
	s_waitcnt lgkmcnt(0)
	v_add_f32_e32 v4, v4, v5
	v_mov_b32_e32 v5, v4
	s_nop 1
	v_permlane32_swap_b32_e32 v5, v4
	s_and_saveexec_b64 s[4:5], vcc
	s_cbranch_execz .LBB0_1838
	v_lshlrev_b64 v[6:7], 6, v[20:21]
	v_lshl_add_u64 v[6:7], s[46:47], 0, v[6:7]
	v_lshl_add_u64 v[6:7], s[52:53], 2, v[6:7]
	s_lshl_b32 s92, s22, 2
	v_lshl_add_u64 v[6:7], v[6:7], 0, s[92:93]
	s_waitcnt lgkmcnt(0)
	v_add_f32_e32 v4, v4, v5
	global_store_dword v[6:7], v4, off
.LBB0_1838:
	s_or_b64 exec, exec, s[4:5]
	v_add_u32_e32 v134, 0x80, v176
	v_ashrrev_i32_e32 v135, 31, v134
	v_add_u32_e32 v132, 0x90, v176
	v_lshlrev_b64 v[138:139], 11, v[134:135]
	v_ashrrev_i32_e32 v133, 31, v132
	s_waitcnt lgkmcnt(0)
	v_lshl_add_u64 v[4:5], v[178:179], 0, v[138:139]
	v_lshlrev_b64 v[136:137], 11, v[132:133]
	global_load_dwordx4 v[28:31], v[4:5], off
	global_load_dwordx4 v[20:23], v[4:5], off offset:256
	v_lshl_add_u64 v[4:5], v[178:179], 0, v[136:137]
	global_load_dwordx4 v[12:15], v[4:5], off
	s_nop 0
	global_load_dwordx4 v[4:7], v[4:5], off offset:256
	v_pk_mul_f32 v[128:129], v[128:129], s[28:29] op_sel_hi:[1,0]
	v_lshlrev_b32_e32 v142, 16, v32
	v_and_b32_e32 v32, 0xffff0000, v32
	v_pk_mul_f32 v[130:131], v[130:131], s[28:29] op_sel_hi:[1,0]
	v_add_f32_e32 v32, v129, v32
	v_lshlrev_b32_e32 v129, 16, v33
	v_pk_mul_f32 v[124:125], v[124:125], s[28:29] op_sel_hi:[1,0]
	v_add_f32_e32 v129, v130, v129
	v_lshlrev_b32_e32 v130, 16, v34
	v_and_b32_e32 v34, 0xffff0000, v34
	v_lshl_add_u64 v[140:141], s[44:45], 0, v[154:155]
	v_pk_mul_f32 v[126:127], v[126:127], s[28:29] op_sel_hi:[1,0]
	v_and_b32_e32 v33, 0xffff0000, v33
	v_add_f32_e32 v34, v125, v34
	v_lshlrev_b32_e32 v125, 16, v35
	v_and_b32_e32 v35, 0xffff0000, v35
	v_lshl_add_u64 v[140:141], v[174:175], 1, v[140:141]
	v_add_f32_e32 v128, v128, v142
	v_add_f32_e32 v33, v131, v33
	v_add_f32_e32 v124, v124, v130
	v_add_f32_e32 v35, v127, v35
	v_cvt_pk_bf16_f32 v32, v128, v32
	v_add_f32_e32 v125, v126, v125
	v_cvt_pk_bf16_f32 v33, v129, v33
	v_cvt_pk_bf16_f32 v34, v124, v34
	v_cvt_pk_bf16_f32 v35, v125, v35
	global_store_dwordx4 v[140:141], v[32:35], off
	v_lshlrev_b32_e32 v124, 16, v32
	v_pk_mul_f32 v[116:117], v[116:117], s[28:29] op_sel_hi:[1,0]
	v_and_b32_e32 v32, 0xffff0000, v32
	v_mul_f32_e32 v32, v32, v32
	v_fmac_f32_e32 v32, v124, v124
	v_lshlrev_b32_e32 v124, 16, v33
	v_and_b32_e32 v33, 0xffff0000, v33
	v_mul_f32_e32 v33, v33, v33
; __device__ __forceinline__ float bflo(unsigned w) { return __uint_as_float(w << 16); }
; __device__ __forceinline__ float bfhi(unsigned w) { return __uint_as_float(w & 0xffff0000u); }
;     __device__ __forceinline__ void operator()(const f32x4 (&acc)[2][2][4][2], const Unit& u, int wr, int wc, int fr, int fq) const {
;     ...
;         for (int q = 0; q < 8; ++q) { const int ai = q >> 2, m = q & 3; const int row = row0 + ai * HALF + m * 16; float s = 0.f;
;             if ((q & 1) == 0 && q + 2 < 8) {
; #pragma unroll
;                 for (int h2 = 0; h2 < 2; ++h2)
; #pragma unroll
;                     for (int bj = 0; bj < 2; ++bj) { const int qn = q + 2 + h2; xnxt[h2][bj] = *(const u32x4*)(X + (size_t)(row0 + (qn >> 2) * HALF + (qn & 3) * 16) * 1024 + col0 + bj * HALF); } }
; #pragma unroll
;                 for (int bj = 0; bj < 2; ++bj) { bf16_t* p = X + (size_t)row * 1024 + col0 + bj * HALF; const u32x4 xv = xcur[q & 1][bj];
;                     f32x4 a = acc[ai][bj][m][0] * scale, b = acc[ai][bj][m][1] * scale;
;                     a[0] += bflo(xv.x); a[1] += bfhi(xv.x); a[2] += bflo(xv.y); a[3] += bfhi(xv.y); b[0] += bflo(xv.z); b[1] += bfhi(xv.z); b[2] += bflo(xv.w); b[3] += bfhi(xv.w);
;                     const u32x4 w = pack8(a, b); *(u32x4*)p = w;
;                     if constexpr (WX8) { unsigned q0 = 0u, q1 = 0u; q0 = __builtin_amdgcn_cvt_pk_fp8_f32(bflo(w.x), bfhi(w.x), q0, false); q0 = __builtin_amdgcn_cvt_pk_fp8_f32(bflo(w.y), bfhi(w.y), q0, true); q1 = __builtin_amdgcn_cvt_pk_fp8_f32(bflo(w.z), bfhi(w.z), q1, false); q1 = __builtin_amdgcn_cvt_pk_fp8_f32(bflo(w.w), bfhi(w.w), q1, true);
;                         *(u32x2*)((unsigned char*)X + (WS_X8 - WS_X) + (size_t)row * 1024 + col0 + bj * HALF) = (u32x2){q0, q1}; }
;                     s += (bflo(w.x) * bflo(w.x) + bfhi(w.x) * bfhi(w.x)) + (bflo(w.y) * bflo(w.y) + bfhi(w.y) * bfhi(w.y)) + (bflo(w.z) * bflo(w.z) + bfhi(w.z) * bfhi(w.z)) + (bflo(w.w) * bflo(w.w) + bfhi(w.w) * bfhi(w.w)); }
;                 s += __shfl_xor(s, 16); s += __shfl_xor(s, 32);
;                 if (fq == 0) ssn[(size_t)row * 16 + u.pn * 4 + wc] = s;
;             if (q & 1) { asm volatile("" ::: "memory");
; #pragma unroll
;                 for (int h2 = 0; h2 < 2; ++h2)
; #pragma unroll
;                     for (int bj = 0; bj < 2; ++bj) xcur[h2][bj] = xnxt[h2][bj]; } }
	v_fmac_f32_e32 v33, v124, v124
	v_add_f32_e32 v32, v32, v33
	v_lshlrev_b32_e32 v33, 16, v34
	v_and_b32_e32 v34, 0xffff0000, v34
	v_mul_f32_e32 v34, v34, v34
	v_fmac_f32_e32 v34, v33, v33
	v_add_f32_e32 v32, v32, v34
	v_and_b32_e32 v34, 0xffff0000, v35
	v_lshlrev_b32_e32 v33, 16, v35
	v_mul_f32_e32 v34, v34, v34
	v_fmac_f32_e32 v34, v33, v33
	v_add_f32_e32 v124, v32, v34
	v_pk_mul_f32 v[34:35], v[120:121], s[28:29] op_sel_hi:[1,0]
	v_lshlrev_b32_e32 v120, 16, v24
	v_and_b32_e32 v24, 0xffff0000, v24
	v_pk_mul_f32 v[32:33], v[122:123], s[28:29] op_sel_hi:[1,0]
	v_add_f32_e32 v24, v35, v24
	v_lshlrev_b32_e32 v35, 16, v25
	v_add_f32_e32 v35, v32, v35
	v_and_b32_e32 v25, 0xffff0000, v25
	v_lshlrev_b32_e32 v32, 16, v26
	v_pk_mul_f32 v[118:119], v[118:119], s[28:29] op_sel_hi:[1,0]
	v_add_f32_e32 v25, v33, v25
	v_add_f32_e32 v116, v116, v32
	v_and_b32_e32 v26, 0xffff0000, v26
	v_lshlrev_b32_e32 v32, 16, v27
	v_add_f32_e32 v34, v34, v120
	v_add_f32_e32 v26, v117, v26
	v_add_f32_e32 v117, v118, v32
	v_cvt_pk_bf16_f32 v32, v34, v24
	v_cvt_pk_bf16_f32 v33, v35, v25
	v_cvt_pk_bf16_f32 v34, v116, v26
	v_and_b32_e32 v27, 0xffff0000, v27
	v_and_b32_e32 v25, 0xffff0000, v32
	v_lshlrev_b32_e32 v24, 16, v32
	v_mul_f32_e32 v25, v25, v25
	v_and_b32_e32 v26, 0xffff0000, v33
	v_fmac_f32_e32 v25, v24, v24
	v_lshlrev_b32_e32 v24, 16, v33
	v_mul_f32_e32 v26, v26, v26
	v_fmac_f32_e32 v26, v24, v24
	v_add_f32_e32 v24, v25, v26
	v_and_b32_e32 v26, 0xffff0000, v34
	v_lshlrev_b32_e32 v25, 16, v34
	v_mul_f32_e32 v26, v26, v26
	v_fmac_f32_e32 v26, v25, v25
	v_add_f32_e32 v27, v119, v27
	v_cvt_pk_bf16_f32 v35, v117, v27
	v_add_f32_e32 v24, v24, v26
	v_and_b32_e32 v26, 0xffff0000, v35
	v_lshlrev_b32_e32 v25, 16, v35
	v_mul_f32_e32 v26, v26, v26
	v_fmac_f32_e32 v26, v25, v25
	v_add_f32_e32 v24, v24, v26
	v_add_f32_e32 v24, v124, v24
	v_mov_b32_e32 v25, v24
	s_nop 1
	v_permlane16_swap_b32_e32 v25, v24
	global_store_dwordx4 v[140:141], v[32:35], off offset:256
	s_waitcnt lgkmcnt(0)
	v_add_f32_e32 v24, v24, v25
	v_mov_b32_e32 v25, v24
	s_nop 1
	v_permlane32_swap_b32_e32 v25, v24
	s_and_saveexec_b64 s[4:5], vcc
	s_cbranch_execz .LBB0_1840
	v_lshlrev_b64 v[26:27], 6, v[152:153]
	v_lshl_add_u64 v[26:27], s[46:47], 0, v[26:27]
	v_lshl_add_u64 v[26:27], s[52:53], 2, v[26:27]
	s_lshl_b32 s92, s22, 2
	v_lshl_add_u64 v[26:27], v[26:27], 0, s[92:93]
	s_waitcnt lgkmcnt(0)
	v_add_f32_e32 v24, v24, v25
	global_store_dword v[26:27], v24, off
.LBB0_1840:
	s_or_b64 exec, exec, s[4:5]
	v_pk_mul_f32 v[32:33], v[112:113], s[28:29] op_sel_hi:[1,0]
	v_pk_mul_f32 v[34:35], v[110:111], s[28:29] op_sel_hi:[1,0]
	v_lshlrev_b32_e32 v110, 16, v16
	v_and_b32_e32 v16, 0xffff0000, v16
	v_pk_mul_f32 v[26:27], v[114:115], s[28:29] op_sel_hi:[1,0]
	v_add_f32_e32 v16, v33, v16
	v_lshlrev_b32_e32 v33, 16, v17
	v_and_b32_e32 v17, 0xffff0000, v17
	s_waitcnt lgkmcnt(0)
	v_lshl_add_u64 v[24:25], s[44:45], 0, v[150:151]
	v_pk_mul_f32 v[108:109], v[108:109], s[28:29] op_sel_hi:[1,0]
	v_add_f32_e32 v26, v26, v33
	v_add_f32_e32 v17, v27, v17
	v_lshlrev_b32_e32 v27, 16, v18
	v_and_b32_e32 v18, 0xffff0000, v18
	v_lshlrev_b32_e32 v33, 16, v19
	v_and_b32_e32 v19, 0xffff0000, v19
	v_lshl_add_u64 v[24:25], v[174:175], 1, v[24:25]
	v_add_f32_e32 v32, v32, v110
	v_add_f32_e32 v18, v109, v18
	v_add_f32_e32 v19, v35, v19
	v_cvt_pk_bf16_f32 v16, v32, v16
	v_add_f32_e32 v27, v108, v27
	v_add_f32_e32 v33, v34, v33
	v_cvt_pk_bf16_f32 v17, v26, v17
	v_cvt_pk_bf16_f32 v18, v27, v18
	v_cvt_pk_bf16_f32 v19, v33, v19
	global_store_dwordx4 v[24:25], v[16:19], off
	v_lshlrev_b32_e32 v26, 16, v16
	v_lshlrev_b32_e32 v35, 16, v8
	v_and_b32_e32 v16, 0xffff0000, v16
	v_mul_f32_e32 v16, v16, v16
	v_fmac_f32_e32 v16, v26, v26
	v_lshlrev_b32_e32 v26, 16, v17
	v_and_b32_e32 v17, 0xffff0000, v17
	v_mul_f32_e32 v17, v17, v17
	v_fmac_f32_e32 v17, v26, v26
	v_add_f32_e32 v16, v16, v17
	v_lshlrev_b32_e32 v17, 16, v18
	v_and_b32_e32 v18, 0xffff0000, v18
	v_mul_f32_e32 v18, v18, v18
	v_fmac_f32_e32 v18, v17, v17
	v_add_f32_e32 v16, v16, v18
	v_and_b32_e32 v18, 0xffff0000, v19
	v_lshlrev_b32_e32 v17, 16, v19
	v_mul_f32_e32 v18, v18, v18
	v_fmac_f32_e32 v18, v17, v17
	v_add_f32_e32 v34, v16, v18
	v_pk_mul_f32 v[18:19], v[104:105], s[28:29] op_sel_hi:[1,0]
	v_and_b32_e32 v8, 0xffff0000, v8
	v_pk_mul_f32 v[16:17], v[106:107], s[28:29] op_sel_hi:[1,0]
	v_add_f32_e32 v8, v19, v8
	v_lshlrev_b32_e32 v19, 16, v9
	v_pk_mul_f32 v[32:33], v[100:101], s[28:29] op_sel_hi:[1,0]
	v_add_f32_e32 v19, v16, v19
	v_and_b32_e32 v9, 0xffff0000, v9
	v_lshlrev_b32_e32 v16, 16, v10
	v_pk_mul_f32 v[26:27], v[102:103], s[28:29] op_sel_hi:[1,0]
	v_add_f32_e32 v9, v17, v9
	v_add_f32_e32 v32, v32, v16
	v_and_b32_e32 v10, 0xffff0000, v10
	v_lshlrev_b32_e32 v16, 16, v11
	v_add_f32_e32 v18, v18, v35
	v_add_f32_e32 v10, v33, v10
	v_add_f32_e32 v26, v26, v16
	v_cvt_pk_bf16_f32 v16, v18, v8
	v_cvt_pk_bf16_f32 v17, v19, v9
	v_cvt_pk_bf16_f32 v18, v32, v10
	v_and_b32_e32 v11, 0xffff0000, v11
	v_and_b32_e32 v9, 0xffff0000, v16
	v_lshlrev_b32_e32 v8, 16, v16
	v_mul_f32_e32 v9, v9, v9
	v_and_b32_e32 v10, 0xffff0000, v17
	v_fmac_f32_e32 v9, v8, v8
	v_lshlrev_b32_e32 v8, 16, v17
	v_mul_f32_e32 v10, v10, v10
	v_fmac_f32_e32 v10, v8, v8
	v_add_f32_e32 v8, v9, v10
	v_and_b32_e32 v10, 0xffff0000, v18
	v_lshlrev_b32_e32 v9, 16, v18
	v_mul_f32_e32 v10, v10, v10
	v_fmac_f32_e32 v10, v9, v9
	v_add_f32_e32 v11, v27, v11
	v_cvt_pk_bf16_f32 v19, v26, v11
	v_add_f32_e32 v8, v8, v10
	v_and_b32_e32 v10, 0xffff0000, v19
	v_lshlrev_b32_e32 v9, 16, v19
	v_mul_f32_e32 v10, v10, v10
	v_fmac_f32_e32 v10, v9, v9
	v_add_f32_e32 v8, v8, v10
	v_add_f32_e32 v8, v34, v8
	v_mov_b32_e32 v9, v8
	s_nop 1
	v_permlane16_swap_b32_e32 v9, v8
	global_store_dwordx4 v[24:25], v[16:19], off offset:256
	s_waitcnt lgkmcnt(0)
	v_add_f32_e32 v8, v8, v9
	v_mov_b32_e32 v9, v8
	s_nop 1
	v_permlane32_swap_b32_e32 v9, v8
	s_and_saveexec_b64 s[4:5], vcc
	s_cbranch_execz .LBB0_1842
	v_lshlrev_b64 v[10:11], 6, v[148:149]
	v_lshl_add_u64 v[10:11], s[46:47], 0, v[10:11]
	v_lshl_add_u64 v[10:11], s[52:53], 2, v[10:11]
	s_lshl_b32 s92, s22, 2
	v_lshl_add_u64 v[10:11], v[10:11], 0, s[92:93]
	s_waitcnt lgkmcnt(0)
	v_add_f32_e32 v8, v8, v9
	global_store_dword v[10:11], v8, off
; __device__ __forceinline__ float bflo(unsigned w) { return __uint_as_float(w << 16); }
; __device__ __forceinline__ float bfhi(unsigned w) { return __uint_as_float(w & 0xffff0000u); }
;     __device__ __forceinline__ void operator()(const f32x4 (&acc)[2][2][4][2], const Unit& u, int wr, int wc, int fr, int fq) const {
;     ...
;         for (int q = 0; q < 8; ++q) { const int ai = q >> 2, m = q & 3; const int row = row0 + ai * HALF + m * 16; float s = 0.f;
;             if ((q & 1) == 0 && q + 2 < 8) {
; #pragma unroll
;                 for (int h2 = 0; h2 < 2; ++h2)
; #pragma unroll
;                     for (int bj = 0; bj < 2; ++bj) { const int qn = q + 2 + h2; xnxt[h2][bj] = *(const u32x4*)(X + (size_t)(row0 + (qn >> 2) * HALF + (qn & 3) * 16) * 1024 + col0 + bj * HALF); } }
; #pragma unroll
;                 for (int bj = 0; bj < 2; ++bj) { bf16_t* p = X + (size_t)row * 1024 + col0 + bj * HALF; const u32x4 xv = xcur[q & 1][bj];
;                     f32x4 a = acc[ai][bj][m][0] * scale, b = acc[ai][bj][m][1] * scale;
;                     a[0] += bflo(xv.x); a[1] += bfhi(xv.x); a[2] += bflo(xv.y); a[3] += bfhi(xv.y); b[0] += bflo(xv.z); b[1] += bfhi(xv.z); b[2] += bflo(xv.w); b[3] += bfhi(xv.w);
;                     const u32x4 w = pack8(a, b); *(u32x4*)p = w;
;                     if constexpr (WX8) { unsigned q0 = 0u, q1 = 0u; q0 = __builtin_amdgcn_cvt_pk_fp8_f32(bflo(w.x), bfhi(w.x), q0, false); q0 = __builtin_amdgcn_cvt_pk_fp8_f32(bflo(w.y), bfhi(w.y), q0, true); q1 = __builtin_amdgcn_cvt_pk_fp8_f32(bflo(w.z), bfhi(w.z), q1, false); q1 = __builtin_amdgcn_cvt_pk_fp8_f32(bflo(w.w), bfhi(w.w), q1, true);
;                         *(u32x2*)((unsigned char*)X + (WS_X8 - WS_X) + (size_t)row * 1024 + col0 + bj * HALF) = (u32x2){q0, q1}; }
;                     s += (bflo(w.x) * bflo(w.x) + bfhi(w.x) * bfhi(w.x)) + (bflo(w.y) * bflo(w.y) + bfhi(w.y) * bfhi(w.y)) + (bflo(w.z) * bflo(w.z) + bfhi(w.z) * bfhi(w.z)) + (bflo(w.w) * bflo(w.w) + bfhi(w.w) * bfhi(w.w)); }
;                 s += __shfl_xor(s, 16); s += __shfl_xor(s, 32);
;                 if (fq == 0) ssn[(size_t)row * 16 + u.pn * 4 + wc] = s;
;             if (q & 1) { asm volatile("" ::: "memory");
; #pragma unroll
;                 for (int h2 = 0; h2 < 2; ++h2)
; #pragma unroll
;                     for (int bj = 0; bj < 2; ++bj) xcur[h2][bj] = xnxt[h2][bj]; } }
.LBB0_1842:
	s_or_b64 exec, exec, s[4:5]
	v_add_u32_e32 v102, 0xa0, v176
	v_ashrrev_i32_e32 v103, 31, v102
	v_add_u32_e32 v100, 0xb0, v176
	v_lshlrev_b64 v[106:107], 11, v[102:103]
	v_ashrrev_i32_e32 v101, 31, v100
	s_waitcnt lgkmcnt(0)
	v_lshl_add_u64 v[8:9], v[178:179], 0, v[106:107]
	v_lshlrev_b64 v[104:105], 11, v[100:101]
	global_load_dwordx4 v[32:35], v[8:9], off
	global_load_dwordx4 v[24:27], v[8:9], off offset:256
	v_lshl_add_u64 v[8:9], v[178:179], 0, v[104:105]
	global_load_dwordx4 v[16:19], v[8:9], off
	s_nop 0
	global_load_dwordx4 v[8:11], v[8:9], off offset:256
	v_pk_mul_f32 v[96:97], v[96:97], s[28:29] op_sel_hi:[1,0]
	s_waitcnt vmcnt(11)
	v_lshlrev_b32_e32 v110, 16, v28
	v_and_b32_e32 v28, 0xffff0000, v28
	v_pk_mul_f32 v[98:99], v[98:99], s[28:29] op_sel_hi:[1,0]
	v_add_f32_e32 v28, v97, v28
	v_lshlrev_b32_e32 v97, 16, v29
	v_pk_mul_f32 v[92:93], v[92:93], s[28:29] op_sel_hi:[1,0]
	v_add_f32_e32 v97, v98, v97
	v_lshlrev_b32_e32 v98, 16, v30
	v_and_b32_e32 v30, 0xffff0000, v30
	v_lshl_add_u64 v[108:109], s[44:45], 0, v[138:139]
	v_pk_mul_f32 v[94:95], v[94:95], s[28:29] op_sel_hi:[1,0]
	v_and_b32_e32 v29, 0xffff0000, v29
	v_add_f32_e32 v30, v93, v30
	v_lshlrev_b32_e32 v93, 16, v31
	v_and_b32_e32 v31, 0xffff0000, v31
	v_lshl_add_u64 v[108:109], v[174:175], 1, v[108:109]
	v_add_f32_e32 v96, v96, v110
	v_add_f32_e32 v29, v99, v29
	v_add_f32_e32 v92, v92, v98
	v_add_f32_e32 v31, v95, v31
	v_cvt_pk_bf16_f32 v28, v96, v28
	v_add_f32_e32 v93, v94, v93
	v_cvt_pk_bf16_f32 v29, v97, v29
	v_cvt_pk_bf16_f32 v30, v92, v30
	v_cvt_pk_bf16_f32 v31, v93, v31
	global_store_dwordx4 v[108:109], v[28:31], off
	v_lshlrev_b32_e32 v92, 16, v28
	v_pk_mul_f32 v[84:85], v[84:85], s[28:29] op_sel_hi:[1,0]
	v_and_b32_e32 v28, 0xffff0000, v28
	v_mul_f32_e32 v28, v28, v28
	v_fmac_f32_e32 v28, v92, v92
	v_lshlrev_b32_e32 v92, 16, v29
	v_and_b32_e32 v29, 0xffff0000, v29
	v_mul_f32_e32 v29, v29, v29
	v_fmac_f32_e32 v29, v92, v92
	v_add_f32_e32 v28, v28, v29
	v_lshlrev_b32_e32 v29, 16, v30
	v_and_b32_e32 v30, 0xffff0000, v30
	v_mul_f32_e32 v30, v30, v30
	v_fmac_f32_e32 v30, v29, v29
	v_add_f32_e32 v28, v28, v30
	v_and_b32_e32 v30, 0xffff0000, v31
	v_lshlrev_b32_e32 v29, 16, v31
	v_mul_f32_e32 v30, v30, v30
	v_fmac_f32_e32 v30, v29, v29
	v_add_f32_e32 v92, v28, v30
	v_pk_mul_f32 v[30:31], v[88:89], s[28:29] op_sel_hi:[1,0]
	s_waitcnt vmcnt(11)
	v_lshlrev_b32_e32 v88, 16, v20
	v_and_b32_e32 v20, 0xffff0000, v20
	v_pk_mul_f32 v[28:29], v[90:91], s[28:29] op_sel_hi:[1,0]
	v_add_f32_e32 v20, v31, v20
	v_lshlrev_b32_e32 v31, 16, v21
	v_add_f32_e32 v31, v28, v31
	v_and_b32_e32 v21, 0xffff0000, v21
	v_lshlrev_b32_e32 v28, 16, v22
	v_pk_mul_f32 v[86:87], v[86:87], s[28:29] op_sel_hi:[1,0]
	v_add_f32_e32 v21, v29, v21
	v_add_f32_e32 v84, v84, v28
	v_and_b32_e32 v22, 0xffff0000, v22
	v_lshlrev_b32_e32 v28, 16, v23
	v_add_f32_e32 v30, v30, v88
	v_add_f32_e32 v22, v85, v22
	v_add_f32_e32 v85, v86, v28
	v_cvt_pk_bf16_f32 v28, v30, v20
	v_cvt_pk_bf16_f32 v29, v31, v21
	v_cvt_pk_bf16_f32 v30, v84, v22
	v_and_b32_e32 v23, 0xffff0000, v23
	v_and_b32_e32 v21, 0xffff0000, v28
	v_lshlrev_b32_e32 v20, 16, v28
	v_mul_f32_e32 v21, v21, v21
	v_and_b32_e32 v22, 0xffff0000, v29
	v_fmac_f32_e32 v21, v20, v20
	v_lshlrev_b32_e32 v20, 16, v29
	v_mul_f32_e32 v22, v22, v22
	v_fmac_f32_e32 v22, v20, v20
	v_add_f32_e32 v20, v21, v22
	v_and_b32_e32 v22, 0xffff0000, v30
	v_lshlrev_b32_e32 v21, 16, v30
	v_mul_f32_e32 v22, v22, v22
	v_fmac_f32_e32 v22, v21, v21
	v_add_f32_e32 v23, v87, v23
	v_cvt_pk_bf16_f32 v31, v85, v23
	v_add_f32_e32 v20, v20, v22
	v_and_b32_e32 v22, 0xffff0000, v31
	v_lshlrev_b32_e32 v21, 16, v31
	v_mul_f32_e32 v22, v22, v22
	v_fmac_f32_e32 v22, v21, v21
	v_add_f32_e32 v20, v20, v22
	v_add_f32_e32 v20, v92, v20
	v_mov_b32_e32 v21, v20
	s_nop 1
	v_permlane16_swap_b32_e32 v21, v20
	global_store_dwordx4 v[108:109], v[28:31], off offset:256
	s_waitcnt lgkmcnt(0)
	v_add_f32_e32 v20, v20, v21
	v_mov_b32_e32 v21, v20
	s_nop 1
	v_permlane32_swap_b32_e32 v21, v20
	s_and_saveexec_b64 s[4:5], vcc
	s_cbranch_execz .LBB0_1844
	v_lshlrev_b64 v[22:23], 6, v[134:135]
	v_lshl_add_u64 v[22:23], s[46:47], 0, v[22:23]
	v_lshl_add_u64 v[22:23], s[52:53], 2, v[22:23]
	s_lshl_b32 s92, s22, 2
	v_lshl_add_u64 v[22:23], v[22:23], 0, s[92:93]
	s_waitcnt lgkmcnt(0)
	v_add_f32_e32 v20, v20, v21
	global_store_dword v[22:23], v20, off
; __device__ __forceinline__ float bflo(unsigned w) { return __uint_as_float(w << 16); }
; __device__ __forceinline__ float bfhi(unsigned w) { return __uint_as_float(w & 0xffff0000u); }
;     __device__ __forceinline__ void operator()(const f32x4 (&acc)[2][2][4][2], const Unit& u, int wr, int wc, int fr, int fq) const {
;     ...
;         for (int q = 0; q < 8; ++q) { const int ai = q >> 2, m = q & 3; const int row = row0 + ai * HALF + m * 16; float s = 0.f;
;             if ((q & 1) == 0 && q + 2 < 8) {
; #pragma unroll
;                 for (int h2 = 0; h2 < 2; ++h2)
; #pragma unroll
;                     for (int bj = 0; bj < 2; ++bj) { const int qn = q + 2 + h2; xnxt[h2][bj] = *(const u32x4*)(X + (size_t)(row0 + (qn >> 2) * HALF + (qn & 3) * 16) * 1024 + col0 + bj * HALF); } }
; #pragma unroll
;                 for (int bj = 0; bj < 2; ++bj) { bf16_t* p = X + (size_t)row * 1024 + col0 + bj * HALF; const u32x4 xv = xcur[q & 1][bj];
;                     f32x4 a = acc[ai][bj][m][0] * scale, b = acc[ai][bj][m][1] * scale;
;                     a[0] += bflo(xv.x); a[1] += bfhi(xv.x); a[2] += bflo(xv.y); a[3] += bfhi(xv.y); b[0] += bflo(xv.z); b[1] += bfhi(xv.z); b[2] += bflo(xv.w); b[3] += bfhi(xv.w);
;                     const u32x4 w = pack8(a, b); *(u32x4*)p = w;
;                     if constexpr (WX8) { unsigned q0 = 0u, q1 = 0u; q0 = __builtin_amdgcn_cvt_pk_fp8_f32(bflo(w.x), bfhi(w.x), q0, false); q0 = __builtin_amdgcn_cvt_pk_fp8_f32(bflo(w.y), bfhi(w.y), q0, true); q1 = __builtin_amdgcn_cvt_pk_fp8_f32(bflo(w.z), bfhi(w.z), q1, false); q1 = __builtin_amdgcn_cvt_pk_fp8_f32(bflo(w.w), bfhi(w.w), q1, true);
;                         *(u32x2*)((unsigned char*)X + (WS_X8 - WS_X) + (size_t)row * 1024 + col0 + bj * HALF) = (u32x2){q0, q1}; }
;                     s += (bflo(w.x) * bflo(w.x) + bfhi(w.x) * bfhi(w.x)) + (bflo(w.y) * bflo(w.y) + bfhi(w.y) * bfhi(w.y)) + (bflo(w.z) * bflo(w.z) + bfhi(w.z) * bfhi(w.z)) + (bflo(w.w) * bflo(w.w) + bfhi(w.w) * bfhi(w.w)); }
;                 s += __shfl_xor(s, 16); s += __shfl_xor(s, 32);
;                 if (fq == 0) ssn[(size_t)row * 16 + u.pn * 4 + wc] = s;
;             if (q & 1) { asm volatile("" ::: "memory");
; #pragma unroll
;                 for (int h2 = 0; h2 < 2; ++h2)
; #pragma unroll
;                     for (int bj = 0; bj < 2; ++bj) xcur[h2][bj] = xnxt[h2][bj]; } }
.LBB0_1844:
	s_or_b64 exec, exec, s[4:5]
	v_pk_mul_f32 v[28:29], v[80:81], s[28:29] op_sel_hi:[1,0]
	v_pk_mul_f32 v[30:31], v[78:79], s[28:29] op_sel_hi:[1,0]
	s_waitcnt vmcnt(11)
	v_lshlrev_b32_e32 v78, 16, v12
	v_and_b32_e32 v12, 0xffff0000, v12
	v_pk_mul_f32 v[22:23], v[82:83], s[28:29] op_sel_hi:[1,0]
	v_add_f32_e32 v12, v29, v12
	v_lshlrev_b32_e32 v29, 16, v13
	v_and_b32_e32 v13, 0xffff0000, v13
	s_waitcnt lgkmcnt(0)
	v_lshl_add_u64 v[20:21], s[44:45], 0, v[136:137]
	v_pk_mul_f32 v[76:77], v[76:77], s[28:29] op_sel_hi:[1,0]
	v_add_f32_e32 v22, v22, v29
	v_add_f32_e32 v13, v23, v13
	v_lshlrev_b32_e32 v23, 16, v14
	v_and_b32_e32 v14, 0xffff0000, v14
	v_lshlrev_b32_e32 v29, 16, v15
	v_and_b32_e32 v15, 0xffff0000, v15
	v_lshl_add_u64 v[20:21], v[174:175], 1, v[20:21]
	v_add_f32_e32 v28, v28, v78
	v_add_f32_e32 v14, v77, v14
	v_add_f32_e32 v15, v31, v15
	v_cvt_pk_bf16_f32 v12, v28, v12
	v_add_f32_e32 v23, v76, v23
	v_add_f32_e32 v29, v30, v29
	v_cvt_pk_bf16_f32 v13, v22, v13
	v_cvt_pk_bf16_f32 v14, v23, v14
	v_cvt_pk_bf16_f32 v15, v29, v15
	global_store_dwordx4 v[20:21], v[12:15], off
	v_lshlrev_b32_e32 v22, 16, v12
	s_waitcnt vmcnt(11)
	v_lshlrev_b32_e32 v31, 16, v4
	v_and_b32_e32 v12, 0xffff0000, v12
	v_mul_f32_e32 v12, v12, v12
	v_fmac_f32_e32 v12, v22, v22
	v_lshlrev_b32_e32 v22, 16, v13
	v_and_b32_e32 v13, 0xffff0000, v13
	v_mul_f32_e32 v13, v13, v13
	v_fmac_f32_e32 v13, v22, v22
	v_add_f32_e32 v12, v12, v13
	v_lshlrev_b32_e32 v13, 16, v14
	v_and_b32_e32 v14, 0xffff0000, v14
	v_mul_f32_e32 v14, v14, v14
	v_fmac_f32_e32 v14, v13, v13
	v_add_f32_e32 v12, v12, v14
	v_and_b32_e32 v14, 0xffff0000, v15
	v_lshlrev_b32_e32 v13, 16, v15
	v_mul_f32_e32 v14, v14, v14
	v_fmac_f32_e32 v14, v13, v13
	v_add_f32_e32 v30, v12, v14
	v_pk_mul_f32 v[14:15], v[72:73], s[28:29] op_sel_hi:[1,0]
	v_and_b32_e32 v4, 0xffff0000, v4
	v_pk_mul_f32 v[12:13], v[74:75], s[28:29] op_sel_hi:[1,0]
	v_add_f32_e32 v4, v15, v4
	v_lshlrev_b32_e32 v15, 16, v5
	v_pk_mul_f32 v[28:29], v[68:69], s[28:29] op_sel_hi:[1,0]
	v_add_f32_e32 v15, v12, v15
	v_and_b32_e32 v5, 0xffff0000, v5
	v_lshlrev_b32_e32 v12, 16, v6
	v_pk_mul_f32 v[22:23], v[70:71], s[28:29] op_sel_hi:[1,0]
	v_add_f32_e32 v5, v13, v5
	v_add_f32_e32 v28, v28, v12
	v_and_b32_e32 v6, 0xffff0000, v6
	v_lshlrev_b32_e32 v12, 16, v7
	v_add_f32_e32 v14, v14, v31
	v_add_f32_e32 v6, v29, v6
	v_add_f32_e32 v22, v22, v12
	v_cvt_pk_bf16_f32 v12, v14, v4
	v_cvt_pk_bf16_f32 v13, v15, v5
	v_cvt_pk_bf16_f32 v14, v28, v6
	v_and_b32_e32 v7, 0xffff0000, v7
	v_and_b32_e32 v5, 0xffff0000, v12
	v_lshlrev_b32_e32 v4, 16, v12
	v_mul_f32_e32 v5, v5, v5
	v_and_b32_e32 v6, 0xffff0000, v13
	v_fmac_f32_e32 v5, v4, v4
	v_lshlrev_b32_e32 v4, 16, v13
	v_mul_f32_e32 v6, v6, v6
	v_fmac_f32_e32 v6, v4, v4
	v_add_f32_e32 v4, v5, v6
	v_and_b32_e32 v6, 0xffff0000, v14
	v_lshlrev_b32_e32 v5, 16, v14
	v_mul_f32_e32 v6, v6, v6
	v_fmac_f32_e32 v6, v5, v5
	v_add_f32_e32 v7, v23, v7
	v_cvt_pk_bf16_f32 v15, v22, v7
	v_add_f32_e32 v4, v4, v6
	v_and_b32_e32 v6, 0xffff0000, v15
	v_lshlrev_b32_e32 v5, 16, v15
	v_mul_f32_e32 v6, v6, v6
	v_fmac_f32_e32 v6, v5, v5
	v_add_f32_e32 v4, v4, v6
	v_add_f32_e32 v4, v30, v4
	v_mov_b32_e32 v5, v4
	s_nop 1
	v_permlane16_swap_b32_e32 v5, v4
	global_store_dwordx4 v[20:21], v[12:15], off offset:256
	s_waitcnt lgkmcnt(0)
	v_add_f32_e32 v4, v4, v5
	v_mov_b32_e32 v5, v4
	s_nop 1
	v_permlane32_swap_b32_e32 v5, v4
	s_and_saveexec_b64 s[4:5], vcc
	s_cbranch_execz .LBB0_1846
	v_lshlrev_b64 v[6:7], 6, v[132:133]
	v_lshl_add_u64 v[6:7], s[46:47], 0, v[6:7]
	v_lshl_add_u64 v[6:7], s[52:53], 2, v[6:7]
	s_lshl_b32 s92, s22, 2
	v_lshl_add_u64 v[6:7], v[6:7], 0, s[92:93]
	s_waitcnt lgkmcnt(0)
	v_add_f32_e32 v4, v4, v5
	global_store_dword v[6:7], v4, off
.LBB0_1846:
	s_or_b64 exec, exec, s[4:5]
	v_pk_mul_f32 v[6:7], v[64:65], s[28:29] op_sel_hi:[1,0]
	s_waitcnt vmcnt(7)
	v_lshlrev_b32_e32 v22, 16, v32
	s_waitcnt lgkmcnt(0)
	v_lshl_add_u64 v[4:5], s[44:45], 0, v[106:107]
	v_add_f32_e32 v6, v6, v22
	v_and_b32_e32 v22, 0xffff0000, v32
	v_lshl_add_u64 v[20:21], v[174:175], 1, v[4:5]
	v_pk_mul_f32 v[4:5], v[66:67], s[28:29] op_sel_hi:[1,0]
	v_add_f32_e32 v7, v7, v22
	v_lshlrev_b32_e32 v22, 16, v33
	v_add_f32_e32 v22, v4, v22
	v_and_b32_e32 v4, 0xffff0000, v33
	v_pk_mul_f32 v[14:15], v[60:61], s[28:29] op_sel_hi:[1,0]
	v_add_f32_e32 v5, v5, v4
	v_lshlrev_b32_e32 v4, 16, v34
	v_add_f32_e32 v14, v14, v4
	v_and_b32_e32 v4, 0xffff0000, v34
	v_pk_mul_f32 v[12:13], v[62:63], s[28:29] op_sel_hi:[1,0]
	v_add_f32_e32 v15, v15, v4
	v_lshlrev_b32_e32 v4, 16, v35
	v_add_f32_e32 v12, v12, v4
	v_and_b32_e32 v4, 0xffff0000, v35
	v_add_f32_e32 v13, v13, v4
	v_cvt_pk_bf16_f32 v4, v6, v7
	v_cvt_pk_bf16_f32 v5, v22, v5
	v_cvt_pk_bf16_f32 v6, v14, v15
	v_cvt_pk_bf16_f32 v7, v12, v13
	global_store_dwordx4 v[20:21], v[4:7], off
	v_lshlrev_b32_e32 v12, 16, v4
	s_waitcnt vmcnt(7)
; __device__ __forceinline__ float bflo(unsigned w) { return __uint_as_float(w << 16); }
; __device__ __forceinline__ float bfhi(unsigned w) { return __uint_as_float(w & 0xffff0000u); }
;     __device__ __forceinline__ void operator()(const f32x4 (&acc)[2][2][4][2], const Unit& u, int wr, int wc, int fr, int fq) const {
;     ...
;         for (int q = 0; q < 8; ++q) { const int ai = q >> 2, m = q & 3; const int row = row0 + ai * HALF + m * 16; float s = 0.f;
;             if ((q & 1) == 0 && q + 2 < 8) {
; #pragma unroll
;                 for (int h2 = 0; h2 < 2; ++h2)
; #pragma unroll
;                     for (int bj = 0; bj < 2; ++bj) { const int qn = q + 2 + h2; xnxt[h2][bj] = *(const u32x4*)(X + (size_t)(row0 + (qn >> 2) * HALF + (qn & 3) * 16) * 1024 + col0 + bj * HALF); } }
; #pragma unroll
;                 for (int bj = 0; bj < 2; ++bj) { bf16_t* p = X + (size_t)row * 1024 + col0 + bj * HALF; const u32x4 xv = xcur[q & 1][bj];
;                     f32x4 a = acc[ai][bj][m][0] * scale, b = acc[ai][bj][m][1] * scale;
;                     a[0] += bflo(xv.x); a[1] += bfhi(xv.x); a[2] += bflo(xv.y); a[3] += bfhi(xv.y); b[0] += bflo(xv.z); b[1] += bfhi(xv.z); b[2] += bflo(xv.w); b[3] += bfhi(xv.w);
;                     const u32x4 w = pack8(a, b); *(u32x4*)p = w;
;                     if constexpr (WX8) { unsigned q0 = 0u, q1 = 0u; q0 = __builtin_amdgcn_cvt_pk_fp8_f32(bflo(w.x), bfhi(w.x), q0, false); q0 = __builtin_amdgcn_cvt_pk_fp8_f32(bflo(w.y), bfhi(w.y), q0, true); q1 = __builtin_amdgcn_cvt_pk_fp8_f32(bflo(w.z), bfhi(w.z), q1, false); q1 = __builtin_amdgcn_cvt_pk_fp8_f32(bflo(w.w), bfhi(w.w), q1, true);
;                         *(u32x2*)((unsigned char*)X + (WS_X8 - WS_X) + (size_t)row * 1024 + col0 + bj * HALF) = (u32x2){q0, q1}; }
;                     s += (bflo(w.x) * bflo(w.x) + bfhi(w.x) * bfhi(w.x)) + (bflo(w.y) * bflo(w.y) + bfhi(w.y) * bfhi(w.y)) + (bflo(w.z) * bflo(w.z) + bfhi(w.z) * bfhi(w.z)) + (bflo(w.w) * bflo(w.w) + bfhi(w.w) * bfhi(w.w)); }
;                 s += __shfl_xor(s, 16); s += __shfl_xor(s, 32);
;                 if (fq == 0) ssn[(size_t)row * 16 + u.pn * 4 + wc] = s;
;             if (q & 1) { asm volatile("" ::: "memory");
; #pragma unroll
;                 for (int h2 = 0; h2 < 2; ++h2)
; #pragma unroll
;                     for (int bj = 0; bj < 2; ++bj) xcur[h2][bj] = xnxt[h2][bj]; } }
	v_lshlrev_b32_e32 v23, 16, v24
	v_and_b32_e32 v4, 0xffff0000, v4
	v_mul_f32_e32 v4, v4, v4
	v_fmac_f32_e32 v4, v12, v12
	v_lshlrev_b32_e32 v12, 16, v5
	v_and_b32_e32 v5, 0xffff0000, v5
	v_mul_f32_e32 v5, v5, v5
	v_fmac_f32_e32 v5, v12, v12
	v_add_f32_e32 v4, v4, v5
	v_lshlrev_b32_e32 v5, 16, v6
	v_and_b32_e32 v6, 0xffff0000, v6
	v_mul_f32_e32 v6, v6, v6
	v_fmac_f32_e32 v6, v5, v5
	v_add_f32_e32 v4, v4, v6
	v_and_b32_e32 v6, 0xffff0000, v7
	v_lshlrev_b32_e32 v5, 16, v7
	v_mul_f32_e32 v6, v6, v6
	v_fmac_f32_e32 v6, v5, v5
	v_add_f32_e32 v22, v4, v6
	v_pk_mul_f32 v[6:7], v[56:57], s[28:29] op_sel_hi:[1,0]
	v_pk_mul_f32 v[4:5], v[58:59], s[28:29] op_sel_hi:[1,0]
	v_add_f32_e32 v6, v6, v23
	v_and_b32_e32 v23, 0xffff0000, v24
	v_add_f32_e32 v7, v7, v23
	v_lshlrev_b32_e32 v23, 16, v25
	v_add_f32_e32 v4, v4, v23
	v_and_b32_e32 v23, 0xffff0000, v25
	v_pk_mul_f32 v[14:15], v[52:53], s[28:29] op_sel_hi:[1,0]
	v_add_f32_e32 v5, v5, v23
	v_lshlrev_b32_e32 v23, 16, v26
	v_add_f32_e32 v14, v14, v23
	v_and_b32_e32 v23, 0xffff0000, v26
	v_pk_mul_f32 v[12:13], v[54:55], s[28:29] op_sel_hi:[1,0]
	v_add_f32_e32 v15, v15, v23
	v_lshlrev_b32_e32 v23, 16, v27
	v_add_f32_e32 v23, v12, v23
	v_and_b32_e32 v12, 0xffff0000, v27
	v_add_f32_e32 v24, v13, v12
	v_cvt_pk_bf16_f32 v12, v6, v7
	v_cvt_pk_bf16_f32 v13, v4, v5
	v_cvt_pk_bf16_f32 v14, v14, v15
	v_cvt_pk_bf16_f32 v15, v23, v24
	global_store_dwordx4 v[20:21], v[12:15], off offset:256
	v_and_b32_e32 v5, 0xffff0000, v12
	v_lshlrev_b32_e32 v4, 16, v12
	v_mul_f32_e32 v5, v5, v5
	v_and_b32_e32 v6, 0xffff0000, v13
	v_fmac_f32_e32 v5, v4, v4
	v_lshlrev_b32_e32 v4, 16, v13
	v_mul_f32_e32 v6, v6, v6
	v_fmac_f32_e32 v6, v4, v4
	v_add_f32_e32 v4, v5, v6
	v_and_b32_e32 v6, 0xffff0000, v14
	v_lshlrev_b32_e32 v5, 16, v14
	v_mul_f32_e32 v6, v6, v6
	v_fmac_f32_e32 v6, v5, v5
	v_add_f32_e32 v4, v4, v6
	v_and_b32_e32 v6, 0xffff0000, v15
	v_lshlrev_b32_e32 v5, 16, v15
	v_mul_f32_e32 v6, v6, v6
	v_fmac_f32_e32 v6, v5, v5
	v_add_f32_e32 v4, v4, v6
	v_add_f32_e32 v4, v22, v4
	v_mov_b32_e32 v5, v4
	s_nop 1
	v_permlane16_swap_b32_e32 v5, v4
	s_waitcnt lgkmcnt(0)
	v_add_f32_e32 v4, v4, v5
	v_mov_b32_e32 v5, v4
	s_nop 1
	v_permlane32_swap_b32_e32 v5, v4
	s_and_saveexec_b64 s[4:5], vcc
	s_cbranch_execz .LBB0_1848
	v_lshlrev_b64 v[6:7], 6, v[102:103]
	v_lshl_add_u64 v[6:7], s[46:47], 0, v[6:7]
	v_lshl_add_u64 v[6:7], s[52:53], 2, v[6:7]
	s_lshl_b32 s92, s22, 2
	v_lshl_add_u64 v[6:7], v[6:7], 0, s[92:93]
	s_waitcnt lgkmcnt(0)
	v_add_f32_e32 v4, v4, v5
	global_store_dword v[6:7], v4, off
.LBB0_1848:
	s_or_b64 exec, exec, s[4:5]
	s_waitcnt lgkmcnt(0)
	v_lshl_add_u64 v[4:5], s[44:45], 0, v[104:105]
	v_pk_mul_f32 v[6:7], v[48:49], s[28:29] op_sel_hi:[1,0]
	s_waitcnt vmcnt(7)
	v_lshlrev_b32_e32 v22, 16, v16
	v_and_b32_e32 v16, 0xffff0000, v16
	v_lshl_add_u64 v[12:13], v[174:175], 1, v[4:5]
	v_pk_mul_f32 v[4:5], v[50:51], s[28:29] op_sel_hi:[1,0]
	v_add_f32_e32 v7, v7, v16
	v_lshlrev_b32_e32 v16, 16, v17
	v_add_f32_e32 v16, v4, v16
	v_and_b32_e32 v4, 0xffff0000, v17
	v_pk_mul_f32 v[20:21], v[44:45], s[28:29] op_sel_hi:[1,0]
	v_add_f32_e32 v5, v5, v4
	v_lshlrev_b32_e32 v4, 16, v18
	v_add_f32_e32 v17, v20, v4
	v_and_b32_e32 v4, 0xffff0000, v18
	v_pk_mul_f32 v[14:15], v[46:47], s[28:29] op_sel_hi:[1,0]
	v_add_f32_e32 v18, v21, v4
	v_lshlrev_b32_e32 v4, 16, v19
	v_add_f32_e32 v14, v14, v4
	v_and_b32_e32 v4, 0xffff0000, v19
	v_add_f32_e32 v6, v6, v22
	v_add_f32_e32 v15, v15, v4
	v_cvt_pk_bf16_f32 v4, v6, v7
	v_cvt_pk_bf16_f32 v5, v16, v5
	v_cvt_pk_bf16_f32 v6, v17, v18
	v_cvt_pk_bf16_f32 v7, v14, v15
	global_store_dwordx4 v[12:13], v[4:7], off
	v_lshlrev_b32_e32 v14, 16, v4
	s_waitcnt vmcnt(7)
	v_lshlrev_b32_e32 v19, 16, v8
	v_and_b32_e32 v4, 0xffff0000, v4
	v_mul_f32_e32 v4, v4, v4
	v_fmac_f32_e32 v4, v14, v14
	v_lshlrev_b32_e32 v14, 16, v5
	v_and_b32_e32 v5, 0xffff0000, v5
	v_mul_f32_e32 v5, v5, v5
	v_fmac_f32_e32 v5, v14, v14
	v_add_f32_e32 v4, v4, v5
	v_lshlrev_b32_e32 v5, 16, v6
	v_and_b32_e32 v6, 0xffff0000, v6
	v_mul_f32_e32 v6, v6, v6
	v_fmac_f32_e32 v6, v5, v5
	v_add_f32_e32 v4, v4, v6
	v_and_b32_e32 v6, 0xffff0000, v7
	v_lshlrev_b32_e32 v5, 16, v7
	v_mul_f32_e32 v6, v6, v6
	v_fmac_f32_e32 v6, v5, v5
	v_add_f32_e32 v18, v4, v6
	v_pk_mul_f32 v[6:7], v[40:41], s[28:29] op_sel_hi:[1,0]
	v_and_b32_e32 v8, 0xffff0000, v8
	v_pk_mul_f32 v[4:5], v[42:43], s[28:29] op_sel_hi:[1,0]
	v_add_f32_e32 v7, v7, v8
	v_lshlrev_b32_e32 v8, 16, v9
	v_add_f32_e32 v4, v4, v8
	v_and_b32_e32 v8, 0xffff0000, v9
	v_pk_mul_f32 v[14:15], v[38:39], s[28:29] op_sel_hi:[1,0]
	v_pk_mul_f32 v[16:17], v[36:37], s[28:29] op_sel_hi:[1,0]
	v_add_f32_e32 v6, v6, v19
	v_add_f32_e32 v5, v5, v8
	v_lshlrev_b32_e32 v8, 16, v10
	v_and_b32_e32 v9, 0xffff0000, v10
	v_lshlrev_b32_e32 v10, 16, v11
	v_add_f32_e32 v8, v16, v8
	v_add_f32_e32 v9, v17, v9
	v_add_f32_e32 v10, v14, v10
	v_and_b32_e32 v11, 0xffff0000, v11
	v_cvt_pk_bf16_f32 v6, v6, v7
	v_cvt_pk_bf16_f32 v7, v4, v5
	v_add_f32_e32 v11, v15, v11
	v_and_b32_e32 v5, 0xffff0000, v6
	v_cvt_pk_bf16_f32 v8, v8, v9
	v_cvt_pk_bf16_f32 v9, v10, v11
	v_lshlrev_b32_e32 v4, 16, v6
	v_mul_f32_e32 v5, v5, v5
	v_and_b32_e32 v10, 0xffff0000, v7
	v_fmac_f32_e32 v5, v4, v4
	v_lshlrev_b32_e32 v4, 16, v7
	v_mul_f32_e32 v10, v10, v10
	v_fmac_f32_e32 v10, v4, v4
	v_add_f32_e32 v4, v5, v10
	v_and_b32_e32 v10, 0xffff0000, v8
	v_lshlrev_b32_e32 v5, 16, v8
	v_mul_f32_e32 v10, v10, v10
	v_fmac_f32_e32 v10, v5, v5
	v_add_f32_e32 v4, v4, v10
	v_and_b32_e32 v10, 0xffff0000, v9
	v_lshlrev_b32_e32 v5, 16, v9
	v_mul_f32_e32 v10, v10, v10
	v_fmac_f32_e32 v10, v5, v5
	v_add_f32_e32 v4, v4, v10
	v_add_f32_e32 v4, v18, v4
	v_mov_b32_e32 v5, v4
	s_nop 1
	v_permlane16_swap_b32_e32 v5, v4
	global_store_dwordx4 v[12:13], v[6:9], off offset:256
	s_waitcnt lgkmcnt(0)
	v_add_f32_e32 v4, v4, v5
	v_mov_b32_e32 v5, v4
	s_nop 1
	v_permlane32_swap_b32_e32 v5, v4
	s_and_saveexec_b64 s[4:5], vcc
	s_cbranch_execz .LBB0_1850
	v_lshlrev_b64 v[6:7], 6, v[100:101]
	v_lshl_add_u64 v[6:7], s[46:47], 0, v[6:7]
	v_lshl_add_u64 v[6:7], s[52:53], 2, v[6:7]
	s_lshl_b32 s92, s22, 2
	v_lshl_add_u64 v[6:7], v[6:7], 0, s[92:93]
	s_waitcnt lgkmcnt(0)
	v_add_f32_e32 v4, v4, v5
	global_store_dword v[6:7], v4, off
